# non-temporal loads on the read-once streams (f32 weights being quantised; expert-output / pre-norm rows in the combine phase)
# speedup vs baseline: 1.0526x; 1.0071x over previous
; template <bool PERMGL, bool FP8>
; __device__ __forceinline__ void q8_cols_item(const float* W, int N, int n0, unsigned char* Bq, float* sc_out, LAS float* AM, int par, int wave, int lane) {
;     const int n = n0 + lane;
;     const float* Wp = W + (size_t)(128 * wave) * N + n;
;     float v[128]; float am = 0.f;
; #pragma unroll
;     for (int i = 0; i < 128; ++i) v[i] = Wp[(size_t)i * N];
; __global__ void __launch_bounds__(NWAVES * 64, 2) mk_fwd(Args args) {
;     ...
;             for (int it = bx; it < 64 + 72; it += G, par ^= 1) {
;                 if (it < 64) { const int mi = it >> 5, nb = it & 31;
;                     q8_cols_item<false, false>(args.in[1] + (size_t)mi * D * EVEN_IN, EVEN_IN, nb * 64, ws + WS_EVIN + (size_t)mi * EVEN_IN * 1024, (float*)(ws + WS_SBIN) + mi * EVEN_IN, AM, par, wave, lane); }
;                 else { const int r = it - 64, mi = r / 36, nb = r % 36;
;                     q8_cols_item<false, false>(args.in[6] + (size_t)mi * D * ODD_IN, ODD_IN, nb * 64, ws + WS_ODIN + (size_t)mi * ODD_IN * 1024, (float*)(ws + WS_SBIN) + 16384 + mi * ODD_IN, AM, par, wave, lane); }
.LBB0_9:
	s_cmp_gt_i32 s77, 63
	s_mov_b64 s[4:5], -1
	s_cbranch_scc0 .LBB0_13
	s_sub_i32 s6, s77, 64
	s_cmp_gt_u32 s6, 35
	s_cselect_b64 s[4:5], -1, 0
	s_add_i32 s7, s77, 0xffffff9c
	s_cmp_lt_u32 s6, 36
	s_cselect_b32 s33, s6, s7
	s_and_b64 s[6:7], s[4:5], exec
	s_cselect_b32 s6, 0x240000, 0
	v_readlane_b32 s7, v252, 26
	s_cselect_b32 s79, 0x900000, 0
	s_add_u32 s6, s7, s6
	v_readlane_b32 s7, v252, 27
	s_addc_u32 s7, s7, 0
	v_lshl_add_u32 v4, s33, 6, v0
	s_add_u32 s80, s8, s79
	s_addc_u32 s81, s9, 0
	v_ashrrev_i32_e32 v5, 31, v4
	v_lshl_add_u64 v[6:7], v[4:5], 2, s[80:81]
	v_add_co_u32_e32 v8, vcc, s16, v6
	s_mov_b32 s33, 0x9000
	s_nop 0
	v_addc_co_u32_e32 v9, vcc, 0, v7, vcc
	global_load_dword v13, v[8:9], off offset:1024 nt
	v_add_co_u32_e32 v8, vcc, s17, v6
	global_load_dword v12, v[6:7], off nt
	s_nop 0
	v_addc_co_u32_e32 v9, vcc, 0, v7, vcc
	global_load_dword v14, v[8:9], off offset:2048 nt
	v_add_co_u32_e32 v8, vcc, s18, v6
	s_nop 1
	v_addc_co_u32_e32 v9, vcc, 0, v7, vcc
	global_load_dword v15, v[8:9], off offset:3072 nt
	v_add_co_u32_e32 v8, vcc, s33, v6
	s_mov_b32 s33, 0xb000
	s_nop 0
	v_addc_co_u32_e32 v9, vcc, 0, v7, vcc
	global_load_dword v16, v[8:9], off nt
	v_add_co_u32_e32 v8, vcc, s33, v6
	s_mov_b32 s33, 0xd000
	s_nop 0
	v_addc_co_u32_e32 v9, vcc, 0, v7, vcc
	global_load_dword v17, v[8:9], off offset:1024 nt
	v_add_co_u32_e32 v8, vcc, s33, v6
	s_mov_b32 s33, 0xf000
	s_nop 0
	v_addc_co_u32_e32 v9, vcc, 0, v7, vcc
	global_load_dword v18, v[8:9], off offset:2048 nt
	v_add_co_u32_e32 v8, vcc, s33, v6
	s_mov_b32 s33, 0x1b000
	s_nop 0
	v_addc_co_u32_e32 v9, vcc, 0, v7, vcc
	global_load_dword v19, v[8:9], off offset:3072 nt
	v_add_co_u32_e32 v8, vcc, s19, v6
	s_nop 1
	v_addc_co_u32_e32 v9, vcc, 0, v7, vcc
	global_load_dword v20, v[8:9], off nt
	v_add_co_u32_e32 v8, vcc, s20, v6
	s_nop 1
	v_addc_co_u32_e32 v9, vcc, 0, v7, vcc
	global_load_dword v21, v[8:9], off offset:1024 nt
	v_add_co_u32_e32 v8, vcc, s21, v6
	s_nop 1
	v_addc_co_u32_e32 v9, vcc, 0, v7, vcc
	global_load_dword v22, v[8:9], off offset:2048 nt
	v_add_co_u32_e32 v8, vcc, s22, v6
	s_nop 1
	v_addc_co_u32_e32 v9, vcc, 0, v7, vcc
	global_load_dword v23, v[8:9], off offset:3072 nt
	v_add_co_u32_e32 v8, vcc, s33, v6
	s_mov_b32 s33, 0x1d000
	s_nop 0
	v_addc_co_u32_e32 v9, vcc, 0, v7, vcc
	global_load_dword v24, v[8:9], off nt
	v_add_co_u32_e32 v8, vcc, s33, v6
	s_mov_b32 s33, 0x1f000
	s_nop 0
	v_addc_co_u32_e32 v9, vcc, 0, v7, vcc
	global_load_dword v25, v[8:9], off offset:1024 nt
	v_add_co_u32_e32 v8, vcc, s33, v6
	s_mov_b32 s33, 0x21000
	s_nop 0
	v_addc_co_u32_e32 v9, vcc, 0, v7, vcc
	global_load_dword v26, v[8:9], off offset:2048 nt
	v_add_co_u32_e32 v8, vcc, s33, v6
	s_mov_b32 s33, 0x2d000
	s_nop 0
	v_addc_co_u32_e32 v9, vcc, 0, v7, vcc
	global_load_dword v27, v[8:9], off offset:3072 nt
	v_add_co_u32_e32 v8, vcc, s23, v6
	s_nop 1
	v_addc_co_u32_e32 v9, vcc, 0, v7, vcc
	global_load_dword v28, v[8:9], off nt
	v_add_co_u32_e32 v8, vcc, s24, v6
	s_nop 1
	v_addc_co_u32_e32 v9, vcc, 0, v7, vcc
	global_load_dword v29, v[8:9], off offset:1024 nt
	v_add_co_u32_e32 v8, vcc, s25, v6
	s_nop 1
	v_addc_co_u32_e32 v9, vcc, 0, v7, vcc
	global_load_dword v30, v[8:9], off offset:2048 nt
	v_add_co_u32_e32 v8, vcc, s26, v6
	s_nop 1
	v_addc_co_u32_e32 v9, vcc, 0, v7, vcc
	global_load_dword v31, v[8:9], off offset:3072 nt
	v_add_co_u32_e32 v8, vcc, s33, v6
	s_mov_b32 s33, 0x2f000
	s_nop 0
	v_addc_co_u32_e32 v9, vcc, 0, v7, vcc
	global_load_dword v32, v[8:9], off nt
	v_add_co_u32_e32 v8, vcc, s33, v6
	s_mov_b32 s33, 0x31000
	s_nop 0
	v_addc_co_u32_e32 v9, vcc, 0, v7, vcc
	global_load_dword v33, v[8:9], off offset:1024 nt
	v_add_co_u32_e32 v8, vcc, s33, v6
	s_mov_b32 s33, 0x33000
	s_nop 0
	v_addc_co_u32_e32 v9, vcc, 0, v7, vcc
	global_load_dword v34, v[8:9], off offset:2048 nt
	v_add_co_u32_e32 v8, vcc, s33, v6
	s_mov_b32 s33, 0x3f000
	s_nop 0
	v_addc_co_u32_e32 v9, vcc, 0, v7, vcc
	global_load_dword v35, v[8:9], off offset:3072 nt
	v_add_co_u32_e32 v8, vcc, s27, v6
	s_nop 1
	v_addc_co_u32_e32 v9, vcc, 0, v7, vcc
	global_load_dword v36, v[8:9], off nt
	v_add_co_u32_e32 v8, vcc, s28, v6
	s_nop 1
	v_addc_co_u32_e32 v9, vcc, 0, v7, vcc
	global_load_dword v37, v[8:9], off offset:1024 nt
	v_add_co_u32_e32 v8, vcc, s29, v6
	s_nop 1
	v_addc_co_u32_e32 v9, vcc, 0, v7, vcc
	global_load_dword v38, v[8:9], off offset:2048 nt
	v_add_co_u32_e32 v8, vcc, s30, v6
	s_nop 1
	v_addc_co_u32_e32 v9, vcc, 0, v7, vcc
	global_load_dword v39, v[8:9], off offset:3072 nt
	v_add_co_u32_e32 v8, vcc, s33, v6
	s_mov_b32 s33, 0x41000
	s_nop 0
	v_addc_co_u32_e32 v9, vcc, 0, v7, vcc
	global_load_dword v40, v[8:9], off nt
	v_add_co_u32_e32 v8, vcc, s33, v6
	s_mov_b32 s33, 0x43000
	s_nop 0
	v_addc_co_u32_e32 v9, vcc, 0, v7, vcc
	global_load_dword v41, v[8:9], off offset:1024 nt
	v_add_co_u32_e32 v8, vcc, s33, v6
	s_mov_b32 s33, 0x45000
	s_nop 0
	v_addc_co_u32_e32 v9, vcc, 0, v7, vcc
	global_load_dword v43, v[8:9], off offset:2048 nt
	v_add_co_u32_e32 v8, vcc, s33, v6
	s_mov_b32 s33, 0x51000
	s_nop 0
	v_addc_co_u32_e32 v9, vcc, 0, v7, vcc
	global_load_dword v46, v[8:9], off offset:3072 nt
	v_add_co_u32_e32 v8, vcc, s31, v6
	s_nop 1
	v_addc_co_u32_e32 v9, vcc, 0, v7, vcc
	global_load_dword v42, v[8:9], off nt
	v_add_co_u32_e32 v8, vcc, s34, v6
	s_nop 1
	v_addc_co_u32_e32 v9, vcc, 0, v7, vcc
	global_load_dword v44, v[8:9], off offset:1024 nt
	v_add_co_u32_e32 v8, vcc, s35, v6
	s_nop 1
	v_addc_co_u32_e32 v9, vcc, 0, v7, vcc
	global_load_dword v45, v[8:9], off offset:2048 nt
	v_add_co_u32_e32 v8, vcc, s36, v6
	s_nop 1
	v_addc_co_u32_e32 v9, vcc, 0, v7, vcc
	global_load_dword v47, v[8:9], off offset:3072 nt
	v_add_co_u32_e32 v8, vcc, s33, v6
; template <bool PERMGL, bool FP8>
; __device__ __forceinline__ void q8_cols_item(const float* W, int N, int n0, unsigned char* Bq, float* sc_out, LAS float* AM, int par, int wave, int lane) {
;     ...
;     for (int i = 0; i < 128; ++i) v[i] = Wp[(size_t)i * N];
	s_mov_b32 s33, 0x53000
	s_nop 0
	v_addc_co_u32_e32 v9, vcc, 0, v7, vcc
	global_load_dword v48, v[8:9], off nt
	v_add_co_u32_e32 v8, vcc, s33, v6
	s_mov_b32 s33, 0x55000
	s_nop 0
	v_addc_co_u32_e32 v9, vcc, 0, v7, vcc
	global_load_dword v49, v[8:9], off offset:1024 nt
	v_add_co_u32_e32 v8, vcc, s33, v6
	s_mov_b32 s33, 0x57000
	s_nop 0
	v_addc_co_u32_e32 v9, vcc, 0, v7, vcc
	global_load_dword v50, v[8:9], off offset:2048 nt
	v_add_co_u32_e32 v8, vcc, s33, v6
	s_mov_b32 s33, 0x63000
	s_nop 0
	v_addc_co_u32_e32 v9, vcc, 0, v7, vcc
	global_load_dword v51, v[8:9], off offset:3072 nt
	v_add_co_u32_e32 v8, vcc, s37, v6
	s_nop 1
	v_addc_co_u32_e32 v9, vcc, 0, v7, vcc
	global_load_dword v52, v[8:9], off nt
	v_add_co_u32_e32 v8, vcc, s38, v6
	s_nop 1
	v_addc_co_u32_e32 v9, vcc, 0, v7, vcc
	global_load_dword v53, v[8:9], off offset:1024 nt
	v_add_co_u32_e32 v8, vcc, s39, v6
	s_nop 1
	v_addc_co_u32_e32 v9, vcc, 0, v7, vcc
	global_load_dword v54, v[8:9], off offset:2048 nt
	v_add_co_u32_e32 v8, vcc, s40, v6
	s_nop 1
	v_addc_co_u32_e32 v9, vcc, 0, v7, vcc
	global_load_dword v55, v[8:9], off offset:3072 nt
	v_add_co_u32_e32 v8, vcc, s33, v6
	s_mov_b32 s33, 0x65000
	s_nop 0
	v_addc_co_u32_e32 v9, vcc, 0, v7, vcc
	global_load_dword v56, v[8:9], off nt
	v_add_co_u32_e32 v8, vcc, s33, v6
	s_mov_b32 s33, 0x67000
	s_nop 0
	v_addc_co_u32_e32 v9, vcc, 0, v7, vcc
	global_load_dword v57, v[8:9], off offset:1024 nt
	v_add_co_u32_e32 v8, vcc, s33, v6
	s_mov_b32 s33, 0x69000
	s_nop 0
	v_addc_co_u32_e32 v9, vcc, 0, v7, vcc
	global_load_dword v58, v[8:9], off offset:2048 nt
	v_add_co_u32_e32 v8, vcc, s33, v6
	s_mov_b32 s33, 0x75000
	s_nop 0
	v_addc_co_u32_e32 v9, vcc, 0, v7, vcc
	global_load_dword v59, v[8:9], off offset:3072 nt
	v_add_co_u32_e32 v8, vcc, s41, v6
	s_nop 1
	v_addc_co_u32_e32 v9, vcc, 0, v7, vcc
	global_load_dword v60, v[8:9], off nt
	v_add_co_u32_e32 v8, vcc, s42, v6
	s_nop 1
	v_addc_co_u32_e32 v9, vcc, 0, v7, vcc
	global_load_dword v61, v[8:9], off offset:1024 nt
	v_add_co_u32_e32 v8, vcc, s43, v6
	s_nop 1
	v_addc_co_u32_e32 v9, vcc, 0, v7, vcc
	global_load_dword v62, v[8:9], off offset:2048 nt
	v_add_co_u32_e32 v8, vcc, s44, v6
	s_nop 1
	v_addc_co_u32_e32 v9, vcc, 0, v7, vcc
	global_load_dword v63, v[8:9], off offset:3072 nt
	v_add_co_u32_e32 v8, vcc, s33, v6
	s_mov_b32 s33, 0x77000
	s_nop 0
	v_addc_co_u32_e32 v9, vcc, 0, v7, vcc
	global_load_dword v64, v[8:9], off nt
	v_add_co_u32_e32 v8, vcc, s33, v6
	s_mov_b32 s33, 0x79000
	s_nop 0
	v_addc_co_u32_e32 v9, vcc, 0, v7, vcc
	global_load_dword v65, v[8:9], off offset:1024 nt
	v_add_co_u32_e32 v8, vcc, s33, v6
	s_mov_b32 s33, 0x7b000
	s_nop 0
	v_addc_co_u32_e32 v9, vcc, 0, v7, vcc
	global_load_dword v66, v[8:9], off offset:2048 nt
	v_add_co_u32_e32 v8, vcc, s33, v6
	s_mov_b32 s33, 0x87000
	s_nop 0
	v_addc_co_u32_e32 v9, vcc, 0, v7, vcc
	global_load_dword v67, v[8:9], off offset:3072 nt
	v_add_co_u32_e32 v8, vcc, s45, v6
	s_nop 1
	v_addc_co_u32_e32 v9, vcc, 0, v7, vcc
	global_load_dword v68, v[8:9], off nt
	v_add_co_u32_e32 v8, vcc, s46, v6
	s_nop 1
	v_addc_co_u32_e32 v9, vcc, 0, v7, vcc
	global_load_dword v69, v[8:9], off offset:1024 nt
	v_add_co_u32_e32 v8, vcc, s47, v6
	s_nop 1
	v_addc_co_u32_e32 v9, vcc, 0, v7, vcc
	global_load_dword v70, v[8:9], off offset:2048 nt
	v_add_co_u32_e32 v8, vcc, s48, v6
	s_nop 1
	v_addc_co_u32_e32 v9, vcc, 0, v7, vcc
	global_load_dword v71, v[8:9], off offset:3072 nt
	v_add_co_u32_e32 v8, vcc, s33, v6
	s_mov_b32 s33, 0x89000
	s_nop 0
	v_addc_co_u32_e32 v9, vcc, 0, v7, vcc
	global_load_dword v72, v[8:9], off nt
	v_add_co_u32_e32 v8, vcc, s33, v6
	s_mov_b32 s33, 0x8b000
	s_nop 0
	v_addc_co_u32_e32 v9, vcc, 0, v7, vcc
	global_load_dword v73, v[8:9], off offset:1024 nt
	v_add_co_u32_e32 v8, vcc, s33, v6
	s_mov_b32 s33, 0x8d000
	s_nop 0
	v_addc_co_u32_e32 v9, vcc, 0, v7, vcc
	global_load_dword v75, v[8:9], off offset:2048 nt
	v_add_co_u32_e32 v8, vcc, s33, v6
	s_mov_b32 s33, 0x99000
	s_nop 0
	v_addc_co_u32_e32 v9, vcc, 0, v7, vcc
	global_load_dword v78, v[8:9], off offset:3072 nt
	v_add_co_u32_e32 v8, vcc, s49, v6
	s_nop 1
	v_addc_co_u32_e32 v9, vcc, 0, v7, vcc
	global_load_dword v74, v[8:9], off nt
	v_add_co_u32_e32 v8, vcc, s50, v6
	s_nop 1
	v_addc_co_u32_e32 v9, vcc, 0, v7, vcc
	global_load_dword v76, v[8:9], off offset:1024 nt
	v_add_co_u32_e32 v8, vcc, s51, v6
	s_nop 1
	v_addc_co_u32_e32 v9, vcc, 0, v7, vcc
	global_load_dword v77, v[8:9], off offset:2048 nt
	v_add_co_u32_e32 v8, vcc, s52, v6
	s_nop 1
	v_addc_co_u32_e32 v9, vcc, 0, v7, vcc
	global_load_dword v79, v[8:9], off offset:3072 nt
	v_add_co_u32_e32 v8, vcc, s33, v6
	s_mov_b32 s33, 0x9b000
	s_nop 0
	v_addc_co_u32_e32 v9, vcc, 0, v7, vcc
	global_load_dword v80, v[8:9], off nt
	v_add_co_u32_e32 v8, vcc, s33, v6
	s_mov_b32 s33, 0x9d000
	s_nop 0
	v_addc_co_u32_e32 v9, vcc, 0, v7, vcc
	global_load_dword v81, v[8:9], off offset:1024 nt
	v_add_co_u32_e32 v8, vcc, s33, v6
	s_mov_b32 s33, 0x9f000
	s_nop 0
	v_addc_co_u32_e32 v9, vcc, 0, v7, vcc
	global_load_dword v82, v[8:9], off offset:2048 nt
	v_add_co_u32_e32 v8, vcc, s33, v6
	s_mov_b32 s33, 0xab000
	s_nop 0
	v_addc_co_u32_e32 v9, vcc, 0, v7, vcc
	global_load_dword v83, v[8:9], off offset:3072 nt
	v_add_co_u32_e32 v8, vcc, s53, v6
	s_nop 1
	v_addc_co_u32_e32 v9, vcc, 0, v7, vcc
	global_load_dword v84, v[8:9], off nt
	v_add_co_u32_e32 v8, vcc, s54, v6
	s_nop 1
	v_addc_co_u32_e32 v9, vcc, 0, v7, vcc
	global_load_dword v85, v[8:9], off offset:1024 nt
	v_add_co_u32_e32 v8, vcc, s55, v6
	s_nop 1
	v_addc_co_u32_e32 v9, vcc, 0, v7, vcc
	global_load_dword v86, v[8:9], off offset:2048 nt
	v_add_co_u32_e32 v8, vcc, s56, v6
	s_nop 1
	v_addc_co_u32_e32 v9, vcc, 0, v7, vcc
; template <bool PERMGL, bool FP8>
; __device__ __forceinline__ void q8_cols_item(const float* W, int N, int n0, unsigned char* Bq, float* sc_out, LAS float* AM, int par, int wave, int lane) {
;     ...
;     for (int i = 0; i < 128; ++i) v[i] = Wp[(size_t)i * N];
	global_load_dword v87, v[8:9], off offset:3072 nt
	v_add_co_u32_e32 v8, vcc, s33, v6
	s_mov_b32 s33, 0xad000
	s_nop 0
	v_addc_co_u32_e32 v9, vcc, 0, v7, vcc
	global_load_dword v88, v[8:9], off nt
	v_add_co_u32_e32 v8, vcc, s33, v6
	s_mov_b32 s33, 0xaf000
	s_nop 0
	v_addc_co_u32_e32 v9, vcc, 0, v7, vcc
	global_load_dword v89, v[8:9], off offset:1024 nt
	v_add_co_u32_e32 v8, vcc, s33, v6
	s_mov_b32 s33, 0xb1000
	s_nop 0
	v_addc_co_u32_e32 v9, vcc, 0, v7, vcc
	global_load_dword v91, v[8:9], off offset:2048 nt
	v_add_co_u32_e32 v8, vcc, s33, v6
	s_mov_b32 s33, 0xbd000
	s_nop 0
	v_addc_co_u32_e32 v9, vcc, 0, v7, vcc
	global_load_dword v92, v[8:9], off offset:3072 nt
	v_add_co_u32_e32 v8, vcc, s57, v6
	s_nop 1
	v_addc_co_u32_e32 v9, vcc, 0, v7, vcc
	global_load_dword v93, v[8:9], off nt
	v_add_co_u32_e32 v8, vcc, s58, v6
	s_nop 1
	v_addc_co_u32_e32 v9, vcc, 0, v7, vcc
	global_load_dword v94, v[8:9], off offset:1024 nt
	v_add_co_u32_e32 v8, vcc, s59, v6
	s_nop 1
	v_addc_co_u32_e32 v9, vcc, 0, v7, vcc
	global_load_dword v95, v[8:9], off offset:2048 nt
	v_add_co_u32_e32 v8, vcc, s60, v6
	s_nop 1
	v_addc_co_u32_e32 v9, vcc, 0, v7, vcc
	global_load_dword v96, v[8:9], off offset:3072 nt
	v_add_co_u32_e32 v8, vcc, s33, v6
	s_mov_b32 s33, 0xbf000
	s_nop 0
	v_addc_co_u32_e32 v9, vcc, 0, v7, vcc
	global_load_dword v97, v[8:9], off nt
	v_add_co_u32_e32 v8, vcc, s33, v6
	s_mov_b32 s33, 0xc1000
	s_nop 0
	v_addc_co_u32_e32 v9, vcc, 0, v7, vcc
	global_load_dword v98, v[8:9], off offset:1024 nt
	v_add_co_u32_e32 v8, vcc, s33, v6
	s_mov_b32 s33, 0xc3000
	s_nop 0
	v_addc_co_u32_e32 v9, vcc, 0, v7, vcc
	global_load_dword v99, v[8:9], off offset:2048 nt
	v_add_co_u32_e32 v8, vcc, s33, v6
	s_mov_b32 s33, 0xcf000
	s_nop 0
	v_addc_co_u32_e32 v9, vcc, 0, v7, vcc
	global_load_dword v100, v[8:9], off offset:3072 nt
	v_add_co_u32_e32 v8, vcc, s61, v6
	s_nop 1
	v_addc_co_u32_e32 v9, vcc, 0, v7, vcc
	global_load_dword v101, v[8:9], off nt
	v_add_co_u32_e32 v8, vcc, s62, v6
	s_nop 1
	v_addc_co_u32_e32 v9, vcc, 0, v7, vcc
	global_load_dword v102, v[8:9], off offset:1024 nt
	v_add_co_u32_e32 v8, vcc, s63, v6
	s_nop 1
	v_addc_co_u32_e32 v9, vcc, 0, v7, vcc
	global_load_dword v103, v[8:9], off offset:2048 nt
	v_add_co_u32_e32 v8, vcc, s64, v6
	s_nop 1
	v_addc_co_u32_e32 v9, vcc, 0, v7, vcc
	global_load_dword v104, v[8:9], off offset:3072 nt
	v_add_co_u32_e32 v8, vcc, s33, v6
	s_mov_b32 s33, 0xd1000
	s_nop 0
	v_addc_co_u32_e32 v9, vcc, 0, v7, vcc
	global_load_dword v105, v[8:9], off nt
	v_add_co_u32_e32 v8, vcc, s33, v6
	s_mov_b32 s33, 0xd3000
	s_nop 0
	v_addc_co_u32_e32 v9, vcc, 0, v7, vcc
	global_load_dword v106, v[8:9], off offset:1024 nt
	v_add_co_u32_e32 v8, vcc, s33, v6
	s_mov_b32 s33, 0xd5000
	s_nop 0
	v_addc_co_u32_e32 v9, vcc, 0, v7, vcc
	global_load_dword v108, v[8:9], off offset:2048 nt
	v_add_co_u32_e32 v8, vcc, s33, v6
	s_mov_b32 s33, 0xe1000
	s_nop 0
	v_addc_co_u32_e32 v9, vcc, 0, v7, vcc
	global_load_dword v111, v[8:9], off offset:3072 nt
	v_add_co_u32_e32 v8, vcc, s65, v6
	s_nop 1
	v_addc_co_u32_e32 v9, vcc, 0, v7, vcc
	global_load_dword v107, v[8:9], off nt
	v_add_co_u32_e32 v8, vcc, s66, v6
	s_nop 1
	v_addc_co_u32_e32 v9, vcc, 0, v7, vcc
	global_load_dword v109, v[8:9], off offset:1024 nt
	v_add_co_u32_e32 v8, vcc, s67, v6
	s_nop 1
	v_addc_co_u32_e32 v9, vcc, 0, v7, vcc
	global_load_dword v110, v[8:9], off offset:2048 nt
	v_add_co_u32_e32 v8, vcc, s68, v6
	s_nop 1
	v_addc_co_u32_e32 v9, vcc, 0, v7, vcc
	global_load_dword v112, v[8:9], off offset:3072 nt
	v_add_co_u32_e32 v8, vcc, s33, v6
	s_mov_b32 s33, 0xe3000
	s_nop 0
	v_addc_co_u32_e32 v9, vcc, 0, v7, vcc
	global_load_dword v113, v[8:9], off nt
	v_add_co_u32_e32 v8, vcc, s33, v6
	s_mov_b32 s33, 0xe5000
	s_nop 0
	v_addc_co_u32_e32 v9, vcc, 0, v7, vcc
	global_load_dword v114, v[8:9], off offset:1024 nt
	v_add_co_u32_e32 v8, vcc, s33, v6
	s_mov_b32 s33, 0xe7000
	s_nop 0
	v_addc_co_u32_e32 v9, vcc, 0, v7, vcc
	global_load_dword v115, v[8:9], off offset:2048 nt
	v_add_co_u32_e32 v8, vcc, s33, v6
	s_mov_b32 s33, 0xf3000
	s_nop 0
	v_addc_co_u32_e32 v9, vcc, 0, v7, vcc
	global_load_dword v116, v[8:9], off offset:3072 nt
	v_add_co_u32_e32 v8, vcc, s69, v6
	s_nop 1
	v_addc_co_u32_e32 v9, vcc, 0, v7, vcc
	global_load_dword v117, v[8:9], off nt
	v_add_co_u32_e32 v8, vcc, s70, v6
	s_nop 1
	v_addc_co_u32_e32 v9, vcc, 0, v7, vcc
	global_load_dword v118, v[8:9], off offset:1024 nt
	v_add_co_u32_e32 v8, vcc, s71, v6
	s_nop 1
	v_addc_co_u32_e32 v9, vcc, 0, v7, vcc
	global_load_dword v119, v[8:9], off offset:2048 nt
	v_add_co_u32_e32 v8, vcc, s72, v6
	s_nop 1
	v_addc_co_u32_e32 v9, vcc, 0, v7, vcc
	global_load_dword v120, v[8:9], off offset:3072 nt
	v_add_co_u32_e32 v8, vcc, s33, v6
	s_mov_b32 s33, 0xf5000
	s_nop 0
	v_addc_co_u32_e32 v9, vcc, 0, v7, vcc
	global_load_dword v121, v[8:9], off nt
	v_add_co_u32_e32 v8, vcc, s33, v6
	s_mov_b32 s33, 0xf7000
	s_nop 0
	v_addc_co_u32_e32 v9, vcc, 0, v7, vcc
	global_load_dword v122, v[8:9], off offset:1024 nt
	v_add_co_u32_e32 v8, vcc, s33, v6
	s_mov_b32 s33, 0xf9000
	s_nop 0
	v_addc_co_u32_e32 v9, vcc, 0, v7, vcc
	global_load_dword v123, v[8:9], off offset:2048 nt
	v_add_co_u32_e32 v8, vcc, s33, v6
	s_mov_b32 s33, 0x100000
	s_nop 0
	v_addc_co_u32_e32 v9, vcc, 0, v7, vcc
	global_load_dword v124, v[8:9], off offset:3072 nt
	v_add_co_u32_e32 v8, vcc, s73, v6
	s_nop 1
	v_addc_co_u32_e32 v9, vcc, 0, v7, vcc
	global_load_dword v125, v[8:9], off nt
	v_add_co_u32_e32 v8, vcc, s74, v6
	s_nop 1
	v_addc_co_u32_e32 v9, vcc, 0, v7, vcc
	global_load_dword v126, v[8:9], off offset:1024 nt
	v_add_co_u32_e32 v8, vcc, s33, v6
	s_mov_b32 s33, 0x102000
	s_nop 0
	v_addc_co_u32_e32 v9, vcc, 0, v7, vcc
; template <bool PERMGL, bool FP8>
; __device__ __forceinline__ void q8_cols_item(const float* W, int N, int n0, unsigned char* Bq, float* sc_out, LAS float* AM, int par, int wave, int lane) {
;     ...
;     for (int i = 0; i < 128; ++i) v[i] = Wp[(size_t)i * N];
;     __builtin_amdgcn_sched_barrier(0);
; #pragma unroll
;     for (int i = 0; i < 128; ++i) am = fmaxf(am, fabsf(v[i]));
;     AM[(par * 8 + wave) * 64 + lane] = am;
;     __syncthreads();
	global_load_dword v127, v[8:9], off offset:2048 nt
	v_add_co_u32_e32 v8, vcc, s33, v6
	s_mov_b32 s33, 0x105000
	s_nop 0
	v_addc_co_u32_e32 v9, vcc, 0, v7, vcc
	global_load_dword v128, v[8:9], off offset:3072 nt
	v_add_co_u32_e32 v8, vcc, s33, v6
	s_mov_b32 s33, 0x107000
	s_nop 0
	v_addc_co_u32_e32 v9, vcc, 0, v7, vcc
	global_load_dword v129, v[8:9], off nt
	v_add_co_u32_e32 v8, vcc, s33, v6
	s_mov_b32 s33, 0x109000
	s_nop 0
	v_addc_co_u32_e32 v9, vcc, 0, v7, vcc
	global_load_dword v130, v[8:9], off offset:1024 nt
	v_add_co_u32_e32 v8, vcc, s33, v6
	s_mov_b32 s33, 0x10b000
	s_nop 0
	v_addc_co_u32_e32 v9, vcc, 0, v7, vcc
	global_load_dword v131, v[8:9], off offset:2048 nt
	v_add_co_u32_e32 v8, vcc, s33, v6
	s_mov_b32 s33, 0x10e000
	s_nop 0
	v_addc_co_u32_e32 v9, vcc, 0, v7, vcc
	global_load_dword v132, v[8:9], off offset:3072 nt
	v_add_co_u32_e32 v8, vcc, s33, v6
	s_mov_b32 s33, 0x110000
	s_nop 0
	v_addc_co_u32_e32 v9, vcc, 0, v7, vcc
	global_load_dword v133, v[8:9], off nt
	v_add_co_u32_e32 v8, vcc, s33, v6
	s_mov_b32 s33, 0x112000
	s_nop 0
	v_addc_co_u32_e32 v9, vcc, 0, v7, vcc
	global_load_dword v134, v[8:9], off offset:1024 nt
	v_add_co_u32_e32 v8, vcc, s33, v6
	s_mov_b32 s33, 0x114000
	s_nop 0
	v_addc_co_u32_e32 v9, vcc, 0, v7, vcc
	global_load_dword v135, v[8:9], off offset:2048 nt
	v_add_co_u32_e32 v8, vcc, s33, v6
	s_mov_b32 s33, 0x117000
	s_nop 0
	v_addc_co_u32_e32 v9, vcc, 0, v7, vcc
	global_load_dword v136, v[8:9], off offset:3072 nt
	v_add_co_u32_e32 v8, vcc, s33, v6
	s_mov_b32 s33, 0x119000
	s_nop 0
	v_addc_co_u32_e32 v9, vcc, 0, v7, vcc
	global_load_dword v137, v[8:9], off nt
	v_add_co_u32_e32 v8, vcc, s33, v6
	s_mov_b32 s33, 0x11b000
	s_nop 0
	v_addc_co_u32_e32 v9, vcc, 0, v7, vcc
	global_load_dword v138, v[8:9], off offset:1024 nt
	v_add_co_u32_e32 v8, vcc, s33, v6
	s_mov_b32 s33, 0x11d000
	s_nop 0
	v_addc_co_u32_e32 v9, vcc, 0, v7, vcc
	v_add_co_u32_e32 v6, vcc, s33, v6
	global_load_dword v139, v[8:9], off offset:2048 nt
	s_nop 0
	v_addc_co_u32_e32 v7, vcc, 0, v7, vcc
	global_load_dword v144, v[6:7], off offset:3072 nt
	s_waitcnt vmcnt(62)
	v_max3_f32 v6, |v12|, 0, |v13|
	v_max3_f32 v6, v6, |v14|, |v15|
	v_max3_f32 v6, v6, |v16|, |v17|
	v_max3_f32 v6, v6, |v18|, |v19|
	v_max3_f32 v6, v6, |v20|, |v21|
	v_max3_f32 v6, v6, |v22|, |v23|
	v_max3_f32 v6, v6, |v24|, |v25|
	v_max3_f32 v6, v6, |v26|, |v27|
	v_max3_f32 v6, v6, |v28|, |v29|
	v_max3_f32 v6, v6, |v30|, |v31|
	v_max3_f32 v6, v6, |v32|, |v33|
	v_max3_f32 v6, v6, |v34|, |v35|
	v_max3_f32 v6, v6, |v36|, |v37|
	v_max3_f32 v6, v6, |v38|, |v39|
	v_max3_f32 v6, v6, |v40|, |v41|
	v_max3_f32 v6, v6, |v43|, |v46|
	v_max3_f32 v6, v6, |v42|, |v44|
	v_max3_f32 v6, v6, |v45|, |v47|
	v_max3_f32 v6, v6, |v48|, |v49|
	v_max3_f32 v6, v6, |v50|, |v51|
	v_max3_f32 v6, v6, |v52|, |v53|
	v_max3_f32 v6, v6, |v54|, |v55|
	v_max3_f32 v6, v6, |v56|, |v57|
	v_max3_f32 v6, v6, |v58|, |v59|
	v_max3_f32 v6, v6, |v60|, |v61|
	v_max3_f32 v6, v6, |v62|, |v63|
	v_max3_f32 v6, v6, |v64|, |v65|
	v_max3_f32 v6, v6, |v66|, |v67|
	v_max3_f32 v6, v6, |v68|, |v69|
	v_max3_f32 v6, v6, |v70|, |v71|
	v_max3_f32 v6, v6, |v72|, |v73|
	v_max3_f32 v6, v6, |v75|, |v78|
	v_max3_f32 v6, v6, |v74|, |v76|
	s_waitcnt vmcnt(60)
	v_max3_f32 v6, v6, |v77|, |v79|
	s_waitcnt vmcnt(58)
	v_max3_f32 v6, v6, |v80|, |v81|
	s_waitcnt vmcnt(56)
	v_max3_f32 v6, v6, |v82|, |v83|
	s_waitcnt vmcnt(54)
	v_max3_f32 v6, v6, |v84|, |v85|
	s_waitcnt vmcnt(52)
	v_max3_f32 v6, v6, |v86|, |v87|
	s_waitcnt vmcnt(50)
	v_max3_f32 v6, v6, |v88|, |v89|
	s_waitcnt vmcnt(48)
	v_max3_f32 v6, v6, |v91|, |v92|
	s_waitcnt vmcnt(46)
	v_max3_f32 v6, v6, |v93|, |v94|
	s_waitcnt vmcnt(44)
	v_max3_f32 v6, v6, |v95|, |v96|
	s_waitcnt vmcnt(42)
	v_max3_f32 v6, v6, |v97|, |v98|
	s_waitcnt vmcnt(40)
	v_max3_f32 v6, v6, |v99|, |v100|
	s_waitcnt vmcnt(38)
	v_max3_f32 v6, v6, |v101|, |v102|
	s_waitcnt vmcnt(36)
	v_max3_f32 v6, v6, |v103|, |v104|
	s_waitcnt vmcnt(34)
	v_max3_f32 v6, v6, |v105|, |v106|
	s_waitcnt vmcnt(32)
	v_max3_f32 v6, v6, |v108|, |v111|
	s_waitcnt vmcnt(30)
	v_max3_f32 v6, v6, |v107|, |v109|
	s_waitcnt vmcnt(28)
	v_max3_f32 v6, v6, |v110|, |v112|
	s_waitcnt vmcnt(26)
	v_max3_f32 v6, v6, |v113|, |v114|
	s_waitcnt vmcnt(24)
	v_max3_f32 v6, v6, |v115|, |v116|
	s_waitcnt vmcnt(22)
	v_max3_f32 v6, v6, |v117|, |v118|
	s_waitcnt vmcnt(20)
	v_max3_f32 v6, v6, |v119|, |v120|
	s_waitcnt vmcnt(18)
	v_max3_f32 v6, v6, |v121|, |v122|
	s_waitcnt vmcnt(16)
	v_max3_f32 v6, v6, |v123|, |v124|
	s_waitcnt vmcnt(14)
	v_max3_f32 v6, v6, |v125|, |v126|
	s_waitcnt vmcnt(12)
	v_max3_f32 v6, v6, |v127|, |v128|
	s_waitcnt vmcnt(10)
	v_max3_f32 v6, v6, |v129|, |v130|
	s_waitcnt vmcnt(8)
	v_max3_f32 v6, v6, |v131|, |v132|
	s_waitcnt vmcnt(6)
	v_max3_f32 v6, v6, |v133|, |v134|
	s_waitcnt vmcnt(4)
	v_max3_f32 v6, v6, |v135|, |v136|
	s_waitcnt vmcnt(2)
	v_max3_f32 v6, v6, |v137|, |v138|
	s_lshl_b32 s33, s78, 11
	s_waitcnt vmcnt(0)
	v_max3_f32 v145, v6, |v139|, |v144|
	v_add_u32_e32 v6, s33, v1
	v_add_u32_e32 v142, s33, v10
	ds_write_b32 v6, v145
	s_waitcnt lgkmcnt(0)
	s_barrier
; template <bool PERMGL, bool FP8>
; __device__ __forceinline__ void q8_cols_item(const float* W, int N, int n0, unsigned char* Bq, float* sc_out, LAS float* AM, int par, int wave, int lane) {
;     ...
;     for (int w = 0; w < 8; ++w) am = fmaxf(am, AM[(par * 8 + w) * 64 + lane]);
;     const float sc = am > 0.f ? am * (FP8 ? (1.0f / 256.0f) : (1.0f / 127.0f)) : 1.0f, inv = 1.0f / sc;
;     int row = n;
;     if (PERMGL) { const int j = n >> 1, pr = n & 1, o = j & 127; row = ((j >> 7) << 8) + (((o >> 2) & 1) << 7) + ((o >> 5) << 5) + (pr << 4) + (((o >> 3) & 3) << 2) + (o & 3); }
;     if (!PERMGL) { const int o = n & 255; row = ((n >> 8) << 8) + (((o >> 3) & 1) << 7) + ((o >> 6) << 5) + (((o >> 4) & 3) << 3) + (o & 7); }
;     auto xq = [](unsigned x) { return (unsigned)__builtin_amdgcn_update_dpp(0, (int)x, 0xB1, 0xf, 0xf, true); };
;     const bool odd = lane & 1;
;     const int rowp = (int)xq((unsigned)row);
;     unsigned char* plo = Bq + (size_t)(odd ? rowp : row) * 1024 + 128 * wave + (odd ? 16 : 0);
;     unsigned char* phi = Bq + (size_t)(odd ? row : rowp) * 1024 + 128 * wave + (odd ? 16 : 0);
;     auto packc = [&](int c) { u32x4 o;
;         if (FP8) { o.x = f8x4(v[16 * c], v[16 * c + 1], v[16 * c + 2], v[16 * c + 3], inv); o.y = f8x4(v[16 * c + 4], v[16 * c + 5], v[16 * c + 6], v[16 * c + 7], inv);
;                    o.z = f8x4(v[16 * c + 8], v[16 * c + 9], v[16 * c + 10], v[16 * c + 11], inv); o.w = f8x4(v[16 * c + 12], v[16 * c + 13], v[16 * c + 14], v[16 * c + 15], inv); }
;         else { o.x = q8x4(v[16 * c], v[16 * c + 1], v[16 * c + 2], v[16 * c + 3], inv); o.y = q8x4(v[16 * c + 4], v[16 * c + 5], v[16 * c + 6], v[16 * c + 7], inv);
;                o.z = q8x4(v[16 * c + 8], v[16 * c + 9], v[16 * c + 10], v[16 * c + 11], inv); o.w = q8x4(v[16 * c + 12], v[16 * c + 13], v[16 * c + 14], v[16 * c + 15], inv); }
;         return o; };
; #pragma unroll
;     for (int j = 0; j < 4; ++j) { const u32x4 p0 = packc(2 * j), p1 = packc(2 * j + 1);
;         u32x4 snd, rcv;
; #pragma unroll
;         for (int q = 0; q < 4; ++q) { snd[q] = odd ? p0[q] : p1[q]; rcv[q] = xq(snd[q]); }
;         u32x4 a, b;
; #pragma unroll
;         for (int q = 0; q < 4; ++q) { a[q] = odd ? rcv[q] : p0[q]; b[q] = odd ? p1[q] : rcv[q]; }
;         *(u32x4*)(plo + 32 * j) = a; *(u32x4*)(phi + 32 * j) = b; }
	ds_read2st64_b32 v[6:7], v142 offset1:1
	ds_read2st64_b32 v[8:9], v142 offset0:2 offset1:3
	ds_read2st64_b32 v[140:141], v142 offset0:4 offset1:5
	ds_read2st64_b32 v[142:143], v142 offset0:6 offset1:7
	s_waitcnt lgkmcnt(3)
	v_max3_f32 v6, v145, v6, v7
	s_waitcnt lgkmcnt(2)
	v_max3_f32 v6, v6, v8, v9
	s_waitcnt lgkmcnt(1)
	v_max3_f32 v6, v6, v140, v141
	s_waitcnt lgkmcnt(0)
	v_max3_f32 v6, v6, v142, v143
	v_mul_f32_e32 v7, 0x3c010204, v6
	v_cmp_lt_f32_e32 vcc, 0, v6
	s_nop 1
	v_cndmask_b32_e32 v140, 1.0, v7, vcc
	v_div_scale_f32 v6, s[80:81], v140, v140, 1.0
	v_rcp_f32_e32 v7, v6
	v_readlane_b32 s80, v252, 31
	v_readlane_b32 s81, v252, 32
	v_fma_f32 v8, -v6, v7, 1.0
	v_fmac_f32_e32 v7, v8, v7
	v_div_scale_f32 v8, vcc, 1.0, v140, 1.0
	v_mul_f32_e32 v9, v8, v7
	v_fma_f32 v141, -v6, v9, v8
	v_fmac_f32_e32 v9, v141, v7
	v_fma_f32 v6, -v6, v9, v8
	v_div_fmas_f32 v6, v6, v7, v9
	v_div_fixup_f32 v141, v6, v140, 1.0
	v_fmaak_f32 v12, v12, v141, 0x4b400000
	v_fmaak_f32 v13, v13, v141, 0x4b400000
	v_fmaak_f32 v14, v14, v141, 0x4b400000
	v_fmaak_f32 v15, v15, v141, 0x4b400000
	v_perm_b32 v14, v15, v14, s75
	v_perm_b32 v12, v13, v12, s75
	v_perm_b32 v12, v14, v12, s76
	v_fmaak_f32 v13, v16, v141, 0x4b400000
	v_fmaak_f32 v14, v17, v141, 0x4b400000
	v_fmaak_f32 v15, v18, v141, 0x4b400000
	v_fmaak_f32 v16, v19, v141, 0x4b400000
	v_perm_b32 v15, v16, v15, s75
	v_perm_b32 v13, v14, v13, s75
	v_perm_b32 v13, v15, v13, s76
	v_fmaak_f32 v14, v20, v141, 0x4b400000
	v_fmaak_f32 v15, v21, v141, 0x4b400000
	v_fmaak_f32 v16, v22, v141, 0x4b400000
	v_fmaak_f32 v17, v23, v141, 0x4b400000
	v_perm_b32 v16, v17, v16, s75
	v_perm_b32 v14, v15, v14, s75
	v_perm_b32 v14, v16, v14, s76
	v_fmaak_f32 v15, v24, v141, 0x4b400000
	v_fmaak_f32 v16, v25, v141, 0x4b400000
	v_fmaak_f32 v17, v26, v141, 0x4b400000
	v_fmaak_f32 v18, v27, v141, 0x4b400000
	v_perm_b32 v17, v18, v17, s75
	v_perm_b32 v15, v16, v15, s75
	v_perm_b32 v15, v17, v15, s76
	v_fmaak_f32 v16, v28, v141, 0x4b400000
	v_fmaak_f32 v17, v29, v141, 0x4b400000
	v_fmaak_f32 v18, v30, v141, 0x4b400000
	v_fmaak_f32 v19, v31, v141, 0x4b400000
	v_perm_b32 v18, v19, v18, s75
	v_perm_b32 v16, v17, v16, s75
	v_lshrrev_b32_e32 v6, 1, v4
	v_perm_b32 v16, v18, v16, s76
	v_fmaak_f32 v17, v32, v141, 0x4b400000
	v_fmaak_f32 v18, v33, v141, 0x4b400000
	v_fmaak_f32 v19, v34, v141, 0x4b400000
	v_fmaak_f32 v20, v35, v141, 0x4b400000
	v_and_b32_e32 v6, 0x78, v6
	v_and_b32_e32 v7, 0xffffff07, v4
	v_perm_b32 v19, v20, v19, s75
	v_perm_b32 v17, v18, v17, s75
	v_or3_b32 v8, v7, v6, v11
	v_perm_b32 v17, v19, v17, s76
	v_fmaak_f32 v18, v36, v141, 0x4b400000
	v_fmaak_f32 v19, v37, v141, 0x4b400000
	v_fmaak_f32 v20, v38, v141, 0x4b400000
	v_fmaak_f32 v21, v39, v141, 0x4b400000
	v_mov_b32_dpp v9, v8 quad_perm:[1,0,3,2] row_mask:0xf bank_mask:0xf bound_ctrl:1
	v_perm_b32 v20, v21, v20, s75
	v_perm_b32 v18, v19, v18, s75
	v_cndmask_b32_e64 v6, v9, v8, s[2:3]
	v_perm_b32 v18, v20, v18, s76
	v_fmaak_f32 v19, v40, v141, 0x4b400000
	v_fmaak_f32 v20, v41, v141, 0x4b400000
	v_fmaak_f32 v21, v43, v141, 0x4b400000
	v_fmaak_f32 v22, v46, v141, 0x4b400000
	v_ashrrev_i32_e32 v7, 31, v6
	v_cndmask_b32_e64 v8, v8, v9, s[2:3]
	v_perm_b32 v21, v22, v21, s75
	v_perm_b32 v19, v20, v19, s75
	v_lshlrev_b64 v[6:7], 10, v[6:7]
	v_ashrrev_i32_e32 v9, 31, v8
	v_perm_b32 v19, v21, v19, s76
	v_lshl_add_u64 v[6:7], s[6:7], 0, v[6:7]
	v_lshlrev_b64 v[8:9], 10, v[8:9]
	v_cndmask_b32_e64 v20, v12, v16, s[2:3]
	v_cndmask_b32_e64 v21, v13, v17, s[2:3]
	v_cndmask_b32_e64 v22, v14, v18, s[2:3]
	v_cndmask_b32_e64 v23, v15, v19, s[2:3]
	v_lshl_add_u64 v[6:7], v[6:7], 0, s[80:81]
	v_lshl_add_u64 v[8:9], s[6:7], 0, v[8:9]
	v_mov_b32_dpp v20, v20 quad_perm:[1,0,3,2] row_mask:0xf bank_mask:0xf bound_ctrl:1
	v_mov_b32_dpp v21, v21 quad_perm:[1,0,3,2] row_mask:0xf bank_mask:0xf bound_ctrl:1
	v_mov_b32_dpp v22, v22 quad_perm:[1,0,3,2] row_mask:0xf bank_mask:0xf bound_ctrl:1
	v_mov_b32_dpp v23, v23 quad_perm:[1,0,3,2] row_mask:0xf bank_mask:0xf bound_ctrl:1
	v_lshl_add_u64 v[6:7], v[6:7], 0, v[2:3]
	v_lshl_add_u64 v[8:9], v[8:9], 0, s[80:81]
	v_cndmask_b32_e64 v12, v20, v12, s[2:3]
	v_cndmask_b32_e64 v13, v21, v13, s[2:3]
	v_cndmask_b32_e64 v14, v22, v14, s[2:3]
	v_cndmask_b32_e64 v15, v23, v15, s[2:3]
	v_lshl_add_u64 v[8:9], v[8:9], 0, v[2:3]
	v_cndmask_b32_e64 v16, v16, v20, s[2:3]
	v_cndmask_b32_e64 v17, v17, v21, s[2:3]
	v_cndmask_b32_e64 v18, v18, v22, s[2:3]
	v_cndmask_b32_e64 v19, v19, v23, s[2:3]
	global_store_dwordx4 v[6:7], v[12:15], off
	global_store_dwordx4 v[8:9], v[16:19], off
	v_fmaak_f32 v20, v67, v141, 0x4b400000
	v_fmaak_f32 v12, v42, v141, 0x4b400000
	v_fmaak_f32 v13, v44, v141, 0x4b400000
	v_fmaak_f32 v14, v45, v141, 0x4b400000
	v_fmaak_f32 v15, v47, v141, 0x4b400000
	v_perm_b32 v14, v15, v14, s75
	v_perm_b32 v12, v13, v12, s75
	v_perm_b32 v12, v14, v12, s76
	v_fmaak_f32 v13, v48, v141, 0x4b400000
	v_fmaak_f32 v14, v49, v141, 0x4b400000
	v_fmaak_f32 v15, v50, v141, 0x4b400000
	v_fmaak_f32 v16, v51, v141, 0x4b400000
	v_perm_b32 v15, v16, v15, s75
	v_perm_b32 v13, v14, v13, s75
	v_perm_b32 v13, v15, v13, s76
	v_fmaak_f32 v14, v52, v141, 0x4b400000
	v_fmaak_f32 v15, v53, v141, 0x4b400000
	v_fmaak_f32 v16, v54, v141, 0x4b400000
	v_fmaak_f32 v17, v55, v141, 0x4b400000
	v_perm_b32 v16, v17, v16, s75
	v_perm_b32 v14, v15, v14, s75
	v_perm_b32 v14, v16, v14, s76
	v_fmaak_f32 v15, v56, v141, 0x4b400000
	v_fmaak_f32 v16, v57, v141, 0x4b400000
	v_fmaak_f32 v17, v58, v141, 0x4b400000
	v_fmaak_f32 v18, v59, v141, 0x4b400000
	v_perm_b32 v17, v18, v17, s75
	v_perm_b32 v15, v16, v15, s75
	v_perm_b32 v15, v17, v15, s76
	v_fmaak_f32 v16, v60, v141, 0x4b400000
	v_fmaak_f32 v17, v61, v141, 0x4b400000
; template <bool PERMGL, bool FP8>
; __device__ __forceinline__ void q8_cols_item(const float* W, int N, int n0, unsigned char* Bq, float* sc_out, LAS float* AM, int par, int wave, int lane) {
;     ...
;     auto packc = [&](int c) { u32x4 o;
;         if (FP8) { o.x = f8x4(v[16 * c], v[16 * c + 1], v[16 * c + 2], v[16 * c + 3], inv); o.y = f8x4(v[16 * c + 4], v[16 * c + 5], v[16 * c + 6], v[16 * c + 7], inv);
;                    o.z = f8x4(v[16 * c + 8], v[16 * c + 9], v[16 * c + 10], v[16 * c + 11], inv); o.w = f8x4(v[16 * c + 12], v[16 * c + 13], v[16 * c + 14], v[16 * c + 15], inv); }
;         else { o.x = q8x4(v[16 * c], v[16 * c + 1], v[16 * c + 2], v[16 * c + 3], inv); o.y = q8x4(v[16 * c + 4], v[16 * c + 5], v[16 * c + 6], v[16 * c + 7], inv);
;                o.z = q8x4(v[16 * c + 8], v[16 * c + 9], v[16 * c + 10], v[16 * c + 11], inv); o.w = q8x4(v[16 * c + 12], v[16 * c + 13], v[16 * c + 14], v[16 * c + 15], inv); }
;         return o; };
; #pragma unroll
;     for (int j = 0; j < 4; ++j) { const u32x4 p0 = packc(2 * j), p1 = packc(2 * j + 1);
;         u32x4 snd, rcv;
; #pragma unroll
;         for (int q = 0; q < 4; ++q) { snd[q] = odd ? p0[q] : p1[q]; rcv[q] = xq(snd[q]); }
;         u32x4 a, b;
; #pragma unroll
;         for (int q = 0; q < 4; ++q) { a[q] = odd ? rcv[q] : p0[q]; b[q] = odd ? p1[q] : rcv[q]; }
;         *(u32x4*)(plo + 32 * j) = a; *(u32x4*)(phi + 32 * j) = b; }
	v_fmaak_f32 v18, v62, v141, 0x4b400000
	v_fmaak_f32 v19, v63, v141, 0x4b400000
	v_perm_b32 v18, v19, v18, s75
	v_perm_b32 v16, v17, v16, s75
	v_perm_b32 v16, v18, v16, s76
	v_fmaak_f32 v17, v64, v141, 0x4b400000
	v_fmaak_f32 v18, v65, v141, 0x4b400000
	v_fmaak_f32 v19, v66, v141, 0x4b400000
	v_perm_b32 v19, v20, v19, s75
	v_perm_b32 v17, v18, v17, s75
	v_perm_b32 v17, v19, v17, s76
	v_fmaak_f32 v18, v68, v141, 0x4b400000
	v_fmaak_f32 v19, v69, v141, 0x4b400000
	v_fmaak_f32 v20, v70, v141, 0x4b400000
	v_fmaak_f32 v21, v71, v141, 0x4b400000
	v_perm_b32 v20, v21, v20, s75
	v_perm_b32 v18, v19, v18, s75
	v_perm_b32 v18, v20, v18, s76
	v_fmaak_f32 v19, v72, v141, 0x4b400000
	v_fmaak_f32 v20, v73, v141, 0x4b400000
	v_fmaak_f32 v21, v75, v141, 0x4b400000
	v_fmaak_f32 v22, v78, v141, 0x4b400000
	v_perm_b32 v21, v22, v21, s75
	v_perm_b32 v19, v20, v19, s75
	v_perm_b32 v19, v21, v19, s76
	v_cndmask_b32_e64 v20, v12, v16, s[2:3]
	v_cndmask_b32_e64 v21, v13, v17, s[2:3]
	v_cndmask_b32_e64 v22, v14, v18, s[2:3]
	v_cndmask_b32_e64 v23, v15, v19, s[2:3]
	v_mov_b32_dpp v20, v20 quad_perm:[1,0,3,2] row_mask:0xf bank_mask:0xf bound_ctrl:1
	v_mov_b32_dpp v21, v21 quad_perm:[1,0,3,2] row_mask:0xf bank_mask:0xf bound_ctrl:1
	v_mov_b32_dpp v22, v22 quad_perm:[1,0,3,2] row_mask:0xf bank_mask:0xf bound_ctrl:1
	v_mov_b32_dpp v23, v23 quad_perm:[1,0,3,2] row_mask:0xf bank_mask:0xf bound_ctrl:1
	v_cndmask_b32_e64 v12, v20, v12, s[2:3]
	v_cndmask_b32_e64 v13, v21, v13, s[2:3]
	v_cndmask_b32_e64 v14, v22, v14, s[2:3]
	v_cndmask_b32_e64 v15, v23, v15, s[2:3]
	v_cndmask_b32_e64 v16, v16, v20, s[2:3]
	v_cndmask_b32_e64 v17, v17, v21, s[2:3]
	v_cndmask_b32_e64 v18, v18, v22, s[2:3]
	v_cndmask_b32_e64 v19, v19, v23, s[2:3]
	global_store_dwordx4 v[6:7], v[12:15], off offset:32
	global_store_dwordx4 v[8:9], v[16:19], off offset:32
	v_fmaak_f32 v20, v100, v141, 0x4b400000
	v_fmaak_f32 v12, v74, v141, 0x4b400000
	v_fmaak_f32 v13, v76, v141, 0x4b400000
	v_fmaak_f32 v14, v77, v141, 0x4b400000
	v_fmaak_f32 v15, v79, v141, 0x4b400000
	v_perm_b32 v14, v15, v14, s75
	v_perm_b32 v12, v13, v12, s75
	v_perm_b32 v12, v14, v12, s76
	v_fmaak_f32 v13, v80, v141, 0x4b400000
	v_fmaak_f32 v14, v81, v141, 0x4b400000
	v_fmaak_f32 v15, v82, v141, 0x4b400000
	v_fmaak_f32 v16, v83, v141, 0x4b400000
	v_perm_b32 v15, v16, v15, s75
	v_perm_b32 v13, v14, v13, s75
	v_perm_b32 v13, v15, v13, s76
	v_fmaak_f32 v14, v84, v141, 0x4b400000
	v_fmaak_f32 v15, v85, v141, 0x4b400000
	v_fmaak_f32 v16, v86, v141, 0x4b400000
	v_fmaak_f32 v17, v87, v141, 0x4b400000
	v_perm_b32 v16, v17, v16, s75
	v_perm_b32 v14, v15, v14, s75
	v_perm_b32 v14, v16, v14, s76
	v_fmaak_f32 v15, v88, v141, 0x4b400000
	v_fmaak_f32 v16, v89, v141, 0x4b400000
	v_fmaak_f32 v17, v91, v141, 0x4b400000
	v_fmaak_f32 v18, v92, v141, 0x4b400000
	v_perm_b32 v17, v18, v17, s75
	v_perm_b32 v15, v16, v15, s75
	v_perm_b32 v15, v17, v15, s76
	v_fmaak_f32 v16, v93, v141, 0x4b400000
	v_fmaak_f32 v17, v94, v141, 0x4b400000
	v_fmaak_f32 v18, v95, v141, 0x4b400000
	v_fmaak_f32 v19, v96, v141, 0x4b400000
	v_perm_b32 v18, v19, v18, s75
	v_perm_b32 v16, v17, v16, s75
	v_perm_b32 v16, v18, v16, s76
	v_fmaak_f32 v17, v97, v141, 0x4b400000
	v_fmaak_f32 v18, v98, v141, 0x4b400000
	v_fmaak_f32 v19, v99, v141, 0x4b400000
	v_perm_b32 v19, v20, v19, s75
	v_perm_b32 v17, v18, v17, s75
	v_perm_b32 v17, v19, v17, s76
	v_fmaak_f32 v18, v101, v141, 0x4b400000
	v_fmaak_f32 v19, v102, v141, 0x4b400000
	v_fmaak_f32 v20, v103, v141, 0x4b400000
	v_fmaak_f32 v21, v104, v141, 0x4b400000
	v_perm_b32 v20, v21, v20, s75
	v_perm_b32 v18, v19, v18, s75
	v_perm_b32 v18, v20, v18, s76
	v_fmaak_f32 v19, v105, v141, 0x4b400000
	v_fmaak_f32 v20, v106, v141, 0x4b400000
	v_fmaak_f32 v21, v108, v141, 0x4b400000
	v_fmaak_f32 v22, v111, v141, 0x4b400000
	v_perm_b32 v21, v22, v21, s75
	v_perm_b32 v19, v20, v19, s75
	v_perm_b32 v19, v21, v19, s76
	v_cndmask_b32_e64 v20, v12, v16, s[2:3]
	v_cndmask_b32_e64 v21, v13, v17, s[2:3]
	v_cndmask_b32_e64 v22, v14, v18, s[2:3]
	v_cndmask_b32_e64 v23, v15, v19, s[2:3]
; template <bool PERMGL, bool FP8>
; __device__ __forceinline__ void q8_cols_item(const float* W, int N, int n0, unsigned char* Bq, float* sc_out, LAS float* AM, int par, int wave, int lane) {
;     ...
;     for (int j = 0; j < 4; ++j) { const u32x4 p0 = packc(2 * j), p1 = packc(2 * j + 1);
;         u32x4 snd, rcv;
; #pragma unroll
;         for (int q = 0; q < 4; ++q) { snd[q] = odd ? p0[q] : p1[q]; rcv[q] = xq(snd[q]); }
;         u32x4 a, b;
; #pragma unroll
;         for (int q = 0; q < 4; ++q) { a[q] = odd ? rcv[q] : p0[q]; b[q] = odd ? p1[q] : rcv[q]; }
;         *(u32x4*)(plo + 32 * j) = a; *(u32x4*)(phi + 32 * j) = b; }
;     if (wave == 0) sc_out[PERMGL ? row : n] = FP8 ? sc * 16.0f : sc;
	v_mov_b32_dpp v20, v20 quad_perm:[1,0,3,2] row_mask:0xf bank_mask:0xf bound_ctrl:1
	v_mov_b32_dpp v21, v21 quad_perm:[1,0,3,2] row_mask:0xf bank_mask:0xf bound_ctrl:1
	v_mov_b32_dpp v22, v22 quad_perm:[1,0,3,2] row_mask:0xf bank_mask:0xf bound_ctrl:1
	v_mov_b32_dpp v23, v23 quad_perm:[1,0,3,2] row_mask:0xf bank_mask:0xf bound_ctrl:1
	v_cndmask_b32_e64 v12, v20, v12, s[2:3]
	v_cndmask_b32_e64 v13, v21, v13, s[2:3]
	v_cndmask_b32_e64 v14, v22, v14, s[2:3]
	v_cndmask_b32_e64 v15, v23, v15, s[2:3]
	v_cndmask_b32_e64 v16, v16, v20, s[2:3]
	v_cndmask_b32_e64 v17, v17, v21, s[2:3]
	v_cndmask_b32_e64 v18, v18, v22, s[2:3]
	v_cndmask_b32_e64 v19, v19, v23, s[2:3]
	global_store_dwordx4 v[6:7], v[12:15], off offset:64
	global_store_dwordx4 v[8:9], v[16:19], off offset:64
	v_fmaak_f32 v20, v132, v141, 0x4b400000
	v_fmaak_f32 v12, v107, v141, 0x4b400000
	v_fmaak_f32 v13, v109, v141, 0x4b400000
	v_fmaak_f32 v14, v110, v141, 0x4b400000
	v_fmaak_f32 v15, v112, v141, 0x4b400000
	v_perm_b32 v14, v15, v14, s75
	v_perm_b32 v12, v13, v12, s75
	v_perm_b32 v12, v14, v12, s76
	v_fmaak_f32 v13, v113, v141, 0x4b400000
	v_fmaak_f32 v14, v114, v141, 0x4b400000
	v_fmaak_f32 v15, v115, v141, 0x4b400000
	v_fmaak_f32 v16, v116, v141, 0x4b400000
	v_perm_b32 v15, v16, v15, s75
	v_perm_b32 v13, v14, v13, s75
	v_perm_b32 v13, v15, v13, s76
	v_fmaak_f32 v14, v117, v141, 0x4b400000
	v_fmaak_f32 v15, v118, v141, 0x4b400000
	v_fmaak_f32 v16, v119, v141, 0x4b400000
	v_fmaak_f32 v17, v120, v141, 0x4b400000
	v_perm_b32 v16, v17, v16, s75
	v_perm_b32 v14, v15, v14, s75
	v_perm_b32 v14, v16, v14, s76
	v_fmaak_f32 v15, v121, v141, 0x4b400000
	v_fmaak_f32 v16, v122, v141, 0x4b400000
	v_fmaak_f32 v17, v123, v141, 0x4b400000
	v_fmaak_f32 v18, v124, v141, 0x4b400000
	v_perm_b32 v17, v18, v17, s75
	v_perm_b32 v15, v16, v15, s75
	v_perm_b32 v15, v17, v15, s76
	v_fmaak_f32 v16, v125, v141, 0x4b400000
	v_fmaak_f32 v17, v126, v141, 0x4b400000
	v_fmaak_f32 v18, v127, v141, 0x4b400000
	v_fmaak_f32 v19, v128, v141, 0x4b400000
	v_perm_b32 v18, v19, v18, s75
	v_perm_b32 v16, v17, v16, s75
	v_perm_b32 v16, v18, v16, s76
	v_fmaak_f32 v17, v129, v141, 0x4b400000
	v_fmaak_f32 v18, v130, v141, 0x4b400000
	v_fmaak_f32 v19, v131, v141, 0x4b400000
	v_perm_b32 v19, v20, v19, s75
	v_perm_b32 v17, v18, v17, s75
	v_perm_b32 v17, v19, v17, s76
	v_fmaak_f32 v18, v133, v141, 0x4b400000
	v_fmaak_f32 v19, v134, v141, 0x4b400000
	v_fmaak_f32 v20, v135, v141, 0x4b400000
	v_fmaak_f32 v21, v136, v141, 0x4b400000
	v_perm_b32 v20, v21, v20, s75
	v_perm_b32 v18, v19, v18, s75
	v_perm_b32 v18, v20, v18, s76
	v_fmaak_f32 v19, v137, v141, 0x4b400000
	v_fmaak_f32 v20, v138, v141, 0x4b400000
	v_fmaak_f32 v21, v139, v141, 0x4b400000
	v_fmaak_f32 v22, v144, v141, 0x4b400000
	v_perm_b32 v21, v22, v21, s75
	v_perm_b32 v19, v20, v19, s75
	v_perm_b32 v19, v21, v19, s76
	v_cndmask_b32_e64 v20, v12, v16, s[2:3]
	v_cndmask_b32_e64 v21, v13, v17, s[2:3]
	v_cndmask_b32_e64 v22, v14, v18, s[2:3]
	v_cndmask_b32_e64 v23, v15, v19, s[2:3]
	v_readlane_b32 s6, v252, 37
	v_mov_b32_dpp v20, v20 quad_perm:[1,0,3,2] row_mask:0xf bank_mask:0xf bound_ctrl:1
	v_mov_b32_dpp v21, v21 quad_perm:[1,0,3,2] row_mask:0xf bank_mask:0xf bound_ctrl:1
	v_mov_b32_dpp v22, v22 quad_perm:[1,0,3,2] row_mask:0xf bank_mask:0xf bound_ctrl:1
	v_mov_b32_dpp v23, v23 quad_perm:[1,0,3,2] row_mask:0xf bank_mask:0xf bound_ctrl:1
	v_readlane_b32 s7, v252, 38
	v_cndmask_b32_e64 v12, v20, v12, s[2:3]
	v_cndmask_b32_e64 v16, v16, v20, s[2:3]
	v_cndmask_b32_e64 v13, v21, v13, s[2:3]
	v_cndmask_b32_e64 v17, v17, v21, s[2:3]
	v_cndmask_b32_e64 v14, v22, v14, s[2:3]
	v_cndmask_b32_e64 v18, v18, v22, s[2:3]
	v_cndmask_b32_e64 v15, v23, v15, s[2:3]
	v_cndmask_b32_e64 v19, v19, v23, s[2:3]
	s_andn2_b64 vcc, exec, s[6:7]
	global_store_dwordx4 v[6:7], v[12:15], off offset:96
	global_store_dwordx4 v[8:9], v[16:19], off offset:96
	s_cbranch_vccnz .LBB0_12
	s_and_b64 s[4:5], s[4:5], exec
	s_cselect_b32 s4, 0x2400, 0
	s_add_u32 s4, s10, s4
	s_addc_u32 s5, s11, 0
	v_lshl_add_u64 v[4:5], v[4:5], 2, s[4:5]
	global_store_dword v[4:5], v140, off

; template <bool PERMGL, bool FP8>
; __device__ __forceinline__ void q8_cols_item(const float* W, int N, int n0, unsigned char* Bq, float* sc_out, LAS float* AM, int par, int wave, int lane) {
;     const int n = n0 + lane;
;     const float* Wp = W + (size_t)(128 * wave) * N + n;
;     float v[128]; float am = 0.f;
; #pragma unroll
;     for (int i = 0; i < 128; ++i) v[i] = Wp[(size_t)i * N];
; __global__ void __launch_bounds__(NWAVES * 64, 2) mk_fwd(Args args) {
;     ...
;                 if (it < 64) { const int mi = it >> 5, nb = it & 31;
;                     q8_cols_item<false, false>(args.in[1] + (size_t)mi * D * EVEN_IN, EVEN_IN, nb * 64, ws + WS_EVIN + (size_t)mi * EVEN_IN * 1024, (float*)(ws + WS_SBIN) + mi * EVEN_IN, AM, par, wave, lane); }
.LBB0_13:
	s_andn2_b64 vcc, exec, s[4:5]
	s_cbranch_vccnz .LBB0_8
	s_ashr_i32 s4, s77, 5
	s_ashr_i32 s5, s4, 31
	s_lshl_b64 s[80:81], s[4:5], 23
	s_and_b32 s33, s14, 0x7c0
	s_lshl_b64 s[6:7], s[4:5], 21
	v_readlane_b32 s5, v252, 29
	s_add_u32 s6, s5, s6
	v_readlane_b32 s5, v252, 30
	s_addc_u32 s7, s5, s7
	v_add_u32_e32 v4, s33, v0
	s_add_u32 s80, s12, s80
	s_addc_u32 s81, s13, s81
	v_ashrrev_i32_e32 v5, 31, v4
	v_lshl_add_u64 v[6:7], v[4:5], 2, s[80:81]
	v_add_co_u32_e32 v12, vcc, s16, v6
	global_load_dword v8, v[6:7], off nt
	s_nop 0
	v_addc_co_u32_e32 v13, vcc, 0, v7, vcc
	global_load_dword v9, v[12:13], off nt
	v_add_co_u32_e32 v12, vcc, s17, v6
	s_mov_b32 s5, 0x8000
	s_nop 0
	v_addc_co_u32_e32 v13, vcc, 0, v7, vcc
	v_add_co_u32_e32 v14, vcc, s18, v6
	global_load_dword v12, v[12:13], off nt
	s_nop 0
	v_addc_co_u32_e32 v15, vcc, 0, v7, vcc
	v_add_co_u32_e32 v16, vcc, s5, v6
	s_mov_b32 s5, 0xa000
	s_nop 0
	v_addc_co_u32_e32 v17, vcc, 0, v7, vcc
	global_load_dword v14, v[14:15], off nt
	s_nop 0
	global_load_dword v13, v[16:17], off nt
	v_add_co_u32_e32 v16, vcc, s5, v6
	s_mov_b32 s5, 0xc000
	s_nop 0
	v_addc_co_u32_e32 v17, vcc, 0, v7, vcc
	global_load_dword v15, v[16:17], off nt
	v_add_co_u32_e32 v16, vcc, s5, v6
	s_mov_b32 s5, 0xe000
	s_nop 0
	v_addc_co_u32_e32 v17, vcc, 0, v7, vcc
	v_add_co_u32_e32 v18, vcc, s5, v6
	s_mov_b32 s5, 0x10000
	s_nop 0
	v_addc_co_u32_e32 v19, vcc, 0, v7, vcc
	v_add_co_u32_e32 v20, vcc, s5, v6
	global_load_dword v16, v[16:17], off nt
	s_nop 0
	v_addc_co_u32_e32 v21, vcc, 0, v7, vcc
	global_load_dword v18, v[18:19], off nt
	s_mov_b32 s5, 0x1a000
	global_load_dword v17, v[20:21], off nt
	v_add_co_u32_e32 v20, vcc, s19, v6
	s_nop 1
	v_addc_co_u32_e32 v21, vcc, 0, v7, vcc
	global_load_dword v19, v[20:21], off nt
	v_add_co_u32_e32 v20, vcc, s20, v6
	s_nop 1
	v_addc_co_u32_e32 v21, vcc, 0, v7, vcc
	v_add_co_u32_e32 v22, vcc, s21, v6
	global_load_dword v20, v[20:21], off nt
	s_nop 0
	v_addc_co_u32_e32 v23, vcc, 0, v7, vcc
	v_add_co_u32_e32 v24, vcc, s22, v6
	global_load_dword v22, v[22:23], off nt
	s_nop 0
	v_addc_co_u32_e32 v25, vcc, 0, v7, vcc
	global_load_dword v21, v[24:25], off nt
	v_add_co_u32_e32 v24, vcc, s5, v6
	s_mov_b32 s5, 0x1c000
	s_nop 0
	v_addc_co_u32_e32 v25, vcc, 0, v7, vcc
	global_load_dword v23, v[24:25], off nt
	v_add_co_u32_e32 v24, vcc, s5, v6
	s_mov_b32 s5, 0x1e000
	s_nop 0
	v_addc_co_u32_e32 v25, vcc, 0, v7, vcc
	v_add_co_u32_e32 v26, vcc, s5, v6
	s_mov_b32 s5, 0x20000
	s_nop 0
	v_addc_co_u32_e32 v27, vcc, 0, v7, vcc
	v_add_co_u32_e32 v28, vcc, s5, v6
	s_mov_b32 s5, 0x22000
	s_nop 0
	v_addc_co_u32_e32 v29, vcc, 0, v7, vcc
	global_load_dword v24, v[24:25], off nt
	s_nop 0
	global_load_dword v26, v[26:27], off nt
	s_nop 0
	global_load_dword v25, v[28:29], off nt
	v_add_co_u32_e32 v28, vcc, s5, v6
	s_mov_b32 s5, 0x2c000
	s_nop 0
	v_addc_co_u32_e32 v29, vcc, 0, v7, vcc
	global_load_dword v27, v[28:29], off nt
	v_add_co_u32_e32 v28, vcc, s23, v6
	s_nop 1
	v_addc_co_u32_e32 v29, vcc, 0, v7, vcc
	v_add_co_u32_e32 v30, vcc, s24, v6
	global_load_dword v28, v[28:29], off nt
	s_nop 0
	v_addc_co_u32_e32 v31, vcc, 0, v7, vcc
	v_add_co_u32_e32 v32, vcc, s25, v6
	global_load_dword v30, v[30:31], off nt
	s_nop 0
	v_addc_co_u32_e32 v33, vcc, 0, v7, vcc
	global_load_dword v29, v[32:33], off nt
	v_add_co_u32_e32 v32, vcc, s26, v6
	s_nop 1
	v_addc_co_u32_e32 v33, vcc, 0, v7, vcc
	global_load_dword v31, v[32:33], off nt
	v_add_co_u32_e32 v32, vcc, s5, v6
	s_mov_b32 s5, 0x2e000
	s_nop 0
	v_addc_co_u32_e32 v33, vcc, 0, v7, vcc
	v_add_co_u32_e32 v34, vcc, s5, v6
	s_mov_b32 s5, 0x30000
	s_nop 0
	v_addc_co_u32_e32 v35, vcc, 0, v7, vcc
	v_add_co_u32_e32 v36, vcc, s5, v6
	s_mov_b32 s5, 0x32000
	s_nop 0
	v_addc_co_u32_e32 v37, vcc, 0, v7, vcc
	global_load_dword v32, v[32:33], off nt
	s_nop 0
	global_load_dword v34, v[34:35], off nt
	s_nop 0
	global_load_dword v33, v[36:37], off nt
	v_add_co_u32_e32 v36, vcc, s5, v6
	s_mov_b32 s5, 0x34000
	s_nop 0
	v_addc_co_u32_e32 v37, vcc, 0, v7, vcc
	global_load_dword v35, v[36:37], off nt
	v_add_co_u32_e32 v36, vcc, s5, v6
	s_mov_b32 s5, 0x3e000
	s_nop 0
	v_addc_co_u32_e32 v37, vcc, 0, v7, vcc
	v_add_co_u32_e32 v38, vcc, s27, v6
	global_load_dword v37, v[36:37], off nt
	s_nop 0
	v_addc_co_u32_e32 v39, vcc, 0, v7, vcc
	global_load_dword v40, v[38:39], off nt
	v_add_co_u32_e32 v38, vcc, s28, v6
	s_nop 1
	v_addc_co_u32_e32 v39, vcc, 0, v7, vcc
	v_add_co_u32_e32 v42, vcc, s29, v6
	global_load_dword v39, v[38:39], off nt
	s_nop 0
	v_addc_co_u32_e32 v43, vcc, 0, v7, vcc
	global_load_dword v41, v[42:43], off nt
	v_add_co_u32_e32 v42, vcc, s30, v6
	s_nop 1
	v_addc_co_u32_e32 v43, vcc, 0, v7, vcc
	global_load_dword v45, v[42:43], off nt
	v_add_co_u32_e32 v42, vcc, s5, v6
	s_mov_b32 s5, 0x40000
	s_nop 0
	v_addc_co_u32_e32 v43, vcc, 0, v7, vcc
	global_load_dword v48, v[42:43], off nt
	v_add_co_u32_e32 v42, vcc, s5, v6
	s_mov_b32 s5, 0x42000
	s_nop 0
	v_addc_co_u32_e32 v43, vcc, 0, v7, vcc
	global_load_dword v36, v[42:43], off nt
	v_add_co_u32_e32 v42, vcc, s5, v6
	s_mov_b32 s5, 0x44000
	s_nop 0
	v_addc_co_u32_e32 v43, vcc, 0, v7, vcc
	global_load_dword v38, v[42:43], off nt
	v_add_co_u32_e32 v42, vcc, s5, v6
	s_mov_b32 s5, 0x46000
	s_nop 0
	v_addc_co_u32_e32 v43, vcc, 0, v7, vcc
	v_add_co_u32_e32 v46, vcc, s5, v6
	global_load_dword v42, v[42:43], off nt
	s_nop 0
	v_addc_co_u32_e32 v47, vcc, 0, v7, vcc
	global_load_dword v44, v[46:47], off nt
	v_add_co_u32_e32 v46, vcc, s31, v6
	s_mov_b32 s5, 0x50000
	s_nop 0
	v_addc_co_u32_e32 v47, vcc, 0, v7, vcc
	global_load_dword v43, v[46:47], off nt
	v_add_co_u32_e32 v46, vcc, s34, v6
	s_nop 1
	v_addc_co_u32_e32 v47, vcc, 0, v7, vcc
	v_add_co_u32_e32 v50, vcc, s35, v6
; template <bool PERMGL, bool FP8>
; __device__ __forceinline__ void q8_cols_item(const float* W, int N, int n0, unsigned char* Bq, float* sc_out, LAS float* AM, int par, int wave, int lane) {
;     ...
;     for (int i = 0; i < 128; ++i) v[i] = Wp[(size_t)i * N];
	global_load_dword v46, v[46:47], off nt
	s_nop 0
	v_addc_co_u32_e32 v51, vcc, 0, v7, vcc
	global_load_dword v47, v[50:51], off nt
	v_add_co_u32_e32 v50, vcc, s36, v6
	s_nop 1
	v_addc_co_u32_e32 v51, vcc, 0, v7, vcc
	v_add_co_u32_e32 v52, vcc, s5, v6
	s_mov_b32 s5, 0x52000
	s_nop 0
	v_addc_co_u32_e32 v53, vcc, 0, v7, vcc
	global_load_dword v50, v[50:51], off nt
	s_nop 0
	global_load_dword v49, v[52:53], off nt
	v_add_co_u32_e32 v52, vcc, s5, v6
	s_mov_b32 s5, 0x54000
	s_nop 0
	v_addc_co_u32_e32 v53, vcc, 0, v7, vcc
	global_load_dword v51, v[52:53], off nt
	v_add_co_u32_e32 v52, vcc, s5, v6
	s_mov_b32 s5, 0x56000
	s_nop 0
	v_addc_co_u32_e32 v53, vcc, 0, v7, vcc
	v_add_co_u32_e32 v54, vcc, s5, v6
	s_mov_b32 s5, 0x58000
	s_nop 0
	v_addc_co_u32_e32 v55, vcc, 0, v7, vcc
	v_add_co_u32_e32 v56, vcc, s5, v6
	global_load_dword v52, v[52:53], off nt
	s_nop 0
	v_addc_co_u32_e32 v57, vcc, 0, v7, vcc
	global_load_dword v54, v[54:55], off nt
	s_mov_b32 s5, 0x62000
	global_load_dword v53, v[56:57], off nt
	v_add_co_u32_e32 v56, vcc, s37, v6
	s_nop 1
	v_addc_co_u32_e32 v57, vcc, 0, v7, vcc
	global_load_dword v55, v[56:57], off nt
	v_add_co_u32_e32 v56, vcc, s38, v6
	s_nop 1
	v_addc_co_u32_e32 v57, vcc, 0, v7, vcc
	v_add_co_u32_e32 v58, vcc, s39, v6
	global_load_dword v56, v[56:57], off nt
	s_nop 0
	v_addc_co_u32_e32 v59, vcc, 0, v7, vcc
	v_add_co_u32_e32 v60, vcc, s40, v6
	global_load_dword v58, v[58:59], off nt
	s_nop 0
	v_addc_co_u32_e32 v61, vcc, 0, v7, vcc
	global_load_dword v57, v[60:61], off nt
	v_add_co_u32_e32 v60, vcc, s5, v6
	s_mov_b32 s5, 0x64000
	s_nop 0
	v_addc_co_u32_e32 v61, vcc, 0, v7, vcc
	global_load_dword v59, v[60:61], off nt
	v_add_co_u32_e32 v60, vcc, s5, v6
	s_mov_b32 s5, 0x66000
	s_nop 0
	v_addc_co_u32_e32 v61, vcc, 0, v7, vcc
	v_add_co_u32_e32 v62, vcc, s5, v6
	s_mov_b32 s5, 0x68000
	s_nop 0
	v_addc_co_u32_e32 v63, vcc, 0, v7, vcc
	v_add_co_u32_e32 v64, vcc, s5, v6
	s_mov_b32 s5, 0x6a000
	s_nop 0
	v_addc_co_u32_e32 v65, vcc, 0, v7, vcc
	global_load_dword v60, v[60:61], off nt
	s_nop 0
	global_load_dword v62, v[62:63], off nt
	s_nop 0
	global_load_dword v61, v[64:65], off nt
	v_add_co_u32_e32 v64, vcc, s5, v6
	s_mov_b32 s5, 0x74000
	s_nop 0
	v_addc_co_u32_e32 v65, vcc, 0, v7, vcc
	global_load_dword v63, v[64:65], off nt
	v_add_co_u32_e32 v64, vcc, s41, v6
	s_nop 1
	v_addc_co_u32_e32 v65, vcc, 0, v7, vcc
	v_add_co_u32_e32 v66, vcc, s42, v6
	global_load_dword v64, v[64:65], off nt
	s_nop 0
	v_addc_co_u32_e32 v67, vcc, 0, v7, vcc
	v_add_co_u32_e32 v68, vcc, s43, v6
	global_load_dword v66, v[66:67], off nt
	s_nop 0
	v_addc_co_u32_e32 v69, vcc, 0, v7, vcc
	global_load_dword v65, v[68:69], off nt
	v_add_co_u32_e32 v68, vcc, s44, v6
	s_nop 1
	v_addc_co_u32_e32 v69, vcc, 0, v7, vcc
	global_load_dword v67, v[68:69], off nt
	v_add_co_u32_e32 v68, vcc, s5, v6
	s_mov_b32 s5, 0x76000
	s_nop 0
	v_addc_co_u32_e32 v69, vcc, 0, v7, vcc
	v_add_co_u32_e32 v70, vcc, s5, v6
	s_mov_b32 s5, 0x78000
	s_nop 0
	v_addc_co_u32_e32 v71, vcc, 0, v7, vcc
	v_add_co_u32_e32 v72, vcc, s5, v6
	s_mov_b32 s5, 0x7a000
	s_nop 0
	v_addc_co_u32_e32 v73, vcc, 0, v7, vcc
	global_load_dword v68, v[68:69], off nt
	s_nop 0
	global_load_dword v70, v[70:71], off nt
	s_nop 0
	global_load_dword v69, v[72:73], off nt
	v_add_co_u32_e32 v72, vcc, s5, v6
	s_mov_b32 s5, 0x7c000
	s_nop 0
	v_addc_co_u32_e32 v73, vcc, 0, v7, vcc
	v_add_co_u32_e32 v74, vcc, s5, v6
	global_load_dword v72, v[72:73], off nt
	s_nop 0
	v_addc_co_u32_e32 v75, vcc, 0, v7, vcc
	v_add_co_u32_e32 v76, vcc, s45, v6
	global_load_dword v75, v[74:75], off nt
	s_nop 0
	v_addc_co_u32_e32 v77, vcc, 0, v7, vcc
	global_load_dword v78, v[76:77], off nt
	v_add_co_u32_e32 v76, vcc, s46, v6
	s_mov_b32 s5, 0x86000
	s_nop 0
	v_addc_co_u32_e32 v77, vcc, 0, v7, vcc
	global_load_dword v71, v[76:77], off nt
	v_add_co_u32_e32 v76, vcc, s47, v6
	s_nop 1
	v_addc_co_u32_e32 v77, vcc, 0, v7, vcc
	global_load_dword v73, v[76:77], off nt
	v_add_co_u32_e32 v76, vcc, s48, v6
	s_nop 1
	v_addc_co_u32_e32 v77, vcc, 0, v7, vcc
	global_load_dword v74, v[76:77], off nt
	v_add_co_u32_e32 v76, vcc, s5, v6
	s_mov_b32 s5, 0x88000
	s_nop 0
	v_addc_co_u32_e32 v77, vcc, 0, v7, vcc
	v_add_co_u32_e32 v80, vcc, s5, v6
	s_mov_b32 s5, 0x8a000
	s_nop 0
	v_addc_co_u32_e32 v81, vcc, 0, v7, vcc
	global_load_dword v77, v[76:77], off nt
	s_nop 0
	global_load_dword v76, v[80:81], off nt
	v_add_co_u32_e32 v80, vcc, s5, v6
	s_mov_b32 s5, 0x8c000
	s_nop 0
	v_addc_co_u32_e32 v81, vcc, 0, v7, vcc
	global_load_dword v79, v[80:81], off nt
	v_add_co_u32_e32 v80, vcc, s5, v6
	s_mov_b32 s5, 0x8e000
	s_nop 0
	v_addc_co_u32_e32 v81, vcc, 0, v7, vcc
	v_add_co_u32_e32 v82, vcc, s5, v6
	global_load_dword v80, v[80:81], off nt
	s_nop 0
	v_addc_co_u32_e32 v83, vcc, 0, v7, vcc
	v_add_co_u32_e32 v84, vcc, s49, v6
	global_load_dword v82, v[82:83], off nt
	s_nop 0
	v_addc_co_u32_e32 v85, vcc, 0, v7, vcc
	global_load_dword v81, v[84:85], off nt
	v_add_co_u32_e32 v84, vcc, s50, v6
	s_mov_b32 s5, 0x98000
	s_nop 0
	v_addc_co_u32_e32 v85, vcc, 0, v7, vcc
	global_load_dword v83, v[84:85], off nt
	v_add_co_u32_e32 v84, vcc, s51, v6
	s_nop 1
	v_addc_co_u32_e32 v85, vcc, 0, v7, vcc
	v_add_co_u32_e32 v86, vcc, s52, v6
	global_load_dword v84, v[84:85], off nt
	s_nop 0
	v_addc_co_u32_e32 v87, vcc, 0, v7, vcc
	v_add_co_u32_e32 v88, vcc, s5, v6
	s_mov_b32 s5, 0x9a000
	s_nop 0
	v_addc_co_u32_e32 v89, vcc, 0, v7, vcc
	global_load_dword v86, v[86:87], off nt
	s_nop 0
	global_load_dword v85, v[88:89], off nt
	v_add_co_u32_e32 v88, vcc, s5, v6
	s_mov_b32 s5, 0x9c000
	s_nop 0
	v_addc_co_u32_e32 v89, vcc, 0, v7, vcc
	global_load_dword v87, v[88:89], off nt
	v_add_co_u32_e32 v88, vcc, s5, v6
	s_mov_b32 s5, 0x9e000
; template <bool PERMGL, bool FP8>
; __device__ __forceinline__ void q8_cols_item(const float* W, int N, int n0, unsigned char* Bq, float* sc_out, LAS float* AM, int par, int wave, int lane) {
;     ...
;     for (int i = 0; i < 128; ++i) v[i] = Wp[(size_t)i * N];
	s_nop 0
	v_addc_co_u32_e32 v89, vcc, 0, v7, vcc
	v_add_co_u32_e32 v92, vcc, s5, v6
	s_mov_b32 s5, 0xa0000
	s_nop 0
	v_addc_co_u32_e32 v93, vcc, 0, v7, vcc
	global_load_dword v88, v[88:89], off nt
	s_nop 0
	global_load_dword v89, v[92:93], off nt
	v_add_co_u32_e32 v92, vcc, s5, v6
	s_mov_b32 s5, 0xaa000
	s_nop 0
	v_addc_co_u32_e32 v93, vcc, 0, v7, vcc
	global_load_dword v91, v[92:93], off nt
	v_add_co_u32_e32 v92, vcc, s53, v6
	s_nop 1
	v_addc_co_u32_e32 v93, vcc, 0, v7, vcc
	v_add_co_u32_e32 v94, vcc, s54, v6
	global_load_dword v92, v[92:93], off nt
	s_nop 0
	v_addc_co_u32_e32 v95, vcc, 0, v7, vcc
	global_load_dword v93, v[94:95], off nt
	v_add_co_u32_e32 v94, vcc, s55, v6
	s_nop 1
	v_addc_co_u32_e32 v95, vcc, 0, v7, vcc
	v_add_co_u32_e32 v96, vcc, s56, v6
	global_load_dword v94, v[94:95], off nt
	s_nop 0
	v_addc_co_u32_e32 v97, vcc, 0, v7, vcc
	global_load_dword v95, v[96:97], off nt
	v_add_co_u32_e32 v96, vcc, s5, v6
	s_mov_b32 s5, 0xac000
	s_nop 0
	v_addc_co_u32_e32 v97, vcc, 0, v7, vcc
	v_add_co_u32_e32 v98, vcc, s5, v6
	s_mov_b32 s5, 0xae000
	s_nop 0
	v_addc_co_u32_e32 v99, vcc, 0, v7, vcc
	global_load_dword v96, v[96:97], off nt
	s_nop 0
	global_load_dword v97, v[98:99], off nt
	v_add_co_u32_e32 v98, vcc, s5, v6
	s_mov_b32 s5, 0xb0000
	s_nop 0
	v_addc_co_u32_e32 v99, vcc, 0, v7, vcc
	v_add_co_u32_e32 v100, vcc, s5, v6
	s_mov_b32 s5, 0xb2000
	s_nop 0
	v_addc_co_u32_e32 v101, vcc, 0, v7, vcc
	global_load_dword v98, v[98:99], off nt
	s_nop 0
	global_load_dword v99, v[100:101], off nt
	v_add_co_u32_e32 v100, vcc, s5, v6
	s_mov_b32 s5, 0xbc000
	s_nop 0
	v_addc_co_u32_e32 v101, vcc, 0, v7, vcc
	v_add_co_u32_e32 v102, vcc, s57, v6
	global_load_dword v100, v[100:101], off nt
	s_nop 0
	v_addc_co_u32_e32 v103, vcc, 0, v7, vcc
	global_load_dword v101, v[102:103], off nt
	v_add_co_u32_e32 v102, vcc, s58, v6
	s_nop 1
	v_addc_co_u32_e32 v103, vcc, 0, v7, vcc
	v_add_co_u32_e32 v104, vcc, s59, v6
	global_load_dword v102, v[102:103], off nt
	s_nop 0
	v_addc_co_u32_e32 v105, vcc, 0, v7, vcc
	global_load_dword v103, v[104:105], off nt
	v_add_co_u32_e32 v104, vcc, s60, v6
	s_nop 1
	v_addc_co_u32_e32 v105, vcc, 0, v7, vcc
	v_add_co_u32_e32 v106, vcc, s5, v6
	s_mov_b32 s5, 0xbe000
	s_nop 0
	v_addc_co_u32_e32 v107, vcc, 0, v7, vcc
	v_add_co_u32_e32 v108, vcc, s5, v6
	s_mov_b32 s5, 0xc0000
	s_nop 0
	v_addc_co_u32_e32 v109, vcc, 0, v7, vcc
	v_add_co_u32_e32 v110, vcc, s5, v6
	s_mov_b32 s5, 0xc2000
	s_nop 0
	v_addc_co_u32_e32 v111, vcc, 0, v7, vcc
	global_load_dword v104, v[104:105], off nt
	s_nop 0
	global_load_dword v106, v[106:107], off nt
	s_nop 0
	global_load_dword v109, v[108:109], off nt
	s_nop 0
	global_load_dword v105, v[110:111], off nt
	v_add_co_u32_e32 v110, vcc, s5, v6
	s_mov_b32 s5, 0xc4000
	s_nop 0
	v_addc_co_u32_e32 v111, vcc, 0, v7, vcc
	global_load_dword v107, v[110:111], off nt
	v_add_co_u32_e32 v110, vcc, s5, v6
	s_mov_b32 s5, 0xce000
	s_nop 0
	v_addc_co_u32_e32 v111, vcc, 0, v7, vcc
	global_load_dword v108, v[110:111], off nt
	v_add_co_u32_e32 v110, vcc, s61, v6
	s_nop 1
	v_addc_co_u32_e32 v111, vcc, 0, v7, vcc
	v_add_co_u32_e32 v112, vcc, s62, v6
	global_load_dword v110, v[110:111], off nt
	s_nop 0
	v_addc_co_u32_e32 v113, vcc, 0, v7, vcc
	global_load_dword v111, v[112:113], off nt
	v_add_co_u32_e32 v112, vcc, s63, v6
	s_nop 1
	v_addc_co_u32_e32 v113, vcc, 0, v7, vcc
	v_add_co_u32_e32 v114, vcc, s64, v6
	global_load_dword v112, v[112:113], off nt
	s_nop 0
	v_addc_co_u32_e32 v115, vcc, 0, v7, vcc
	global_load_dword v113, v[114:115], off nt
	v_add_co_u32_e32 v114, vcc, s5, v6
	s_mov_b32 s5, 0xd0000
	s_nop 0
	v_addc_co_u32_e32 v115, vcc, 0, v7, vcc
	v_add_co_u32_e32 v116, vcc, s5, v6
	s_mov_b32 s5, 0xd2000
	s_nop 0
	v_addc_co_u32_e32 v117, vcc, 0, v7, vcc
	global_load_dword v114, v[114:115], off nt
	s_nop 0
	global_load_dword v115, v[116:117], off nt
	v_add_co_u32_e32 v116, vcc, s5, v6
	s_mov_b32 s5, 0xd4000
	s_nop 0
	v_addc_co_u32_e32 v117, vcc, 0, v7, vcc
	v_add_co_u32_e32 v118, vcc, s5, v6
	s_mov_b32 s5, 0xd6000
	s_nop 0
	v_addc_co_u32_e32 v119, vcc, 0, v7, vcc
	global_load_dword v116, v[116:117], off nt
	s_nop 0
	global_load_dword v117, v[118:119], off nt
	v_add_co_u32_e32 v118, vcc, s5, v6
	s_mov_b32 s5, 0xe0000
	s_nop 0
	v_addc_co_u32_e32 v119, vcc, 0, v7, vcc
	v_add_co_u32_e32 v120, vcc, s65, v6
	global_load_dword v118, v[118:119], off nt
	s_nop 0
	v_addc_co_u32_e32 v121, vcc, 0, v7, vcc
	global_load_dword v119, v[120:121], off nt
	v_add_co_u32_e32 v120, vcc, s66, v6
	s_nop 1
	v_addc_co_u32_e32 v121, vcc, 0, v7, vcc
	v_add_co_u32_e32 v122, vcc, s67, v6
	global_load_dword v120, v[120:121], off nt
	s_nop 0
	v_addc_co_u32_e32 v123, vcc, 0, v7, vcc
	global_load_dword v121, v[122:123], off nt
	v_add_co_u32_e32 v122, vcc, s68, v6
	s_nop 1
	v_addc_co_u32_e32 v123, vcc, 0, v7, vcc
	v_add_co_u32_e32 v124, vcc, s5, v6
	s_mov_b32 s5, 0xe2000
	s_nop 0
	v_addc_co_u32_e32 v125, vcc, 0, v7, vcc
	global_load_dword v122, v[122:123], off nt
	s_nop 0
	global_load_dword v123, v[124:125], off nt
	v_add_co_u32_e32 v124, vcc, s5, v6
	s_mov_b32 s5, 0xe4000
	s_nop 0
	v_addc_co_u32_e32 v125, vcc, 0, v7, vcc
	v_add_co_u32_e32 v126, vcc, s5, v6
	s_mov_b32 s5, 0xe6000
	s_nop 0
	v_addc_co_u32_e32 v127, vcc, 0, v7, vcc
	global_load_dword v124, v[124:125], off nt
	s_nop 0
	global_load_dword v125, v[126:127], off nt
	v_add_co_u32_e32 v126, vcc, s5, v6
	s_mov_b32 s5, 0xe8000
	s_nop 0
	v_addc_co_u32_e32 v127, vcc, 0, v7, vcc
	v_add_co_u32_e32 v128, vcc, s5, v6
	global_load_dword v126, v[126:127], off nt
	s_nop 0
	v_addc_co_u32_e32 v129, vcc, 0, v7, vcc
	global_load_dword v127, v[128:129], off nt
	v_add_co_u32_e32 v128, vcc, s69, v6
	s_mov_b32 s5, 0xf2000
	s_nop 0
; template <bool PERMGL, bool FP8>
; __device__ __forceinline__ void q8_cols_item(const float* W, int N, int n0, unsigned char* Bq, float* sc_out, LAS float* AM, int par, int wave, int lane) {
;     ...
;     for (int i = 0; i < 128; ++i) v[i] = Wp[(size_t)i * N];
;     __builtin_amdgcn_sched_barrier(0);
; #pragma unroll
;     for (int i = 0; i < 128; ++i) am = fmaxf(am, fabsf(v[i]));
;     AM[(par * 8 + wave) * 64 + lane] = am;
;     __syncthreads();
	v_addc_co_u32_e32 v129, vcc, 0, v7, vcc
	v_add_co_u32_e32 v130, vcc, s70, v6
	global_load_dword v128, v[128:129], off nt
	s_nop 0
	v_addc_co_u32_e32 v131, vcc, 0, v7, vcc
	global_load_dword v129, v[130:131], off nt
	v_add_co_u32_e32 v130, vcc, s71, v6
	s_nop 1
	v_addc_co_u32_e32 v131, vcc, 0, v7, vcc
	v_add_co_u32_e32 v132, vcc, s72, v6
	global_load_dword v130, v[130:131], off nt
	s_nop 0
	v_addc_co_u32_e32 v133, vcc, 0, v7, vcc
	global_load_dword v131, v[132:133], off nt
	v_add_co_u32_e32 v132, vcc, s5, v6
	s_mov_b32 s5, 0xf4000
	s_nop 0
	v_addc_co_u32_e32 v133, vcc, 0, v7, vcc
	v_add_co_u32_e32 v134, vcc, s5, v6
	s_mov_b32 s5, 0xf6000
	s_nop 0
	v_addc_co_u32_e32 v135, vcc, 0, v7, vcc
	global_load_dword v132, v[132:133], off nt
	s_nop 0
	global_load_dword v133, v[134:135], off nt
	v_add_co_u32_e32 v134, vcc, s5, v6
	s_mov_b32 s5, 0xf8000
	s_nop 0
	v_addc_co_u32_e32 v135, vcc, 0, v7, vcc
	v_add_co_u32_e32 v136, vcc, s5, v6
	s_mov_b32 s5, 0xfa000
	s_nop 0
	v_addc_co_u32_e32 v137, vcc, 0, v7, vcc
	global_load_dword v134, v[134:135], off nt
	s_nop 0
	global_load_dword v135, v[136:137], off nt
	v_add_co_u32_e32 v136, vcc, s5, v6
	s_nop 1
	v_addc_co_u32_e32 v137, vcc, 0, v7, vcc
	v_add_co_u32_e32 v138, vcc, s73, v6
	global_load_dword v136, v[136:137], off nt
	s_nop 0
	v_addc_co_u32_e32 v139, vcc, 0, v7, vcc
	v_add_co_u32_e32 v6, vcc, s74, v6
	s_nop 1
	v_addc_co_u32_e32 v7, vcc, 0, v7, vcc
	global_load_dword v144, v[6:7], off nt
	global_load_dword v137, v[138:139], off nt
	s_waitcnt vmcnt(62)
	v_max3_f32 v6, |v8|, 0, |v9|
	v_max3_f32 v6, v6, |v12|, |v14|
	v_max3_f32 v6, v6, |v13|, |v15|
	v_max3_f32 v6, v6, |v16|, |v18|
	v_max3_f32 v6, v6, |v17|, |v19|
	v_max3_f32 v6, v6, |v20|, |v22|
	v_max3_f32 v6, v6, |v21|, |v23|
	v_max3_f32 v6, v6, |v24|, |v26|
	v_max3_f32 v6, v6, |v25|, |v27|
	v_max3_f32 v6, v6, |v28|, |v30|
	v_max3_f32 v6, v6, |v29|, |v31|
	v_max3_f32 v6, v6, |v32|, |v34|
	v_max3_f32 v6, v6, |v33|, |v35|
	v_max3_f32 v6, v6, |v37|, |v40|
	v_max3_f32 v6, v6, |v39|, |v41|
	v_max3_f32 v6, v6, |v45|, |v48|
	v_max3_f32 v6, v6, |v36|, |v38|
	v_max3_f32 v6, v6, |v42|, |v44|
	v_max3_f32 v6, v6, |v43|, |v46|
	v_max3_f32 v6, v6, |v47|, |v50|
	v_max3_f32 v6, v6, |v49|, |v51|
	v_max3_f32 v6, v6, |v52|, |v54|
	v_max3_f32 v6, v6, |v53|, |v55|
	v_max3_f32 v6, v6, |v56|, |v58|
	v_max3_f32 v6, v6, |v57|, |v59|
	v_max3_f32 v6, v6, |v60|, |v62|
	v_max3_f32 v6, v6, |v61|, |v63|
	v_max3_f32 v6, v6, |v64|, |v66|
	v_max3_f32 v6, v6, |v65|, |v67|
	v_max3_f32 v6, v6, |v68|, |v70|
	v_max3_f32 v6, v6, |v69|, |v72|
	v_max3_f32 v6, v6, |v75|, |v78|
	v_max3_f32 v6, v6, |v71|, |v73|
	s_waitcnt vmcnt(60)
	v_max3_f32 v6, v6, |v74|, |v77|
	s_waitcnt vmcnt(58)
	v_max3_f32 v6, v6, |v76|, |v79|
	s_waitcnt vmcnt(56)
	v_max3_f32 v6, v6, |v80|, |v82|
	s_waitcnt vmcnt(54)
	v_max3_f32 v6, v6, |v81|, |v83|
	s_waitcnt vmcnt(52)
	v_max3_f32 v6, v6, |v84|, |v86|
	s_waitcnt vmcnt(50)
	v_max3_f32 v6, v6, |v85|, |v87|
	s_waitcnt vmcnt(48)
	v_max3_f32 v6, v6, |v88|, |v89|
	s_waitcnt vmcnt(46)
	v_max3_f32 v6, v6, |v91|, |v92|
	s_waitcnt vmcnt(44)
	v_max3_f32 v6, v6, |v93|, |v94|
	s_waitcnt vmcnt(42)
	v_max3_f32 v6, v6, |v95|, |v96|
	s_waitcnt vmcnt(40)
	v_max3_f32 v6, v6, |v97|, |v98|
	s_waitcnt vmcnt(38)
	v_max3_f32 v6, v6, |v99|, |v100|
	s_waitcnt vmcnt(36)
	v_max3_f32 v6, v6, |v101|, |v102|
	s_waitcnt vmcnt(34)
	v_max3_f32 v6, v6, |v103|, |v104|
	s_waitcnt vmcnt(32)
	v_max3_f32 v6, v6, |v106|, |v109|
	s_waitcnt vmcnt(30)
	v_max3_f32 v6, v6, |v105|, |v107|
	s_waitcnt vmcnt(28)
	v_max3_f32 v6, v6, |v108|, |v110|
	s_waitcnt vmcnt(26)
	v_max3_f32 v6, v6, |v111|, |v112|
	s_waitcnt vmcnt(24)
	v_max3_f32 v6, v6, |v113|, |v114|
	s_waitcnt vmcnt(22)
	v_max3_f32 v6, v6, |v115|, |v116|
	s_waitcnt vmcnt(20)
	v_max3_f32 v6, v6, |v117|, |v118|
	s_waitcnt vmcnt(18)
	v_max3_f32 v6, v6, |v119|, |v120|
	s_waitcnt vmcnt(16)
	v_max3_f32 v6, v6, |v121|, |v122|
	s_waitcnt vmcnt(14)
	v_max3_f32 v6, v6, |v123|, |v124|
	s_waitcnt vmcnt(12)
	v_max3_f32 v6, v6, |v125|, |v126|
	s_waitcnt vmcnt(10)
	v_max3_f32 v6, v6, |v127|, |v128|
	s_waitcnt vmcnt(8)
	v_max3_f32 v6, v6, |v129|, |v130|
	s_waitcnt vmcnt(6)
	v_max3_f32 v6, v6, |v131|, |v132|
	s_waitcnt vmcnt(4)
	v_max3_f32 v6, v6, |v133|, |v134|
	s_waitcnt vmcnt(2)
	v_max3_f32 v6, v6, |v135|, |v136|
	s_lshl_b32 s5, s78, 11
	s_waitcnt vmcnt(0)
	v_max3_f32 v145, v6, |v137|, |v144|
	v_add_u32_e32 v6, s5, v1
	v_add_u32_e32 v142, s5, v10
	ds_write_b32 v6, v145
	s_waitcnt lgkmcnt(0)
	s_barrier
; template <bool PERMGL, bool FP8>
; __device__ __forceinline__ void q8_cols_item(const float* W, int N, int n0, unsigned char* Bq, float* sc_out, LAS float* AM, int par, int wave, int lane) {
;     ...
;     for (int w = 0; w < 8; ++w) am = fmaxf(am, AM[(par * 8 + w) * 64 + lane]);
;     const float sc = am > 0.f ? am * (FP8 ? (1.0f / 256.0f) : (1.0f / 127.0f)) : 1.0f, inv = 1.0f / sc;
;     int row = n;
;     if (PERMGL) { const int j = n >> 1, pr = n & 1, o = j & 127; row = ((j >> 7) << 8) + (((o >> 2) & 1) << 7) + ((o >> 5) << 5) + (pr << 4) + (((o >> 3) & 3) << 2) + (o & 3); }
;     if (!PERMGL) { const int o = n & 255; row = ((n >> 8) << 8) + (((o >> 3) & 1) << 7) + ((o >> 6) << 5) + (((o >> 4) & 3) << 3) + (o & 7); }
;     auto xq = [](unsigned x) { return (unsigned)__builtin_amdgcn_update_dpp(0, (int)x, 0xB1, 0xf, 0xf, true); };
;     const bool odd = lane & 1;
;     const int rowp = (int)xq((unsigned)row);
;     unsigned char* plo = Bq + (size_t)(odd ? rowp : row) * 1024 + 128 * wave + (odd ? 16 : 0);
;     unsigned char* phi = Bq + (size_t)(odd ? row : rowp) * 1024 + 128 * wave + (odd ? 16 : 0);
;     auto packc = [&](int c) { u32x4 o;
;         if (FP8) { o.x = f8x4(v[16 * c], v[16 * c + 1], v[16 * c + 2], v[16 * c + 3], inv); o.y = f8x4(v[16 * c + 4], v[16 * c + 5], v[16 * c + 6], v[16 * c + 7], inv);
;                    o.z = f8x4(v[16 * c + 8], v[16 * c + 9], v[16 * c + 10], v[16 * c + 11], inv); o.w = f8x4(v[16 * c + 12], v[16 * c + 13], v[16 * c + 14], v[16 * c + 15], inv); }
;         else { o.x = q8x4(v[16 * c], v[16 * c + 1], v[16 * c + 2], v[16 * c + 3], inv); o.y = q8x4(v[16 * c + 4], v[16 * c + 5], v[16 * c + 6], v[16 * c + 7], inv);
;                o.z = q8x4(v[16 * c + 8], v[16 * c + 9], v[16 * c + 10], v[16 * c + 11], inv); o.w = q8x4(v[16 * c + 12], v[16 * c + 13], v[16 * c + 14], v[16 * c + 15], inv); }
;         return o; };
; #pragma unroll
;     for (int j = 0; j < 4; ++j) { const u32x4 p0 = packc(2 * j), p1 = packc(2 * j + 1);
;         u32x4 snd, rcv;
; #pragma unroll
;         for (int q = 0; q < 4; ++q) { snd[q] = odd ? p0[q] : p1[q]; rcv[q] = xq(snd[q]); }
;         u32x4 a, b;
; #pragma unroll
;         for (int q = 0; q < 4; ++q) { a[q] = odd ? rcv[q] : p0[q]; b[q] = odd ? p1[q] : rcv[q]; }
;         *(u32x4*)(plo + 32 * j) = a; *(u32x4*)(phi + 32 * j) = b; }
	ds_read2st64_b32 v[6:7], v142 offset1:1
	ds_read2st64_b32 v[138:139], v142 offset0:2 offset1:3
	ds_read2st64_b32 v[140:141], v142 offset0:4 offset1:5
	ds_read2st64_b32 v[142:143], v142 offset0:6 offset1:7
	s_waitcnt lgkmcnt(3)
	v_max3_f32 v6, v145, v6, v7
	s_waitcnt lgkmcnt(2)
	v_max3_f32 v6, v6, v138, v139
	s_waitcnt lgkmcnt(1)
	v_max3_f32 v6, v6, v140, v141
	s_waitcnt lgkmcnt(0)
	v_max3_f32 v6, v6, v142, v143
	v_mul_f32_e32 v7, 0x3c010204, v6
	v_cmp_lt_f32_e32 vcc, 0, v6
	s_nop 1
	v_cndmask_b32_e32 v138, 1.0, v7, vcc
	v_div_scale_f32 v6, s[80:81], v138, v138, 1.0
	v_rcp_f32_e32 v7, v6
	v_readlane_b32 s80, v252, 31
	v_readlane_b32 s81, v252, 32
	v_fma_f32 v139, -v6, v7, 1.0
	v_fmac_f32_e32 v7, v139, v7
	v_div_scale_f32 v139, vcc, 1.0, v138, 1.0
	v_mul_f32_e32 v140, v139, v7
	v_fma_f32 v141, -v6, v140, v139
	v_fmac_f32_e32 v140, v141, v7
	v_fma_f32 v6, -v6, v140, v139
	v_div_fmas_f32 v6, v6, v7, v140
	v_lshrrev_b32_e32 v7, 1, v4
	v_and_b32_e32 v7, 0x78, v7
	v_and_b32_e32 v139, 0xffffff07, v4
	v_div_fixup_f32 v140, v6, v138, 1.0
	v_or3_b32 v139, v139, v7, v11
	v_fmaak_f32 v6, v12, v140, 0x4b400000
	v_fmaak_f32 v7, v14, v140, 0x4b400000
	v_perm_b32 v6, v7, v6, s75
	v_fmaak_f32 v7, v8, v140, 0x4b400000
	v_fmaak_f32 v8, v9, v140, 0x4b400000
	v_perm_b32 v7, v8, v7, s75
	v_perm_b32 v6, v6, v7, s76
	v_fmaak_f32 v7, v16, v140, 0x4b400000
	v_fmaak_f32 v8, v18, v140, 0x4b400000
	v_perm_b32 v7, v8, v7, s75
	v_fmaak_f32 v8, v13, v140, 0x4b400000
	v_fmaak_f32 v9, v15, v140, 0x4b400000
	v_perm_b32 v8, v9, v8, s75
	v_perm_b32 v7, v7, v8, s76
	v_fmaak_f32 v8, v20, v140, 0x4b400000
	v_fmaak_f32 v9, v22, v140, 0x4b400000
	v_perm_b32 v8, v9, v8, s75
	v_fmaak_f32 v9, v17, v140, 0x4b400000
	v_fmaak_f32 v12, v19, v140, 0x4b400000
	v_perm_b32 v9, v12, v9, s75
	v_perm_b32 v8, v8, v9, s76
	v_fmaak_f32 v9, v24, v140, 0x4b400000
	v_fmaak_f32 v12, v26, v140, 0x4b400000
	v_perm_b32 v9, v12, v9, s75
	v_fmaak_f32 v12, v21, v140, 0x4b400000
	v_fmaak_f32 v13, v23, v140, 0x4b400000
	v_perm_b32 v12, v13, v12, s75
	v_perm_b32 v9, v9, v12, s76
	v_fmaak_f32 v12, v28, v140, 0x4b400000
	v_fmaak_f32 v13, v30, v140, 0x4b400000
	v_perm_b32 v12, v13, v12, s75
	v_fmaak_f32 v13, v25, v140, 0x4b400000
	v_fmaak_f32 v14, v27, v140, 0x4b400000
	v_perm_b32 v13, v14, v13, s75
	v_perm_b32 v16, v12, v13, s76
	v_fmaak_f32 v12, v32, v140, 0x4b400000
	v_fmaak_f32 v13, v34, v140, 0x4b400000
	v_perm_b32 v12, v13, v12, s75
	v_fmaak_f32 v13, v29, v140, 0x4b400000
	v_fmaak_f32 v14, v31, v140, 0x4b400000
	v_perm_b32 v13, v14, v13, s75
	v_perm_b32 v17, v12, v13, s76
	v_fmaak_f32 v12, v37, v140, 0x4b400000
	v_fmaak_f32 v13, v40, v140, 0x4b400000
	v_perm_b32 v12, v13, v12, s75
	v_fmaak_f32 v13, v33, v140, 0x4b400000
	v_fmaak_f32 v14, v35, v140, 0x4b400000
	v_perm_b32 v13, v14, v13, s75
	v_perm_b32 v18, v12, v13, s76
	v_fmaak_f32 v12, v45, v140, 0x4b400000
	v_fmaak_f32 v13, v48, v140, 0x4b400000
	v_perm_b32 v12, v13, v12, s75
	v_fmaak_f32 v13, v39, v140, 0x4b400000
	v_fmaak_f32 v14, v41, v140, 0x4b400000
	v_perm_b32 v13, v14, v13, s75
	v_perm_b32 v19, v12, v13, s76
	v_cndmask_b32_e64 v12, v6, v16, s[2:3]
	s_nop 1
	v_mov_b32_dpp v20, v12 quad_perm:[1,0,3,2] row_mask:0xf bank_mask:0xf bound_ctrl:1
	v_cndmask_b32_e64 v12, v7, v17, s[2:3]
	s_nop 1
	v_mov_b32_dpp v21, v12 quad_perm:[1,0,3,2] row_mask:0xf bank_mask:0xf bound_ctrl:1
	v_cndmask_b32_e64 v12, v20, v6, s[2:3]
	v_cndmask_b32_e64 v6, v8, v18, s[2:3]
	v_cndmask_b32_e64 v13, v21, v7, s[2:3]
	s_nop 0
	v_mov_b32_dpp v22, v6 quad_perm:[1,0,3,2] row_mask:0xf bank_mask:0xf bound_ctrl:1
	v_cndmask_b32_e64 v6, v9, v19, s[2:3]
	v_cndmask_b32_e64 v14, v22, v8, s[2:3]
	s_nop 0
	v_mov_b32_dpp v8, v6 quad_perm:[1,0,3,2] row_mask:0xf bank_mask:0xf bound_ctrl:1
	v_cndmask_b32_e64 v15, v8, v9, s[2:3]
	v_mov_b32_dpp v9, v139 quad_perm:[1,0,3,2] row_mask:0xf bank_mask:0xf bound_ctrl:1
	v_cndmask_b32_e64 v6, v9, v139, s[2:3]
	v_ashrrev_i32_e32 v7, 31, v6
	v_lshlrev_b64 v[6:7], 10, v[6:7]
	v_lshl_add_u64 v[6:7], s[6:7], 0, v[6:7]
	v_lshl_add_u64 v[6:7], v[6:7], 0, s[80:81]
	v_lshl_add_u64 v[6:7], v[6:7], 0, v[2:3]
	global_store_dwordx4 v[6:7], v[12:15], off
	s_nop 1
	v_cndmask_b32_e64 v15, v19, v8, s[2:3]
	v_cndmask_b32_e64 v8, v139, v9, s[2:3]
	v_ashrrev_i32_e32 v9, 31, v8
	v_lshlrev_b64 v[8:9], 10, v[8:9]
	v_lshl_add_u64 v[8:9], s[6:7], 0, v[8:9]
	v_lshl_add_u64 v[8:9], v[8:9], 0, s[80:81]
	v_cndmask_b32_e64 v12, v16, v20, s[2:3]
	v_cndmask_b32_e64 v13, v17, v21, s[2:3]
	v_cndmask_b32_e64 v14, v18, v22, s[2:3]
	v_lshl_add_u64 v[8:9], v[8:9], 0, v[2:3]
	global_store_dwordx4 v[8:9], v[12:15], off
	v_fmaak_f32 v16, v51, v140, 0x4b400000
	v_fmaak_f32 v17, v55, v140, 0x4b400000
	v_fmaak_f32 v12, v42, v140, 0x4b400000
	v_fmaak_f32 v13, v44, v140, 0x4b400000
	v_perm_b32 v12, v13, v12, s75
	v_fmaak_f32 v13, v36, v140, 0x4b400000
	v_fmaak_f32 v14, v38, v140, 0x4b400000
	v_perm_b32 v13, v14, v13, s75
	v_perm_b32 v12, v12, v13, s76
	v_fmaak_f32 v13, v47, v140, 0x4b400000
	v_fmaak_f32 v14, v50, v140, 0x4b400000
	v_perm_b32 v13, v14, v13, s75
	v_fmaak_f32 v14, v43, v140, 0x4b400000
	v_fmaak_f32 v15, v46, v140, 0x4b400000
	v_perm_b32 v14, v15, v14, s75
	v_perm_b32 v13, v13, v14, s76
	v_fmaak_f32 v14, v52, v140, 0x4b400000
	v_fmaak_f32 v15, v54, v140, 0x4b400000
	v_perm_b32 v14, v15, v14, s75
	v_fmaak_f32 v15, v49, v140, 0x4b400000
	v_perm_b32 v15, v16, v15, s75
	v_perm_b32 v14, v14, v15, s76
	v_fmaak_f32 v15, v56, v140, 0x4b400000
	v_fmaak_f32 v16, v58, v140, 0x4b400000
	v_perm_b32 v15, v16, v15, s75
	v_fmaak_f32 v16, v53, v140, 0x4b400000
	v_perm_b32 v16, v17, v16, s75
	v_perm_b32 v15, v15, v16, s76
	v_fmaak_f32 v16, v60, v140, 0x4b400000
	v_fmaak_f32 v17, v62, v140, 0x4b400000
; template <bool PERMGL, bool FP8>
; __device__ __forceinline__ void q8_cols_item(const float* W, int N, int n0, unsigned char* Bq, float* sc_out, LAS float* AM, int par, int wave, int lane) {
;     ...
;     auto packc = [&](int c) { u32x4 o;
;         if (FP8) { o.x = f8x4(v[16 * c], v[16 * c + 1], v[16 * c + 2], v[16 * c + 3], inv); o.y = f8x4(v[16 * c + 4], v[16 * c + 5], v[16 * c + 6], v[16 * c + 7], inv);
;                    o.z = f8x4(v[16 * c + 8], v[16 * c + 9], v[16 * c + 10], v[16 * c + 11], inv); o.w = f8x4(v[16 * c + 12], v[16 * c + 13], v[16 * c + 14], v[16 * c + 15], inv); }
;         else { o.x = q8x4(v[16 * c], v[16 * c + 1], v[16 * c + 2], v[16 * c + 3], inv); o.y = q8x4(v[16 * c + 4], v[16 * c + 5], v[16 * c + 6], v[16 * c + 7], inv);
;                o.z = q8x4(v[16 * c + 8], v[16 * c + 9], v[16 * c + 10], v[16 * c + 11], inv); o.w = q8x4(v[16 * c + 12], v[16 * c + 13], v[16 * c + 14], v[16 * c + 15], inv); }
;         return o; };
; #pragma unroll
;     for (int j = 0; j < 4; ++j) { const u32x4 p0 = packc(2 * j), p1 = packc(2 * j + 1);
;         u32x4 snd, rcv;
; #pragma unroll
;         for (int q = 0; q < 4; ++q) { snd[q] = odd ? p0[q] : p1[q]; rcv[q] = xq(snd[q]); }
;         u32x4 a, b;
; #pragma unroll
;         for (int q = 0; q < 4; ++q) { a[q] = odd ? rcv[q] : p0[q]; b[q] = odd ? p1[q] : rcv[q]; }
;         *(u32x4*)(plo + 32 * j) = a; *(u32x4*)(phi + 32 * j) = b; }
	v_perm_b32 v16, v17, v16, s75
	v_fmaak_f32 v17, v57, v140, 0x4b400000
	v_fmaak_f32 v18, v59, v140, 0x4b400000
	v_perm_b32 v17, v18, v17, s75
	v_perm_b32 v16, v16, v17, s76
	v_fmaak_f32 v17, v64, v140, 0x4b400000
	v_fmaak_f32 v18, v66, v140, 0x4b400000
	v_perm_b32 v17, v18, v17, s75
	v_fmaak_f32 v18, v61, v140, 0x4b400000
	v_fmaak_f32 v19, v63, v140, 0x4b400000
	v_perm_b32 v18, v19, v18, s75
	v_perm_b32 v17, v17, v18, s76
	v_fmaak_f32 v18, v68, v140, 0x4b400000
	v_fmaak_f32 v19, v70, v140, 0x4b400000
	v_perm_b32 v18, v19, v18, s75
	v_fmaak_f32 v19, v65, v140, 0x4b400000
	v_fmaak_f32 v20, v67, v140, 0x4b400000
	v_perm_b32 v19, v20, v19, s75
	v_perm_b32 v18, v18, v19, s76
	v_fmaak_f32 v19, v75, v140, 0x4b400000
	v_fmaak_f32 v20, v78, v140, 0x4b400000
	v_perm_b32 v19, v20, v19, s75
	v_fmaak_f32 v20, v69, v140, 0x4b400000
	v_fmaak_f32 v21, v72, v140, 0x4b400000
	v_perm_b32 v20, v21, v20, s75
	v_perm_b32 v19, v19, v20, s76
	v_cndmask_b32_e64 v20, v12, v16, s[2:3]
	v_cndmask_b32_e64 v21, v13, v17, s[2:3]
	v_cndmask_b32_e64 v22, v14, v18, s[2:3]
	v_cndmask_b32_e64 v23, v15, v19, s[2:3]
	v_mov_b32_dpp v20, v20 quad_perm:[1,0,3,2] row_mask:0xf bank_mask:0xf bound_ctrl:1
	v_mov_b32_dpp v21, v21 quad_perm:[1,0,3,2] row_mask:0xf bank_mask:0xf bound_ctrl:1
	v_mov_b32_dpp v22, v22 quad_perm:[1,0,3,2] row_mask:0xf bank_mask:0xf bound_ctrl:1
	v_mov_b32_dpp v23, v23 quad_perm:[1,0,3,2] row_mask:0xf bank_mask:0xf bound_ctrl:1
	v_cndmask_b32_e64 v12, v20, v12, s[2:3]
	v_cndmask_b32_e64 v13, v21, v13, s[2:3]
	v_cndmask_b32_e64 v14, v22, v14, s[2:3]
	v_cndmask_b32_e64 v15, v23, v15, s[2:3]
	global_store_dwordx4 v[6:7], v[12:15], off offset:32
	v_readlane_b32 s6, v252, 37
	v_readlane_b32 s7, v252, 38
	v_cndmask_b32_e64 v12, v16, v20, s[2:3]
	v_cndmask_b32_e64 v13, v17, v21, s[2:3]
	v_cndmask_b32_e64 v14, v18, v22, s[2:3]
	v_cndmask_b32_e64 v15, v19, v23, s[2:3]
	global_store_dwordx4 v[8:9], v[12:15], off offset:32
	v_fmaak_f32 v16, v83, v140, 0x4b400000
	v_fmaak_f32 v17, v87, v140, 0x4b400000
	v_fmaak_f32 v12, v74, v140, 0x4b400000
	v_fmaak_f32 v13, v77, v140, 0x4b400000
	v_perm_b32 v12, v13, v12, s75
	v_fmaak_f32 v13, v71, v140, 0x4b400000
	v_fmaak_f32 v14, v73, v140, 0x4b400000
	v_perm_b32 v13, v14, v13, s75
	v_perm_b32 v12, v12, v13, s76
	v_fmaak_f32 v13, v80, v140, 0x4b400000
	v_fmaak_f32 v14, v82, v140, 0x4b400000
	v_perm_b32 v13, v14, v13, s75
	v_fmaak_f32 v14, v76, v140, 0x4b400000
	v_fmaak_f32 v15, v79, v140, 0x4b400000
	v_perm_b32 v14, v15, v14, s75
	v_perm_b32 v13, v13, v14, s76
	v_fmaak_f32 v14, v84, v140, 0x4b400000
	v_fmaak_f32 v15, v86, v140, 0x4b400000
	v_perm_b32 v14, v15, v14, s75
	v_fmaak_f32 v15, v81, v140, 0x4b400000
	v_perm_b32 v15, v16, v15, s75
	v_perm_b32 v14, v14, v15, s76
	v_fmaak_f32 v15, v88, v140, 0x4b400000
	v_fmaak_f32 v16, v89, v140, 0x4b400000
	v_perm_b32 v15, v16, v15, s75
	v_fmaak_f32 v16, v85, v140, 0x4b400000
	v_perm_b32 v16, v17, v16, s75
	v_perm_b32 v15, v15, v16, s76
	v_fmaak_f32 v16, v91, v140, 0x4b400000
	v_fmaak_f32 v17, v92, v140, 0x4b400000
	v_fmaak_f32 v18, v93, v140, 0x4b400000
	v_fmaak_f32 v19, v94, v140, 0x4b400000
	v_perm_b32 v18, v19, v18, s75
	v_perm_b32 v16, v17, v16, s75
	v_perm_b32 v16, v18, v16, s76
	v_fmaak_f32 v17, v95, v140, 0x4b400000
	v_fmaak_f32 v18, v96, v140, 0x4b400000
	v_fmaak_f32 v19, v97, v140, 0x4b400000
	v_fmaak_f32 v20, v98, v140, 0x4b400000
	v_perm_b32 v19, v20, v19, s75
	v_perm_b32 v17, v18, v17, s75
	v_perm_b32 v17, v19, v17, s76
	v_fmaak_f32 v18, v99, v140, 0x4b400000
	v_fmaak_f32 v19, v100, v140, 0x4b400000
	v_fmaak_f32 v20, v101, v140, 0x4b400000
	v_fmaak_f32 v21, v102, v140, 0x4b400000
	v_perm_b32 v20, v21, v20, s75
	v_perm_b32 v18, v19, v18, s75
	v_perm_b32 v18, v20, v18, s76
	v_fmaak_f32 v19, v103, v140, 0x4b400000
	v_fmaak_f32 v20, v104, v140, 0x4b400000
	v_fmaak_f32 v21, v106, v140, 0x4b400000
	v_fmaak_f32 v22, v109, v140, 0x4b400000
	v_perm_b32 v21, v22, v21, s75
	v_perm_b32 v19, v20, v19, s75
	v_perm_b32 v19, v21, v19, s76
	v_cndmask_b32_e64 v20, v12, v16, s[2:3]
	v_cndmask_b32_e64 v21, v13, v17, s[2:3]
	v_cndmask_b32_e64 v22, v14, v18, s[2:3]
	v_cndmask_b32_e64 v23, v15, v19, s[2:3]
; template <bool PERMGL, bool FP8>
; __device__ __forceinline__ void q8_cols_item(const float* W, int N, int n0, unsigned char* Bq, float* sc_out, LAS float* AM, int par, int wave, int lane) {
;     ...
;     for (int j = 0; j < 4; ++j) { const u32x4 p0 = packc(2 * j), p1 = packc(2 * j + 1);
;         u32x4 snd, rcv;
; #pragma unroll
;         for (int q = 0; q < 4; ++q) { snd[q] = odd ? p0[q] : p1[q]; rcv[q] = xq(snd[q]); }
;         u32x4 a, b;
; #pragma unroll
;         for (int q = 0; q < 4; ++q) { a[q] = odd ? rcv[q] : p0[q]; b[q] = odd ? p1[q] : rcv[q]; }
;         *(u32x4*)(plo + 32 * j) = a; *(u32x4*)(phi + 32 * j) = b; }
;     if (wave == 0) sc_out[PERMGL ? row : n] = FP8 ? sc * 16.0f : sc;
	v_mov_b32_dpp v20, v20 quad_perm:[1,0,3,2] row_mask:0xf bank_mask:0xf bound_ctrl:1
	v_mov_b32_dpp v21, v21 quad_perm:[1,0,3,2] row_mask:0xf bank_mask:0xf bound_ctrl:1
	v_mov_b32_dpp v22, v22 quad_perm:[1,0,3,2] row_mask:0xf bank_mask:0xf bound_ctrl:1
	v_mov_b32_dpp v23, v23 quad_perm:[1,0,3,2] row_mask:0xf bank_mask:0xf bound_ctrl:1
	v_cndmask_b32_e64 v12, v20, v12, s[2:3]
	v_cndmask_b32_e64 v13, v21, v13, s[2:3]
	v_cndmask_b32_e64 v14, v22, v14, s[2:3]
	v_cndmask_b32_e64 v15, v23, v15, s[2:3]
	v_cndmask_b32_e64 v16, v16, v20, s[2:3]
	v_cndmask_b32_e64 v17, v17, v21, s[2:3]
	v_cndmask_b32_e64 v18, v18, v22, s[2:3]
	v_cndmask_b32_e64 v19, v19, v23, s[2:3]
	global_store_dwordx4 v[6:7], v[12:15], off offset:64
	global_store_dwordx4 v[8:9], v[16:19], off offset:64
	v_fmaak_f32 v20, v130, v140, 0x4b400000
	v_fmaak_f32 v12, v105, v140, 0x4b400000
	v_fmaak_f32 v13, v107, v140, 0x4b400000
	v_fmaak_f32 v14, v108, v140, 0x4b400000
	v_fmaak_f32 v15, v110, v140, 0x4b400000
	v_perm_b32 v14, v15, v14, s75
	v_perm_b32 v12, v13, v12, s75
	v_perm_b32 v12, v14, v12, s76
	v_fmaak_f32 v13, v111, v140, 0x4b400000
	v_fmaak_f32 v14, v112, v140, 0x4b400000
	v_fmaak_f32 v15, v113, v140, 0x4b400000
	v_fmaak_f32 v16, v114, v140, 0x4b400000
	v_perm_b32 v15, v16, v15, s75
	v_perm_b32 v13, v14, v13, s75
	v_perm_b32 v13, v15, v13, s76
	v_fmaak_f32 v14, v115, v140, 0x4b400000
	v_fmaak_f32 v15, v116, v140, 0x4b400000
	v_fmaak_f32 v16, v117, v140, 0x4b400000
	v_fmaak_f32 v17, v118, v140, 0x4b400000
	v_perm_b32 v16, v17, v16, s75
	v_perm_b32 v14, v15, v14, s75
	v_perm_b32 v14, v16, v14, s76
	v_fmaak_f32 v15, v119, v140, 0x4b400000
	v_fmaak_f32 v16, v120, v140, 0x4b400000
	v_fmaak_f32 v17, v121, v140, 0x4b400000
	v_fmaak_f32 v18, v122, v140, 0x4b400000
	v_perm_b32 v17, v18, v17, s75
	v_perm_b32 v15, v16, v15, s75
	v_perm_b32 v15, v17, v15, s76
	v_fmaak_f32 v16, v123, v140, 0x4b400000
	v_fmaak_f32 v17, v124, v140, 0x4b400000
	v_fmaak_f32 v18, v125, v140, 0x4b400000
	v_fmaak_f32 v19, v126, v140, 0x4b400000
	v_perm_b32 v18, v19, v18, s75
	v_perm_b32 v16, v17, v16, s75
	v_perm_b32 v16, v18, v16, s76
	v_fmaak_f32 v17, v127, v140, 0x4b400000
	v_fmaak_f32 v18, v128, v140, 0x4b400000
	v_fmaak_f32 v19, v129, v140, 0x4b400000
	v_perm_b32 v19, v20, v19, s75
	v_perm_b32 v17, v18, v17, s75
	v_perm_b32 v17, v19, v17, s76
	v_fmaak_f32 v18, v131, v140, 0x4b400000
	v_fmaak_f32 v19, v132, v140, 0x4b400000
	v_fmaak_f32 v20, v133, v140, 0x4b400000
	v_fmaak_f32 v21, v134, v140, 0x4b400000
	v_perm_b32 v20, v21, v20, s75
	v_perm_b32 v18, v19, v18, s75
	v_perm_b32 v18, v20, v18, s76
	v_fmaak_f32 v19, v135, v140, 0x4b400000
	v_fmaak_f32 v20, v136, v140, 0x4b400000
	v_fmaak_f32 v21, v137, v140, 0x4b400000
	v_fmaak_f32 v22, v144, v140, 0x4b400000
	v_perm_b32 v21, v22, v21, s75
	v_perm_b32 v19, v20, v19, s75
	v_perm_b32 v19, v21, v19, s76
	v_cndmask_b32_e64 v20, v12, v16, s[2:3]
	v_cndmask_b32_e64 v21, v13, v17, s[2:3]
	v_cndmask_b32_e64 v22, v14, v18, s[2:3]
	v_cndmask_b32_e64 v23, v15, v19, s[2:3]
	v_mov_b32_dpp v20, v20 quad_perm:[1,0,3,2] row_mask:0xf bank_mask:0xf bound_ctrl:1
	v_mov_b32_dpp v21, v21 quad_perm:[1,0,3,2] row_mask:0xf bank_mask:0xf bound_ctrl:1
	v_mov_b32_dpp v22, v22 quad_perm:[1,0,3,2] row_mask:0xf bank_mask:0xf bound_ctrl:1
	v_mov_b32_dpp v23, v23 quad_perm:[1,0,3,2] row_mask:0xf bank_mask:0xf bound_ctrl:1
	v_cndmask_b32_e64 v12, v20, v12, s[2:3]
	v_cndmask_b32_e64 v16, v16, v20, s[2:3]
	v_cndmask_b32_e64 v13, v21, v13, s[2:3]
	v_cndmask_b32_e64 v17, v17, v21, s[2:3]
	v_cndmask_b32_e64 v14, v22, v14, s[2:3]
	v_cndmask_b32_e64 v18, v18, v22, s[2:3]
	v_cndmask_b32_e64 v15, v23, v15, s[2:3]
	v_cndmask_b32_e64 v19, v19, v23, s[2:3]
	s_andn2_b64 vcc, exec, s[6:7]
	global_store_dwordx4 v[6:7], v[12:15], off offset:96
	global_store_dwordx4 v[8:9], v[16:19], off offset:96
	s_cbranch_vccnz .LBB0_8
	s_lshl_b32 s4, s4, 11
	s_ashr_i32 s5, s4, 31
	s_lshl_b64 s[4:5], s[4:5], 2
	v_readlane_b32 s6, v252, 35
	s_add_u32 s4, s6, s4
	v_readlane_b32 s6, v252, 36
	s_addc_u32 s5, s6, s5
	v_lshl_add_u64 v[4:5], v[4:5], 2, s[4:5]
	global_store_dword v[4:5], v138, off
	s_branch .LBB0_8

; template <bool PERMGL, bool FP8>
; __device__ __forceinline__ void q8_cols_item(const float* W, int N, int n0, unsigned char* Bq, float* sc_out, LAS float* AM, int par, int wave, int lane) {
;     const int n = n0 + lane;
;     const float* Wp = W + (size_t)(128 * wave) * N + n;
;     float v[128]; float am = 0.f;
; #pragma unroll
;     for (int i = 0; i < 128; ++i) v[i] = Wp[(size_t)i * N];
; __global__ void __launch_bounds__(NWAVES * 64, 2) mk_fwd(Args args) {
;     ...
;                     else { const int r2 = r - 1024, mi = r2 >> 4, nb = ((r2 & 15) + 8 * ((r2 >> 6) & 1)) & 15;
;                         q8_cols_item<false, true>(args.in[13] + (size_t)mi * D * D, D, nb * 64, ws + WS_WDN + (size_t)mi * D * 1024, (float*)(ws + WS_SBD) + (size_t)mi * D, CAM, par, wave_s, lane_h); } }
.LBB0_94:
	s_lshr_b32 s17, s16, 6
	s_cmpk_gt_i32 s16, 0x3ff
	s_mov_b64 s[10:11], -1
	s_cbranch_scc0 .LBB0_98
	s_lshl_b32 s10, s17, 9
	s_add_i32 s14, s9, s10
	s_add_i32 s10, s16, 0xfffffc00
	s_lshr_b32 s68, s10, 4
	s_lshl_b64 s[10:11], s[68:69], 20
	s_and_b32 s18, s14, 0x3c0
	s_add_u32 s10, s83, s10
	s_addc_u32 s11, s74, s11
	s_lshl_b64 s[14:15], s[68:69], 22
	v_add_u32_e32 v16, s18, v11
	s_add_u32 s14, s48, s14
	s_addc_u32 s15, s51, s15
	v_lshlrev_b32_e32 v32, 2, v16
	v_lshl_add_u64 v[2:3], s[14:15], 0, v[32:33]
	s_movk_i32 s19, 0x2000
	v_add_co_u32_e32 v4, vcc, s19, v2
	s_movk_i32 s19, 0x4000
	s_nop 0
	v_addc_co_u32_e32 v5, vcc, 0, v3, vcc
	v_add_co_u32_e32 v6, vcc, s19, v2
	s_movk_i32 s19, 0x6000
	s_nop 0
	v_addc_co_u32_e32 v7, vcc, 0, v3, vcc
	v_add_co_u32_e32 v8, vcc, s19, v2
	s_mov_b32 s19, 0x8000
	s_nop 0
	v_addc_co_u32_e32 v9, vcc, 0, v3, vcc
	v_add_co_u32_e32 v18, vcc, s19, v2
	s_mov_b32 s19, 0xa000
	s_nop 0
	v_addc_co_u32_e32 v19, vcc, 0, v3, vcc
	v_add_co_u32_e32 v20, vcc, s19, v2
	s_mov_b32 s19, 0xc000
	s_nop 0
	v_addc_co_u32_e32 v21, vcc, 0, v3, vcc
	v_add_co_u32_e32 v26, vcc, s19, v2
	s_mov_b32 s19, 0xe000
	s_nop 0
	v_addc_co_u32_e32 v27, vcc, 0, v3, vcc
	v_add_co_u32_e32 v28, vcc, s19, v2
	s_mov_b32 s19, 0x10000
	s_nop 0
	v_addc_co_u32_e32 v29, vcc, 0, v3, vcc
	global_load_dword v24, v[18:19], off offset:-4096 nt
	global_load_dword v22, v[18:19], off nt
	global_load_dword v23, v[20:21], off offset:-4096 nt
	s_nop 0
	global_load_dword v19, v[20:21], off nt
	s_nop 0
	global_load_dword v20, v[26:27], off offset:-4096 nt
	global_load_dword v18, v[26:27], off nt
	global_load_dword v21, v[28:29], off offset:-4096 nt
	global_load_dword v17, v[28:29], off nt
	v_add_co_u32_e32 v26, vcc, s19, v2
	s_mov_b32 s19, 0x12000
	s_nop 0
	v_addc_co_u32_e32 v27, vcc, 0, v3, vcc
	v_add_co_u32_e32 v28, vcc, s19, v2
	s_mov_b32 s19, 0x14000
	s_nop 0
	v_addc_co_u32_e32 v29, vcc, 0, v3, vcc
	v_add_co_u32_e32 v36, vcc, s19, v2
	s_mov_b32 s19, 0x16000
	s_nop 0
	v_addc_co_u32_e32 v37, vcc, 0, v3, vcc
	v_add_co_u32_e32 v38, vcc, s19, v2
	s_mov_b32 s19, 0x18000
	s_nop 0
	v_addc_co_u32_e32 v39, vcc, 0, v3, vcc
	global_load_dword v34, v[26:27], off offset:-4096 nt
	global_load_dword v30, v[26:27], off nt
	global_load_dword v31, v[28:29], off offset:-4096 nt
	s_nop 0
	global_load_dword v27, v[28:29], off nt
	s_nop 0
	global_load_dword v28, v[36:37], off offset:-4096 nt
	global_load_dword v26, v[36:37], off nt
	global_load_dword v29, v[38:39], off offset:-4096 nt
	global_load_dword v25, v[38:39], off nt
	v_add_co_u32_e32 v36, vcc, s19, v2
	s_mov_b32 s19, 0x1a000
	s_nop 0
	v_addc_co_u32_e32 v37, vcc, 0, v3, vcc
	v_add_co_u32_e32 v38, vcc, s19, v2
	s_mov_b32 s19, 0x1c000
	s_nop 0
	v_addc_co_u32_e32 v39, vcc, 0, v3, vcc
	v_add_co_u32_e32 v40, vcc, s19, v2
	s_mov_b32 s19, 0x1e000
	s_nop 0
	v_addc_co_u32_e32 v41, vcc, 0, v3, vcc
	v_add_co_u32_e32 v50, vcc, s19, v2
	s_mov_b32 s19, 0x20000
	s_nop 0
	v_addc_co_u32_e32 v51, vcc, 0, v3, vcc
	global_load_dword v49, v[36:37], off offset:-4096 nt
	global_load_dword v47, v[36:37], off nt
	global_load_dword v48, v[38:39], off offset:-4096 nt
	global_load_dword v44, v[38:39], off nt
	global_load_dword v45, v[40:41], off offset:-4096 nt
	global_load_dword v43, v[40:41], off nt
	global_load_dword v46, v[50:51], off offset:-4096 nt
	global_load_dword v42, v[50:51], off nt
	v_add_co_u32_e32 v36, vcc, s19, v2
	s_mov_b32 s19, 0x22000
	s_nop 0
	v_addc_co_u32_e32 v37, vcc, 0, v3, vcc
	v_add_co_u32_e32 v38, vcc, s19, v2
	s_mov_b32 s19, 0x24000
	s_nop 0
	v_addc_co_u32_e32 v39, vcc, 0, v3, vcc
	v_add_co_u32_e32 v50, vcc, s19, v2
	s_mov_b32 s19, 0x26000
	s_nop 0
	v_addc_co_u32_e32 v51, vcc, 0, v3, vcc
	v_add_co_u32_e32 v52, vcc, s19, v2
	s_mov_b32 s19, 0x28000
	s_nop 0
	v_addc_co_u32_e32 v53, vcc, 0, v3, vcc
	global_load_dword v58, v[36:37], off offset:-4096 nt
	global_load_dword v40, v[36:37], off nt
	global_load_dword v41, v[38:39], off offset:-4096 nt
	s_nop 0
	global_load_dword v37, v[38:39], off nt
	s_nop 0
	global_load_dword v38, v[50:51], off offset:-4096 nt
	global_load_dword v36, v[50:51], off nt
	global_load_dword v39, v[52:53], off offset:-4096 nt
	global_load_dword v35, v[52:53], off nt
	v_add_co_u32_e32 v50, vcc, s19, v2
	s_mov_b32 s19, 0x2a000
	s_nop 0
	v_addc_co_u32_e32 v51, vcc, 0, v3, vcc
	v_add_co_u32_e32 v52, vcc, s19, v2
	s_mov_b32 s19, 0x2c000
	s_nop 0
	v_addc_co_u32_e32 v53, vcc, 0, v3, vcc
	v_add_co_u32_e32 v60, vcc, s19, v2
	s_mov_b32 s19, 0x2e000
	s_nop 0
	v_addc_co_u32_e32 v61, vcc, 0, v3, vcc
	v_add_co_u32_e32 v62, vcc, s19, v2
	s_mov_b32 s19, 0x30000
	s_nop 0
	v_addc_co_u32_e32 v63, vcc, 0, v3, vcc
	global_load_dword v57, v[50:51], off offset:-4096 nt
	global_load_dword v55, v[50:51], off nt
	global_load_dword v56, v[52:53], off offset:-4096 nt
	s_nop 0
	global_load_dword v52, v[52:53], off nt
	s_nop 0
	global_load_dword v53, v[60:61], off offset:-4096 nt
	global_load_dword v51, v[60:61], off nt
	global_load_dword v54, v[62:63], off offset:-4096 nt
	global_load_dword v50, v[62:63], off nt
	v_add_co_u32_e32 v60, vcc, s19, v2
	s_mov_b32 s19, 0x32000
	s_nop 0
	v_addc_co_u32_e32 v61, vcc, 0, v3, vcc
	v_add_co_u32_e32 v62, vcc, s19, v2
	s_mov_b32 s19, 0x34000
	s_nop 0
	v_addc_co_u32_e32 v63, vcc, 0, v3, vcc
	v_add_co_u32_e32 v68, vcc, s19, v2
	s_mov_b32 s19, 0x36000
	s_nop 0
	v_addc_co_u32_e32 v69, vcc, 0, v3, vcc
	v_add_co_u32_e32 v70, vcc, s19, v2
	s_mov_b32 s19, 0x38000
	s_nop 0
	v_addc_co_u32_e32 v71, vcc, 0, v3, vcc
	global_load_dword v66, v[60:61], off offset:-4096 nt
	global_load_dword v64, v[60:61], off nt
	global_load_dword v65, v[62:63], off offset:-4096 nt
	s_nop 0
	global_load_dword v61, v[62:63], off nt
; template <bool PERMGL, bool FP8>
; __device__ __forceinline__ void q8_cols_item(const float* W, int N, int n0, unsigned char* Bq, float* sc_out, LAS float* AM, int par, int wave, int lane) {
;     ...
;     for (int i = 0; i < 128; ++i) v[i] = Wp[(size_t)i * N];
	s_nop 0
	global_load_dword v62, v[68:69], off offset:-4096 nt
	global_load_dword v60, v[68:69], off nt
	global_load_dword v63, v[70:71], off offset:-4096 nt
	global_load_dword v59, v[70:71], off nt
	v_add_co_u32_e32 v68, vcc, s19, v2
	s_mov_b32 s19, 0x3a000
	s_nop 0
	v_addc_co_u32_e32 v69, vcc, 0, v3, vcc
	v_add_co_u32_e32 v70, vcc, s19, v2
	s_mov_b32 s19, 0x3c000
	s_nop 0
	v_addc_co_u32_e32 v71, vcc, 0, v3, vcc
	v_add_co_u32_e32 v72, vcc, s19, v2
	s_mov_b32 s19, 0x3e000
	s_nop 0
	v_addc_co_u32_e32 v73, vcc, 0, v3, vcc
	v_add_co_u32_e32 v82, vcc, s19, v2
	s_mov_b32 s19, 0x40000
	s_nop 0
	v_addc_co_u32_e32 v83, vcc, 0, v3, vcc
	global_load_dword v81, v[68:69], off offset:-4096 nt
	global_load_dword v79, v[68:69], off nt
	global_load_dword v80, v[70:71], off offset:-4096 nt
	global_load_dword v76, v[70:71], off nt
	global_load_dword v77, v[72:73], off offset:-4096 nt
	global_load_dword v75, v[72:73], off nt
	global_load_dword v78, v[82:83], off offset:-4096 nt
	global_load_dword v74, v[82:83], off nt
	v_add_co_u32_e32 v68, vcc, s19, v2
	s_mov_b32 s19, 0x42000
	s_nop 0
	v_addc_co_u32_e32 v69, vcc, 0, v3, vcc
	v_add_co_u32_e32 v70, vcc, s19, v2
	s_mov_b32 s19, 0x44000
	s_nop 0
	v_addc_co_u32_e32 v71, vcc, 0, v3, vcc
	v_add_co_u32_e32 v82, vcc, s19, v2
	s_mov_b32 s19, 0x46000
	s_nop 0
	v_addc_co_u32_e32 v83, vcc, 0, v3, vcc
	v_add_co_u32_e32 v84, vcc, s19, v2
	s_mov_b32 s19, 0x48000
	s_nop 0
	v_addc_co_u32_e32 v85, vcc, 0, v3, vcc
	global_load_dword v90, v[68:69], off offset:-4096 nt
	global_load_dword v72, v[68:69], off nt
	global_load_dword v73, v[70:71], off offset:-4096 nt
	s_nop 0
	global_load_dword v69, v[70:71], off nt
	s_nop 0
	global_load_dword v70, v[82:83], off offset:-4096 nt
	global_load_dword v68, v[82:83], off nt
	global_load_dword v71, v[84:85], off offset:-4096 nt
	global_load_dword v67, v[84:85], off nt
	v_add_co_u32_e32 v82, vcc, s19, v2
	s_mov_b32 s19, 0x4a000
	s_nop 0
	v_addc_co_u32_e32 v83, vcc, 0, v3, vcc
	v_add_co_u32_e32 v84, vcc, s19, v2
	s_mov_b32 s19, 0x4c000
	s_nop 0
	v_addc_co_u32_e32 v85, vcc, 0, v3, vcc
	v_add_co_u32_e32 v92, vcc, s19, v2
	s_mov_b32 s19, 0x4e000
	s_nop 0
	v_addc_co_u32_e32 v93, vcc, 0, v3, vcc
	v_add_co_u32_e32 v94, vcc, s19, v2
	s_mov_b32 s19, 0x50000
	s_nop 0
	v_addc_co_u32_e32 v95, vcc, 0, v3, vcc
	global_load_dword v89, v[82:83], off offset:-4096 nt
	global_load_dword v87, v[82:83], off nt
	global_load_dword v88, v[84:85], off offset:-4096 nt
	s_nop 0
	global_load_dword v84, v[84:85], off nt
	s_nop 0
	global_load_dword v85, v[92:93], off offset:-4096 nt
	global_load_dword v83, v[92:93], off nt
	global_load_dword v86, v[94:95], off offset:-4096 nt
	global_load_dword v82, v[94:95], off nt
	v_add_co_u32_e32 v92, vcc, s19, v2
	s_mov_b32 s19, 0x52000
	s_nop 0
	v_addc_co_u32_e32 v93, vcc, 0, v3, vcc
	v_add_co_u32_e32 v94, vcc, s19, v2
	s_mov_b32 s19, 0x54000
	s_nop 0
	v_addc_co_u32_e32 v95, vcc, 0, v3, vcc
	v_add_co_u32_e32 v100, vcc, s19, v2
	s_mov_b32 s19, 0x56000
	s_nop 0
	v_addc_co_u32_e32 v101, vcc, 0, v3, vcc
	v_add_co_u32_e32 v102, vcc, s19, v2
	s_mov_b32 s19, 0x58000
	s_nop 0
	v_addc_co_u32_e32 v103, vcc, 0, v3, vcc
	global_load_dword v98, v[92:93], off offset:-4096 nt
	global_load_dword v96, v[92:93], off nt
	global_load_dword v97, v[94:95], off offset:-4096 nt
	s_nop 0
	global_load_dword v93, v[94:95], off nt
	s_nop 0
	global_load_dword v94, v[100:101], off offset:-4096 nt
	global_load_dword v92, v[100:101], off nt
	global_load_dword v95, v[102:103], off offset:-4096 nt
	global_load_dword v91, v[102:103], off nt
	v_add_co_u32_e32 v100, vcc, s19, v2
	s_mov_b32 s19, 0x5a000
	s_nop 0
	v_addc_co_u32_e32 v101, vcc, 0, v3, vcc
	v_add_co_u32_e32 v102, vcc, s19, v2
	s_mov_b32 s19, 0x5c000
	s_nop 0
	v_addc_co_u32_e32 v103, vcc, 0, v3, vcc
	v_add_co_u32_e32 v104, vcc, s19, v2
	s_mov_b32 s19, 0x5e000
	s_nop 0
	v_addc_co_u32_e32 v105, vcc, 0, v3, vcc
	v_add_co_u32_e32 v114, vcc, s19, v2
	s_mov_b32 s19, 0x60000
	s_nop 0
	v_addc_co_u32_e32 v115, vcc, 0, v3, vcc
	global_load_dword v113, v[100:101], off offset:-4096 nt
	global_load_dword v111, v[100:101], off nt
	global_load_dword v112, v[102:103], off offset:-4096 nt
	global_load_dword v108, v[102:103], off nt
	global_load_dword v109, v[104:105], off offset:-4096 nt
	global_load_dword v107, v[104:105], off nt
	global_load_dword v110, v[114:115], off offset:-4096 nt
	global_load_dword v106, v[114:115], off nt
	v_add_co_u32_e32 v100, vcc, s19, v2
	s_mov_b32 s19, 0x62000
	s_nop 0
	v_addc_co_u32_e32 v101, vcc, 0, v3, vcc
	v_add_co_u32_e32 v102, vcc, s19, v2
	s_mov_b32 s19, 0x64000
	s_nop 0
	v_addc_co_u32_e32 v103, vcc, 0, v3, vcc
	v_add_co_u32_e32 v114, vcc, s19, v2
	s_mov_b32 s19, 0x66000
	s_nop 0
	v_addc_co_u32_e32 v115, vcc, 0, v3, vcc
	v_add_co_u32_e32 v116, vcc, s19, v2
	s_mov_b32 s19, 0x68000
	s_nop 0
	v_addc_co_u32_e32 v117, vcc, 0, v3, vcc
	global_load_dword v130, v[100:101], off offset:-4096 nt
	global_load_dword v104, v[100:101], off nt
	global_load_dword v105, v[102:103], off offset:-4096 nt
	s_nop 0
	global_load_dword v101, v[102:103], off nt
	s_nop 0
	global_load_dword v102, v[114:115], off offset:-4096 nt
	global_load_dword v100, v[114:115], off nt
	global_load_dword v103, v[116:117], off offset:-4096 nt
	global_load_dword v99, v[116:117], off nt
	v_add_co_u32_e32 v114, vcc, s19, v2
	s_mov_b32 s19, 0x6a000
	s_nop 0
	v_addc_co_u32_e32 v115, vcc, 0, v3, vcc
	v_add_co_u32_e32 v116, vcc, s19, v2
	s_mov_b32 s19, 0x6c000
	s_nop 0
	v_addc_co_u32_e32 v117, vcc, 0, v3, vcc
	v_add_co_u32_e32 v122, vcc, s19, v2
	s_mov_b32 s19, 0x6e000
	s_nop 0
	v_addc_co_u32_e32 v123, vcc, 0, v3, vcc
	v_add_co_u32_e32 v124, vcc, s19, v2
	s_mov_b32 s19, 0x70000
; template <bool PERMGL, bool FP8>
; __device__ __forceinline__ void q8_cols_item(const float* W, int N, int n0, unsigned char* Bq, float* sc_out, LAS float* AM, int par, int wave, int lane) {
;     ...
;     for (int i = 0; i < 128; ++i) v[i] = Wp[(size_t)i * N];
;     __builtin_amdgcn_sched_barrier(0);
; #pragma unroll
;     for (int i = 0; i < 128; ++i) am = fmaxf(am, fabsf(v[i]));
;     AM[(par * 8 + wave) * 64 + lane] = am;
;     __syncthreads();
	s_nop 0
	v_addc_co_u32_e32 v125, vcc, 0, v3, vcc
	global_load_dword v121, v[114:115], off offset:-4096 nt
	global_load_dword v119, v[114:115], off nt
	global_load_dword v120, v[116:117], off offset:-4096 nt
	s_nop 0
	global_load_dword v116, v[116:117], off nt
	s_nop 0
	global_load_dword v117, v[122:123], off offset:-4096 nt
	global_load_dword v115, v[122:123], off nt
	global_load_dword v118, v[124:125], off offset:-4096 nt
	global_load_dword v114, v[124:125], off nt
	v_add_co_u32_e32 v122, vcc, s19, v2
	s_mov_b32 s19, 0x72000
	s_nop 0
	v_addc_co_u32_e32 v123, vcc, 0, v3, vcc
	v_add_co_u32_e32 v124, vcc, s19, v2
	s_mov_b32 s19, 0x74000
	s_nop 0
	v_addc_co_u32_e32 v125, vcc, 0, v3, vcc
	v_add_co_u32_e32 v126, vcc, s19, v2
	s_mov_b32 s19, 0x76000
	s_nop 0
	v_addc_co_u32_e32 v127, vcc, 0, v3, vcc
	v_add_co_u32_e32 v128, vcc, s19, v2
	s_mov_b32 s19, 0x78000
	s_nop 0
	v_addc_co_u32_e32 v129, vcc, 0, v3, vcc
	global_load_dword v131, v[122:123], off offset:-4096 nt
	global_load_dword v132, v[122:123], off nt
	global_load_dword v133, v[124:125], off offset:-4096 nt
	global_load_dword v134, v[124:125], off nt
	global_load_dword v135, v[126:127], off offset:-4096 nt
	global_load_dword v136, v[126:127], off nt
	global_load_dword v137, v[128:129], off offset:-4096 nt
	global_load_dword v138, v[128:129], off nt
	v_add_co_u32_e32 v122, vcc, s19, v2
	s_mov_b32 s19, 0x7a000
	s_nop 0
	v_addc_co_u32_e32 v123, vcc, 0, v3, vcc
	v_add_co_u32_e32 v124, vcc, s19, v2
	s_mov_b32 s19, 0x7c000
	s_nop 0
	v_addc_co_u32_e32 v125, vcc, 0, v3, vcc
	v_add_co_u32_e32 v126, vcc, s19, v2
	s_mov_b32 s19, 0x7e000
	s_nop 0
	v_addc_co_u32_e32 v127, vcc, 0, v3, vcc
	v_add_co_u32_e32 v128, vcc, s19, v2
	s_mov_b32 s19, 0x7f000
	s_nop 0
	v_addc_co_u32_e32 v129, vcc, 0, v3, vcc
	v_add_co_u32_e32 v2, vcc, s19, v2
	global_load_dword v139, v[122:123], off offset:-4096 nt
	s_nop 0
	global_load_dword v122, v[122:123], off nt
	s_nop 0
	global_load_dword v123, v[124:125], off offset:-4096 nt
	s_nop 0
	global_load_dword v124, v[124:125], off nt
	s_nop 0
	global_load_dword v125, v[126:127], off offset:-4096 nt
	s_nop 0
	global_load_dword v126, v[126:127], off nt
	s_nop 0
	global_load_dword v127, v[128:129], off offset:-4096 nt
	s_nop 0
	global_load_dword v128, v[128:129], off nt
	v_addc_co_u32_e32 v3, vcc, 0, v3, vcc
	global_load_dword v129, v32, s[14:15] nt
	global_load_dword v140, v[4:5], off offset:-4096 nt
	global_load_dword v141, v[4:5], off nt
	global_load_dword v142, v[6:7], off offset:-4096 nt
	global_load_dword v143, v[6:7], off nt
	global_load_dword v144, v[8:9], off offset:-4096 nt
	global_load_dword v145, v[8:9], off nt
	global_load_dword v146, v[2:3], off nt
	s_waitcnt vmcnt(0)
	v_max3_f32 v2, |v129|, 0, |v140|
	v_max3_f32 v2, v2, |v141|, |v142|
	v_max3_f32 v2, v2, |v143|, |v144|
	v_max3_f32 v2, v2, |v145|, |v24|
	v_max3_f32 v2, v2, |v22|, |v23|
	v_max3_f32 v2, v2, |v19|, |v20|
	v_max3_f32 v2, v2, |v18|, |v21|
	v_max3_f32 v2, v2, |v17|, |v34|
	v_max3_f32 v2, v2, |v30|, |v31|
	v_max3_f32 v2, v2, |v27|, |v28|
	v_max3_f32 v2, v2, |v26|, |v29|
	v_max3_f32 v2, v2, |v25|, |v49|
	v_max3_f32 v2, v2, |v47|, |v48|
	v_max3_f32 v2, v2, |v44|, |v45|
	v_max3_f32 v2, v2, |v43|, |v46|
	v_max3_f32 v2, v2, |v42|, |v58|
	v_max3_f32 v2, v2, |v40|, |v41|
	v_max3_f32 v2, v2, |v37|, |v38|
	v_max3_f32 v2, v2, |v36|, |v39|
	v_max3_f32 v2, v2, |v35|, |v57|
	v_max3_f32 v2, v2, |v55|, |v56|
	v_max3_f32 v2, v2, |v52|, |v53|
	v_max3_f32 v2, v2, |v51|, |v54|
	v_max3_f32 v2, v2, |v50|, |v66|
	v_max3_f32 v2, v2, |v64|, |v65|
	v_max3_f32 v2, v2, |v61|, |v62|
	v_max3_f32 v2, v2, |v60|, |v63|
	v_max3_f32 v2, v2, |v59|, |v81|
	v_max3_f32 v2, v2, |v79|, |v80|
	v_max3_f32 v2, v2, |v76|, |v77|
	v_max3_f32 v2, v2, |v75|, |v78|
	v_max3_f32 v2, v2, |v74|, |v90|
	v_max3_f32 v2, v2, |v72|, |v73|
	v_max3_f32 v2, v2, |v69|, |v70|
	v_max3_f32 v2, v2, |v68|, |v71|
	v_max3_f32 v2, v2, |v67|, |v89|
	v_max3_f32 v2, v2, |v87|, |v88|
	v_max3_f32 v2, v2, |v84|, |v85|
	v_max3_f32 v2, v2, |v83|, |v86|
	v_max3_f32 v2, v2, |v82|, |v98|
	v_max3_f32 v2, v2, |v96|, |v97|
	v_max3_f32 v2, v2, |v93|, |v94|
	v_max3_f32 v2, v2, |v92|, |v95|
	v_max3_f32 v2, v2, |v91|, |v113|
	v_max3_f32 v2, v2, |v111|, |v112|
	v_max3_f32 v2, v2, |v108|, |v109|
	v_max3_f32 v2, v2, |v107|, |v110|
	v_max3_f32 v2, v2, |v106|, |v130|
	v_max3_f32 v2, v2, |v104|, |v105|
	v_max3_f32 v2, v2, |v101|, |v102|
	v_max3_f32 v2, v2, |v100|, |v103|
	v_max3_f32 v2, v2, |v99|, |v121|
	v_max3_f32 v2, v2, |v119|, |v120|
	v_max3_f32 v2, v2, |v116|, |v117|
	v_max3_f32 v2, v2, |v115|, |v118|
	v_max3_f32 v2, v2, |v114|, |v131|
	v_max3_f32 v2, v2, |v132|, |v133|
	v_max3_f32 v2, v2, |v134|, |v135|
	v_max3_f32 v2, v2, |v136|, |v137|
	v_max3_f32 v2, v2, |v138|, |v139|
	v_max3_f32 v2, v2, |v122|, |v123|
	v_max3_f32 v2, v2, |v124|, |v125|
	v_max3_f32 v2, v2, |v126|, |v127|
	s_lshl_b32 s14, s5, 11
	v_max3_f32 v147, v2, |v128|, |v146|
	v_add_u32_e32 v2, s14, v15
	v_add_u32_e32 v8, s14, v12
	ds_write_b32 v2, v147
	s_waitcnt lgkmcnt(0)
	s_barrier
; template <bool PERMGL, bool FP8>
; __device__ __forceinline__ void q8_cols_item(const float* W, int N, int n0, unsigned char* Bq, float* sc_out, LAS float* AM, int par, int wave, int lane) {
;     ...
;     for (int w = 0; w < 8; ++w) am = fmaxf(am, AM[(par * 8 + w) * 64 + lane]);
;     const float sc = am > 0.f ? am * (FP8 ? (1.0f / 256.0f) : (1.0f / 127.0f)) : 1.0f, inv = 1.0f / sc;
;     int row = n;
;     if (PERMGL) { const int j = n >> 1, pr = n & 1, o = j & 127; row = ((j >> 7) << 8) + (((o >> 2) & 1) << 7) + ((o >> 5) << 5) + (pr << 4) + (((o >> 3) & 3) << 2) + (o & 3); }
;     if (!PERMGL) { const int o = n & 255; row = ((n >> 8) << 8) + (((o >> 3) & 1) << 7) + ((o >> 6) << 5) + (((o >> 4) & 3) << 3) + (o & 7); }
;     auto xq = [](unsigned x) { return (unsigned)__builtin_amdgcn_update_dpp(0, (int)x, 0xB1, 0xf, 0xf, true); };
;     const bool odd = lane & 1;
;     const int rowp = (int)xq((unsigned)row);
;     unsigned char* plo = Bq + (size_t)(odd ? rowp : row) * 1024 + 128 * wave + (odd ? 16 : 0);
;     unsigned char* phi = Bq + (size_t)(odd ? row : rowp) * 1024 + 128 * wave + (odd ? 16 : 0);
;     auto packc = [&](int c) { u32x4 o;
;         if (FP8) { o.x = f8x4(v[16 * c], v[16 * c + 1], v[16 * c + 2], v[16 * c + 3], inv); o.y = f8x4(v[16 * c + 4], v[16 * c + 5], v[16 * c + 6], v[16 * c + 7], inv);
;                    o.z = f8x4(v[16 * c + 8], v[16 * c + 9], v[16 * c + 10], v[16 * c + 11], inv); o.w = f8x4(v[16 * c + 12], v[16 * c + 13], v[16 * c + 14], v[16 * c + 15], inv); }
;         else { o.x = q8x4(v[16 * c], v[16 * c + 1], v[16 * c + 2], v[16 * c + 3], inv); o.y = q8x4(v[16 * c + 4], v[16 * c + 5], v[16 * c + 6], v[16 * c + 7], inv);
;                o.z = q8x4(v[16 * c + 8], v[16 * c + 9], v[16 * c + 10], v[16 * c + 11], inv); o.w = q8x4(v[16 * c + 12], v[16 * c + 13], v[16 * c + 14], v[16 * c + 15], inv); }
;         return o; };
; #pragma unroll
;     for (int j = 0; j < 4; ++j) { const u32x4 p0 = packc(2 * j), p1 = packc(2 * j + 1);
;         u32x4 snd, rcv;
; #pragma unroll
;         for (int q = 0; q < 4; ++q) { snd[q] = odd ? p0[q] : p1[q]; rcv[q] = xq(snd[q]); }
;         u32x4 a, b;
; #pragma unroll
;         for (int q = 0; q < 4; ++q) { a[q] = odd ? rcv[q] : p0[q]; b[q] = odd ? p1[q] : rcv[q]; }
;         *(u32x4*)(plo + 32 * j) = a; *(u32x4*)(phi + 32 * j) = b; }
	ds_read2st64_b32 v[2:3], v8 offset1:1
	ds_read2st64_b32 v[4:5], v8 offset0:2 offset1:3
	ds_read2st64_b32 v[6:7], v8 offset0:4 offset1:5
	ds_read2st64_b32 v[8:9], v8 offset0:6 offset1:7
	s_waitcnt lgkmcnt(3)
	v_max3_f32 v2, v147, v2, v3
	s_waitcnt lgkmcnt(2)
	v_max3_f32 v2, v2, v4, v5
	s_waitcnt lgkmcnt(1)
	v_max3_f32 v2, v2, v6, v7
	s_waitcnt lgkmcnt(0)
	v_max3_f32 v2, v2, v8, v9
	v_mul_f32_e32 v3, 0x3b800000, v2
	v_cmp_lt_f32_e32 vcc, 0, v2
	s_nop 1
	v_cndmask_b32_e32 v6, 1.0, v3, vcc
	v_div_scale_f32 v2, s[14:15], v6, v6, 1.0
	v_rcp_f32_e32 v3, v2
	s_nop 0
	v_fma_f32 v4, -v2, v3, 1.0
	v_fmac_f32_e32 v3, v4, v3
	v_div_scale_f32 v4, vcc, 1.0, v6, 1.0
	v_mul_f32_e32 v5, v4, v3
	v_fma_f32 v7, -v2, v5, v4
	v_fmac_f32_e32 v5, v7, v3
	v_fma_f32 v2, -v2, v5, v4
	v_div_fmas_f32 v2, v2, v3, v5
	v_div_fixup_f32 v7, v2, v6, 1.0
	v_and_b32_e32 v3, 0x707, v16
	v_mul_f32_e32 v8, v129, v7
	v_mul_f32_e32 v9, v140, v7
	v_mov_b32_e32 v16, v33
	v_cvt_pk_fp8_f32 v16, v8, v9
	v_mul_f32_e32 v8, v141, v7
	v_mul_f32_e32 v129, v143, v7
	v_mul_f32_e32 v140, v144, v7
	v_mov_b32_e32 v141, v33
	v_cvt_pk_fp8_f32 v141, v129, v140
	v_mul_f32_e32 v9, v142, v7
	v_cvt_pk_fp8_f32 v16, v8, v9 op_sel:[0,0,1]
	v_mul_f32_e32 v8, v145, v7
	v_mul_f32_e32 v9, v24, v7
	v_cvt_pk_fp8_f32 v141, v8, v9 op_sel:[0,0,1]
	v_mul_f32_e32 v8, v22, v7
	v_mul_f32_e32 v9, v23, v7
	v_mov_b32_e32 v22, v33
	v_cvt_pk_fp8_f32 v22, v8, v9
	v_mul_f32_e32 v8, v19, v7
	v_mul_f32_e32 v18, v18, v7
	v_mul_f32_e32 v19, v21, v7
	v_mov_b32_e32 v23, v33
	v_cvt_pk_fp8_f32 v23, v18, v19
	v_mul_f32_e32 v9, v20, v7
	v_cvt_pk_fp8_f32 v22, v8, v9 op_sel:[0,0,1]
	v_mul_f32_e32 v8, v17, v7
	v_mul_f32_e32 v9, v34, v7
	v_cvt_pk_fp8_f32 v23, v8, v9 op_sel:[0,0,1]
	v_mul_f32_e32 v8, v30, v7
	v_mul_f32_e32 v9, v31, v7
	v_mov_b32_e32 v17, v33
	v_cvt_pk_fp8_f32 v17, v8, v9
	v_mul_f32_e32 v18, v26, v7
	v_mul_f32_e32 v19, v29, v7
	v_mov_b32_e32 v21, v33
	v_cvt_pk_fp8_f32 v21, v18, v19
	v_mul_f32_e32 v8, v27, v7
	v_mul_f32_e32 v9, v28, v7
	v_cvt_pk_fp8_f32 v17, v8, v9 op_sel:[0,0,1]
	v_mul_f32_e32 v8, v25, v7
	v_mul_f32_e32 v9, v49, v7
	v_cvt_pk_fp8_f32 v21, v8, v9 op_sel:[0,0,1]
	v_mul_f32_e32 v8, v47, v7
	v_mul_f32_e32 v9, v48, v7
	v_mov_b32_e32 v19, v33
	v_cvt_pk_fp8_f32 v19, v8, v9
	v_mul_f32_e32 v18, v43, v7
	v_mul_f32_e32 v20, v46, v7
	v_mov_b32_e32 v24, v33
	v_add_u16_e32 v2, s18, v11
	v_cvt_pk_fp8_f32 v24, v18, v20
	v_lshrrev_b16_e32 v2, 1, v2
	v_and_b32_e32 v2, 0x78, v2
	v_mul_f32_e32 v8, v44, v7
	v_mul_f32_e32 v9, v45, v7
	v_or3_b32 v4, v3, v13, v2
	v_cvt_pk_fp8_f32 v19, v8, v9 op_sel:[0,0,1]
	v_mul_f32_e32 v8, v42, v7
	v_mul_f32_e32 v9, v58, v7
	v_mov_b32_dpp v5, v4 quad_perm:[1,0,3,2] row_mask:0xf bank_mask:0xf bound_ctrl:1
	v_cvt_pk_fp8_f32 v24, v8, v9 op_sel:[0,0,1]
	v_cndmask_b32_e64 v2, v5, v4, s[2:3]
	v_ashrrev_i32_e32 v3, 31, v2
	v_cndmask_b32_e64 v4, v4, v5, s[2:3]
	v_lshlrev_b64 v[2:3], 10, v[2:3]
	v_ashrrev_i32_e32 v5, 31, v4
	v_cndmask_b32_e64 v18, v22, v19, s[2:3]
	v_lshl_add_u64 v[2:3], s[10:11], 0, v[2:3]
	v_lshlrev_b64 v[4:5], 10, v[4:5]
	v_cndmask_b32_e64 v8, v16, v17, s[2:3]
	v_cndmask_b32_e64 v9, v141, v21, s[2:3]
	v_mov_b32_dpp v25, v18 quad_perm:[1,0,3,2] row_mask:0xf bank_mask:0xf bound_ctrl:1
	v_cndmask_b32_e64 v18, v23, v24, s[2:3]
	v_lshl_add_u64 v[2:3], v[2:3], 0, s[42:43]
	v_lshl_add_u64 v[4:5], s[10:11], 0, v[4:5]
	v_mov_b32_dpp v8, v8 quad_perm:[1,0,3,2] row_mask:0xf bank_mask:0xf bound_ctrl:1
	v_mov_b32_dpp v9, v9 quad_perm:[1,0,3,2] row_mask:0xf bank_mask:0xf bound_ctrl:1
	v_mov_b32_dpp v26, v18 quad_perm:[1,0,3,2] row_mask:0xf bank_mask:0xf bound_ctrl:1
	v_lshl_add_u64 v[2:3], v[2:3], 0, v[0:1]
	v_lshl_add_u64 v[4:5], v[4:5], 0, s[42:43]
	v_cndmask_b32_e64 v16, v8, v16, s[2:3]
	v_cndmask_b32_e64 v20, v17, v8, s[2:3]
	v_cndmask_b32_e64 v17, v9, v141, s[2:3]
	v_cndmask_b32_e64 v18, v25, v22, s[2:3]
	v_cndmask_b32_e64 v22, v19, v25, s[2:3]
	v_cndmask_b32_e64 v19, v26, v23, s[2:3]
	v_lshl_add_u64 v[4:5], v[4:5], 0, v[0:1]
	v_cndmask_b32_e64 v21, v21, v9, s[2:3]
	v_cndmask_b32_e64 v23, v24, v26, s[2:3]
	global_store_dwordx4 v[2:3], v[16:19], off
	global_store_dwordx4 v[4:5], v[20:23], off
	v_mul_f32_e32 v8, v40, v7
	v_mul_f32_e32 v9, v41, v7
	v_mov_b32_e32 v16, v33
	v_cvt_pk_fp8_f32 v16, v8, v9
	v_mul_f32_e32 v17, v36, v7
	v_mul_f32_e32 v18, v39, v7
	v_mov_b32_e32 v19, v33
	v_cvt_pk_fp8_f32 v19, v17, v18
	v_mul_f32_e32 v8, v37, v7
	v_mul_f32_e32 v9, v38, v7
	v_cvt_pk_fp8_f32 v16, v8, v9 op_sel:[0,0,1]
	v_mul_f32_e32 v8, v35, v7
	v_mul_f32_e32 v9, v57, v7
	v_cvt_pk_fp8_f32 v19, v8, v9 op_sel:[0,0,1]
	v_mul_f32_e32 v8, v55, v7
	v_mul_f32_e32 v9, v56, v7
	v_mov_b32_e32 v18, v33
	v_cvt_pk_fp8_f32 v18, v8, v9
	v_mul_f32_e32 v17, v51, v7
	v_mul_f32_e32 v20, v54, v7
	v_mov_b32_e32 v23, v33
	v_cvt_pk_fp8_f32 v23, v17, v20
	v_mul_f32_e32 v8, v52, v7
	v_mul_f32_e32 v9, v53, v7
	v_cvt_pk_fp8_f32 v18, v8, v9 op_sel:[0,0,1]
	v_mul_f32_e32 v8, v50, v7
	v_mul_f32_e32 v9, v66, v7
	v_cvt_pk_fp8_f32 v23, v8, v9 op_sel:[0,0,1]
	v_mul_f32_e32 v8, v64, v7
	v_mul_f32_e32 v9, v65, v7
	v_mov_b32_e32 v17, v33
	v_cvt_pk_fp8_f32 v17, v8, v9
	v_mul_f32_e32 v20, v60, v7
	v_mul_f32_e32 v21, v63, v7
	v_mov_b32_e32 v22, v33
	v_cvt_pk_fp8_f32 v22, v20, v21
	v_mul_f32_e32 v8, v61, v7
	v_mul_f32_e32 v9, v62, v7
	v_cvt_pk_fp8_f32 v17, v8, v9 op_sel:[0,0,1]
	v_mul_f32_e32 v8, v59, v7
	v_mul_f32_e32 v9, v81, v7
	v_cvt_pk_fp8_f32 v22, v8, v9 op_sel:[0,0,1]
	v_mul_f32_e32 v8, v79, v7
	v_mul_f32_e32 v9, v80, v7
	v_mov_b32_e32 v24, v33
	v_cvt_pk_fp8_f32 v24, v8, v9
	v_mul_f32_e32 v20, v75, v7
	v_mul_f32_e32 v21, v78, v7
	v_mov_b32_e32 v25, v33
	v_cvt_pk_fp8_f32 v25, v20, v21
	v_mul_f32_e32 v8, v76, v7
	v_mul_f32_e32 v9, v77, v7
; template <bool PERMGL, bool FP8>
; __device__ __forceinline__ void q8_cols_item(const float* W, int N, int n0, unsigned char* Bq, float* sc_out, LAS float* AM, int par, int wave, int lane) {
;     ...
;     auto packc = [&](int c) { u32x4 o;
;         if (FP8) { o.x = f8x4(v[16 * c], v[16 * c + 1], v[16 * c + 2], v[16 * c + 3], inv); o.y = f8x4(v[16 * c + 4], v[16 * c + 5], v[16 * c + 6], v[16 * c + 7], inv);
;                    o.z = f8x4(v[16 * c + 8], v[16 * c + 9], v[16 * c + 10], v[16 * c + 11], inv); o.w = f8x4(v[16 * c + 12], v[16 * c + 13], v[16 * c + 14], v[16 * c + 15], inv); }
;         else { o.x = q8x4(v[16 * c], v[16 * c + 1], v[16 * c + 2], v[16 * c + 3], inv); o.y = q8x4(v[16 * c + 4], v[16 * c + 5], v[16 * c + 6], v[16 * c + 7], inv);
;                o.z = q8x4(v[16 * c + 8], v[16 * c + 9], v[16 * c + 10], v[16 * c + 11], inv); o.w = q8x4(v[16 * c + 12], v[16 * c + 13], v[16 * c + 14], v[16 * c + 15], inv); }
;         return o; };
; #pragma unroll
;     for (int j = 0; j < 4; ++j) { const u32x4 p0 = packc(2 * j), p1 = packc(2 * j + 1);
;         u32x4 snd, rcv;
; #pragma unroll
;         for (int q = 0; q < 4; ++q) { snd[q] = odd ? p0[q] : p1[q]; rcv[q] = xq(snd[q]); }
;         u32x4 a, b;
; #pragma unroll
;         for (int q = 0; q < 4; ++q) { a[q] = odd ? rcv[q] : p0[q]; b[q] = odd ? p1[q] : rcv[q]; }
;         *(u32x4*)(plo + 32 * j) = a; *(u32x4*)(phi + 32 * j) = b; }
;     if (wave == 0) sc_out[PERMGL ? row : n] = FP8 ? sc * 16.0f : sc;
	v_cvt_pk_fp8_f32 v24, v8, v9 op_sel:[0,0,1]
	v_mul_f32_e32 v8, v74, v7
	v_mul_f32_e32 v9, v90, v7
	v_cvt_pk_fp8_f32 v25, v8, v9 op_sel:[0,0,1]
	v_cndmask_b32_e64 v20, v18, v24, s[2:3]
	v_cndmask_b32_e64 v8, v16, v17, s[2:3]
	v_cndmask_b32_e64 v9, v19, v22, s[2:3]
	v_mov_b32_dpp v26, v20 quad_perm:[1,0,3,2] row_mask:0xf bank_mask:0xf bound_ctrl:1
	v_cndmask_b32_e64 v20, v23, v25, s[2:3]
	v_mov_b32_dpp v8, v8 quad_perm:[1,0,3,2] row_mask:0xf bank_mask:0xf bound_ctrl:1
	v_mov_b32_dpp v9, v9 quad_perm:[1,0,3,2] row_mask:0xf bank_mask:0xf bound_ctrl:1
	v_mov_b32_dpp v27, v20 quad_perm:[1,0,3,2] row_mask:0xf bank_mask:0xf bound_ctrl:1
	v_cndmask_b32_e64 v16, v8, v16, s[2:3]
	v_cndmask_b32_e64 v20, v17, v8, s[2:3]
	v_cndmask_b32_e64 v17, v9, v19, s[2:3]
	v_cndmask_b32_e64 v18, v26, v18, s[2:3]
	v_cndmask_b32_e64 v19, v27, v23, s[2:3]
	v_cndmask_b32_e64 v21, v22, v9, s[2:3]
	v_cndmask_b32_e64 v22, v24, v26, s[2:3]
	v_cndmask_b32_e64 v23, v25, v27, s[2:3]
	global_store_dwordx4 v[2:3], v[16:19], off offset:32
	global_store_dwordx4 v[4:5], v[20:23], off offset:32
	v_mul_f32_e32 v8, v72, v7
	v_mul_f32_e32 v9, v73, v7
	v_mov_b32_e32 v16, v33
	v_cvt_pk_fp8_f32 v16, v8, v9
	v_mul_f32_e32 v17, v68, v7
	v_mul_f32_e32 v18, v71, v7
	v_mov_b32_e32 v19, v33
	v_cvt_pk_fp8_f32 v19, v17, v18
	v_mul_f32_e32 v8, v69, v7
	v_mul_f32_e32 v9, v70, v7
	v_cvt_pk_fp8_f32 v16, v8, v9 op_sel:[0,0,1]
	v_mul_f32_e32 v8, v67, v7
	v_mul_f32_e32 v9, v89, v7
	v_cvt_pk_fp8_f32 v19, v8, v9 op_sel:[0,0,1]
	v_mul_f32_e32 v8, v87, v7
	v_mul_f32_e32 v9, v88, v7
	v_mov_b32_e32 v18, v33
	v_cvt_pk_fp8_f32 v18, v8, v9
	v_mul_f32_e32 v17, v83, v7
	v_mul_f32_e32 v20, v86, v7
	v_mov_b32_e32 v23, v33
	v_cvt_pk_fp8_f32 v23, v17, v20
	v_mul_f32_e32 v8, v84, v7
	v_mul_f32_e32 v9, v85, v7
	v_cvt_pk_fp8_f32 v18, v8, v9 op_sel:[0,0,1]
	v_mul_f32_e32 v8, v82, v7
	v_mul_f32_e32 v9, v98, v7
	v_cvt_pk_fp8_f32 v23, v8, v9 op_sel:[0,0,1]
	v_mul_f32_e32 v8, v96, v7
	v_mul_f32_e32 v9, v97, v7
	v_mov_b32_e32 v17, v33
	v_cvt_pk_fp8_f32 v17, v8, v9
	v_mul_f32_e32 v20, v92, v7
	v_mul_f32_e32 v21, v95, v7
	v_mov_b32_e32 v22, v33
	v_cvt_pk_fp8_f32 v22, v20, v21
	v_mul_f32_e32 v8, v93, v7
	v_mul_f32_e32 v9, v94, v7
	v_cvt_pk_fp8_f32 v17, v8, v9 op_sel:[0,0,1]
	v_mul_f32_e32 v8, v91, v7
	v_mul_f32_e32 v9, v113, v7
	v_cvt_pk_fp8_f32 v22, v8, v9 op_sel:[0,0,1]
	v_mul_f32_e32 v8, v111, v7
	v_mul_f32_e32 v9, v112, v7
	v_mov_b32_e32 v24, v33
	v_cvt_pk_fp8_f32 v24, v8, v9
	v_mul_f32_e32 v20, v107, v7
	v_mul_f32_e32 v21, v110, v7
	v_mov_b32_e32 v25, v33
	v_cvt_pk_fp8_f32 v25, v20, v21
	v_mul_f32_e32 v8, v108, v7
	v_mul_f32_e32 v9, v109, v7
	v_cvt_pk_fp8_f32 v24, v8, v9 op_sel:[0,0,1]
	v_mul_f32_e32 v8, v106, v7
	v_mul_f32_e32 v9, v130, v7
	v_cvt_pk_fp8_f32 v25, v8, v9 op_sel:[0,0,1]
	v_cndmask_b32_e64 v20, v18, v24, s[2:3]
	v_cndmask_b32_e64 v8, v16, v17, s[2:3]
	v_cndmask_b32_e64 v9, v19, v22, s[2:3]
	v_mov_b32_dpp v26, v20 quad_perm:[1,0,3,2] row_mask:0xf bank_mask:0xf bound_ctrl:1
	v_cndmask_b32_e64 v20, v23, v25, s[2:3]
	v_mov_b32_dpp v8, v8 quad_perm:[1,0,3,2] row_mask:0xf bank_mask:0xf bound_ctrl:1
	v_mov_b32_dpp v9, v9 quad_perm:[1,0,3,2] row_mask:0xf bank_mask:0xf bound_ctrl:1
	v_mov_b32_dpp v27, v20 quad_perm:[1,0,3,2] row_mask:0xf bank_mask:0xf bound_ctrl:1
	v_cndmask_b32_e64 v16, v8, v16, s[2:3]
	v_cndmask_b32_e64 v20, v17, v8, s[2:3]
	v_cndmask_b32_e64 v17, v9, v19, s[2:3]
	v_cndmask_b32_e64 v18, v26, v18, s[2:3]
	v_cndmask_b32_e64 v19, v27, v23, s[2:3]
	v_cndmask_b32_e64 v21, v22, v9, s[2:3]
	v_cndmask_b32_e64 v22, v24, v26, s[2:3]
	v_cndmask_b32_e64 v23, v25, v27, s[2:3]
	global_store_dwordx4 v[2:3], v[16:19], off offset:64
	global_store_dwordx4 v[4:5], v[20:23], off offset:64
	v_mul_f32_e32 v8, v104, v7
	v_mul_f32_e32 v9, v105, v7
	v_mov_b32_e32 v16, v33
	v_cvt_pk_fp8_f32 v16, v8, v9
	v_mul_f32_e32 v17, v100, v7
	v_mul_f32_e32 v18, v103, v7
	v_mov_b32_e32 v19, v33
	v_cvt_pk_fp8_f32 v19, v17, v18
	v_mul_f32_e32 v8, v101, v7
	v_mul_f32_e32 v9, v102, v7
	v_cvt_pk_fp8_f32 v16, v8, v9 op_sel:[0,0,1]
	v_mul_f32_e32 v8, v99, v7
	v_mul_f32_e32 v9, v121, v7
	v_cvt_pk_fp8_f32 v19, v8, v9 op_sel:[0,0,1]
	v_mul_f32_e32 v8, v119, v7
	v_mul_f32_e32 v9, v120, v7
	v_mov_b32_e32 v18, v33
	v_cvt_pk_fp8_f32 v18, v8, v9
	v_mul_f32_e32 v17, v115, v7
	v_mul_f32_e32 v20, v118, v7
	v_mov_b32_e32 v23, v33
	v_cvt_pk_fp8_f32 v23, v17, v20
	v_mul_f32_e32 v8, v116, v7
	v_mul_f32_e32 v9, v117, v7
	v_cvt_pk_fp8_f32 v18, v8, v9 op_sel:[0,0,1]
	v_mul_f32_e32 v8, v114, v7
	v_mul_f32_e32 v9, v131, v7
	v_cvt_pk_fp8_f32 v23, v8, v9 op_sel:[0,0,1]
	v_mul_f32_e32 v8, v132, v7
	v_mul_f32_e32 v9, v133, v7
	v_mov_b32_e32 v17, v33
	v_cvt_pk_fp8_f32 v17, v8, v9
	v_mul_f32_e32 v20, v136, v7
	v_mul_f32_e32 v21, v137, v7
	v_mov_b32_e32 v22, v33
	v_cvt_pk_fp8_f32 v22, v20, v21
	v_mul_f32_e32 v8, v134, v7
	v_mul_f32_e32 v9, v135, v7
	v_cvt_pk_fp8_f32 v17, v8, v9 op_sel:[0,0,1]
	v_mul_f32_e32 v8, v138, v7
	v_mul_f32_e32 v9, v139, v7
	v_cvt_pk_fp8_f32 v22, v8, v9 op_sel:[0,0,1]
	v_mul_f32_e32 v8, v122, v7
	v_mul_f32_e32 v9, v123, v7
	v_mov_b32_e32 v24, v33
	v_cvt_pk_fp8_f32 v24, v8, v9
	v_mul_f32_e32 v20, v126, v7
	v_mul_f32_e32 v21, v127, v7
	v_mov_b32_e32 v25, v33
	v_cvt_pk_fp8_f32 v25, v20, v21
	v_mul_f32_e32 v8, v124, v7
	v_mul_f32_e32 v9, v125, v7
	v_cvt_pk_fp8_f32 v24, v8, v9 op_sel:[0,0,1]
	v_mul_f32_e32 v8, v128, v7
	v_mul_f32_e32 v7, v146, v7
	v_cvt_pk_fp8_f32 v25, v8, v7 op_sel:[0,0,1]
	v_cndmask_b32_e64 v7, v16, v17, s[2:3]
	v_cndmask_b32_e64 v8, v19, v22, s[2:3]
	v_cndmask_b32_e64 v9, v18, v24, s[2:3]
	v_cndmask_b32_e64 v20, v23, v25, s[2:3]
	v_mov_b32_dpp v7, v7 quad_perm:[1,0,3,2] row_mask:0xf bank_mask:0xf bound_ctrl:1
	v_mov_b32_dpp v8, v8 quad_perm:[1,0,3,2] row_mask:0xf bank_mask:0xf bound_ctrl:1
	v_mov_b32_dpp v9, v9 quad_perm:[1,0,3,2] row_mask:0xf bank_mask:0xf bound_ctrl:1
	v_mov_b32_dpp v26, v20 quad_perm:[1,0,3,2] row_mask:0xf bank_mask:0xf bound_ctrl:1
	v_cndmask_b32_e64 v16, v7, v16, s[2:3]
	v_cndmask_b32_e64 v20, v17, v7, s[2:3]
	v_cndmask_b32_e64 v17, v8, v19, s[2:3]
	v_cndmask_b32_e64 v21, v22, v8, s[2:3]
	v_cndmask_b32_e64 v18, v9, v18, s[2:3]
	v_cndmask_b32_e64 v22, v24, v9, s[2:3]
	v_cndmask_b32_e64 v19, v26, v23, s[2:3]
	v_cndmask_b32_e64 v23, v25, v26, s[2:3]
	s_and_b64 vcc, exec, s[0:1]
	global_store_dwordx4 v[2:3], v[16:19], off offset:96
	global_store_dwordx4 v[4:5], v[20:23], off offset:96
	s_cbranch_vccnz .LBB0_97
	s_lshl_b64 s[10:11], s[68:69], 12
	v_readlane_b32 s14, v252, 60
	s_add_u32 s10, s14, s10
	v_readlane_b32 s14, v252, 61
	s_addc_u32 s11, s14, s11
	v_mul_f32_e32 v2, 0x41800000, v6
	global_store_dword v32, v2, s[10:11]

; template <bool PERMGL, bool FP8>
; __device__ __forceinline__ void q8_cols_item(const float* W, int N, int n0, unsigned char* Bq, float* sc_out, LAS float* AM, int par, int wave, int lane) {
;     const int n = n0 + lane;
;     const float* Wp = W + (size_t)(128 * wave) * N + n;
;     float v[128]; float am = 0.f;
; #pragma unroll
;     for (int i = 0; i < 128; ++i) v[i] = Wp[(size_t)i * N];
; __global__ void __launch_bounds__(NWAVES * 64, 2) mk_fwd(Args args) {
;     ...
;                     if (r < 1024) { const int mi = r >> 5, nb = ((r & 31) + 8 * ((r >> 6) & 3)) & 31;
;                         q8_cols_item<true, false>(args.in[11] + (size_t)mi * D * 2048, 2048, nb * 64, ws + WS_WGU + (size_t)mi * 2048 * 1024, (float*)(ws + WS_SB) + (size_t)mi * 2048, CAM, par, wave_s, lane_h); }
.LBB0_98:
	s_andn2_b64 vcc, exec, s[10:11]
	s_cbranch_vccnz .LBB0_93
	s_lshl_b32 s10, s17, 9
	s_add_i32 s14, s9, s10
	s_ashr_i32 s10, s16, 5
	s_ashr_i32 s11, s10, 31
	s_lshl_b64 s[18:19], s[10:11], 23
	s_and_b32 s17, s14, 0x7c0
	s_lshl_b64 s[14:15], s[10:11], 21
	s_add_u32 s14, s57, s14
	s_addc_u32 s15, s65, s15
	v_readlane_b32 s22, v252, 62
	v_add_u32_e32 v4, s17, v11
	s_add_u32 s18, s22, s18
	v_readlane_b32 s22, v253, 0
	s_addc_u32 s19, s22, s19
	v_lshlrev_b32_e32 v32, 2, v4
	v_lshl_add_u64 v[2:3], s[18:19], 0, v[32:33]
	global_load_dword v6, v32, s[18:19] nt
	s_movk_i32 s18, 0x2000
	v_add_co_u32_e32 v8, vcc, s18, v2
	s_movk_i32 s18, 0x4000
	s_nop 0
	v_addc_co_u32_e32 v9, vcc, 0, v3, vcc
	global_load_dword v7, v[8:9], off nt
	v_add_co_u32_e32 v8, vcc, s18, v2
	s_movk_i32 s18, 0x6000
	s_nop 0
	v_addc_co_u32_e32 v9, vcc, 0, v3, vcc
	v_add_co_u32_e32 v16, vcc, s18, v2
	s_mov_b32 s18, 0x8000
	s_nop 0
	v_addc_co_u32_e32 v17, vcc, 0, v3, vcc
	global_load_dword v8, v[8:9], off nt
	s_nop 0
	global_load_dword v9, v[16:17], off nt
	v_add_co_u32_e32 v16, vcc, s18, v2
	s_mov_b32 s18, 0xa000
	s_nop 0
	v_addc_co_u32_e32 v17, vcc, 0, v3, vcc
	v_add_co_u32_e32 v18, vcc, s18, v2
	s_mov_b32 s18, 0xc000
	s_nop 0
	v_addc_co_u32_e32 v19, vcc, 0, v3, vcc
	global_load_dword v16, v[16:17], off nt
	s_nop 0
	global_load_dword v17, v[18:19], off nt
	v_add_co_u32_e32 v18, vcc, s18, v2
	s_mov_b32 s18, 0xe000
	s_nop 0
	v_addc_co_u32_e32 v19, vcc, 0, v3, vcc
	v_add_co_u32_e32 v20, vcc, s18, v2
	s_mov_b32 s18, 0x10000
	s_nop 0
	v_addc_co_u32_e32 v21, vcc, 0, v3, vcc
	global_load_dword v18, v[18:19], off nt
	s_nop 0
	global_load_dword v19, v[20:21], off nt
	v_add_co_u32_e32 v20, vcc, s18, v2
	s_mov_b32 s18, 0x12000
	s_nop 0
	v_addc_co_u32_e32 v21, vcc, 0, v3, vcc
	v_add_co_u32_e32 v22, vcc, s18, v2
	s_mov_b32 s18, 0x14000
	s_nop 0
	v_addc_co_u32_e32 v23, vcc, 0, v3, vcc
	global_load_dword v20, v[20:21], off nt
	s_nop 0
	global_load_dword v21, v[22:23], off nt
	v_add_co_u32_e32 v22, vcc, s18, v2
	s_mov_b32 s18, 0x16000
	s_nop 0
	v_addc_co_u32_e32 v23, vcc, 0, v3, vcc
	v_add_co_u32_e32 v24, vcc, s18, v2
	s_mov_b32 s18, 0x18000
	s_nop 0
	v_addc_co_u32_e32 v25, vcc, 0, v3, vcc
	global_load_dword v22, v[22:23], off nt
	s_nop 0
	global_load_dword v23, v[24:25], off nt
	v_add_co_u32_e32 v24, vcc, s18, v2
	s_mov_b32 s18, 0x1a000
	s_nop 0
	v_addc_co_u32_e32 v25, vcc, 0, v3, vcc
	v_add_co_u32_e32 v26, vcc, s18, v2
	s_mov_b32 s18, 0x1c000
	s_nop 0
	v_addc_co_u32_e32 v27, vcc, 0, v3, vcc
	global_load_dword v24, v[24:25], off nt
	s_nop 0
	global_load_dword v25, v[26:27], off nt
	v_add_co_u32_e32 v26, vcc, s18, v2
	s_mov_b32 s18, 0x1e000
	s_nop 0
	v_addc_co_u32_e32 v27, vcc, 0, v3, vcc
	v_add_co_u32_e32 v28, vcc, s18, v2
	s_mov_b32 s18, 0x20000
	s_nop 0
	v_addc_co_u32_e32 v29, vcc, 0, v3, vcc
	global_load_dword v26, v[26:27], off nt
	s_nop 0
	global_load_dword v27, v[28:29], off nt
	v_add_co_u32_e32 v28, vcc, s18, v2
	s_mov_b32 s18, 0x22000
	s_nop 0
	v_addc_co_u32_e32 v29, vcc, 0, v3, vcc
	v_add_co_u32_e32 v30, vcc, s18, v2
	s_mov_b32 s18, 0x24000
	s_nop 0
	v_addc_co_u32_e32 v31, vcc, 0, v3, vcc
	global_load_dword v28, v[28:29], off nt
	s_nop 0
	global_load_dword v29, v[30:31], off nt
	v_add_co_u32_e32 v30, vcc, s18, v2
	s_mov_b32 s18, 0x26000
	s_nop 0
	v_addc_co_u32_e32 v31, vcc, 0, v3, vcc
	v_add_co_u32_e32 v34, vcc, s18, v2
	s_mov_b32 s18, 0x28000
	s_nop 0
	v_addc_co_u32_e32 v35, vcc, 0, v3, vcc
	global_load_dword v30, v[30:31], off nt
	s_nop 0
	global_load_dword v31, v[34:35], off nt
	v_add_co_u32_e32 v34, vcc, s18, v2
	s_mov_b32 s18, 0x2a000
	s_nop 0
	v_addc_co_u32_e32 v35, vcc, 0, v3, vcc
	global_load_dword v32, v[34:35], off nt
	v_add_co_u32_e32 v34, vcc, s18, v2
	s_mov_b32 s18, 0x2c000
	s_nop 0
	v_addc_co_u32_e32 v35, vcc, 0, v3, vcc
	v_add_co_u32_e32 v36, vcc, s18, v2
	s_mov_b32 s18, 0x2e000
	s_nop 0
	v_addc_co_u32_e32 v37, vcc, 0, v3, vcc
	global_load_dword v34, v[34:35], off nt
	s_nop 0
	global_load_dword v35, v[36:37], off nt
	v_add_co_u32_e32 v36, vcc, s18, v2
	s_mov_b32 s18, 0x30000
	s_nop 0
	v_addc_co_u32_e32 v37, vcc, 0, v3, vcc
	v_add_co_u32_e32 v38, vcc, s18, v2
	s_mov_b32 s18, 0x32000
	s_nop 0
	v_addc_co_u32_e32 v39, vcc, 0, v3, vcc
	global_load_dword v36, v[36:37], off nt
	s_nop 0
	global_load_dword v37, v[38:39], off nt
	v_add_co_u32_e32 v38, vcc, s18, v2
	s_mov_b32 s18, 0x34000
	s_nop 0
	v_addc_co_u32_e32 v39, vcc, 0, v3, vcc
	v_add_co_u32_e32 v40, vcc, s18, v2
	s_mov_b32 s18, 0x36000
	s_nop 0
	v_addc_co_u32_e32 v41, vcc, 0, v3, vcc
	global_load_dword v38, v[38:39], off nt
	s_nop 0
	global_load_dword v39, v[40:41], off nt
	v_add_co_u32_e32 v40, vcc, s18, v2
	s_mov_b32 s18, 0x38000
	s_nop 0
	v_addc_co_u32_e32 v41, vcc, 0, v3, vcc
	v_add_co_u32_e32 v42, vcc, s18, v2
	s_mov_b32 s18, 0x3a000
	s_nop 0
	v_addc_co_u32_e32 v43, vcc, 0, v3, vcc
	global_load_dword v40, v[40:41], off nt
	s_nop 0
	global_load_dword v41, v[42:43], off nt
	v_add_co_u32_e32 v42, vcc, s18, v2
	s_mov_b32 s18, 0x3c000
	s_nop 0
	v_addc_co_u32_e32 v43, vcc, 0, v3, vcc
	v_add_co_u32_e32 v44, vcc, s18, v2
	s_mov_b32 s18, 0x3e000
	s_nop 0
	v_addc_co_u32_e32 v45, vcc, 0, v3, vcc
	v_add_co_u32_e32 v46, vcc, s18, v2
	s_mov_b32 s18, 0x40000
	s_nop 0
	v_addc_co_u32_e32 v47, vcc, 0, v3, vcc
	v_add_co_u32_e32 v48, vcc, s18, v2
	s_mov_b32 s18, 0x42000
	s_nop 0
	v_addc_co_u32_e32 v49, vcc, 0, v3, vcc
	global_load_dword v43, v[42:43], off nt
	s_nop 0
	global_load_dword v45, v[44:45], off nt
	s_nop 0
	global_load_dword v47, v[46:47], off nt
	s_nop 0
	global_load_dword v42, v[48:49], off nt
	v_add_co_u32_e32 v48, vcc, s18, v2
	s_mov_b32 s18, 0x44000
	s_nop 0
	v_addc_co_u32_e32 v49, vcc, 0, v3, vcc
; #define LAS __attribute__((address_space(3)))
; template <bool PERMGL, bool FP8>
; __device__ __forceinline__ void q8_cols_item(const float* W, int N, int n0, unsigned char* Bq, float* sc_out, LAS float* AM, int par, int wave, int lane) {
;     const int n = n0 + lane;
;     const float* Wp = W + (size_t)(128 * wave) * N + n;
;     float v[128]; float am = 0.f;
; #pragma unroll
;     for (int i = 0; i < 128; ++i) v[i] = Wp[(size_t)i * N];
	global_load_dword v44, v[48:49], off nt
	v_add_co_u32_e32 v48, vcc, s18, v2
	s_mov_b32 s18, 0x46000
	s_nop 0
	v_addc_co_u32_e32 v49, vcc, 0, v3, vcc
	global_load_dword v46, v[48:49], off nt
	v_add_co_u32_e32 v48, vcc, s18, v2
	s_mov_b32 s18, 0x48000
	s_nop 0
	v_addc_co_u32_e32 v49, vcc, 0, v3, vcc
	v_add_co_u32_e32 v50, vcc, s18, v2
	s_mov_b32 s18, 0x4a000
	s_nop 0
	v_addc_co_u32_e32 v51, vcc, 0, v3, vcc
	global_load_dword v48, v[48:49], off nt
	s_nop 0
	global_load_dword v49, v[50:51], off nt
	v_add_co_u32_e32 v50, vcc, s18, v2
	s_mov_b32 s18, 0x4c000
	s_nop 0
	v_addc_co_u32_e32 v51, vcc, 0, v3, vcc
	v_add_co_u32_e32 v52, vcc, s18, v2
	s_mov_b32 s18, 0x4e000
	s_nop 0
	v_addc_co_u32_e32 v53, vcc, 0, v3, vcc
	global_load_dword v50, v[50:51], off nt
	s_nop 0
	global_load_dword v51, v[52:53], off nt
	v_add_co_u32_e32 v52, vcc, s18, v2
	s_mov_b32 s18, 0x50000
	s_nop 0
	v_addc_co_u32_e32 v53, vcc, 0, v3, vcc
	v_add_co_u32_e32 v54, vcc, s18, v2
	s_mov_b32 s18, 0x52000
	s_nop 0
	v_addc_co_u32_e32 v55, vcc, 0, v3, vcc
	global_load_dword v52, v[52:53], off nt
	s_nop 0
	global_load_dword v53, v[54:55], off nt
	v_add_co_u32_e32 v54, vcc, s18, v2
	s_mov_b32 s18, 0x54000
	s_nop 0
	v_addc_co_u32_e32 v55, vcc, 0, v3, vcc
	v_add_co_u32_e32 v56, vcc, s18, v2
	s_mov_b32 s18, 0x56000
	s_nop 0
	v_addc_co_u32_e32 v57, vcc, 0, v3, vcc
	global_load_dword v54, v[54:55], off nt
	s_nop 0
	global_load_dword v55, v[56:57], off nt
	v_add_co_u32_e32 v56, vcc, s18, v2
	s_mov_b32 s18, 0x58000
	s_nop 0
	v_addc_co_u32_e32 v57, vcc, 0, v3, vcc
	v_add_co_u32_e32 v58, vcc, s18, v2
	s_mov_b32 s18, 0x5a000
	s_nop 0
	v_addc_co_u32_e32 v59, vcc, 0, v3, vcc
	global_load_dword v56, v[56:57], off nt
	s_nop 0
	global_load_dword v57, v[58:59], off nt
	v_add_co_u32_e32 v58, vcc, s18, v2
	s_mov_b32 s18, 0x5c000
	s_nop 0
	v_addc_co_u32_e32 v59, vcc, 0, v3, vcc
	v_add_co_u32_e32 v60, vcc, s18, v2
	s_mov_b32 s18, 0x5e000
	s_nop 0
	v_addc_co_u32_e32 v61, vcc, 0, v3, vcc
	global_load_dword v58, v[58:59], off nt
	s_nop 0
	global_load_dword v59, v[60:61], off nt
	v_add_co_u32_e32 v60, vcc, s18, v2
	s_mov_b32 s18, 0x60000
	s_nop 0
	v_addc_co_u32_e32 v61, vcc, 0, v3, vcc
	v_add_co_u32_e32 v62, vcc, s18, v2
	s_mov_b32 s18, 0x62000
	s_nop 0
	v_addc_co_u32_e32 v63, vcc, 0, v3, vcc
	global_load_dword v60, v[60:61], off nt
	s_nop 0
	global_load_dword v61, v[62:63], off nt
	v_add_co_u32_e32 v62, vcc, s18, v2
	s_mov_b32 s18, 0x64000
	s_nop 0
	v_addc_co_u32_e32 v63, vcc, 0, v3, vcc
	v_add_co_u32_e32 v64, vcc, s18, v2
	s_mov_b32 s18, 0x66000
	s_nop 0
	v_addc_co_u32_e32 v65, vcc, 0, v3, vcc
	global_load_dword v62, v[62:63], off nt
	s_nop 0
	global_load_dword v63, v[64:65], off nt
	v_add_co_u32_e32 v64, vcc, s18, v2
	s_mov_b32 s18, 0x68000
	s_nop 0
	v_addc_co_u32_e32 v65, vcc, 0, v3, vcc
	v_add_co_u32_e32 v66, vcc, s18, v2
	s_mov_b32 s18, 0x6a000
	s_nop 0
	v_addc_co_u32_e32 v67, vcc, 0, v3, vcc
	global_load_dword v64, v[64:65], off nt
	s_nop 0
	global_load_dword v65, v[66:67], off nt
	v_add_co_u32_e32 v66, vcc, s18, v2
	s_mov_b32 s18, 0x6c000
	s_nop 0
	v_addc_co_u32_e32 v67, vcc, 0, v3, vcc
	v_add_co_u32_e32 v68, vcc, s18, v2
	s_mov_b32 s18, 0x6e000
	s_nop 0
	v_addc_co_u32_e32 v69, vcc, 0, v3, vcc
	global_load_dword v66, v[66:67], off nt
	s_nop 0
	global_load_dword v67, v[68:69], off nt
	v_add_co_u32_e32 v68, vcc, s18, v2
	s_mov_b32 s18, 0x70000
	s_nop 0
	v_addc_co_u32_e32 v69, vcc, 0, v3, vcc
	v_add_co_u32_e32 v70, vcc, s18, v2
	s_mov_b32 s18, 0x72000
	s_nop 0
	v_addc_co_u32_e32 v71, vcc, 0, v3, vcc
	global_load_dword v68, v[68:69], off nt
	s_nop 0
	global_load_dword v69, v[70:71], off nt
	v_add_co_u32_e32 v70, vcc, s18, v2
	s_mov_b32 s18, 0x74000
	s_nop 0
	v_addc_co_u32_e32 v71, vcc, 0, v3, vcc
	v_add_co_u32_e32 v72, vcc, s18, v2
	s_mov_b32 s18, 0x76000
	s_nop 0
	v_addc_co_u32_e32 v73, vcc, 0, v3, vcc
	global_load_dword v70, v[70:71], off nt
	s_nop 0
	global_load_dword v71, v[72:73], off nt
	v_add_co_u32_e32 v72, vcc, s18, v2
	s_mov_b32 s18, 0x78000
	s_nop 0
	v_addc_co_u32_e32 v73, vcc, 0, v3, vcc
	v_add_co_u32_e32 v74, vcc, s18, v2
	s_mov_b32 s18, 0x7a000
	s_nop 0
	v_addc_co_u32_e32 v75, vcc, 0, v3, vcc
	global_load_dword v72, v[72:73], off nt
	s_nop 0
	global_load_dword v73, v[74:75], off nt
	v_add_co_u32_e32 v74, vcc, s18, v2
	s_mov_b32 s18, 0x7c000
	s_nop 0
	v_addc_co_u32_e32 v75, vcc, 0, v3, vcc
	v_add_co_u32_e32 v76, vcc, s18, v2
	s_mov_b32 s18, 0x7e000
	s_nop 0
	v_addc_co_u32_e32 v77, vcc, 0, v3, vcc
	v_add_co_u32_e32 v78, vcc, s18, v2
	s_mov_b32 s18, 0x80000
	s_nop 0
	v_addc_co_u32_e32 v79, vcc, 0, v3, vcc
	v_add_co_u32_e32 v80, vcc, s18, v2
	s_mov_b32 s18, 0x82000
	s_nop 0
	v_addc_co_u32_e32 v81, vcc, 0, v3, vcc
	global_load_dword v75, v[74:75], off nt
	s_nop 0
	global_load_dword v77, v[76:77], off nt
	s_nop 0
	global_load_dword v79, v[78:79], off nt
	s_nop 0
	global_load_dword v74, v[80:81], off nt
	v_add_co_u32_e32 v80, vcc, s18, v2
	s_mov_b32 s18, 0x84000
	s_nop 0
	v_addc_co_u32_e32 v81, vcc, 0, v3, vcc
	global_load_dword v76, v[80:81], off nt
	v_add_co_u32_e32 v80, vcc, s18, v2
	s_mov_b32 s18, 0x86000
	s_nop 0
	v_addc_co_u32_e32 v81, vcc, 0, v3, vcc
	global_load_dword v78, v[80:81], off nt
	v_add_co_u32_e32 v80, vcc, s18, v2
	s_mov_b32 s18, 0x88000
	s_nop 0
	v_addc_co_u32_e32 v81, vcc, 0, v3, vcc
	v_add_co_u32_e32 v82, vcc, s18, v2
	s_mov_b32 s18, 0x8a000
	s_nop 0
	v_addc_co_u32_e32 v83, vcc, 0, v3, vcc
	global_load_dword v80, v[80:81], off nt
	s_nop 0
	global_load_dword v81, v[82:83], off nt
	v_add_co_u32_e32 v82, vcc, s18, v2
	s_mov_b32 s18, 0x8c000
	s_nop 0
	v_addc_co_u32_e32 v83, vcc, 0, v3, vcc
	v_add_co_u32_e32 v84, vcc, s18, v2
	s_mov_b32 s18, 0x8e000
	s_nop 0
; template <bool PERMGL, bool FP8>
; __device__ __forceinline__ void q8_cols_item(const float* W, int N, int n0, unsigned char* Bq, float* sc_out, LAS float* AM, int par, int wave, int lane) {
;     ...
;     for (int i = 0; i < 128; ++i) v[i] = Wp[(size_t)i * N];
	v_addc_co_u32_e32 v85, vcc, 0, v3, vcc
	global_load_dword v82, v[82:83], off nt
	s_nop 0
	global_load_dword v83, v[84:85], off nt
	v_add_co_u32_e32 v84, vcc, s18, v2
	s_mov_b32 s18, 0x90000
	s_nop 0
	v_addc_co_u32_e32 v85, vcc, 0, v3, vcc
	v_add_co_u32_e32 v86, vcc, s18, v2
	s_mov_b32 s18, 0x92000
	s_nop 0
	v_addc_co_u32_e32 v87, vcc, 0, v3, vcc
	global_load_dword v84, v[84:85], off nt
	s_nop 0
	global_load_dword v85, v[86:87], off nt
	v_add_co_u32_e32 v86, vcc, s18, v2
	s_mov_b32 s18, 0x94000
	s_nop 0
	v_addc_co_u32_e32 v87, vcc, 0, v3, vcc
	v_add_co_u32_e32 v88, vcc, s18, v2
	s_mov_b32 s18, 0x96000
	s_nop 0
	v_addc_co_u32_e32 v89, vcc, 0, v3, vcc
	global_load_dword v86, v[86:87], off nt
	s_nop 0
	global_load_dword v87, v[88:89], off nt
	v_add_co_u32_e32 v88, vcc, s18, v2
	s_mov_b32 s18, 0x98000
	s_nop 0
	v_addc_co_u32_e32 v89, vcc, 0, v3, vcc
	v_add_co_u32_e32 v90, vcc, s18, v2
	s_mov_b32 s18, 0x9a000
	s_nop 0
	v_addc_co_u32_e32 v91, vcc, 0, v3, vcc
	global_load_dword v88, v[88:89], off nt
	s_nop 0
	global_load_dword v89, v[90:91], off nt
	v_add_co_u32_e32 v90, vcc, s18, v2
	s_mov_b32 s18, 0x9c000
	s_nop 0
	v_addc_co_u32_e32 v91, vcc, 0, v3, vcc
	v_add_co_u32_e32 v92, vcc, s18, v2
	s_mov_b32 s18, 0x9e000
	s_nop 0
	v_addc_co_u32_e32 v93, vcc, 0, v3, vcc
	global_load_dword v90, v[90:91], off nt
	s_nop 0
	global_load_dword v91, v[92:93], off nt
	v_add_co_u32_e32 v92, vcc, s18, v2
	s_mov_b32 s18, 0xa0000
	s_nop 0
	v_addc_co_u32_e32 v93, vcc, 0, v3, vcc
	v_add_co_u32_e32 v94, vcc, s18, v2
	s_mov_b32 s18, 0xa2000
	s_nop 0
	v_addc_co_u32_e32 v95, vcc, 0, v3, vcc
	global_load_dword v92, v[92:93], off nt
	s_nop 0
	global_load_dword v93, v[94:95], off nt
	v_add_co_u32_e32 v94, vcc, s18, v2
	s_mov_b32 s18, 0xa4000
	s_nop 0
	v_addc_co_u32_e32 v95, vcc, 0, v3, vcc
	v_add_co_u32_e32 v96, vcc, s18, v2
	s_mov_b32 s18, 0xa6000
	s_nop 0
	v_addc_co_u32_e32 v97, vcc, 0, v3, vcc
	global_load_dword v94, v[94:95], off nt
	s_nop 0
	global_load_dword v95, v[96:97], off nt
	v_add_co_u32_e32 v96, vcc, s18, v2
	s_mov_b32 s18, 0xa8000
	s_nop 0
	v_addc_co_u32_e32 v97, vcc, 0, v3, vcc
	v_add_co_u32_e32 v98, vcc, s18, v2
	s_mov_b32 s18, 0xaa000
	s_nop 0
	v_addc_co_u32_e32 v99, vcc, 0, v3, vcc
	global_load_dword v96, v[96:97], off nt
	s_nop 0
	global_load_dword v97, v[98:99], off nt
	v_add_co_u32_e32 v98, vcc, s18, v2
	s_mov_b32 s18, 0xac000
	s_nop 0
	v_addc_co_u32_e32 v99, vcc, 0, v3, vcc
	v_add_co_u32_e32 v100, vcc, s18, v2
	s_mov_b32 s18, 0xae000
	s_nop 0
	v_addc_co_u32_e32 v101, vcc, 0, v3, vcc
	global_load_dword v98, v[98:99], off nt
	s_nop 0
	global_load_dword v99, v[100:101], off nt
	v_add_co_u32_e32 v100, vcc, s18, v2
	s_mov_b32 s18, 0xb0000
	s_nop 0
	v_addc_co_u32_e32 v101, vcc, 0, v3, vcc
	v_add_co_u32_e32 v102, vcc, s18, v2
	s_mov_b32 s18, 0xb2000
	s_nop 0
	v_addc_co_u32_e32 v103, vcc, 0, v3, vcc
	global_load_dword v100, v[100:101], off nt
	s_nop 0
	global_load_dword v101, v[102:103], off nt
	v_add_co_u32_e32 v102, vcc, s18, v2
	s_mov_b32 s18, 0xb4000
	s_nop 0
	v_addc_co_u32_e32 v103, vcc, 0, v3, vcc
	v_add_co_u32_e32 v104, vcc, s18, v2
	s_mov_b32 s18, 0xb6000
	s_nop 0
	v_addc_co_u32_e32 v105, vcc, 0, v3, vcc
	global_load_dword v102, v[102:103], off nt
	s_nop 0
	global_load_dword v103, v[104:105], off nt
	v_add_co_u32_e32 v104, vcc, s18, v2
	s_mov_b32 s18, 0xb8000
	s_nop 0
	v_addc_co_u32_e32 v105, vcc, 0, v3, vcc
	v_add_co_u32_e32 v106, vcc, s18, v2
	s_mov_b32 s18, 0xba000
	s_nop 0
	v_addc_co_u32_e32 v107, vcc, 0, v3, vcc
	global_load_dword v104, v[104:105], off nt
	s_nop 0
	global_load_dword v105, v[106:107], off nt
	v_add_co_u32_e32 v106, vcc, s18, v2
	s_mov_b32 s18, 0xbc000
	s_nop 0
	v_addc_co_u32_e32 v107, vcc, 0, v3, vcc
	v_add_co_u32_e32 v108, vcc, s18, v2
	s_mov_b32 s18, 0xbe000
	s_nop 0
	v_addc_co_u32_e32 v109, vcc, 0, v3, vcc
	v_add_co_u32_e32 v110, vcc, s18, v2
	s_mov_b32 s18, 0xc0000
	s_nop 0
	v_addc_co_u32_e32 v111, vcc, 0, v3, vcc
	v_add_co_u32_e32 v112, vcc, s18, v2
	s_mov_b32 s18, 0xc2000
	s_nop 0
	v_addc_co_u32_e32 v113, vcc, 0, v3, vcc
	global_load_dword v107, v[106:107], off nt
	s_nop 0
	global_load_dword v109, v[108:109], off nt
	s_nop 0
	global_load_dword v111, v[110:111], off nt
	s_nop 0
	global_load_dword v106, v[112:113], off nt
	v_add_co_u32_e32 v112, vcc, s18, v2
	s_mov_b32 s18, 0xc4000
	s_nop 0
	v_addc_co_u32_e32 v113, vcc, 0, v3, vcc
	global_load_dword v108, v[112:113], off nt
	v_add_co_u32_e32 v112, vcc, s18, v2
	s_mov_b32 s18, 0xc6000
	s_nop 0
	v_addc_co_u32_e32 v113, vcc, 0, v3, vcc
	global_load_dword v110, v[112:113], off nt
	v_add_co_u32_e32 v112, vcc, s18, v2
	s_mov_b32 s18, 0xc8000
	s_nop 0
	v_addc_co_u32_e32 v113, vcc, 0, v3, vcc
	v_add_co_u32_e32 v114, vcc, s18, v2
	s_mov_b32 s18, 0xca000
	s_nop 0
	v_addc_co_u32_e32 v115, vcc, 0, v3, vcc
	global_load_dword v112, v[112:113], off nt
	s_nop 0
	global_load_dword v113, v[114:115], off nt
	v_add_co_u32_e32 v114, vcc, s18, v2
	s_mov_b32 s18, 0xcc000
	s_nop 0
	v_addc_co_u32_e32 v115, vcc, 0, v3, vcc
	v_add_co_u32_e32 v116, vcc, s18, v2
	s_mov_b32 s18, 0xce000
	s_nop 0
	v_addc_co_u32_e32 v117, vcc, 0, v3, vcc
	global_load_dword v114, v[114:115], off nt
	s_nop 0
	global_load_dword v115, v[116:117], off nt
	v_add_co_u32_e32 v116, vcc, s18, v2
	s_mov_b32 s18, 0xd0000
	s_nop 0
	v_addc_co_u32_e32 v117, vcc, 0, v3, vcc
	v_add_co_u32_e32 v118, vcc, s18, v2
	s_mov_b32 s18, 0xd2000
	s_nop 0
	v_addc_co_u32_e32 v119, vcc, 0, v3, vcc
	global_load_dword v116, v[116:117], off nt
	s_nop 0
	global_load_dword v117, v[118:119], off nt
	v_add_co_u32_e32 v118, vcc, s18, v2
	s_mov_b32 s18, 0xd4000
	s_nop 0
	v_addc_co_u32_e32 v119, vcc, 0, v3, vcc
	v_add_co_u32_e32 v120, vcc, s18, v2
	s_mov_b32 s18, 0xd6000
; template <bool PERMGL, bool FP8>
; __device__ __forceinline__ void q8_cols_item(const float* W, int N, int n0, unsigned char* Bq, float* sc_out, LAS float* AM, int par, int wave, int lane) {
;     ...
;     for (int i = 0; i < 128; ++i) v[i] = Wp[(size_t)i * N];
;     __builtin_amdgcn_sched_barrier(0);
; #pragma unroll
;     for (int i = 0; i < 128; ++i) am = fmaxf(am, fabsf(v[i]));
;     AM[(par * 8 + wave) * 64 + lane] = am;
;     __syncthreads();
	s_nop 0
	v_addc_co_u32_e32 v121, vcc, 0, v3, vcc
	global_load_dword v118, v[118:119], off nt
	s_nop 0
	global_load_dword v119, v[120:121], off nt
	v_add_co_u32_e32 v120, vcc, s18, v2
	s_mov_b32 s18, 0xd8000
	s_nop 0
	v_addc_co_u32_e32 v121, vcc, 0, v3, vcc
	v_add_co_u32_e32 v122, vcc, s18, v2
	s_mov_b32 s18, 0xda000
	s_nop 0
	v_addc_co_u32_e32 v123, vcc, 0, v3, vcc
	global_load_dword v120, v[120:121], off nt
	s_nop 0
	global_load_dword v121, v[122:123], off nt
	v_add_co_u32_e32 v122, vcc, s18, v2
	s_mov_b32 s18, 0xdc000
	s_nop 0
	v_addc_co_u32_e32 v123, vcc, 0, v3, vcc
	v_add_co_u32_e32 v124, vcc, s18, v2
	s_mov_b32 s18, 0xde000
	s_nop 0
	v_addc_co_u32_e32 v125, vcc, 0, v3, vcc
	global_load_dword v122, v[122:123], off nt
	s_nop 0
	global_load_dword v123, v[124:125], off nt
	v_add_co_u32_e32 v124, vcc, s18, v2
	s_mov_b32 s18, 0xe0000
	s_nop 0
	v_addc_co_u32_e32 v125, vcc, 0, v3, vcc
	v_add_co_u32_e32 v126, vcc, s18, v2
	s_mov_b32 s18, 0xe2000
	s_nop 0
	v_addc_co_u32_e32 v127, vcc, 0, v3, vcc
	global_load_dword v124, v[124:125], off nt
	s_nop 0
	global_load_dword v125, v[126:127], off nt
	v_add_co_u32_e32 v126, vcc, s18, v2
	s_mov_b32 s18, 0xe4000
	s_nop 0
	v_addc_co_u32_e32 v127, vcc, 0, v3, vcc
	v_add_co_u32_e32 v128, vcc, s18, v2
	s_mov_b32 s18, 0xe6000
	s_nop 0
	v_addc_co_u32_e32 v129, vcc, 0, v3, vcc
	global_load_dword v126, v[126:127], off nt
	s_nop 0
	global_load_dword v127, v[128:129], off nt
	v_add_co_u32_e32 v128, vcc, s18, v2
	s_mov_b32 s18, 0xe8000
	s_nop 0
	v_addc_co_u32_e32 v129, vcc, 0, v3, vcc
	v_add_co_u32_e32 v130, vcc, s18, v2
	s_mov_b32 s18, 0xea000
	s_nop 0
	v_addc_co_u32_e32 v131, vcc, 0, v3, vcc
	global_load_dword v128, v[128:129], off nt
	s_nop 0
	global_load_dword v129, v[130:131], off nt
	v_add_co_u32_e32 v130, vcc, s18, v2
	s_mov_b32 s18, 0xec000
	s_nop 0
	v_addc_co_u32_e32 v131, vcc, 0, v3, vcc
	v_add_co_u32_e32 v132, vcc, s18, v2
	s_mov_b32 s18, 0xee000
	s_nop 0
	v_addc_co_u32_e32 v133, vcc, 0, v3, vcc
	global_load_dword v130, v[130:131], off nt
	s_nop 0
	global_load_dword v131, v[132:133], off nt
	v_add_co_u32_e32 v132, vcc, s18, v2
	s_mov_b32 s18, 0xf0000
	s_nop 0
	v_addc_co_u32_e32 v133, vcc, 0, v3, vcc
	v_add_co_u32_e32 v134, vcc, s18, v2
	s_mov_b32 s18, 0xf2000
	s_nop 0
	v_addc_co_u32_e32 v135, vcc, 0, v3, vcc
	global_load_dword v132, v[132:133], off nt
	s_nop 0
	global_load_dword v133, v[134:135], off nt
	v_add_co_u32_e32 v134, vcc, s18, v2
	s_mov_b32 s18, 0xf4000
	s_nop 0
	v_addc_co_u32_e32 v135, vcc, 0, v3, vcc
	v_add_co_u32_e32 v136, vcc, s18, v2
	s_mov_b32 s18, 0xf6000
	s_nop 0
	v_addc_co_u32_e32 v137, vcc, 0, v3, vcc
	global_load_dword v134, v[134:135], off nt
	s_nop 0
	global_load_dword v135, v[136:137], off nt
	v_add_co_u32_e32 v136, vcc, s18, v2
	s_mov_b32 s18, 0xf8000
	s_nop 0
	v_addc_co_u32_e32 v137, vcc, 0, v3, vcc
	v_add_co_u32_e32 v138, vcc, s18, v2
	s_mov_b32 s18, 0xfa000
	s_nop 0
	v_addc_co_u32_e32 v139, vcc, 0, v3, vcc
	global_load_dword v136, v[136:137], off nt
	s_nop 0
	global_load_dword v137, v[138:139], off nt
	v_add_co_u32_e32 v138, vcc, s18, v2
	s_mov_b32 s18, 0xfc000
	s_nop 0
	v_addc_co_u32_e32 v139, vcc, 0, v3, vcc
	v_add_co_u32_e32 v140, vcc, s18, v2
	s_mov_b32 s18, 0xfe000
	s_nop 0
	v_addc_co_u32_e32 v141, vcc, 0, v3, vcc
	v_add_co_u32_e32 v2, vcc, s18, v2
	global_load_dword v138, v[138:139], off nt
	s_nop 0
	v_addc_co_u32_e32 v3, vcc, 0, v3, vcc
	global_load_dword v146, v[2:3], off nt
	global_load_dword v139, v[140:141], off nt
	s_waitcnt vmcnt(0)
	v_max3_f32 v2, |v6|, 0, |v7|
	v_max3_f32 v2, v2, |v8|, |v9|
	v_max3_f32 v2, v2, |v16|, |v17|
	v_max3_f32 v2, v2, |v18|, |v19|
	v_max3_f32 v2, v2, |v20|, |v21|
	v_max3_f32 v2, v2, |v22|, |v23|
	v_max3_f32 v2, v2, |v24|, |v25|
	v_max3_f32 v2, v2, |v26|, |v27|
	v_max3_f32 v2, v2, |v28|, |v29|
	v_max3_f32 v2, v2, |v30|, |v31|
	v_max3_f32 v2, v2, |v32|, |v34|
	v_max3_f32 v2, v2, |v35|, |v36|
	v_max3_f32 v2, v2, |v37|, |v38|
	v_max3_f32 v2, v2, |v39|, |v40|
	v_max3_f32 v2, v2, |v41|, |v43|
	v_max3_f32 v2, v2, |v45|, |v47|
	v_max3_f32 v2, v2, |v42|, |v44|
	v_max3_f32 v2, v2, |v46|, |v48|
	v_max3_f32 v2, v2, |v49|, |v50|
	v_max3_f32 v2, v2, |v51|, |v52|
	v_max3_f32 v2, v2, |v53|, |v54|
	v_max3_f32 v2, v2, |v55|, |v56|
	v_max3_f32 v2, v2, |v57|, |v58|
	v_max3_f32 v2, v2, |v59|, |v60|
	v_max3_f32 v2, v2, |v61|, |v62|
	v_max3_f32 v2, v2, |v63|, |v64|
	v_max3_f32 v2, v2, |v65|, |v66|
	v_max3_f32 v2, v2, |v67|, |v68|
	v_max3_f32 v2, v2, |v69|, |v70|
	v_max3_f32 v2, v2, |v71|, |v72|
	v_max3_f32 v2, v2, |v73|, |v75|
	v_max3_f32 v2, v2, |v77|, |v79|
	v_max3_f32 v2, v2, |v74|, |v76|
	v_max3_f32 v2, v2, |v78|, |v80|
	v_max3_f32 v2, v2, |v81|, |v82|
	v_max3_f32 v2, v2, |v83|, |v84|
	v_max3_f32 v2, v2, |v85|, |v86|
	v_max3_f32 v2, v2, |v87|, |v88|
	v_max3_f32 v2, v2, |v89|, |v90|
	v_max3_f32 v2, v2, |v91|, |v92|
	v_max3_f32 v2, v2, |v93|, |v94|
	v_max3_f32 v2, v2, |v95|, |v96|
	v_max3_f32 v2, v2, |v97|, |v98|
	v_max3_f32 v2, v2, |v99|, |v100|
	v_max3_f32 v2, v2, |v101|, |v102|
	v_max3_f32 v2, v2, |v103|, |v104|
	v_max3_f32 v2, v2, |v105|, |v107|
	v_max3_f32 v2, v2, |v109|, |v111|
	v_max3_f32 v2, v2, |v106|, |v108|
	v_max3_f32 v2, v2, |v110|, |v112|
	v_max3_f32 v2, v2, |v113|, |v114|
	v_max3_f32 v2, v2, |v115|, |v116|
	v_max3_f32 v2, v2, |v117|, |v118|
	v_max3_f32 v2, v2, |v119|, |v120|
	v_max3_f32 v2, v2, |v121|, |v122|
	v_max3_f32 v2, v2, |v123|, |v124|
	v_max3_f32 v2, v2, |v125|, |v126|
	v_max3_f32 v2, v2, |v127|, |v128|
	v_max3_f32 v2, v2, |v129|, |v130|
	v_max3_f32 v2, v2, |v131|, |v132|
	v_max3_f32 v2, v2, |v133|, |v134|
	v_max3_f32 v2, v2, |v135|, |v136|
	v_max3_f32 v2, v2, |v137|, |v138|
	s_lshl_b32 s18, s5, 11
	v_max3_f32 v5, v2, |v139|, |v146|
	v_add_u32_e32 v2, s18, v15
	v_add_u32_e32 v144, s18, v12
	ds_write_b32 v2, v5
	s_waitcnt lgkmcnt(0)
	s_barrier
; template <bool PERMGL, bool FP8>
; __device__ __forceinline__ void q8_cols_item(const float* W, int N, int n0, unsigned char* Bq, float* sc_out, LAS float* AM, int par, int wave, int lane) {
;     ...
; #pragma unroll
;     for (int w = 0; w < 8; ++w) am = fmaxf(am, AM[(par * 8 + w) * 64 + lane]);
;     const float sc = am > 0.f ? am * (FP8 ? (1.0f / 256.0f) : (1.0f / 127.0f)) : 1.0f, inv = 1.0f / sc;
;     int row = n;
;     if (PERMGL) { const int j = n >> 1, pr = n & 1, o = j & 127; row = ((j >> 7) << 8) + (((o >> 2) & 1) << 7) + ((o >> 5) << 5) + (pr << 4) + (((o >> 3) & 3) << 2) + (o & 3); }
;     if (!PERMGL) { const int o = n & 255; row = ((n >> 8) << 8) + (((o >> 3) & 1) << 7) + ((o >> 6) << 5) + (((o >> 4) & 3) << 3) + (o & 7); }
;     auto xq = [](unsigned x) { return (unsigned)__builtin_amdgcn_update_dpp(0, (int)x, 0xB1, 0xf, 0xf, true); };
;     const bool odd = lane & 1;
;     const int rowp = (int)xq((unsigned)row);
;     unsigned char* plo = Bq + (size_t)(odd ? rowp : row) * 1024 + 128 * wave + (odd ? 16 : 0);
;     unsigned char* phi = Bq + (size_t)(odd ? row : rowp) * 1024 + 128 * wave + (odd ? 16 : 0);
;     auto packc = [&](int c) { u32x4 o;
;         if (FP8) { o.x = f8x4(v[16 * c], v[16 * c + 1], v[16 * c + 2], v[16 * c + 3], inv); o.y = f8x4(v[16 * c + 4], v[16 * c + 5], v[16 * c + 6], v[16 * c + 7], inv);
;                    o.z = f8x4(v[16 * c + 8], v[16 * c + 9], v[16 * c + 10], v[16 * c + 11], inv); o.w = f8x4(v[16 * c + 12], v[16 * c + 13], v[16 * c + 14], v[16 * c + 15], inv); }
;         else { o.x = q8x4(v[16 * c], v[16 * c + 1], v[16 * c + 2], v[16 * c + 3], inv); o.y = q8x4(v[16 * c + 4], v[16 * c + 5], v[16 * c + 6], v[16 * c + 7], inv);
;                o.z = q8x4(v[16 * c + 8], v[16 * c + 9], v[16 * c + 10], v[16 * c + 11], inv); o.w = q8x4(v[16 * c + 12], v[16 * c + 13], v[16 * c + 14], v[16 * c + 15], inv); }
;         return o; };
; #pragma unroll
;     for (int j = 0; j < 4; ++j) { const u32x4 p0 = packc(2 * j), p1 = packc(2 * j + 1);
;         u32x4 snd, rcv;
; #pragma unroll
;         for (int q = 0; q < 4; ++q) { snd[q] = odd ? p0[q] : p1[q]; rcv[q] = xq(snd[q]); }
;         u32x4 a, b;
; #pragma unroll
;         for (int q = 0; q < 4; ++q) { a[q] = odd ? rcv[q] : p0[q]; b[q] = odd ? p1[q] : rcv[q]; }
;         *(u32x4*)(plo + 32 * j) = a; *(u32x4*)(phi + 32 * j) = b; }
	ds_read2st64_b32 v[2:3], v144 offset1:1
	ds_read2st64_b32 v[140:141], v144 offset0:2 offset1:3
	ds_read2st64_b32 v[142:143], v144 offset0:4 offset1:5
	ds_read2st64_b32 v[144:145], v144 offset0:6 offset1:7
	s_waitcnt lgkmcnt(3)
	v_max3_f32 v2, v5, v2, v3
	s_waitcnt lgkmcnt(2)
	v_max3_f32 v2, v2, v140, v141
	s_waitcnt lgkmcnt(1)
	v_max3_f32 v2, v2, v142, v143
	s_waitcnt lgkmcnt(0)
	v_max3_f32 v2, v2, v144, v145
	v_mul_f32_e32 v3, 0x3c010204, v2
	v_cmp_lt_f32_e32 vcc, 0, v2
	s_nop 1
	v_cndmask_b32_e32 v140, 1.0, v3, vcc
	v_div_scale_f32 v2, s[18:19], v140, v140, 1.0
	v_rcp_f32_e32 v3, v2
	s_nop 0
	v_fma_f32 v5, -v2, v3, 1.0
	v_fmac_f32_e32 v3, v5, v3
	v_div_scale_f32 v5, vcc, 1.0, v140, 1.0
	v_mul_f32_e32 v141, v5, v3
	v_fma_f32 v142, -v2, v141, v5
	v_fmac_f32_e32 v141, v142, v3
	v_fma_f32 v2, -v2, v141, v5
	v_div_fmas_f32 v2, v2, v3, v141
	v_div_fixup_f32 v142, v2, v140, 1.0
	v_fmaak_f32 v6, v6, v142, 0x4b400000
	v_fmaak_f32 v7, v7, v142, 0x4b400000
	v_fmaak_f32 v8, v8, v142, 0x4b400000
	v_fmaak_f32 v9, v9, v142, 0x4b400000
	v_perm_b32 v8, v9, v8, s61
	v_perm_b32 v6, v7, v6, s61
	v_perm_b32 v6, v8, v6, s79
	v_fmaak_f32 v7, v16, v142, 0x4b400000
	v_fmaak_f32 v8, v17, v142, 0x4b400000
	v_fmaak_f32 v9, v18, v142, 0x4b400000
	v_fmaak_f32 v16, v19, v142, 0x4b400000
	v_perm_b32 v9, v16, v9, s61
	v_perm_b32 v7, v8, v7, s61
	v_perm_b32 v7, v9, v7, s79
	v_fmaak_f32 v8, v20, v142, 0x4b400000
	v_fmaak_f32 v9, v21, v142, 0x4b400000
	v_fmaak_f32 v16, v22, v142, 0x4b400000
	v_fmaak_f32 v17, v23, v142, 0x4b400000
	v_perm_b32 v16, v17, v16, s61
	v_perm_b32 v8, v9, v8, s61
	v_perm_b32 v8, v16, v8, s79
	v_fmaak_f32 v9, v24, v142, 0x4b400000
	v_fmaak_f32 v16, v25, v142, 0x4b400000
	v_fmaak_f32 v17, v26, v142, 0x4b400000
	v_fmaak_f32 v18, v27, v142, 0x4b400000
	v_perm_b32 v17, v18, v17, s61
	v_perm_b32 v9, v16, v9, s61
	v_add_u16_e32 v2, s17, v11
	v_perm_b32 v9, v17, v9, s79
	v_fmaak_f32 v16, v28, v142, 0x4b400000
	v_fmaak_f32 v17, v29, v142, 0x4b400000
	v_fmaak_f32 v18, v30, v142, 0x4b400000
	v_fmaak_f32 v19, v31, v142, 0x4b400000
	v_lshrrev_b16_e32 v2, 1, v2
	v_lshlrev_b32_e32 v3, 4, v4
	s_movk_i32 s17, 0xf00
	v_perm_b32 v18, v19, v18, s61
	v_perm_b32 v16, v17, v16, s61
	v_and_b32_e32 v5, 0x80, v3
	v_and_b32_e32 v141, 0x60, v2
	v_and_or_b32 v4, v4, s17, v14
	v_perm_b32 v16, v18, v16, s79
	v_fmaak_f32 v17, v32, v142, 0x4b400000
	v_fmaak_f32 v18, v34, v142, 0x4b400000
	v_fmaak_f32 v19, v35, v142, 0x4b400000
	v_fmaak_f32 v20, v36, v142, 0x4b400000
	v_and_b32_e32 v3, 16, v3
	v_and_b32_e32 v2, 3, v2
	v_or3_b32 v4, v4, v5, v141
	v_perm_b32 v19, v20, v19, s61
	v_perm_b32 v17, v18, v17, s61
	v_or3_b32 v141, v4, v3, v2
	v_perm_b32 v17, v19, v17, s79
	v_fmaak_f32 v18, v37, v142, 0x4b400000
	v_fmaak_f32 v19, v38, v142, 0x4b400000
	v_fmaak_f32 v20, v39, v142, 0x4b400000
	v_fmaak_f32 v21, v40, v142, 0x4b400000
	v_mov_b32_dpp v4, v141 quad_perm:[1,0,3,2] row_mask:0xf bank_mask:0xf bound_ctrl:1
	v_perm_b32 v20, v21, v20, s61
	v_perm_b32 v18, v19, v18, s61
	v_cndmask_b32_e64 v2, v4, v141, s[2:3]
	v_perm_b32 v18, v20, v18, s79
	v_fmaak_f32 v19, v41, v142, 0x4b400000
	v_fmaak_f32 v20, v43, v142, 0x4b400000
	v_fmaak_f32 v21, v45, v142, 0x4b400000
	v_fmaak_f32 v22, v47, v142, 0x4b400000
	v_ashrrev_i32_e32 v3, 31, v2
	v_cndmask_b32_e64 v4, v141, v4, s[2:3]
	v_perm_b32 v21, v22, v21, s61
	v_perm_b32 v19, v20, v19, s61
	v_lshlrev_b64 v[2:3], 10, v[2:3]
	v_ashrrev_i32_e32 v5, 31, v4
	v_perm_b32 v19, v21, v19, s79
	v_lshl_add_u64 v[2:3], s[14:15], 0, v[2:3]
	v_lshlrev_b64 v[4:5], 10, v[4:5]
	v_cndmask_b32_e64 v20, v6, v16, s[2:3]
	v_cndmask_b32_e64 v21, v7, v17, s[2:3]
	v_cndmask_b32_e64 v22, v8, v18, s[2:3]
	v_cndmask_b32_e64 v23, v9, v19, s[2:3]
	v_lshl_add_u64 v[2:3], v[2:3], 0, s[42:43]
	v_lshl_add_u64 v[4:5], s[14:15], 0, v[4:5]
	v_mov_b32_dpp v20, v20 quad_perm:[1,0,3,2] row_mask:0xf bank_mask:0xf bound_ctrl:1
	v_mov_b32_dpp v21, v21 quad_perm:[1,0,3,2] row_mask:0xf bank_mask:0xf bound_ctrl:1
	v_mov_b32_dpp v22, v22 quad_perm:[1,0,3,2] row_mask:0xf bank_mask:0xf bound_ctrl:1
	v_mov_b32_dpp v23, v23 quad_perm:[1,0,3,2] row_mask:0xf bank_mask:0xf bound_ctrl:1
	v_lshl_add_u64 v[2:3], v[2:3], 0, v[0:1]
	v_lshl_add_u64 v[4:5], v[4:5], 0, s[42:43]
	v_cndmask_b32_e64 v6, v20, v6, s[2:3]
	v_cndmask_b32_e64 v7, v21, v7, s[2:3]
	v_cndmask_b32_e64 v8, v22, v8, s[2:3]
	v_cndmask_b32_e64 v9, v23, v9, s[2:3]
	v_lshl_add_u64 v[4:5], v[4:5], 0, v[0:1]
	v_cndmask_b32_e64 v16, v16, v20, s[2:3]
	v_cndmask_b32_e64 v17, v17, v21, s[2:3]
	v_cndmask_b32_e64 v18, v18, v22, s[2:3]
	v_cndmask_b32_e64 v19, v19, v23, s[2:3]
	global_store_dwordx4 v[2:3], v[6:9], off
	global_store_dwordx4 v[4:5], v[16:19], off
	v_fmaak_f32 v20, v68, v142, 0x4b400000
	v_fmaak_f32 v6, v42, v142, 0x4b400000
	v_fmaak_f32 v7, v44, v142, 0x4b400000
	v_fmaak_f32 v8, v46, v142, 0x4b400000
	v_fmaak_f32 v9, v48, v142, 0x4b400000
	v_perm_b32 v8, v9, v8, s61
	v_perm_b32 v6, v7, v6, s61
	v_perm_b32 v6, v8, v6, s79
	v_fmaak_f32 v7, v49, v142, 0x4b400000
	v_fmaak_f32 v8, v50, v142, 0x4b400000
	v_fmaak_f32 v9, v51, v142, 0x4b400000
	v_fmaak_f32 v16, v52, v142, 0x4b400000
	v_perm_b32 v9, v16, v9, s61
	v_perm_b32 v7, v8, v7, s61
	v_perm_b32 v7, v9, v7, s79
	v_fmaak_f32 v8, v53, v142, 0x4b400000
	v_fmaak_f32 v9, v54, v142, 0x4b400000
	v_fmaak_f32 v16, v55, v142, 0x4b400000
	v_fmaak_f32 v17, v56, v142, 0x4b400000
	v_perm_b32 v16, v17, v16, s61
	v_perm_b32 v8, v9, v8, s61
	v_perm_b32 v8, v16, v8, s79
	v_fmaak_f32 v9, v57, v142, 0x4b400000
	v_fmaak_f32 v16, v58, v142, 0x4b400000
	v_fmaak_f32 v17, v59, v142, 0x4b400000
	v_fmaak_f32 v18, v60, v142, 0x4b400000
	v_perm_b32 v17, v18, v17, s61
	v_perm_b32 v9, v16, v9, s61
	v_perm_b32 v9, v17, v9, s79
; template <bool PERMGL, bool FP8>
; __device__ __forceinline__ void q8_cols_item(const float* W, int N, int n0, unsigned char* Bq, float* sc_out, LAS float* AM, int par, int wave, int lane) {
;     ...
;     auto packc = [&](int c) { u32x4 o;
;         if (FP8) { o.x = f8x4(v[16 * c], v[16 * c + 1], v[16 * c + 2], v[16 * c + 3], inv); o.y = f8x4(v[16 * c + 4], v[16 * c + 5], v[16 * c + 6], v[16 * c + 7], inv);
;                    o.z = f8x4(v[16 * c + 8], v[16 * c + 9], v[16 * c + 10], v[16 * c + 11], inv); o.w = f8x4(v[16 * c + 12], v[16 * c + 13], v[16 * c + 14], v[16 * c + 15], inv); }
;         else { o.x = q8x4(v[16 * c], v[16 * c + 1], v[16 * c + 2], v[16 * c + 3], inv); o.y = q8x4(v[16 * c + 4], v[16 * c + 5], v[16 * c + 6], v[16 * c + 7], inv);
;                o.z = q8x4(v[16 * c + 8], v[16 * c + 9], v[16 * c + 10], v[16 * c + 11], inv); o.w = q8x4(v[16 * c + 12], v[16 * c + 13], v[16 * c + 14], v[16 * c + 15], inv); }
;         return o; };
; #pragma unroll
;     for (int j = 0; j < 4; ++j) { const u32x4 p0 = packc(2 * j), p1 = packc(2 * j + 1);
;         u32x4 snd, rcv;
; #pragma unroll
;         for (int q = 0; q < 4; ++q) { snd[q] = odd ? p0[q] : p1[q]; rcv[q] = xq(snd[q]); }
;         u32x4 a, b;
; #pragma unroll
;         for (int q = 0; q < 4; ++q) { a[q] = odd ? rcv[q] : p0[q]; b[q] = odd ? p1[q] : rcv[q]; }
;         *(u32x4*)(plo + 32 * j) = a; *(u32x4*)(phi + 32 * j) = b; }
	v_fmaak_f32 v16, v61, v142, 0x4b400000
	v_fmaak_f32 v17, v62, v142, 0x4b400000
	v_fmaak_f32 v18, v63, v142, 0x4b400000
	v_fmaak_f32 v19, v64, v142, 0x4b400000
	v_perm_b32 v18, v19, v18, s61
	v_perm_b32 v16, v17, v16, s61
	v_perm_b32 v16, v18, v16, s79
	v_fmaak_f32 v17, v65, v142, 0x4b400000
	v_fmaak_f32 v18, v66, v142, 0x4b400000
	v_fmaak_f32 v19, v67, v142, 0x4b400000
	v_perm_b32 v19, v20, v19, s61
	v_perm_b32 v17, v18, v17, s61
	v_perm_b32 v17, v19, v17, s79
	v_fmaak_f32 v18, v69, v142, 0x4b400000
	v_fmaak_f32 v19, v70, v142, 0x4b400000
	v_fmaak_f32 v20, v71, v142, 0x4b400000
	v_fmaak_f32 v21, v72, v142, 0x4b400000
	v_perm_b32 v20, v21, v20, s61
	v_perm_b32 v18, v19, v18, s61
	v_perm_b32 v18, v20, v18, s79
	v_fmaak_f32 v19, v73, v142, 0x4b400000
	v_fmaak_f32 v20, v75, v142, 0x4b400000
	v_fmaak_f32 v21, v77, v142, 0x4b400000
	v_fmaak_f32 v22, v79, v142, 0x4b400000
	v_perm_b32 v21, v22, v21, s61
	v_perm_b32 v19, v20, v19, s61
	v_perm_b32 v19, v21, v19, s79
	v_cndmask_b32_e64 v20, v6, v16, s[2:3]
	v_cndmask_b32_e64 v21, v7, v17, s[2:3]
	v_cndmask_b32_e64 v22, v8, v18, s[2:3]
	v_cndmask_b32_e64 v23, v9, v19, s[2:3]
	v_mov_b32_dpp v20, v20 quad_perm:[1,0,3,2] row_mask:0xf bank_mask:0xf bound_ctrl:1
	v_mov_b32_dpp v21, v21 quad_perm:[1,0,3,2] row_mask:0xf bank_mask:0xf bound_ctrl:1
	v_mov_b32_dpp v22, v22 quad_perm:[1,0,3,2] row_mask:0xf bank_mask:0xf bound_ctrl:1
	v_mov_b32_dpp v23, v23 quad_perm:[1,0,3,2] row_mask:0xf bank_mask:0xf bound_ctrl:1
	v_cndmask_b32_e64 v6, v20, v6, s[2:3]
	v_cndmask_b32_e64 v7, v21, v7, s[2:3]
	v_cndmask_b32_e64 v8, v22, v8, s[2:3]
	v_cndmask_b32_e64 v9, v23, v9, s[2:3]
	v_cndmask_b32_e64 v16, v16, v20, s[2:3]
	v_cndmask_b32_e64 v17, v17, v21, s[2:3]
	v_cndmask_b32_e64 v18, v18, v22, s[2:3]
	v_cndmask_b32_e64 v19, v19, v23, s[2:3]
	global_store_dwordx4 v[2:3], v[6:9], off offset:32
	global_store_dwordx4 v[4:5], v[16:19], off offset:32
	v_fmaak_f32 v20, v100, v142, 0x4b400000
	v_fmaak_f32 v6, v74, v142, 0x4b400000
	v_fmaak_f32 v7, v76, v142, 0x4b400000
	v_fmaak_f32 v8, v78, v142, 0x4b400000
	v_fmaak_f32 v9, v80, v142, 0x4b400000
	v_perm_b32 v8, v9, v8, s61
	v_perm_b32 v6, v7, v6, s61
	v_perm_b32 v6, v8, v6, s79
	v_fmaak_f32 v7, v81, v142, 0x4b400000
	v_fmaak_f32 v8, v82, v142, 0x4b400000
	v_fmaak_f32 v9, v83, v142, 0x4b400000
	v_fmaak_f32 v16, v84, v142, 0x4b400000
	v_perm_b32 v9, v16, v9, s61
	v_perm_b32 v7, v8, v7, s61
	v_perm_b32 v7, v9, v7, s79
	v_fmaak_f32 v8, v85, v142, 0x4b400000
	v_fmaak_f32 v9, v86, v142, 0x4b400000
	v_fmaak_f32 v16, v87, v142, 0x4b400000
	v_fmaak_f32 v17, v88, v142, 0x4b400000
	v_perm_b32 v16, v17, v16, s61
	v_perm_b32 v8, v9, v8, s61
	v_perm_b32 v8, v16, v8, s79
	v_fmaak_f32 v9, v89, v142, 0x4b400000
	v_fmaak_f32 v16, v90, v142, 0x4b400000
	v_fmaak_f32 v17, v91, v142, 0x4b400000
	v_fmaak_f32 v18, v92, v142, 0x4b400000
	v_perm_b32 v17, v18, v17, s61
	v_perm_b32 v9, v16, v9, s61
	v_perm_b32 v9, v17, v9, s79
	v_fmaak_f32 v16, v93, v142, 0x4b400000
	v_fmaak_f32 v17, v94, v142, 0x4b400000
	v_fmaak_f32 v18, v95, v142, 0x4b400000
	v_fmaak_f32 v19, v96, v142, 0x4b400000
	v_perm_b32 v18, v19, v18, s61
	v_perm_b32 v16, v17, v16, s61
	v_perm_b32 v16, v18, v16, s79
	v_fmaak_f32 v17, v97, v142, 0x4b400000
	v_fmaak_f32 v18, v98, v142, 0x4b400000
	v_fmaak_f32 v19, v99, v142, 0x4b400000
	v_perm_b32 v19, v20, v19, s61
	v_perm_b32 v17, v18, v17, s61
	v_perm_b32 v17, v19, v17, s79
	v_fmaak_f32 v18, v101, v142, 0x4b400000
	v_fmaak_f32 v19, v102, v142, 0x4b400000
	v_fmaak_f32 v20, v103, v142, 0x4b400000
	v_fmaak_f32 v21, v104, v142, 0x4b400000
	v_perm_b32 v20, v21, v20, s61
	v_perm_b32 v18, v19, v18, s61
	v_perm_b32 v18, v20, v18, s79
	v_fmaak_f32 v19, v105, v142, 0x4b400000
	v_fmaak_f32 v20, v107, v142, 0x4b400000
	v_fmaak_f32 v21, v109, v142, 0x4b400000
	v_fmaak_f32 v22, v111, v142, 0x4b400000
	v_perm_b32 v21, v22, v21, s61
	v_perm_b32 v19, v20, v19, s61
	v_perm_b32 v19, v21, v19, s79
	v_cndmask_b32_e64 v20, v6, v16, s[2:3]
	v_cndmask_b32_e64 v21, v7, v17, s[2:3]
	v_cndmask_b32_e64 v22, v8, v18, s[2:3]
; template <bool PERMGL, bool FP8>
; __device__ __forceinline__ void q8_cols_item(const float* W, int N, int n0, unsigned char* Bq, float* sc_out, LAS float* AM, int par, int wave, int lane) {
;     ...
;     for (int j = 0; j < 4; ++j) { const u32x4 p0 = packc(2 * j), p1 = packc(2 * j + 1);
;         u32x4 snd, rcv;
; #pragma unroll
;         for (int q = 0; q < 4; ++q) { snd[q] = odd ? p0[q] : p1[q]; rcv[q] = xq(snd[q]); }
;         u32x4 a, b;
; #pragma unroll
;         for (int q = 0; q < 4; ++q) { a[q] = odd ? rcv[q] : p0[q]; b[q] = odd ? p1[q] : rcv[q]; }
;         *(u32x4*)(plo + 32 * j) = a; *(u32x4*)(phi + 32 * j) = b; }
;     if (wave == 0) sc_out[PERMGL ? row : n] = FP8 ? sc * 16.0f : sc;
	v_cndmask_b32_e64 v23, v9, v19, s[2:3]
	v_mov_b32_dpp v20, v20 quad_perm:[1,0,3,2] row_mask:0xf bank_mask:0xf bound_ctrl:1
	v_mov_b32_dpp v21, v21 quad_perm:[1,0,3,2] row_mask:0xf bank_mask:0xf bound_ctrl:1
	v_mov_b32_dpp v22, v22 quad_perm:[1,0,3,2] row_mask:0xf bank_mask:0xf bound_ctrl:1
	v_mov_b32_dpp v23, v23 quad_perm:[1,0,3,2] row_mask:0xf bank_mask:0xf bound_ctrl:1
	v_cndmask_b32_e64 v6, v20, v6, s[2:3]
	v_cndmask_b32_e64 v7, v21, v7, s[2:3]
	v_cndmask_b32_e64 v8, v22, v8, s[2:3]
	v_cndmask_b32_e64 v9, v23, v9, s[2:3]
	v_cndmask_b32_e64 v16, v16, v20, s[2:3]
	v_cndmask_b32_e64 v17, v17, v21, s[2:3]
	v_cndmask_b32_e64 v18, v18, v22, s[2:3]
	v_cndmask_b32_e64 v19, v19, v23, s[2:3]
	global_store_dwordx4 v[2:3], v[6:9], off offset:64
	global_store_dwordx4 v[4:5], v[16:19], off offset:64
	v_fmaak_f32 v20, v132, v142, 0x4b400000
	v_fmaak_f32 v6, v106, v142, 0x4b400000
	v_fmaak_f32 v7, v108, v142, 0x4b400000
	v_fmaak_f32 v8, v110, v142, 0x4b400000
	v_fmaak_f32 v9, v112, v142, 0x4b400000
	v_perm_b32 v8, v9, v8, s61
	v_perm_b32 v6, v7, v6, s61
	v_perm_b32 v6, v8, v6, s79
	v_fmaak_f32 v7, v113, v142, 0x4b400000
	v_fmaak_f32 v8, v114, v142, 0x4b400000
	v_fmaak_f32 v9, v115, v142, 0x4b400000
	v_fmaak_f32 v16, v116, v142, 0x4b400000
	v_perm_b32 v9, v16, v9, s61
	v_perm_b32 v7, v8, v7, s61
	v_perm_b32 v7, v9, v7, s79
	v_fmaak_f32 v8, v117, v142, 0x4b400000
	v_fmaak_f32 v9, v118, v142, 0x4b400000
	v_fmaak_f32 v16, v119, v142, 0x4b400000
	v_fmaak_f32 v17, v120, v142, 0x4b400000
	v_perm_b32 v16, v17, v16, s61
	v_perm_b32 v8, v9, v8, s61
	v_perm_b32 v8, v16, v8, s79
	v_fmaak_f32 v9, v121, v142, 0x4b400000
	v_fmaak_f32 v16, v122, v142, 0x4b400000
	v_fmaak_f32 v17, v123, v142, 0x4b400000
	v_fmaak_f32 v18, v124, v142, 0x4b400000
	v_perm_b32 v17, v18, v17, s61
	v_perm_b32 v9, v16, v9, s61
	v_perm_b32 v9, v17, v9, s79
	v_fmaak_f32 v16, v125, v142, 0x4b400000
	v_fmaak_f32 v17, v126, v142, 0x4b400000
	v_fmaak_f32 v18, v127, v142, 0x4b400000
	v_fmaak_f32 v19, v128, v142, 0x4b400000
	v_perm_b32 v18, v19, v18, s61
	v_perm_b32 v16, v17, v16, s61
	v_perm_b32 v16, v18, v16, s79
	v_fmaak_f32 v17, v129, v142, 0x4b400000
	v_fmaak_f32 v18, v130, v142, 0x4b400000
	v_fmaak_f32 v19, v131, v142, 0x4b400000
	v_perm_b32 v19, v20, v19, s61
	v_perm_b32 v17, v18, v17, s61
	v_perm_b32 v17, v19, v17, s79
	v_fmaak_f32 v18, v133, v142, 0x4b400000
	v_fmaak_f32 v19, v134, v142, 0x4b400000
	v_fmaak_f32 v20, v135, v142, 0x4b400000
	v_fmaak_f32 v21, v136, v142, 0x4b400000
	v_perm_b32 v20, v21, v20, s61
	v_perm_b32 v18, v19, v18, s61
	v_perm_b32 v18, v20, v18, s79
	v_fmaak_f32 v19, v137, v142, 0x4b400000
	v_fmaak_f32 v20, v138, v142, 0x4b400000
	v_fmaak_f32 v21, v139, v142, 0x4b400000
	v_fmaak_f32 v22, v146, v142, 0x4b400000
	v_perm_b32 v21, v22, v21, s61
	v_perm_b32 v19, v20, v19, s61
	v_perm_b32 v19, v21, v19, s79
	v_cndmask_b32_e64 v20, v6, v16, s[2:3]
	v_cndmask_b32_e64 v21, v7, v17, s[2:3]
	v_cndmask_b32_e64 v22, v8, v18, s[2:3]
	v_cndmask_b32_e64 v23, v9, v19, s[2:3]
	v_mov_b32_dpp v20, v20 quad_perm:[1,0,3,2] row_mask:0xf bank_mask:0xf bound_ctrl:1
	v_mov_b32_dpp v21, v21 quad_perm:[1,0,3,2] row_mask:0xf bank_mask:0xf bound_ctrl:1
	v_mov_b32_dpp v22, v22 quad_perm:[1,0,3,2] row_mask:0xf bank_mask:0xf bound_ctrl:1
	v_mov_b32_dpp v23, v23 quad_perm:[1,0,3,2] row_mask:0xf bank_mask:0xf bound_ctrl:1
	v_cndmask_b32_e64 v6, v20, v6, s[2:3]
	v_cndmask_b32_e64 v16, v16, v20, s[2:3]
	v_cndmask_b32_e64 v7, v21, v7, s[2:3]
	v_cndmask_b32_e64 v17, v17, v21, s[2:3]
	v_cndmask_b32_e64 v8, v22, v8, s[2:3]
	v_cndmask_b32_e64 v18, v18, v22, s[2:3]
	v_cndmask_b32_e64 v9, v23, v9, s[2:3]
	v_cndmask_b32_e64 v19, v19, v23, s[2:3]
	s_and_b64 vcc, exec, s[0:1]
	global_store_dwordx4 v[2:3], v[6:9], off offset:96
	global_store_dwordx4 v[4:5], v[16:19], off offset:96
	s_cbranch_vccnz .LBB0_93
	s_lshl_b64 s[10:11], s[10:11], 13
	v_readlane_b32 s14, v253, 2
	s_add_u32 s10, s14, s10
	v_readlane_b32 s14, v253, 3
	s_addc_u32 s11, s14, s11
	v_lshlrev_b32_e32 v2, 2, v141
	global_store_dword v2, v140, s[10:11]
	s_branch .LBB0_93

; template <bool PERMGL, bool FP8>
; __device__ __forceinline__ void q8_cols_item(const float* W, int N, int n0, unsigned char* Bq, float* sc_out, LAS float* AM, int par, int wave, int lane) {
;     const int n = n0 + lane;
;     const float* Wp = W + (size_t)(128 * wave) * N + n;
;     float v[128]; float am = 0.f;
; #pragma unroll
;     for (int i = 0; i < 128; ++i) v[i] = Wp[(size_t)i * N];
; __global__ void __launch_bounds__(NWAVES * 64, 2) mk_fwd(Args args) {
;     ...
;                             const int lyr = cv_first + cv_it / 1536, r = cv_it % 1536;
;                             if (r < 1024) { const int mi = lyr * 32 + (r >> 5), nb = ((r & 31) + 8 * ((r >> 6) & 3)) & 31;
;                                 q8_cols_item<true, false>(args.in[11] + (size_t)mi * D * 2048, 2048, nb * 64, ws + WS_WGU + (size_t)mi * 2048 * 1024, (float*)(ws + WS_SB) + (size_t)mi * 2048, CAM, cv_par, wave, lane); }
;                             else { const int r2 = r - 1024, mi = lyr * 32 + (r2 >> 4), nb = ((r2 & 15) + 8 * ((r2 >> 6) & 1)) & 15;
;                                 q8_cols_item<false, true>(args.in[13] + (size_t)mi * D * D, D, nb * 64, ws + WS_WDN + (size_t)mi * D * 1024, (float*)(ws + WS_SBD) + (size_t)mi * D, CAM, cv_par, wave, lane); }
.LBB0_127:
	s_lshr_b32 s29, s27, 6
	s_cmpk_gt_i32 s27, 0x3ff
	s_mov_b64 s[18:19], -1
	s_cbranch_scc0 .LBB0_131
	s_lshl_b32 s18, s29, 9
	s_add_i32 s19, s27, 0xfffffc00
	s_add_i32 s18, s25, s18
	s_lshr_b32 s68, s19, 4
	s_lshl_b64 s[42:43], s[68:69], 20
	s_and_b32 s18, s18, 0x3c0
	s_add_u32 s46, s83, s42
	v_readlane_b32 s19, v254, 24
	s_addc_u32 s47, s19, s43
	s_lshl_b64 s[42:43], s[68:69], 22
	v_readlane_b32 s19, v254, 25
	v_add_u32_e32 v4, s18, v6
	s_add_u32 s42, s19, s42
	v_readlane_b32 s19, v252, 33
	s_addc_u32 s43, s19, s43
	v_lshlrev_b32_e32 v32, 2, v4
	v_lshl_add_u64 v[2:3], s[42:43], 0, v[32:33]
	s_movk_i32 s19, 0x2000
	v_add_co_u32_e32 v14, vcc, s19, v2
	s_movk_i32 s19, 0x4000
	s_nop 0
	v_addc_co_u32_e32 v15, vcc, 0, v3, vcc
	global_load_dword v11, v32, s[42:43] nt
	global_load_dword v13, v[14:15], off offset:-4096 nt
	global_load_dword v12, v[14:15], off nt
	v_add_co_u32_e32 v14, vcc, s19, v2
	s_movk_i32 s19, 0x6000
	s_nop 0
	v_addc_co_u32_e32 v15, vcc, 0, v3, vcc
	v_add_co_u32_e32 v18, vcc, s19, v2
	s_mov_b32 s19, 0x8000
	s_nop 0
	v_addc_co_u32_e32 v19, vcc, 0, v3, vcc
	v_add_co_u32_e32 v20, vcc, s19, v2
	s_mov_b32 s19, 0xa000
	s_nop 0
	v_addc_co_u32_e32 v21, vcc, 0, v3, vcc
	v_add_co_u32_e32 v22, vcc, s19, v2
	s_mov_b32 s19, 0xc000
	s_nop 0
	v_addc_co_u32_e32 v23, vcc, 0, v3, vcc
	v_add_co_u32_e32 v24, vcc, s19, v2
	s_mov_b32 s19, 0xe000
	s_nop 0
	v_addc_co_u32_e32 v25, vcc, 0, v3, vcc
	global_load_dword v16, v[14:15], off offset:-4096 nt
	s_nop 0
	global_load_dword v14, v[14:15], off nt
	s_nop 0
	global_load_dword v17, v[18:19], off offset:-4096 nt
	global_load_dword v15, v[18:19], off nt
	s_nop 0
	global_load_dword v19, v[20:21], off offset:-4096 nt
	global_load_dword v18, v[20:21], off nt
	s_nop 0
	global_load_dword v21, v[22:23], off offset:-4096 nt
	global_load_dword v20, v[22:23], off nt
	s_nop 0
	global_load_dword v23, v[24:25], off offset:-4096 nt
	global_load_dword v22, v[24:25], off nt
	v_add_co_u32_e32 v24, vcc, s19, v2
	s_mov_b32 s19, 0x10000
	s_nop 0
	v_addc_co_u32_e32 v25, vcc, 0, v3, vcc
	v_add_co_u32_e32 v28, vcc, s19, v2
	s_mov_b32 s19, 0x12000
	s_nop 0
	v_addc_co_u32_e32 v29, vcc, 0, v3, vcc
	v_add_co_u32_e32 v30, vcc, s19, v2
	s_mov_b32 s19, 0x14000
	s_nop 0
	v_addc_co_u32_e32 v31, vcc, 0, v3, vcc
	v_add_co_u32_e32 v34, vcc, s19, v2
	s_mov_b32 s19, 0x16000
	s_nop 0
	v_addc_co_u32_e32 v35, vcc, 0, v3, vcc
	global_load_dword v27, v[24:25], off offset:-4096 nt
	s_nop 0
	global_load_dword v24, v[24:25], off nt
	s_nop 0
	global_load_dword v26, v[28:29], off offset:-4096 nt
	global_load_dword v25, v[28:29], off nt
	s_nop 0
	global_load_dword v29, v[30:31], off offset:-4096 nt
	global_load_dword v28, v[30:31], off nt
	s_nop 0
	global_load_dword v31, v[34:35], off offset:-4096 nt
	global_load_dword v30, v[34:35], off nt
	v_add_co_u32_e32 v34, vcc, s19, v2
	s_mov_b32 s19, 0x18000
	s_nop 0
	v_addc_co_u32_e32 v35, vcc, 0, v3, vcc
	v_add_co_u32_e32 v38, vcc, s19, v2
	s_mov_b32 s19, 0x1a000
	s_nop 0
	v_addc_co_u32_e32 v39, vcc, 0, v3, vcc
	v_add_co_u32_e32 v40, vcc, s19, v2
	s_mov_b32 s19, 0x1c000
	s_nop 0
	v_addc_co_u32_e32 v41, vcc, 0, v3, vcc
	global_load_dword v37, v[34:35], off offset:-4096 nt
	s_nop 0
	global_load_dword v34, v[34:35], off nt
	s_nop 0
	global_load_dword v36, v[38:39], off offset:-4096 nt
	global_load_dword v35, v[38:39], off nt
	s_nop 0
	global_load_dword v39, v[40:41], off offset:-4096 nt
	global_load_dword v38, v[40:41], off nt
	v_add_co_u32_e32 v40, vcc, s19, v2
	s_mov_b32 s19, 0x1e000
	s_nop 0
	v_addc_co_u32_e32 v41, vcc, 0, v3, vcc
	v_add_co_u32_e32 v44, vcc, s19, v2
	s_mov_b32 s19, 0x20000
	s_nop 0
	v_addc_co_u32_e32 v45, vcc, 0, v3, vcc
	global_load_dword v42, v[40:41], off offset:-4096 nt
	s_nop 0
	global_load_dword v40, v[40:41], off nt
	s_nop 0
	global_load_dword v49, v[44:45], off offset:-4096 nt
	global_load_dword v47, v[44:45], off nt
	v_add_co_u32_e32 v44, vcc, s19, v2
	s_mov_b32 s19, 0x22000
	s_nop 0
	v_addc_co_u32_e32 v45, vcc, 0, v3, vcc
	v_add_co_u32_e32 v50, vcc, s19, v2
	s_mov_b32 s19, 0x24000
	s_nop 0
	v_addc_co_u32_e32 v51, vcc, 0, v3, vcc
	global_load_dword v48, v[44:45], off offset:-4096 nt
	global_load_dword v41, v[44:45], off nt
	s_nop 0
	global_load_dword v44, v[50:51], off offset:-4096 nt
	global_load_dword v43, v[50:51], off nt
	v_add_co_u32_e32 v50, vcc, s19, v2
	s_mov_b32 s19, 0x26000
	s_nop 0
	v_addc_co_u32_e32 v51, vcc, 0, v3, vcc
	global_load_dword v46, v[50:51], off offset:-4096 nt
	global_load_dword v45, v[50:51], off nt
	v_add_co_u32_e32 v50, vcc, s19, v2
	s_mov_b32 s19, 0x28000
	s_nop 0
	v_addc_co_u32_e32 v51, vcc, 0, v3, vcc
	v_add_co_u32_e32 v54, vcc, s19, v2
	s_mov_b32 s19, 0x2a000
	s_nop 0
	v_addc_co_u32_e32 v55, vcc, 0, v3, vcc
	v_add_co_u32_e32 v56, vcc, s19, v2
	s_mov_b32 s19, 0x2c000
	s_nop 0
	v_addc_co_u32_e32 v57, vcc, 0, v3, vcc
	v_add_co_u32_e32 v58, vcc, s19, v2
	s_mov_b32 s19, 0x2e000
	s_nop 0
	v_addc_co_u32_e32 v59, vcc, 0, v3, vcc
	global_load_dword v53, v[50:51], off offset:-4096 nt
	s_nop 0
	global_load_dword v50, v[50:51], off nt
	s_nop 0
	global_load_dword v52, v[54:55], off offset:-4096 nt
	global_load_dword v51, v[54:55], off nt
	s_nop 0
	global_load_dword v55, v[56:57], off offset:-4096 nt
	global_load_dword v54, v[56:57], off nt
	s_nop 0
	global_load_dword v57, v[58:59], off offset:-4096 nt
	global_load_dword v56, v[58:59], off nt
	v_add_co_u32_e32 v58, vcc, s19, v2
	s_mov_b32 s19, 0x30000
	s_nop 0
	v_addc_co_u32_e32 v59, vcc, 0, v3, vcc
	v_add_co_u32_e32 v62, vcc, s19, v2
	s_mov_b32 s19, 0x32000
	s_nop 0
	v_addc_co_u32_e32 v63, vcc, 0, v3, vcc
	v_add_co_u32_e32 v64, vcc, s19, v2
	s_mov_b32 s19, 0x34000
	s_nop 0
	v_addc_co_u32_e32 v65, vcc, 0, v3, vcc
; template <bool PERMGL, bool FP8>
; __device__ __forceinline__ void q8_cols_item(const float* W, int N, int n0, unsigned char* Bq, float* sc_out, LAS float* AM, int par, int wave, int lane) {
;     ...
;     for (int i = 0; i < 128; ++i) v[i] = Wp[(size_t)i * N];
	v_add_co_u32_e32 v66, vcc, s19, v2
	s_mov_b32 s19, 0x36000
	s_nop 0
	v_addc_co_u32_e32 v67, vcc, 0, v3, vcc
	global_load_dword v61, v[58:59], off offset:-4096 nt
	s_nop 0
	global_load_dword v58, v[58:59], off nt
	s_nop 0
	global_load_dword v60, v[62:63], off offset:-4096 nt
	global_load_dword v59, v[62:63], off nt
	s_nop 0
	global_load_dword v63, v[64:65], off offset:-4096 nt
	global_load_dword v62, v[64:65], off nt
	s_nop 0
	global_load_dword v65, v[66:67], off offset:-4096 nt
	global_load_dword v64, v[66:67], off nt
	v_add_co_u32_e32 v66, vcc, s19, v2
	s_mov_b32 s19, 0x38000
	s_nop 0
	v_addc_co_u32_e32 v67, vcc, 0, v3, vcc
	v_add_co_u32_e32 v70, vcc, s19, v2
	s_mov_b32 s19, 0x3a000
	s_nop 0
	v_addc_co_u32_e32 v71, vcc, 0, v3, vcc
	v_add_co_u32_e32 v72, vcc, s19, v2
	s_mov_b32 s19, 0x3c000
	s_nop 0
	v_addc_co_u32_e32 v73, vcc, 0, v3, vcc
	global_load_dword v69, v[66:67], off offset:-4096 nt
	s_nop 0
	global_load_dword v66, v[66:67], off nt
	s_nop 0
	global_load_dword v68, v[70:71], off offset:-4096 nt
	global_load_dword v67, v[70:71], off nt
	s_nop 0
	global_load_dword v71, v[72:73], off offset:-4096 nt
	global_load_dword v70, v[72:73], off nt
	v_add_co_u32_e32 v72, vcc, s19, v2
	s_mov_b32 s19, 0x3e000
	s_nop 0
	v_addc_co_u32_e32 v73, vcc, 0, v3, vcc
	v_add_co_u32_e32 v76, vcc, s19, v2
	s_mov_b32 s19, 0x40000
	s_nop 0
	v_addc_co_u32_e32 v77, vcc, 0, v3, vcc
	global_load_dword v74, v[72:73], off offset:-4096 nt
	s_nop 0
	global_load_dword v72, v[72:73], off nt
	s_nop 0
	global_load_dword v81, v[76:77], off offset:-4096 nt
	global_load_dword v79, v[76:77], off nt
	v_add_co_u32_e32 v76, vcc, s19, v2
	s_mov_b32 s19, 0x42000
	s_nop 0
	v_addc_co_u32_e32 v77, vcc, 0, v3, vcc
	v_add_co_u32_e32 v82, vcc, s19, v2
	s_mov_b32 s19, 0x44000
	s_nop 0
	v_addc_co_u32_e32 v83, vcc, 0, v3, vcc
	global_load_dword v80, v[76:77], off offset:-4096 nt
	global_load_dword v73, v[76:77], off nt
	s_nop 0
	global_load_dword v76, v[82:83], off offset:-4096 nt
	global_load_dword v75, v[82:83], off nt
	v_add_co_u32_e32 v82, vcc, s19, v2
	s_mov_b32 s19, 0x46000
	s_nop 0
	v_addc_co_u32_e32 v83, vcc, 0, v3, vcc
	global_load_dword v78, v[82:83], off offset:-4096 nt
	global_load_dword v77, v[82:83], off nt
	v_add_co_u32_e32 v82, vcc, s19, v2
	s_mov_b32 s19, 0x48000
	s_nop 0
	v_addc_co_u32_e32 v83, vcc, 0, v3, vcc
	v_add_co_u32_e32 v86, vcc, s19, v2
	s_mov_b32 s19, 0x4a000
	s_nop 0
	v_addc_co_u32_e32 v87, vcc, 0, v3, vcc
	v_add_co_u32_e32 v88, vcc, s19, v2
	s_mov_b32 s19, 0x4c000
	s_nop 0
	v_addc_co_u32_e32 v89, vcc, 0, v3, vcc
	v_add_co_u32_e32 v90, vcc, s19, v2
	s_mov_b32 s19, 0x4e000
	s_nop 0
	v_addc_co_u32_e32 v91, vcc, 0, v3, vcc
	global_load_dword v85, v[82:83], off offset:-4096 nt
	s_nop 0
	global_load_dword v82, v[82:83], off nt
	s_nop 0
	global_load_dword v84, v[86:87], off offset:-4096 nt
	global_load_dword v83, v[86:87], off nt
	s_nop 0
	global_load_dword v87, v[88:89], off offset:-4096 nt
	global_load_dword v86, v[88:89], off nt
	s_nop 0
	global_load_dword v89, v[90:91], off offset:-4096 nt
	global_load_dword v88, v[90:91], off nt
	v_add_co_u32_e32 v90, vcc, s19, v2
	s_mov_b32 s19, 0x50000
	s_nop 0
	v_addc_co_u32_e32 v91, vcc, 0, v3, vcc
	v_add_co_u32_e32 v94, vcc, s19, v2
	s_mov_b32 s19, 0x52000
	s_nop 0
	v_addc_co_u32_e32 v95, vcc, 0, v3, vcc
	v_add_co_u32_e32 v96, vcc, s19, v2
	s_mov_b32 s19, 0x54000
	s_nop 0
	v_addc_co_u32_e32 v97, vcc, 0, v3, vcc
	v_add_co_u32_e32 v98, vcc, s19, v2
	s_mov_b32 s19, 0x56000
	s_nop 0
	v_addc_co_u32_e32 v99, vcc, 0, v3, vcc
	global_load_dword v93, v[90:91], off offset:-4096 nt
	s_nop 0
	global_load_dword v90, v[90:91], off nt
	s_nop 0
	global_load_dword v92, v[94:95], off offset:-4096 nt
	global_load_dword v91, v[94:95], off nt
	s_nop 0
	global_load_dword v95, v[96:97], off offset:-4096 nt
	global_load_dword v94, v[96:97], off nt
	s_nop 0
	global_load_dword v97, v[98:99], off offset:-4096 nt
	global_load_dword v96, v[98:99], off nt
	v_add_co_u32_e32 v98, vcc, s19, v2
	s_mov_b32 s19, 0x58000
	s_nop 0
	v_addc_co_u32_e32 v99, vcc, 0, v3, vcc
	v_add_co_u32_e32 v102, vcc, s19, v2
	s_mov_b32 s19, 0x5a000
	s_nop 0
	v_addc_co_u32_e32 v103, vcc, 0, v3, vcc
	v_add_co_u32_e32 v104, vcc, s19, v2
	s_mov_b32 s19, 0x5c000
	s_nop 0
	v_addc_co_u32_e32 v105, vcc, 0, v3, vcc
	global_load_dword v101, v[98:99], off offset:-4096 nt
	s_nop 0
	global_load_dword v98, v[98:99], off nt
	s_nop 0
	global_load_dword v100, v[102:103], off offset:-4096 nt
	global_load_dword v99, v[102:103], off nt
	s_nop 0
	global_load_dword v103, v[104:105], off offset:-4096 nt
	global_load_dword v102, v[104:105], off nt
	v_add_co_u32_e32 v104, vcc, s19, v2
	s_mov_b32 s19, 0x5e000
	s_nop 0
	v_addc_co_u32_e32 v105, vcc, 0, v3, vcc
	v_add_co_u32_e32 v108, vcc, s19, v2
	s_mov_b32 s19, 0x60000
	s_nop 0
	v_addc_co_u32_e32 v109, vcc, 0, v3, vcc
	global_load_dword v106, v[104:105], off offset:-4096 nt
	s_nop 0
	global_load_dword v104, v[104:105], off nt
	s_nop 0
	global_load_dword v113, v[108:109], off offset:-4096 nt
	global_load_dword v111, v[108:109], off nt
	v_add_co_u32_e32 v108, vcc, s19, v2
	s_mov_b32 s19, 0x62000
	s_nop 0
	v_addc_co_u32_e32 v109, vcc, 0, v3, vcc
	v_add_co_u32_e32 v114, vcc, s19, v2
	s_mov_b32 s19, 0x64000
	s_nop 0
	v_addc_co_u32_e32 v115, vcc, 0, v3, vcc
	global_load_dword v112, v[108:109], off offset:-4096 nt
	global_load_dword v105, v[108:109], off nt
	s_nop 0
	global_load_dword v108, v[114:115], off offset:-4096 nt
	global_load_dword v107, v[114:115], off nt
	v_add_co_u32_e32 v114, vcc, s19, v2
	s_mov_b32 s19, 0x66000
	s_nop 0
	v_addc_co_u32_e32 v115, vcc, 0, v3, vcc
	global_load_dword v110, v[114:115], off offset:-4096 nt
	global_load_dword v109, v[114:115], off nt
; template <bool PERMGL, bool FP8>
; __device__ __forceinline__ void q8_cols_item(const float* W, int N, int n0, unsigned char* Bq, float* sc_out, LAS float* AM, int par, int wave, int lane) {
;     ...
;     for (int i = 0; i < 128; ++i) v[i] = Wp[(size_t)i * N];
;     __builtin_amdgcn_sched_barrier(0);
; #pragma unroll
;     for (int i = 0; i < 128; ++i) am = fmaxf(am, fabsf(v[i]));
;     AM[(par * 8 + wave) * 64 + lane] = am;
;     __syncthreads();
	v_add_co_u32_e32 v114, vcc, s19, v2
	s_mov_b32 s19, 0x68000
	s_nop 0
	v_addc_co_u32_e32 v115, vcc, 0, v3, vcc
	v_add_co_u32_e32 v118, vcc, s19, v2
	s_mov_b32 s19, 0x6a000
	s_nop 0
	v_addc_co_u32_e32 v119, vcc, 0, v3, vcc
	v_add_co_u32_e32 v120, vcc, s19, v2
	s_mov_b32 s19, 0x6c000
	s_nop 0
	v_addc_co_u32_e32 v121, vcc, 0, v3, vcc
	v_add_co_u32_e32 v122, vcc, s19, v2
	s_mov_b32 s19, 0x6e000
	s_nop 0
	v_addc_co_u32_e32 v123, vcc, 0, v3, vcc
	global_load_dword v117, v[114:115], off offset:-4096 nt
	s_nop 0
	global_load_dword v114, v[114:115], off nt
	s_nop 0
	global_load_dword v116, v[118:119], off offset:-4096 nt
	global_load_dword v115, v[118:119], off nt
	s_nop 0
	global_load_dword v119, v[120:121], off offset:-4096 nt
	global_load_dword v118, v[120:121], off nt
	s_nop 0
	global_load_dword v121, v[122:123], off offset:-4096 nt
	global_load_dword v120, v[122:123], off nt
	v_add_co_u32_e32 v122, vcc, s19, v2
	s_mov_b32 s19, 0x70000
	s_nop 0
	v_addc_co_u32_e32 v123, vcc, 0, v3, vcc
	v_add_co_u32_e32 v126, vcc, s19, v2
	s_mov_b32 s19, 0x72000
	s_nop 0
	v_addc_co_u32_e32 v127, vcc, 0, v3, vcc
	v_add_co_u32_e32 v128, vcc, s19, v2
	s_mov_b32 s19, 0x74000
	s_nop 0
	v_addc_co_u32_e32 v129, vcc, 0, v3, vcc
	v_add_co_u32_e32 v130, vcc, s19, v2
	s_mov_b32 s19, 0x76000
	s_nop 0
	v_addc_co_u32_e32 v131, vcc, 0, v3, vcc
	global_load_dword v125, v[122:123], off offset:-4096 nt
	s_nop 0
	global_load_dword v122, v[122:123], off nt
	s_nop 0
	global_load_dword v124, v[126:127], off offset:-4096 nt
	global_load_dword v123, v[126:127], off nt
	s_nop 0
	global_load_dword v127, v[128:129], off offset:-4096 nt
	global_load_dword v126, v[128:129], off nt
	s_nop 0
	global_load_dword v129, v[130:131], off offset:-4096 nt
	global_load_dword v128, v[130:131], off nt
	v_add_co_u32_e32 v130, vcc, s19, v2
	s_mov_b32 s19, 0x78000
	s_nop 0
	v_addc_co_u32_e32 v131, vcc, 0, v3, vcc
	v_add_co_u32_e32 v134, vcc, s19, v2
	s_mov_b32 s19, 0x7a000
	s_nop 0
	v_addc_co_u32_e32 v135, vcc, 0, v3, vcc
	v_add_co_u32_e32 v136, vcc, s19, v2
	s_mov_b32 s19, 0x7c000
	s_nop 0
	v_addc_co_u32_e32 v137, vcc, 0, v3, vcc
	v_add_co_u32_e32 v138, vcc, s19, v2
	s_mov_b32 s19, 0x7e000
	s_nop 0
	v_addc_co_u32_e32 v139, vcc, 0, v3, vcc
	v_add_co_u32_e32 v140, vcc, s19, v2
	s_mov_b32 s19, 0x7f000
	s_nop 0
	v_addc_co_u32_e32 v141, vcc, 0, v3, vcc
	v_add_co_u32_e32 v2, vcc, s19, v2
	global_load_dword v133, v[130:131], off offset:-4096 nt
	s_nop 0
	global_load_dword v130, v[130:131], off nt
	s_nop 0
	global_load_dword v132, v[134:135], off offset:-4096 nt
	global_load_dword v131, v[134:135], off nt
	s_nop 0
	global_load_dword v135, v[136:137], off offset:-4096 nt
	global_load_dword v134, v[136:137], off nt
	s_nop 0
	global_load_dword v137, v[138:139], off offset:-4096 nt
	global_load_dword v136, v[138:139], off nt
	s_nop 0
	global_load_dword v139, v[140:141], off offset:-4096 nt
	global_load_dword v138, v[140:141], off nt
	v_addc_co_u32_e32 v3, vcc, 0, v3, vcc
	global_load_dword v140, v[2:3], off nt
	s_waitcnt vmcnt(0)
	v_max3_f32 v2, |v11|, 0, |v13|
	v_max3_f32 v2, v2, |v12|, |v16|
	v_max3_f32 v2, v2, |v14|, |v17|
	v_max3_f32 v2, v2, |v15|, |v19|
	v_max3_f32 v2, v2, |v18|, |v21|
	v_max3_f32 v2, v2, |v20|, |v23|
	v_max3_f32 v2, v2, |v22|, |v27|
	v_max3_f32 v2, v2, |v24|, |v26|
	v_max3_f32 v2, v2, |v25|, |v29|
	v_max3_f32 v2, v2, |v28|, |v31|
	v_max3_f32 v2, v2, |v30|, |v37|
	v_max3_f32 v2, v2, |v34|, |v36|
	v_max3_f32 v2, v2, |v35|, |v39|
	v_max3_f32 v2, v2, |v38|, |v42|
	v_max3_f32 v2, v2, |v40|, |v49|
	v_max3_f32 v2, v2, |v47|, |v48|
	v_max3_f32 v2, v2, |v41|, |v44|
	v_max3_f32 v2, v2, |v43|, |v46|
	v_max3_f32 v2, v2, |v45|, |v53|
	v_max3_f32 v2, v2, |v50|, |v52|
	v_max3_f32 v2, v2, |v51|, |v55|
	v_max3_f32 v2, v2, |v54|, |v57|
	v_max3_f32 v2, v2, |v56|, |v61|
	v_max3_f32 v2, v2, |v58|, |v60|
	v_max3_f32 v2, v2, |v59|, |v63|
	v_max3_f32 v2, v2, |v62|, |v65|
	v_max3_f32 v2, v2, |v64|, |v69|
	v_max3_f32 v2, v2, |v66|, |v68|
	v_max3_f32 v2, v2, |v67|, |v71|
	v_max3_f32 v2, v2, |v70|, |v74|
	v_max3_f32 v2, v2, |v72|, |v81|
	v_max3_f32 v2, v2, |v79|, |v80|
	v_max3_f32 v2, v2, |v73|, |v76|
	v_max3_f32 v2, v2, |v75|, |v78|
	v_max3_f32 v2, v2, |v77|, |v85|
	v_max3_f32 v2, v2, |v82|, |v84|
	v_max3_f32 v2, v2, |v83|, |v87|
	v_max3_f32 v2, v2, |v86|, |v89|
	v_max3_f32 v2, v2, |v88|, |v93|
	v_max3_f32 v2, v2, |v90|, |v92|
	v_max3_f32 v2, v2, |v91|, |v95|
	v_max3_f32 v2, v2, |v94|, |v97|
	v_max3_f32 v2, v2, |v96|, |v101|
	v_max3_f32 v2, v2, |v98|, |v100|
	v_max3_f32 v2, v2, |v99|, |v103|
	v_max3_f32 v2, v2, |v102|, |v106|
	v_max3_f32 v2, v2, |v104|, |v113|
	v_max3_f32 v2, v2, |v111|, |v112|
	v_max3_f32 v2, v2, |v105|, |v108|
	v_max3_f32 v2, v2, |v107|, |v110|
	v_max3_f32 v2, v2, |v109|, |v117|
	v_max3_f32 v2, v2, |v114|, |v116|
	v_max3_f32 v2, v2, |v115|, |v119|
	v_max3_f32 v2, v2, |v118|, |v121|
	v_max3_f32 v2, v2, |v120|, |v125|
	v_max3_f32 v2, v2, |v122|, |v124|
	v_max3_f32 v2, v2, |v123|, |v127|
	v_max3_f32 v2, v2, |v126|, |v129|
	v_max3_f32 v2, v2, |v128|, |v133|
	v_max3_f32 v2, v2, |v130|, |v132|
	v_max3_f32 v2, v2, |v131|, |v135|
	v_max3_f32 v2, v2, |v134|, |v137|
	v_max3_f32 v2, v2, |v136|, |v139|
	s_lshl_b32 s19, s15, 11
	v_max3_f32 v5, v2, |v138|, |v140|
	v_add_u32_e32 v2, s19, v10
	v_add_u32_e32 v141, s19, v7
	ds_write_b32 v2, v5
	s_waitcnt lgkmcnt(0)
	s_barrier
; template <bool PERMGL, bool FP8>
; __device__ __forceinline__ void q8_cols_item(const float* W, int N, int n0, unsigned char* Bq, float* sc_out, LAS float* AM, int par, int wave, int lane) {
;     ...
; #pragma unroll
;     for (int w = 0; w < 8; ++w) am = fmaxf(am, AM[(par * 8 + w) * 64 + lane]);
;     const float sc = am > 0.f ? am * (FP8 ? (1.0f / 256.0f) : (1.0f / 127.0f)) : 1.0f, inv = 1.0f / sc;
;     int row = n;
;     if (PERMGL) { const int j = n >> 1, pr = n & 1, o = j & 127; row = ((j >> 7) << 8) + (((o >> 2) & 1) << 7) + ((o >> 5) << 5) + (pr << 4) + (((o >> 3) & 3) << 2) + (o & 3); }
;     if (!PERMGL) { const int o = n & 255; row = ((n >> 8) << 8) + (((o >> 3) & 1) << 7) + ((o >> 6) << 5) + (((o >> 4) & 3) << 3) + (o & 7); }
;     auto xq = [](unsigned x) { return (unsigned)__builtin_amdgcn_update_dpp(0, (int)x, 0xB1, 0xf, 0xf, true); };
;     const bool odd = lane & 1;
;     const int rowp = (int)xq((unsigned)row);
;     unsigned char* plo = Bq + (size_t)(odd ? rowp : row) * 1024 + 128 * wave + (odd ? 16 : 0);
;     unsigned char* phi = Bq + (size_t)(odd ? row : rowp) * 1024 + 128 * wave + (odd ? 16 : 0);
;     auto packc = [&](int c) { u32x4 o;
;         if (FP8) { o.x = f8x4(v[16 * c], v[16 * c + 1], v[16 * c + 2], v[16 * c + 3], inv); o.y = f8x4(v[16 * c + 4], v[16 * c + 5], v[16 * c + 6], v[16 * c + 7], inv);
;                    o.z = f8x4(v[16 * c + 8], v[16 * c + 9], v[16 * c + 10], v[16 * c + 11], inv); o.w = f8x4(v[16 * c + 12], v[16 * c + 13], v[16 * c + 14], v[16 * c + 15], inv); }
;         else { o.x = q8x4(v[16 * c], v[16 * c + 1], v[16 * c + 2], v[16 * c + 3], inv); o.y = q8x4(v[16 * c + 4], v[16 * c + 5], v[16 * c + 6], v[16 * c + 7], inv);
;                o.z = q8x4(v[16 * c + 8], v[16 * c + 9], v[16 * c + 10], v[16 * c + 11], inv); o.w = q8x4(v[16 * c + 12], v[16 * c + 13], v[16 * c + 14], v[16 * c + 15], inv); }
;         return o; };
; #pragma unroll
;     for (int j = 0; j < 4; ++j) { const u32x4 p0 = packc(2 * j), p1 = packc(2 * j + 1);
;         u32x4 snd, rcv;
; #pragma unroll
;         for (int q = 0; q < 4; ++q) { snd[q] = odd ? p0[q] : p1[q]; rcv[q] = xq(snd[q]); }
;         u32x4 a, b;
; #pragma unroll
;         for (int q = 0; q < 4; ++q) { a[q] = odd ? rcv[q] : p0[q]; b[q] = odd ? p1[q] : rcv[q]; }
;         *(u32x4*)(plo + 32 * j) = a; *(u32x4*)(phi + 32 * j) = b; }
	ds_read2st64_b32 v[2:3], v141 offset1:1
	s_waitcnt lgkmcnt(0)
	v_max3_f32 v5, v5, v2, v3
	ds_read2st64_b32 v[2:3], v141 offset0:2 offset1:3
	s_waitcnt lgkmcnt(0)
	v_max3_f32 v5, v5, v2, v3
	ds_read2st64_b32 v[2:3], v141 offset0:4 offset1:5
	s_waitcnt lgkmcnt(0)
	v_max3_f32 v5, v5, v2, v3
	ds_read2st64_b32 v[2:3], v141 offset0:6 offset1:7
	s_waitcnt lgkmcnt(0)
	v_max3_f32 v2, v5, v2, v3
	v_cmp_lt_f32_e32 vcc, 0, v2
	v_mul_f32_e32 v2, 0x3b800000, v2
	s_nop 0
	v_cndmask_b32_e32 v141, 1.0, v2, vcc
	v_div_scale_f32 v2, s[42:43], v141, v141, 1.0
	v_rcp_f32_e32 v3, v2
	s_nop 0
	v_fma_f32 v5, -v2, v3, 1.0
	v_fmac_f32_e32 v3, v5, v3
	v_div_scale_f32 v5, vcc, 1.0, v141, 1.0
	v_mul_f32_e32 v142, v5, v3
	v_fma_f32 v143, -v2, v142, v5
	v_fmac_f32_e32 v142, v143, v3
	v_fma_f32 v2, -v2, v142, v5
	v_div_fmas_f32 v2, v2, v3, v142
	v_div_fixup_f32 v142, v2, v141, 1.0
	v_mul_f32_e32 v11, v11, v142
	v_mul_f32_e32 v13, v13, v142
	v_mov_b32_e32 v143, v33
	v_cvt_pk_fp8_f32 v143, v11, v13
	v_mul_f32_e32 v11, v12, v142
	v_mul_f32_e32 v12, v16, v142
	v_mov_b32_e32 v13, v33
	v_cvt_pk_fp8_f32 v143, v11, v12 op_sel:[0,0,1]
	v_mul_f32_e32 v11, v14, v142
	v_mul_f32_e32 v12, v17, v142
	v_cvt_pk_fp8_f32 v13, v11, v12
	v_mul_f32_e32 v11, v15, v142
	v_mul_f32_e32 v12, v19, v142
	v_mov_b32_e32 v14, v33
	v_cvt_pk_fp8_f32 v13, v11, v12 op_sel:[0,0,1]
	v_mul_f32_e32 v11, v18, v142
	v_mul_f32_e32 v12, v21, v142
	v_cvt_pk_fp8_f32 v14, v11, v12
	v_mul_f32_e32 v11, v20, v142
	v_mul_f32_e32 v12, v23, v142
	v_mov_b32_e32 v15, v33
	v_cvt_pk_fp8_f32 v14, v11, v12 op_sel:[0,0,1]
	v_mul_f32_e32 v11, v22, v142
	v_mul_f32_e32 v12, v27, v142
	v_cvt_pk_fp8_f32 v15, v11, v12
	v_mul_f32_e32 v11, v24, v142
	v_mul_f32_e32 v12, v26, v142
	v_mov_b32_e32 v16, v33
	v_cvt_pk_fp8_f32 v15, v11, v12 op_sel:[0,0,1]
	v_mul_f32_e32 v11, v25, v142
	v_mul_f32_e32 v12, v29, v142
	v_cvt_pk_fp8_f32 v16, v11, v12
	v_mul_f32_e32 v11, v28, v142
	v_mul_f32_e32 v12, v31, v142
	v_mov_b32_e32 v17, v33
	v_cvt_pk_fp8_f32 v16, v11, v12 op_sel:[0,0,1]
	v_mul_f32_e32 v11, v30, v142
	v_mul_f32_e32 v12, v37, v142
	v_cvt_pk_fp8_f32 v17, v11, v12
	v_mul_f32_e32 v11, v34, v142
	v_mul_f32_e32 v12, v36, v142
	v_mov_b32_e32 v18, v33
	v_cvt_pk_fp8_f32 v17, v11, v12 op_sel:[0,0,1]
	v_mul_f32_e32 v11, v35, v142
	v_mul_f32_e32 v12, v39, v142
	v_cvt_pk_fp8_f32 v18, v11, v12
	v_mul_f32_e32 v11, v38, v142
	v_mul_f32_e32 v12, v42, v142
	v_mov_b32_e32 v19, v33
	v_cvt_pk_fp8_f32 v18, v11, v12 op_sel:[0,0,1]
	v_mul_f32_e32 v11, v40, v142
	v_mul_f32_e32 v12, v49, v142
	v_add_u16_e32 v2, s18, v6
	v_cvt_pk_fp8_f32 v19, v11, v12
	v_lshrrev_b16_e32 v2, 1, v2
	v_and_b32_e32 v2, 0x78, v2
	v_and_b32_e32 v3, 0x707, v4
	v_or3_b32 v4, v3, v8, v2
	v_mul_f32_e32 v11, v47, v142
	v_mul_f32_e32 v12, v48, v142
	v_mov_b32_dpp v5, v4 quad_perm:[1,0,3,2] row_mask:0xf bank_mask:0xf bound_ctrl:1
	v_cvt_pk_fp8_f32 v19, v11, v12 op_sel:[0,0,1]
	v_cndmask_b32_e64 v2, v5, v4, s[4:5]
	v_ashrrev_i32_e32 v3, 31, v2
	v_cndmask_b32_e64 v4, v4, v5, s[4:5]
	v_cndmask_b32_e64 v12, v13, v17, s[4:5]
	v_lshlrev_b64 v[2:3], 10, v[2:3]
	v_readlane_b32 s18, v252, 31
	v_ashrrev_i32_e32 v5, 31, v4
	v_mov_b32_dpp v20, v12 quad_perm:[1,0,3,2] row_mask:0xf bank_mask:0xf bound_ctrl:1
	v_cndmask_b32_e64 v12, v14, v18, s[4:5]
	v_lshl_add_u64 v[2:3], s[46:47], 0, v[2:3]
	v_readlane_b32 s19, v252, 32
	v_lshlrev_b64 v[4:5], 10, v[4:5]
	v_cndmask_b32_e64 v11, v143, v16, s[4:5]
	v_mov_b32_dpp v21, v12 quad_perm:[1,0,3,2] row_mask:0xf bank_mask:0xf bound_ctrl:1
	v_cndmask_b32_e64 v12, v15, v19, s[4:5]
	v_lshl_add_u64 v[2:3], v[2:3], 0, s[18:19]
	v_lshl_add_u64 v[4:5], s[46:47], 0, v[4:5]
	v_mov_b32_dpp v11, v11 quad_perm:[1,0,3,2] row_mask:0xf bank_mask:0xf bound_ctrl:1
	v_mov_b32_dpp v22, v12 quad_perm:[1,0,3,2] row_mask:0xf bank_mask:0xf bound_ctrl:1
	v_lshl_add_u64 v[2:3], v[2:3], 0, v[0:1]
	v_lshl_add_u64 v[4:5], v[4:5], 0, s[18:19]
	v_cndmask_b32_e64 v12, v11, v143, s[4:5]
	v_cndmask_b32_e64 v13, v20, v13, s[4:5]
	v_cndmask_b32_e64 v14, v21, v14, s[4:5]
	v_cndmask_b32_e64 v15, v22, v15, s[4:5]
	v_lshl_add_u64 v[4:5], v[4:5], 0, v[0:1]
	v_cndmask_b32_e64 v16, v16, v11, s[4:5]
	v_cndmask_b32_e64 v17, v17, v20, s[4:5]
	v_cndmask_b32_e64 v18, v18, v21, s[4:5]
	v_cndmask_b32_e64 v19, v19, v22, s[4:5]
	global_store_dwordx4 v[2:3], v[12:15], off
	global_store_dwordx4 v[4:5], v[16:19], off
	v_mul_f32_e32 v11, v41, v142
	v_mul_f32_e32 v12, v44, v142
	v_mov_b32_e32 v13, v33
	v_cvt_pk_fp8_f32 v13, v11, v12
	v_mul_f32_e32 v11, v43, v142
	v_mul_f32_e32 v12, v46, v142
	v_mov_b32_e32 v14, v33
	v_cvt_pk_fp8_f32 v13, v11, v12 op_sel:[0,0,1]
	v_mul_f32_e32 v11, v45, v142
	v_mul_f32_e32 v12, v53, v142
	v_cvt_pk_fp8_f32 v14, v11, v12
	v_mul_f32_e32 v11, v50, v142
	v_mul_f32_e32 v12, v52, v142
	v_mov_b32_e32 v15, v33
	v_cvt_pk_fp8_f32 v14, v11, v12 op_sel:[0,0,1]
	v_mul_f32_e32 v11, v51, v142
	v_mul_f32_e32 v12, v55, v142
	v_cvt_pk_fp8_f32 v15, v11, v12
	v_mul_f32_e32 v11, v54, v142
	v_mul_f32_e32 v12, v57, v142
	v_mov_b32_e32 v19, v33
	v_cvt_pk_fp8_f32 v15, v11, v12 op_sel:[0,0,1]
	v_mul_f32_e32 v11, v56, v142
	v_mul_f32_e32 v12, v61, v142
	v_cvt_pk_fp8_f32 v19, v11, v12
	v_mul_f32_e32 v11, v58, v142
	v_mul_f32_e32 v12, v60, v142
	v_mov_b32_e32 v16, v33
	v_cvt_pk_fp8_f32 v19, v11, v12 op_sel:[0,0,1]
	v_mul_f32_e32 v11, v59, v142
	v_mul_f32_e32 v12, v63, v142
	v_cvt_pk_fp8_f32 v16, v11, v12
	v_mul_f32_e32 v11, v62, v142
	v_mul_f32_e32 v12, v65, v142
	v_mov_b32_e32 v17, v33
	v_cvt_pk_fp8_f32 v16, v11, v12 op_sel:[0,0,1]
	v_mul_f32_e32 v11, v64, v142
	v_mul_f32_e32 v12, v69, v142
	v_cvt_pk_fp8_f32 v17, v11, v12
	v_mul_f32_e32 v11, v66, v142
	v_mul_f32_e32 v12, v68, v142
	v_mov_b32_e32 v18, v33
; template <bool PERMGL, bool FP8>
; __device__ __forceinline__ void q8_cols_item(const float* W, int N, int n0, unsigned char* Bq, float* sc_out, LAS float* AM, int par, int wave, int lane) {
;     ...
;     auto packc = [&](int c) { u32x4 o;
;         if (FP8) { o.x = f8x4(v[16 * c], v[16 * c + 1], v[16 * c + 2], v[16 * c + 3], inv); o.y = f8x4(v[16 * c + 4], v[16 * c + 5], v[16 * c + 6], v[16 * c + 7], inv);
;                    o.z = f8x4(v[16 * c + 8], v[16 * c + 9], v[16 * c + 10], v[16 * c + 11], inv); o.w = f8x4(v[16 * c + 12], v[16 * c + 13], v[16 * c + 14], v[16 * c + 15], inv); }
;         else { o.x = q8x4(v[16 * c], v[16 * c + 1], v[16 * c + 2], v[16 * c + 3], inv); o.y = q8x4(v[16 * c + 4], v[16 * c + 5], v[16 * c + 6], v[16 * c + 7], inv);
;                o.z = q8x4(v[16 * c + 8], v[16 * c + 9], v[16 * c + 10], v[16 * c + 11], inv); o.w = q8x4(v[16 * c + 12], v[16 * c + 13], v[16 * c + 14], v[16 * c + 15], inv); }
;         return o; };
; #pragma unroll
;     for (int j = 0; j < 4; ++j) { const u32x4 p0 = packc(2 * j), p1 = packc(2 * j + 1);
;         u32x4 snd, rcv;
; #pragma unroll
;         for (int q = 0; q < 4; ++q) { snd[q] = odd ? p0[q] : p1[q]; rcv[q] = xq(snd[q]); }
;         u32x4 a, b;
; #pragma unroll
;         for (int q = 0; q < 4; ++q) { a[q] = odd ? rcv[q] : p0[q]; b[q] = odd ? p1[q] : rcv[q]; }
;         *(u32x4*)(plo + 32 * j) = a; *(u32x4*)(phi + 32 * j) = b; }
	v_cvt_pk_fp8_f32 v17, v11, v12 op_sel:[0,0,1]
	v_mul_f32_e32 v11, v67, v142
	v_mul_f32_e32 v12, v71, v142
	v_cvt_pk_fp8_f32 v18, v11, v12
	v_mul_f32_e32 v11, v70, v142
	v_mul_f32_e32 v12, v74, v142
	v_mov_b32_e32 v20, v33
	v_cvt_pk_fp8_f32 v18, v11, v12 op_sel:[0,0,1]
	v_mul_f32_e32 v11, v72, v142
	v_mul_f32_e32 v12, v81, v142
	v_cvt_pk_fp8_f32 v20, v11, v12
	v_mul_f32_e32 v11, v79, v142
	v_mul_f32_e32 v12, v80, v142
	s_and_b64 vcc, exec, s[0:1]
	v_cvt_pk_fp8_f32 v20, v11, v12 op_sel:[0,0,1]
	v_cndmask_b32_e64 v12, v14, v17, s[4:5]
	v_cndmask_b32_e64 v11, v13, v16, s[4:5]
	s_nop 0
	v_mov_b32_dpp v21, v12 quad_perm:[1,0,3,2] row_mask:0xf bank_mask:0xf bound_ctrl:1
	v_cndmask_b32_e64 v12, v15, v18, s[4:5]
	v_mov_b32_dpp v11, v11 quad_perm:[1,0,3,2] row_mask:0xf bank_mask:0xf bound_ctrl:1
	v_cndmask_b32_e64 v16, v16, v11, s[4:5]
	v_mov_b32_dpp v22, v12 quad_perm:[1,0,3,2] row_mask:0xf bank_mask:0xf bound_ctrl:1
	v_cndmask_b32_e64 v12, v19, v20, s[4:5]
	v_cndmask_b32_e64 v17, v17, v21, s[4:5]
	v_cndmask_b32_e64 v18, v18, v22, s[4:5]
	v_mov_b32_dpp v23, v12 quad_perm:[1,0,3,2] row_mask:0xf bank_mask:0xf bound_ctrl:1
	v_cndmask_b32_e64 v12, v11, v13, s[4:5]
	v_cndmask_b32_e64 v13, v21, v14, s[4:5]
	v_cndmask_b32_e64 v14, v22, v15, s[4:5]
	v_cndmask_b32_e64 v15, v23, v19, s[4:5]
	v_cndmask_b32_e64 v19, v20, v23, s[4:5]
	global_store_dwordx4 v[2:3], v[12:15], off offset:32
	global_store_dwordx4 v[4:5], v[16:19], off offset:32
	v_mul_f32_e32 v11, v73, v142
	v_mul_f32_e32 v12, v76, v142
	v_mov_b32_e32 v13, v33
	v_cvt_pk_fp8_f32 v13, v11, v12
	v_mul_f32_e32 v11, v75, v142
	v_mul_f32_e32 v12, v78, v142
	v_mov_b32_e32 v14, v33
	v_cvt_pk_fp8_f32 v13, v11, v12 op_sel:[0,0,1]
	v_mul_f32_e32 v11, v77, v142
	v_mul_f32_e32 v12, v85, v142
	v_cvt_pk_fp8_f32 v14, v11, v12
	v_mul_f32_e32 v11, v82, v142
	v_mul_f32_e32 v12, v84, v142
	v_mov_b32_e32 v15, v33
	v_cvt_pk_fp8_f32 v14, v11, v12 op_sel:[0,0,1]
	v_mul_f32_e32 v11, v83, v142
	v_mul_f32_e32 v12, v87, v142
	v_cvt_pk_fp8_f32 v15, v11, v12
	v_mul_f32_e32 v11, v86, v142
	v_mul_f32_e32 v12, v89, v142
	v_mov_b32_e32 v19, v33
	v_cvt_pk_fp8_f32 v15, v11, v12 op_sel:[0,0,1]
	v_mul_f32_e32 v11, v88, v142
	v_mul_f32_e32 v12, v93, v142
	v_cvt_pk_fp8_f32 v19, v11, v12
	v_mul_f32_e32 v11, v90, v142
	v_mul_f32_e32 v12, v92, v142
	v_mov_b32_e32 v16, v33
	v_cvt_pk_fp8_f32 v19, v11, v12 op_sel:[0,0,1]
	v_mul_f32_e32 v11, v91, v142
	v_mul_f32_e32 v12, v95, v142
	v_cvt_pk_fp8_f32 v16, v11, v12
	v_mul_f32_e32 v11, v94, v142
	v_mul_f32_e32 v12, v97, v142
	v_mov_b32_e32 v17, v33
	v_cvt_pk_fp8_f32 v16, v11, v12 op_sel:[0,0,1]
	v_mul_f32_e32 v11, v96, v142
	v_mul_f32_e32 v12, v101, v142
	v_cvt_pk_fp8_f32 v17, v11, v12
	v_mul_f32_e32 v11, v98, v142
	v_mul_f32_e32 v12, v100, v142
	v_mov_b32_e32 v18, v33
	v_cvt_pk_fp8_f32 v17, v11, v12 op_sel:[0,0,1]
	v_mul_f32_e32 v11, v99, v142
	v_mul_f32_e32 v12, v103, v142
	v_cvt_pk_fp8_f32 v18, v11, v12
	v_mul_f32_e32 v11, v102, v142
	v_mul_f32_e32 v12, v106, v142
	v_mov_b32_e32 v20, v33
	v_cvt_pk_fp8_f32 v18, v11, v12 op_sel:[0,0,1]
	v_mul_f32_e32 v11, v104, v142
	v_mul_f32_e32 v12, v113, v142
	v_cvt_pk_fp8_f32 v20, v11, v12
	v_mul_f32_e32 v11, v111, v142
	v_mul_f32_e32 v12, v112, v142
	v_cvt_pk_fp8_f32 v20, v11, v12 op_sel:[0,0,1]
	v_cndmask_b32_e64 v12, v14, v17, s[4:5]
	v_cndmask_b32_e64 v11, v13, v16, s[4:5]
	s_nop 0
	v_mov_b32_dpp v21, v12 quad_perm:[1,0,3,2] row_mask:0xf bank_mask:0xf bound_ctrl:1
	v_cndmask_b32_e64 v12, v15, v18, s[4:5]
	v_mov_b32_dpp v11, v11 quad_perm:[1,0,3,2] row_mask:0xf bank_mask:0xf bound_ctrl:1
	v_cndmask_b32_e64 v16, v16, v11, s[4:5]
	v_mov_b32_dpp v22, v12 quad_perm:[1,0,3,2] row_mask:0xf bank_mask:0xf bound_ctrl:1
	v_cndmask_b32_e64 v12, v19, v20, s[4:5]
	v_cndmask_b32_e64 v17, v17, v21, s[4:5]
	v_cndmask_b32_e64 v18, v18, v22, s[4:5]
	v_mov_b32_dpp v23, v12 quad_perm:[1,0,3,2] row_mask:0xf bank_mask:0xf bound_ctrl:1
	v_cndmask_b32_e64 v12, v11, v13, s[4:5]
	v_cndmask_b32_e64 v13, v21, v14, s[4:5]
	v_cndmask_b32_e64 v14, v22, v15, s[4:5]
	v_cndmask_b32_e64 v15, v23, v19, s[4:5]
	v_cndmask_b32_e64 v19, v20, v23, s[4:5]
	global_store_dwordx4 v[2:3], v[12:15], off offset:64
	global_store_dwordx4 v[4:5], v[16:19], off offset:64
	v_mul_f32_e32 v11, v105, v142
	v_mul_f32_e32 v12, v108, v142
	v_mov_b32_e32 v13, v33
	v_cvt_pk_fp8_f32 v13, v11, v12
	v_mul_f32_e32 v11, v107, v142
	v_mul_f32_e32 v12, v110, v142
	v_mov_b32_e32 v14, v33
	v_cvt_pk_fp8_f32 v13, v11, v12 op_sel:[0,0,1]
	v_mul_f32_e32 v11, v109, v142
	v_mul_f32_e32 v12, v117, v142
	v_cvt_pk_fp8_f32 v14, v11, v12
	v_mul_f32_e32 v11, v114, v142
	v_mul_f32_e32 v12, v116, v142
	v_mov_b32_e32 v15, v33
	v_cvt_pk_fp8_f32 v14, v11, v12 op_sel:[0,0,1]
	v_mul_f32_e32 v11, v115, v142
	v_mul_f32_e32 v12, v119, v142
	v_cvt_pk_fp8_f32 v15, v11, v12
	v_mul_f32_e32 v11, v118, v142
	v_mul_f32_e32 v12, v121, v142
	v_mov_b32_e32 v19, v33
	v_cvt_pk_fp8_f32 v15, v11, v12 op_sel:[0,0,1]
	v_mul_f32_e32 v11, v120, v142
	v_mul_f32_e32 v12, v125, v142
	v_cvt_pk_fp8_f32 v19, v11, v12
	v_mul_f32_e32 v11, v122, v142
	v_mul_f32_e32 v12, v124, v142
	v_mov_b32_e32 v16, v33
	v_cvt_pk_fp8_f32 v19, v11, v12 op_sel:[0,0,1]
	v_mul_f32_e32 v11, v123, v142
	v_mul_f32_e32 v12, v127, v142
	v_cvt_pk_fp8_f32 v16, v11, v12
	v_mul_f32_e32 v11, v126, v142
	v_mul_f32_e32 v12, v129, v142
	v_mov_b32_e32 v17, v33
	v_cvt_pk_fp8_f32 v16, v11, v12 op_sel:[0,0,1]
	v_mul_f32_e32 v11, v128, v142
	v_mul_f32_e32 v12, v133, v142
	v_cvt_pk_fp8_f32 v17, v11, v12
	v_mul_f32_e32 v11, v130, v142
	v_mul_f32_e32 v12, v132, v142
	v_mov_b32_e32 v18, v33
	v_cvt_pk_fp8_f32 v17, v11, v12 op_sel:[0,0,1]
	v_mul_f32_e32 v11, v131, v142
	v_mul_f32_e32 v12, v135, v142
	v_cvt_pk_fp8_f32 v18, v11, v12
	v_mul_f32_e32 v11, v134, v142
	v_mul_f32_e32 v12, v137, v142
	v_mov_b32_e32 v20, v33
	v_cvt_pk_fp8_f32 v18, v11, v12 op_sel:[0,0,1]
	v_mul_f32_e32 v11, v136, v142
	v_mul_f32_e32 v12, v139, v142
	v_cvt_pk_fp8_f32 v20, v11, v12
	v_mul_f32_e32 v11, v138, v142
	v_mul_f32_e32 v12, v140, v142
	v_cvt_pk_fp8_f32 v20, v11, v12 op_sel:[0,0,1]
	v_cndmask_b32_e64 v12, v14, v17, s[4:5]
	v_cndmask_b32_e64 v11, v13, v16, s[4:5]
	s_nop 0
	v_mov_b32_dpp v21, v12 quad_perm:[1,0,3,2] row_mask:0xf bank_mask:0xf bound_ctrl:1
	v_cndmask_b32_e64 v12, v15, v18, s[4:5]
	v_mov_b32_dpp v11, v11 quad_perm:[1,0,3,2] row_mask:0xf bank_mask:0xf bound_ctrl:1
	v_cndmask_b32_e64 v16, v16, v11, s[4:5]
	v_mov_b32_dpp v22, v12 quad_perm:[1,0,3,2] row_mask:0xf bank_mask:0xf bound_ctrl:1
	v_cndmask_b32_e64 v12, v19, v20, s[4:5]
	v_cndmask_b32_e64 v17, v17, v21, s[4:5]
	v_cndmask_b32_e64 v18, v18, v22, s[4:5]
	v_mov_b32_dpp v23, v12 quad_perm:[1,0,3,2] row_mask:0xf bank_mask:0xf bound_ctrl:1
	v_cndmask_b32_e64 v12, v11, v13, s[4:5]
	v_cndmask_b32_e64 v13, v21, v14, s[4:5]
	v_cndmask_b32_e64 v14, v22, v15, s[4:5]
	v_cndmask_b32_e64 v15, v23, v19, s[4:5]
	v_cndmask_b32_e64 v19, v20, v23, s[4:5]
	global_store_dwordx4 v[2:3], v[12:15], off offset:96
	global_store_dwordx4 v[4:5], v[16:19], off offset:96
	s_cbranch_vccnz .LBB0_130
; template <bool PERMGL, bool FP8>
; __device__ __forceinline__ void q8_cols_item(const float* W, int N, int n0, unsigned char* Bq, float* sc_out, LAS float* AM, int par, int wave, int lane) {
;     ...
;     if (wave == 0) sc_out[PERMGL ? row : n] = FP8 ? sc * 16.0f : sc;
	s_lshl_b64 s[18:19], s[68:69], 12
	v_readlane_b32 s42, v252, 60
	s_add_u32 s18, s42, s18
	v_readlane_b32 s42, v252, 61
	s_addc_u32 s19, s42, s19
	v_mul_f32_e32 v2, 0x41800000, v141
	global_store_dword v32, v2, s[18:19]

; template <bool PERMGL, bool FP8>
; __device__ __forceinline__ void q8_cols_item(const float* W, int N, int n0, unsigned char* Bq, float* sc_out, LAS float* AM, int par, int wave, int lane) {
;     const int n = n0 + lane;
;     const float* Wp = W + (size_t)(128 * wave) * N + n;
;     float v[128]; float am = 0.f;
; #pragma unroll
;     for (int i = 0; i < 128; ++i) v[i] = Wp[(size_t)i * N];
; __global__ void __launch_bounds__(NWAVES * 64, 2) mk_fwd(Args args) {
;     ...
;                             if (r < 1024) { const int mi = lyr * 32 + (r >> 5), nb = ((r & 31) + 8 * ((r >> 6) & 3)) & 31;
;                                 q8_cols_item<true, false>(args.in[11] + (size_t)mi * D * 2048, 2048, nb * 64, ws + WS_WGU + (size_t)mi * 2048 * 1024, (float*)(ws + WS_SB) + (size_t)mi * 2048, CAM, cv_par, wave, lane); }
.LBB0_131:
	s_andn2_b64 vcc, exec, s[18:19]
	s_cbranch_vccnz .LBB0_126
	s_lshl_b32 s18, s29, 9
	s_ashr_i32 s76, s27, 5
	s_add_i32 s18, s25, s18
	s_ashr_i32 s77, s76, 31
	s_lshl_b64 s[42:43], s[76:77], 23
	s_and_b32 s18, s18, 0x7c0
	s_lshl_b64 s[46:47], s[76:77], 21
	v_readlane_b32 s19, v253, 8
	s_add_u32 s46, s19, s46
	v_readlane_b32 s19, v254, 26
	s_addc_u32 s47, s19, s47
	v_readlane_b32 s19, v252, 62
	v_add_u32_e32 v4, s18, v6
	s_add_u32 s42, s19, s42
	v_readlane_b32 s19, v253, 0
	s_addc_u32 s43, s19, s43
	v_lshlrev_b32_e32 v32, 2, v4
	v_lshl_add_u64 v[2:3], s[42:43], 0, v[32:33]
	s_movk_i32 s19, 0x2000
	v_add_co_u32_e32 v12, vcc, s19, v2
	s_movk_i32 s19, 0x4000
	s_nop 0
	v_addc_co_u32_e32 v13, vcc, 0, v3, vcc
	v_add_co_u32_e32 v14, vcc, s19, v2
	s_movk_i32 s19, 0x6000
	s_nop 0
	v_addc_co_u32_e32 v15, vcc, 0, v3, vcc
	global_load_dword v11, v32, s[42:43] nt
	s_nop 0
	global_load_dword v12, v[12:13], off nt
	s_nop 0
	global_load_dword v13, v[14:15], off nt
	v_add_co_u32_e32 v14, vcc, s19, v2
	s_mov_b32 s19, 0x8000
	s_nop 0
	v_addc_co_u32_e32 v15, vcc, 0, v3, vcc
	v_add_co_u32_e32 v16, vcc, s19, v2
	s_mov_b32 s19, 0xa000
	s_nop 0
	v_addc_co_u32_e32 v17, vcc, 0, v3, vcc
	global_load_dword v14, v[14:15], off nt
	s_nop 0
	global_load_dword v15, v[16:17], off nt
	v_add_co_u32_e32 v16, vcc, s19, v2
	s_mov_b32 s19, 0xc000
	s_nop 0
	v_addc_co_u32_e32 v17, vcc, 0, v3, vcc
	v_add_co_u32_e32 v18, vcc, s19, v2
	s_mov_b32 s19, 0xe000
	s_nop 0
	v_addc_co_u32_e32 v19, vcc, 0, v3, vcc
	global_load_dword v16, v[16:17], off nt
	s_nop 0
	global_load_dword v17, v[18:19], off nt
	v_add_co_u32_e32 v18, vcc, s19, v2
	s_mov_b32 s19, 0x10000
	s_nop 0
	v_addc_co_u32_e32 v19, vcc, 0, v3, vcc
	v_add_co_u32_e32 v20, vcc, s19, v2
	s_mov_b32 s19, 0x12000
	s_nop 0
	v_addc_co_u32_e32 v21, vcc, 0, v3, vcc
	global_load_dword v18, v[18:19], off nt
	s_nop 0
	global_load_dword v19, v[20:21], off nt
	v_add_co_u32_e32 v20, vcc, s19, v2
	s_mov_b32 s19, 0x14000
	s_nop 0
	v_addc_co_u32_e32 v21, vcc, 0, v3, vcc
	v_add_co_u32_e32 v22, vcc, s19, v2
	s_mov_b32 s19, 0x16000
	s_nop 0
	v_addc_co_u32_e32 v23, vcc, 0, v3, vcc
	global_load_dword v20, v[20:21], off nt
	s_nop 0
	global_load_dword v21, v[22:23], off nt
	v_add_co_u32_e32 v22, vcc, s19, v2
	s_mov_b32 s19, 0x18000
	s_nop 0
	v_addc_co_u32_e32 v23, vcc, 0, v3, vcc
	v_add_co_u32_e32 v24, vcc, s19, v2
	s_mov_b32 s19, 0x1a000
	s_nop 0
	v_addc_co_u32_e32 v25, vcc, 0, v3, vcc
	global_load_dword v22, v[22:23], off nt
	s_nop 0
	global_load_dword v23, v[24:25], off nt
	v_add_co_u32_e32 v24, vcc, s19, v2
	s_mov_b32 s19, 0x1c000
	s_nop 0
	v_addc_co_u32_e32 v25, vcc, 0, v3, vcc
	v_add_co_u32_e32 v26, vcc, s19, v2
	s_mov_b32 s19, 0x1e000
	s_nop 0
	v_addc_co_u32_e32 v27, vcc, 0, v3, vcc
	global_load_dword v24, v[24:25], off nt
	s_nop 0
	global_load_dword v25, v[26:27], off nt
	v_add_co_u32_e32 v26, vcc, s19, v2
	s_mov_b32 s19, 0x20000
	s_nop 0
	v_addc_co_u32_e32 v27, vcc, 0, v3, vcc
	v_add_co_u32_e32 v28, vcc, s19, v2
	s_mov_b32 s19, 0x22000
	s_nop 0
	v_addc_co_u32_e32 v29, vcc, 0, v3, vcc
	global_load_dword v26, v[26:27], off nt
	s_nop 0
	global_load_dword v27, v[28:29], off nt
	v_add_co_u32_e32 v28, vcc, s19, v2
	s_mov_b32 s19, 0x24000
	s_nop 0
	v_addc_co_u32_e32 v29, vcc, 0, v3, vcc
	v_add_co_u32_e32 v30, vcc, s19, v2
	s_mov_b32 s19, 0x26000
	s_nop 0
	v_addc_co_u32_e32 v31, vcc, 0, v3, vcc
	global_load_dword v28, v[28:29], off nt
	s_nop 0
	global_load_dword v29, v[30:31], off nt
	v_add_co_u32_e32 v30, vcc, s19, v2
	s_mov_b32 s19, 0x28000
	s_nop 0
	v_addc_co_u32_e32 v31, vcc, 0, v3, vcc
	v_add_co_u32_e32 v34, vcc, s19, v2
	s_mov_b32 s19, 0x2a000
	s_nop 0
	v_addc_co_u32_e32 v35, vcc, 0, v3, vcc
	global_load_dword v30, v[30:31], off nt
	s_nop 0
	global_load_dword v31, v[34:35], off nt
	v_add_co_u32_e32 v34, vcc, s19, v2
	s_mov_b32 s19, 0x2c000
	s_nop 0
	v_addc_co_u32_e32 v35, vcc, 0, v3, vcc
	global_load_dword v32, v[34:35], off nt
	v_add_co_u32_e32 v34, vcc, s19, v2
	s_mov_b32 s19, 0x2e000
	s_nop 0
	v_addc_co_u32_e32 v35, vcc, 0, v3, vcc
	v_add_co_u32_e32 v36, vcc, s19, v2
	s_mov_b32 s19, 0x30000
	s_nop 0
	v_addc_co_u32_e32 v37, vcc, 0, v3, vcc
	global_load_dword v34, v[34:35], off nt
	s_nop 0
	global_load_dword v35, v[36:37], off nt
	v_add_co_u32_e32 v36, vcc, s19, v2
	s_mov_b32 s19, 0x32000
	s_nop 0
	v_addc_co_u32_e32 v37, vcc, 0, v3, vcc
	v_add_co_u32_e32 v38, vcc, s19, v2
	s_mov_b32 s19, 0x34000
	s_nop 0
	v_addc_co_u32_e32 v39, vcc, 0, v3, vcc
	global_load_dword v36, v[36:37], off nt
	s_nop 0
	global_load_dword v37, v[38:39], off nt
	v_add_co_u32_e32 v38, vcc, s19, v2
	s_mov_b32 s19, 0x36000
	s_nop 0
	v_addc_co_u32_e32 v39, vcc, 0, v3, vcc
	v_add_co_u32_e32 v40, vcc, s19, v2
	s_mov_b32 s19, 0x38000
	s_nop 0
	v_addc_co_u32_e32 v41, vcc, 0, v3, vcc
	global_load_dword v38, v[38:39], off nt
	s_nop 0
	global_load_dword v39, v[40:41], off nt
	v_add_co_u32_e32 v40, vcc, s19, v2
	s_mov_b32 s19, 0x3a000
	s_nop 0
	v_addc_co_u32_e32 v41, vcc, 0, v3, vcc
	v_add_co_u32_e32 v42, vcc, s19, v2
	s_mov_b32 s19, 0x3c000
	s_nop 0
	v_addc_co_u32_e32 v43, vcc, 0, v3, vcc
	v_add_co_u32_e32 v44, vcc, s19, v2
	s_mov_b32 s19, 0x3e000
	s_nop 0
	v_addc_co_u32_e32 v45, vcc, 0, v3, vcc
	v_add_co_u32_e32 v46, vcc, s19, v2
	s_mov_b32 s19, 0x40000
	s_nop 0
	v_addc_co_u32_e32 v47, vcc, 0, v3, vcc
	v_add_co_u32_e32 v48, vcc, s19, v2
	s_mov_b32 s19, 0x42000
	s_nop 0
	v_addc_co_u32_e32 v49, vcc, 0, v3, vcc
	global_load_dword v40, v[40:41], off nt
	s_nop 0
	global_load_dword v42, v[42:43], off nt
	s_nop 0
	global_load_dword v44, v[44:45], off nt
	s_nop 0
	global_load_dword v46, v[46:47], off nt
	s_nop 0
	global_load_dword v41, v[48:49], off nt
	v_add_co_u32_e32 v48, vcc, s19, v2
; template <bool PERMGL, bool FP8>
; __device__ __forceinline__ void q8_cols_item(const float* W, int N, int n0, unsigned char* Bq, float* sc_out, LAS float* AM, int par, int wave, int lane) {
;     ...
;     for (int i = 0; i < 128; ++i) v[i] = Wp[(size_t)i * N];
	s_mov_b32 s19, 0x44000
	s_nop 0
	v_addc_co_u32_e32 v49, vcc, 0, v3, vcc
	global_load_dword v43, v[48:49], off nt
	v_add_co_u32_e32 v48, vcc, s19, v2
	s_mov_b32 s19, 0x46000
	s_nop 0
	v_addc_co_u32_e32 v49, vcc, 0, v3, vcc
	global_load_dword v45, v[48:49], off nt
	v_add_co_u32_e32 v48, vcc, s19, v2
	s_mov_b32 s19, 0x48000
	s_nop 0
	v_addc_co_u32_e32 v49, vcc, 0, v3, vcc
	global_load_dword v47, v[48:49], off nt
	v_add_co_u32_e32 v48, vcc, s19, v2
	s_mov_b32 s19, 0x4a000
	s_nop 0
	v_addc_co_u32_e32 v49, vcc, 0, v3, vcc
	v_add_co_u32_e32 v50, vcc, s19, v2
	s_mov_b32 s19, 0x4c000
	s_nop 0
	v_addc_co_u32_e32 v51, vcc, 0, v3, vcc
	global_load_dword v48, v[48:49], off nt
	s_nop 0
	global_load_dword v49, v[50:51], off nt
	v_add_co_u32_e32 v50, vcc, s19, v2
	s_mov_b32 s19, 0x4e000
	s_nop 0
	v_addc_co_u32_e32 v51, vcc, 0, v3, vcc
	v_add_co_u32_e32 v52, vcc, s19, v2
	s_mov_b32 s19, 0x50000
	s_nop 0
	v_addc_co_u32_e32 v53, vcc, 0, v3, vcc
	global_load_dword v50, v[50:51], off nt
	s_nop 0
	global_load_dword v51, v[52:53], off nt
	v_add_co_u32_e32 v52, vcc, s19, v2
	s_mov_b32 s19, 0x52000
	s_nop 0
	v_addc_co_u32_e32 v53, vcc, 0, v3, vcc
	v_add_co_u32_e32 v54, vcc, s19, v2
	s_mov_b32 s19, 0x54000
	s_nop 0
	v_addc_co_u32_e32 v55, vcc, 0, v3, vcc
	global_load_dword v52, v[52:53], off nt
	s_nop 0
	global_load_dword v53, v[54:55], off nt
	v_add_co_u32_e32 v54, vcc, s19, v2
	s_mov_b32 s19, 0x56000
	s_nop 0
	v_addc_co_u32_e32 v55, vcc, 0, v3, vcc
	v_add_co_u32_e32 v56, vcc, s19, v2
	s_mov_b32 s19, 0x58000
	s_nop 0
	v_addc_co_u32_e32 v57, vcc, 0, v3, vcc
	global_load_dword v54, v[54:55], off nt
	s_nop 0
	global_load_dword v55, v[56:57], off nt
	v_add_co_u32_e32 v56, vcc, s19, v2
	s_mov_b32 s19, 0x5a000
	s_nop 0
	v_addc_co_u32_e32 v57, vcc, 0, v3, vcc
	v_add_co_u32_e32 v58, vcc, s19, v2
	s_mov_b32 s19, 0x5c000
	s_nop 0
	v_addc_co_u32_e32 v59, vcc, 0, v3, vcc
	global_load_dword v56, v[56:57], off nt
	s_nop 0
	global_load_dword v57, v[58:59], off nt
	v_add_co_u32_e32 v58, vcc, s19, v2
	s_mov_b32 s19, 0x5e000
	s_nop 0
	v_addc_co_u32_e32 v59, vcc, 0, v3, vcc
	v_add_co_u32_e32 v60, vcc, s19, v2
	s_mov_b32 s19, 0x60000
	s_nop 0
	v_addc_co_u32_e32 v61, vcc, 0, v3, vcc
	global_load_dword v58, v[58:59], off nt
	s_nop 0
	global_load_dword v59, v[60:61], off nt
	v_add_co_u32_e32 v60, vcc, s19, v2
	s_mov_b32 s19, 0x62000
	s_nop 0
	v_addc_co_u32_e32 v61, vcc, 0, v3, vcc
	v_add_co_u32_e32 v62, vcc, s19, v2
	s_mov_b32 s19, 0x64000
	s_nop 0
	v_addc_co_u32_e32 v63, vcc, 0, v3, vcc
	global_load_dword v60, v[60:61], off nt
	s_nop 0
	global_load_dword v61, v[62:63], off nt
	v_add_co_u32_e32 v62, vcc, s19, v2
	s_mov_b32 s19, 0x66000
	s_nop 0
	v_addc_co_u32_e32 v63, vcc, 0, v3, vcc
	v_add_co_u32_e32 v64, vcc, s19, v2
	s_mov_b32 s19, 0x68000
	s_nop 0
	v_addc_co_u32_e32 v65, vcc, 0, v3, vcc
	global_load_dword v62, v[62:63], off nt
	s_nop 0
	global_load_dword v63, v[64:65], off nt
	v_add_co_u32_e32 v64, vcc, s19, v2
	s_mov_b32 s19, 0x6a000
	s_nop 0
	v_addc_co_u32_e32 v65, vcc, 0, v3, vcc
	v_add_co_u32_e32 v66, vcc, s19, v2
	s_mov_b32 s19, 0x6c000
	s_nop 0
	v_addc_co_u32_e32 v67, vcc, 0, v3, vcc
	global_load_dword v64, v[64:65], off nt
	s_nop 0
	global_load_dword v65, v[66:67], off nt
	v_add_co_u32_e32 v66, vcc, s19, v2
	s_mov_b32 s19, 0x6e000
	s_nop 0
	v_addc_co_u32_e32 v67, vcc, 0, v3, vcc
	v_add_co_u32_e32 v68, vcc, s19, v2
	s_mov_b32 s19, 0x70000
	s_nop 0
	v_addc_co_u32_e32 v69, vcc, 0, v3, vcc
	global_load_dword v66, v[66:67], off nt
	s_nop 0
	global_load_dword v67, v[68:69], off nt
	v_add_co_u32_e32 v68, vcc, s19, v2
	s_mov_b32 s19, 0x72000
	s_nop 0
	v_addc_co_u32_e32 v69, vcc, 0, v3, vcc
	v_add_co_u32_e32 v70, vcc, s19, v2
	s_mov_b32 s19, 0x74000
	s_nop 0
	v_addc_co_u32_e32 v71, vcc, 0, v3, vcc
	global_load_dword v68, v[68:69], off nt
	s_nop 0
	global_load_dword v69, v[70:71], off nt
	v_add_co_u32_e32 v70, vcc, s19, v2
	s_mov_b32 s19, 0x76000
	s_nop 0
	v_addc_co_u32_e32 v71, vcc, 0, v3, vcc
	v_add_co_u32_e32 v72, vcc, s19, v2
	s_mov_b32 s19, 0x78000
	s_nop 0
	v_addc_co_u32_e32 v73, vcc, 0, v3, vcc
	global_load_dword v70, v[70:71], off nt
	s_nop 0
	global_load_dword v71, v[72:73], off nt
	v_add_co_u32_e32 v72, vcc, s19, v2
	s_mov_b32 s19, 0x7a000
	s_nop 0
	v_addc_co_u32_e32 v73, vcc, 0, v3, vcc
	v_add_co_u32_e32 v74, vcc, s19, v2
	s_mov_b32 s19, 0x7c000
	s_nop 0
	v_addc_co_u32_e32 v75, vcc, 0, v3, vcc
	v_add_co_u32_e32 v76, vcc, s19, v2
	s_mov_b32 s19, 0x7e000
	s_nop 0
	v_addc_co_u32_e32 v77, vcc, 0, v3, vcc
	v_add_co_u32_e32 v78, vcc, s19, v2
	s_mov_b32 s19, 0x80000
	s_nop 0
	v_addc_co_u32_e32 v79, vcc, 0, v3, vcc
	v_add_co_u32_e32 v80, vcc, s19, v2
	s_mov_b32 s19, 0x82000
	s_nop 0
	v_addc_co_u32_e32 v81, vcc, 0, v3, vcc
	global_load_dword v72, v[72:73], off nt
	s_nop 0
	global_load_dword v74, v[74:75], off nt
	s_nop 0
	global_load_dword v76, v[76:77], off nt
	s_nop 0
	global_load_dword v78, v[78:79], off nt
	s_nop 0
	global_load_dword v73, v[80:81], off nt
	v_add_co_u32_e32 v80, vcc, s19, v2
	s_mov_b32 s19, 0x84000
	s_nop 0
	v_addc_co_u32_e32 v81, vcc, 0, v3, vcc
	global_load_dword v75, v[80:81], off nt
	v_add_co_u32_e32 v80, vcc, s19, v2
	s_mov_b32 s19, 0x86000
	s_nop 0
	v_addc_co_u32_e32 v81, vcc, 0, v3, vcc
	global_load_dword v77, v[80:81], off nt
	v_add_co_u32_e32 v80, vcc, s19, v2
	s_mov_b32 s19, 0x88000
	s_nop 0
	v_addc_co_u32_e32 v81, vcc, 0, v3, vcc
	global_load_dword v79, v[80:81], off nt
	v_add_co_u32_e32 v80, vcc, s19, v2
	s_mov_b32 s19, 0x8a000
	s_nop 0
	v_addc_co_u32_e32 v81, vcc, 0, v3, vcc
	v_add_co_u32_e32 v82, vcc, s19, v2
	s_mov_b32 s19, 0x8c000
	s_nop 0
	v_addc_co_u32_e32 v83, vcc, 0, v3, vcc
	global_load_dword v80, v[80:81], off nt
	s_nop 0
; template <bool PERMGL, bool FP8>
; __device__ __forceinline__ void q8_cols_item(const float* W, int N, int n0, unsigned char* Bq, float* sc_out, LAS float* AM, int par, int wave, int lane) {
;     ...
;     for (int i = 0; i < 128; ++i) v[i] = Wp[(size_t)i * N];
	global_load_dword v81, v[82:83], off nt
	v_add_co_u32_e32 v82, vcc, s19, v2
	s_mov_b32 s19, 0x8e000
	s_nop 0
	v_addc_co_u32_e32 v83, vcc, 0, v3, vcc
	v_add_co_u32_e32 v84, vcc, s19, v2
	s_mov_b32 s19, 0x90000
	s_nop 0
	v_addc_co_u32_e32 v85, vcc, 0, v3, vcc
	global_load_dword v82, v[82:83], off nt
	s_nop 0
	global_load_dword v83, v[84:85], off nt
	v_add_co_u32_e32 v84, vcc, s19, v2
	s_mov_b32 s19, 0x92000
	s_nop 0
	v_addc_co_u32_e32 v85, vcc, 0, v3, vcc
	v_add_co_u32_e32 v86, vcc, s19, v2
	s_mov_b32 s19, 0x94000
	s_nop 0
	v_addc_co_u32_e32 v87, vcc, 0, v3, vcc
	global_load_dword v84, v[84:85], off nt
	s_nop 0
	global_load_dword v85, v[86:87], off nt
	v_add_co_u32_e32 v86, vcc, s19, v2
	s_mov_b32 s19, 0x96000
	s_nop 0
	v_addc_co_u32_e32 v87, vcc, 0, v3, vcc
	v_add_co_u32_e32 v88, vcc, s19, v2
	s_mov_b32 s19, 0x98000
	s_nop 0
	v_addc_co_u32_e32 v89, vcc, 0, v3, vcc
	global_load_dword v86, v[86:87], off nt
	s_nop 0
	global_load_dword v87, v[88:89], off nt
	v_add_co_u32_e32 v88, vcc, s19, v2
	s_mov_b32 s19, 0x9a000
	s_nop 0
	v_addc_co_u32_e32 v89, vcc, 0, v3, vcc
	v_add_co_u32_e32 v90, vcc, s19, v2
	s_mov_b32 s19, 0x9c000
	s_nop 0
	v_addc_co_u32_e32 v91, vcc, 0, v3, vcc
	global_load_dword v88, v[88:89], off nt
	s_nop 0
	global_load_dword v89, v[90:91], off nt
	v_add_co_u32_e32 v90, vcc, s19, v2
	s_mov_b32 s19, 0x9e000
	s_nop 0
	v_addc_co_u32_e32 v91, vcc, 0, v3, vcc
	v_add_co_u32_e32 v92, vcc, s19, v2
	s_mov_b32 s19, 0xa0000
	s_nop 0
	v_addc_co_u32_e32 v93, vcc, 0, v3, vcc
	global_load_dword v90, v[90:91], off nt
	s_nop 0
	global_load_dword v91, v[92:93], off nt
	v_add_co_u32_e32 v92, vcc, s19, v2
	s_mov_b32 s19, 0xa2000
	s_nop 0
	v_addc_co_u32_e32 v93, vcc, 0, v3, vcc
	v_add_co_u32_e32 v94, vcc, s19, v2
	s_mov_b32 s19, 0xa4000
	s_nop 0
	v_addc_co_u32_e32 v95, vcc, 0, v3, vcc
	global_load_dword v92, v[92:93], off nt
	s_nop 0
	global_load_dword v93, v[94:95], off nt
	v_add_co_u32_e32 v94, vcc, s19, v2
	s_mov_b32 s19, 0xa6000
	s_nop 0
	v_addc_co_u32_e32 v95, vcc, 0, v3, vcc
	v_add_co_u32_e32 v96, vcc, s19, v2
	s_mov_b32 s19, 0xa8000
	s_nop 0
	v_addc_co_u32_e32 v97, vcc, 0, v3, vcc
	global_load_dword v94, v[94:95], off nt
	s_nop 0
	global_load_dword v95, v[96:97], off nt
	v_add_co_u32_e32 v96, vcc, s19, v2
	s_mov_b32 s19, 0xaa000
	s_nop 0
	v_addc_co_u32_e32 v97, vcc, 0, v3, vcc
	v_add_co_u32_e32 v98, vcc, s19, v2
	s_mov_b32 s19, 0xac000
	s_nop 0
	v_addc_co_u32_e32 v99, vcc, 0, v3, vcc
	global_load_dword v96, v[96:97], off nt
	s_nop 0
	global_load_dword v97, v[98:99], off nt
	v_add_co_u32_e32 v98, vcc, s19, v2
	s_mov_b32 s19, 0xae000
	s_nop 0
	v_addc_co_u32_e32 v99, vcc, 0, v3, vcc
	v_add_co_u32_e32 v100, vcc, s19, v2
	s_mov_b32 s19, 0xb0000
	s_nop 0
	v_addc_co_u32_e32 v101, vcc, 0, v3, vcc
	global_load_dword v98, v[98:99], off nt
	s_nop 0
	global_load_dword v99, v[100:101], off nt
	v_add_co_u32_e32 v100, vcc, s19, v2
	s_mov_b32 s19, 0xb2000
	s_nop 0
	v_addc_co_u32_e32 v101, vcc, 0, v3, vcc
	v_add_co_u32_e32 v102, vcc, s19, v2
	s_mov_b32 s19, 0xb4000
	s_nop 0
	v_addc_co_u32_e32 v103, vcc, 0, v3, vcc
	global_load_dword v100, v[100:101], off nt
	s_nop 0
	global_load_dword v101, v[102:103], off nt
	v_add_co_u32_e32 v102, vcc, s19, v2
	s_mov_b32 s19, 0xb6000
	s_nop 0
	v_addc_co_u32_e32 v103, vcc, 0, v3, vcc
	v_add_co_u32_e32 v104, vcc, s19, v2
	s_mov_b32 s19, 0xb8000
	s_nop 0
	v_addc_co_u32_e32 v105, vcc, 0, v3, vcc
	global_load_dword v102, v[102:103], off nt
	s_nop 0
	global_load_dword v103, v[104:105], off nt
	v_add_co_u32_e32 v104, vcc, s19, v2
	s_mov_b32 s19, 0xba000
	s_nop 0
	v_addc_co_u32_e32 v105, vcc, 0, v3, vcc
	v_add_co_u32_e32 v106, vcc, s19, v2
	s_mov_b32 s19, 0xbc000
	s_nop 0
	v_addc_co_u32_e32 v107, vcc, 0, v3, vcc
	v_add_co_u32_e32 v108, vcc, s19, v2
	s_mov_b32 s19, 0xbe000
	s_nop 0
	v_addc_co_u32_e32 v109, vcc, 0, v3, vcc
	v_add_co_u32_e32 v110, vcc, s19, v2
	s_mov_b32 s19, 0xc0000
	s_nop 0
	v_addc_co_u32_e32 v111, vcc, 0, v3, vcc
	v_add_co_u32_e32 v112, vcc, s19, v2
	s_mov_b32 s19, 0xc2000
	s_nop 0
	v_addc_co_u32_e32 v113, vcc, 0, v3, vcc
	global_load_dword v104, v[104:105], off nt
	s_nop 0
	global_load_dword v106, v[106:107], off nt
	s_nop 0
	global_load_dword v108, v[108:109], off nt
	s_nop 0
	global_load_dword v110, v[110:111], off nt
	s_nop 0
	global_load_dword v105, v[112:113], off nt
	v_add_co_u32_e32 v112, vcc, s19, v2
	s_mov_b32 s19, 0xc4000
	s_nop 0
	v_addc_co_u32_e32 v113, vcc, 0, v3, vcc
	global_load_dword v107, v[112:113], off nt
	v_add_co_u32_e32 v112, vcc, s19, v2
	s_mov_b32 s19, 0xc6000
	s_nop 0
	v_addc_co_u32_e32 v113, vcc, 0, v3, vcc
	global_load_dword v109, v[112:113], off nt
	v_add_co_u32_e32 v112, vcc, s19, v2
	s_mov_b32 s19, 0xc8000
	s_nop 0
	v_addc_co_u32_e32 v113, vcc, 0, v3, vcc
	global_load_dword v111, v[112:113], off nt
	v_add_co_u32_e32 v112, vcc, s19, v2
	s_mov_b32 s19, 0xca000
	s_nop 0
	v_addc_co_u32_e32 v113, vcc, 0, v3, vcc
	v_add_co_u32_e32 v114, vcc, s19, v2
	s_mov_b32 s19, 0xcc000
	s_nop 0
	v_addc_co_u32_e32 v115, vcc, 0, v3, vcc
	global_load_dword v112, v[112:113], off nt
	s_nop 0
	global_load_dword v113, v[114:115], off nt
	v_add_co_u32_e32 v114, vcc, s19, v2
	s_mov_b32 s19, 0xce000
	s_nop 0
	v_addc_co_u32_e32 v115, vcc, 0, v3, vcc
	v_add_co_u32_e32 v116, vcc, s19, v2
	s_mov_b32 s19, 0xd0000
	s_nop 0
	v_addc_co_u32_e32 v117, vcc, 0, v3, vcc
	global_load_dword v114, v[114:115], off nt
	s_nop 0
	global_load_dword v115, v[116:117], off nt
	v_add_co_u32_e32 v116, vcc, s19, v2
	s_mov_b32 s19, 0xd2000
	s_nop 0
	v_addc_co_u32_e32 v117, vcc, 0, v3, vcc
	v_add_co_u32_e32 v118, vcc, s19, v2
	s_mov_b32 s19, 0xd4000
	s_nop 0
	v_addc_co_u32_e32 v119, vcc, 0, v3, vcc
	global_load_dword v116, v[116:117], off nt
; template <bool PERMGL, bool FP8>
; __device__ __forceinline__ void q8_cols_item(const float* W, int N, int n0, unsigned char* Bq, float* sc_out, LAS float* AM, int par, int wave, int lane) {
;     ...
;     for (int i = 0; i < 128; ++i) v[i] = Wp[(size_t)i * N];
;     __builtin_amdgcn_sched_barrier(0);
; #pragma unroll
;     for (int i = 0; i < 128; ++i) am = fmaxf(am, fabsf(v[i]));
;     AM[(par * 8 + wave) * 64 + lane] = am;
;     __syncthreads();
	s_nop 0
	global_load_dword v117, v[118:119], off nt
	v_add_co_u32_e32 v118, vcc, s19, v2
	s_mov_b32 s19, 0xd6000
	s_nop 0
	v_addc_co_u32_e32 v119, vcc, 0, v3, vcc
	v_add_co_u32_e32 v120, vcc, s19, v2
	s_mov_b32 s19, 0xd8000
	s_nop 0
	v_addc_co_u32_e32 v121, vcc, 0, v3, vcc
	global_load_dword v118, v[118:119], off nt
	s_nop 0
	global_load_dword v119, v[120:121], off nt
	v_add_co_u32_e32 v120, vcc, s19, v2
	s_mov_b32 s19, 0xda000
	s_nop 0
	v_addc_co_u32_e32 v121, vcc, 0, v3, vcc
	v_add_co_u32_e32 v122, vcc, s19, v2
	s_mov_b32 s19, 0xdc000
	s_nop 0
	v_addc_co_u32_e32 v123, vcc, 0, v3, vcc
	global_load_dword v120, v[120:121], off nt
	s_nop 0
	global_load_dword v121, v[122:123], off nt
	v_add_co_u32_e32 v122, vcc, s19, v2
	s_mov_b32 s19, 0xde000
	s_nop 0
	v_addc_co_u32_e32 v123, vcc, 0, v3, vcc
	v_add_co_u32_e32 v124, vcc, s19, v2
	s_mov_b32 s19, 0xe0000
	s_nop 0
	v_addc_co_u32_e32 v125, vcc, 0, v3, vcc
	global_load_dword v122, v[122:123], off nt
	s_nop 0
	global_load_dword v123, v[124:125], off nt
	v_add_co_u32_e32 v124, vcc, s19, v2
	s_mov_b32 s19, 0xe2000
	s_nop 0
	v_addc_co_u32_e32 v125, vcc, 0, v3, vcc
	v_add_co_u32_e32 v126, vcc, s19, v2
	s_mov_b32 s19, 0xe4000
	s_nop 0
	v_addc_co_u32_e32 v127, vcc, 0, v3, vcc
	global_load_dword v124, v[124:125], off nt
	s_nop 0
	global_load_dword v125, v[126:127], off nt
	v_add_co_u32_e32 v126, vcc, s19, v2
	s_mov_b32 s19, 0xe6000
	s_nop 0
	v_addc_co_u32_e32 v127, vcc, 0, v3, vcc
	v_add_co_u32_e32 v128, vcc, s19, v2
	s_mov_b32 s19, 0xe8000
	s_nop 0
	v_addc_co_u32_e32 v129, vcc, 0, v3, vcc
	global_load_dword v126, v[126:127], off nt
	s_nop 0
	global_load_dword v127, v[128:129], off nt
	v_add_co_u32_e32 v128, vcc, s19, v2
	s_mov_b32 s19, 0xea000
	s_nop 0
	v_addc_co_u32_e32 v129, vcc, 0, v3, vcc
	v_add_co_u32_e32 v130, vcc, s19, v2
	s_mov_b32 s19, 0xec000
	s_nop 0
	v_addc_co_u32_e32 v131, vcc, 0, v3, vcc
	global_load_dword v128, v[128:129], off nt
	s_nop 0
	global_load_dword v129, v[130:131], off nt
	v_add_co_u32_e32 v130, vcc, s19, v2
	s_mov_b32 s19, 0xee000
	s_nop 0
	v_addc_co_u32_e32 v131, vcc, 0, v3, vcc
	v_add_co_u32_e32 v132, vcc, s19, v2
	s_mov_b32 s19, 0xf0000
	s_nop 0
	v_addc_co_u32_e32 v133, vcc, 0, v3, vcc
	global_load_dword v130, v[130:131], off nt
	s_nop 0
	global_load_dword v131, v[132:133], off nt
	v_add_co_u32_e32 v132, vcc, s19, v2
	s_mov_b32 s19, 0xf2000
	s_nop 0
	v_addc_co_u32_e32 v133, vcc, 0, v3, vcc
	v_add_co_u32_e32 v134, vcc, s19, v2
	s_mov_b32 s19, 0xf4000
	s_nop 0
	v_addc_co_u32_e32 v135, vcc, 0, v3, vcc
	global_load_dword v132, v[132:133], off nt
	s_nop 0
	global_load_dword v133, v[134:135], off nt
	v_add_co_u32_e32 v134, vcc, s19, v2
	s_mov_b32 s19, 0xf6000
	s_nop 0
	v_addc_co_u32_e32 v135, vcc, 0, v3, vcc
	v_add_co_u32_e32 v136, vcc, s19, v2
	s_mov_b32 s19, 0xf8000
	s_nop 0
	v_addc_co_u32_e32 v137, vcc, 0, v3, vcc
	global_load_dword v134, v[134:135], off nt
	s_nop 0
	global_load_dword v135, v[136:137], off nt
	v_add_co_u32_e32 v136, vcc, s19, v2
	s_mov_b32 s19, 0xfa000
	s_nop 0
	v_addc_co_u32_e32 v137, vcc, 0, v3, vcc
	v_add_co_u32_e32 v138, vcc, s19, v2
	s_mov_b32 s19, 0xfc000
	s_nop 0
	v_addc_co_u32_e32 v139, vcc, 0, v3, vcc
	global_load_dword v136, v[136:137], off nt
	s_nop 0
	global_load_dword v137, v[138:139], off nt
	v_add_co_u32_e32 v138, vcc, s19, v2
	s_mov_b32 s19, 0xfe000
	s_nop 0
	v_addc_co_u32_e32 v139, vcc, 0, v3, vcc
	v_add_co_u32_e32 v2, vcc, s19, v2
	global_load_dword v138, v[138:139], off nt
	s_nop 0
	v_addc_co_u32_e32 v3, vcc, 0, v3, vcc
	global_load_dword v141, v[2:3], off nt
	s_waitcnt vmcnt(0)
	v_max3_f32 v2, |v11|, 0, |v12|
	v_max3_f32 v2, v2, |v13|, |v14|
	v_max3_f32 v2, v2, |v15|, |v16|
	v_max3_f32 v2, v2, |v17|, |v18|
	v_max3_f32 v2, v2, |v19|, |v20|
	v_max3_f32 v2, v2, |v21|, |v22|
	v_max3_f32 v2, v2, |v23|, |v24|
	v_max3_f32 v2, v2, |v25|, |v26|
	v_max3_f32 v2, v2, |v27|, |v28|
	v_max3_f32 v2, v2, |v29|, |v30|
	v_max3_f32 v2, v2, |v31|, |v32|
	v_max3_f32 v2, v2, |v34|, |v35|
	v_max3_f32 v2, v2, |v36|, |v37|
	v_max3_f32 v2, v2, |v38|, |v39|
	v_max3_f32 v2, v2, |v40|, |v42|
	v_max3_f32 v2, v2, |v44|, |v46|
	v_max3_f32 v2, v2, |v41|, |v43|
	v_max3_f32 v2, v2, |v45|, |v47|
	v_max3_f32 v2, v2, |v48|, |v49|
	v_max3_f32 v2, v2, |v50|, |v51|
	v_max3_f32 v2, v2, |v52|, |v53|
	v_max3_f32 v2, v2, |v54|, |v55|
	v_max3_f32 v2, v2, |v56|, |v57|
	v_max3_f32 v2, v2, |v58|, |v59|
	v_max3_f32 v2, v2, |v60|, |v61|
	v_max3_f32 v2, v2, |v62|, |v63|
	v_max3_f32 v2, v2, |v64|, |v65|
	v_max3_f32 v2, v2, |v66|, |v67|
	v_max3_f32 v2, v2, |v68|, |v69|
	v_max3_f32 v2, v2, |v70|, |v71|
	v_max3_f32 v2, v2, |v72|, |v74|
	v_max3_f32 v2, v2, |v76|, |v78|
	v_max3_f32 v2, v2, |v73|, |v75|
	v_max3_f32 v2, v2, |v77|, |v79|
	v_max3_f32 v2, v2, |v80|, |v81|
	v_max3_f32 v2, v2, |v82|, |v83|
	v_max3_f32 v2, v2, |v84|, |v85|
	v_max3_f32 v2, v2, |v86|, |v87|
	v_max3_f32 v2, v2, |v88|, |v89|
	v_max3_f32 v2, v2, |v90|, |v91|
	v_max3_f32 v2, v2, |v92|, |v93|
	v_max3_f32 v2, v2, |v94|, |v95|
	v_max3_f32 v2, v2, |v96|, |v97|
	v_max3_f32 v2, v2, |v98|, |v99|
	v_max3_f32 v2, v2, |v100|, |v101|
	v_max3_f32 v2, v2, |v102|, |v103|
	v_max3_f32 v2, v2, |v104|, |v106|
	v_max3_f32 v2, v2, |v108|, |v110|
	v_max3_f32 v2, v2, |v105|, |v107|
	v_max3_f32 v2, v2, |v109|, |v111|
	v_max3_f32 v2, v2, |v112|, |v113|
	v_max3_f32 v2, v2, |v114|, |v115|
	v_max3_f32 v2, v2, |v116|, |v117|
	v_max3_f32 v2, v2, |v118|, |v119|
	v_max3_f32 v2, v2, |v120|, |v121|
	v_max3_f32 v2, v2, |v122|, |v123|
	v_max3_f32 v2, v2, |v124|, |v125|
	v_max3_f32 v2, v2, |v126|, |v127|
	v_max3_f32 v2, v2, |v128|, |v129|
	v_max3_f32 v2, v2, |v130|, |v131|
	v_max3_f32 v2, v2, |v132|, |v133|
	v_max3_f32 v2, v2, |v134|, |v135|
	v_max3_f32 v2, v2, |v136|, |v137|
	s_lshl_b32 s19, s15, 11
	v_max3_f32 v5, v2, |v138|, |v141|
	v_add_u32_e32 v2, s19, v10
	v_add_u32_e32 v139, s19, v7
	ds_write_b32 v2, v5
	s_waitcnt lgkmcnt(0)
	s_barrier
; template <bool PERMGL, bool FP8>
; __device__ __forceinline__ void q8_cols_item(const float* W, int N, int n0, unsigned char* Bq, float* sc_out, LAS float* AM, int par, int wave, int lane) {
;     ...
; #pragma unroll
;     for (int w = 0; w < 8; ++w) am = fmaxf(am, AM[(par * 8 + w) * 64 + lane]);
;     const float sc = am > 0.f ? am * (FP8 ? (1.0f / 256.0f) : (1.0f / 127.0f)) : 1.0f, inv = 1.0f / sc;
;     int row = n;
;     if (PERMGL) { const int j = n >> 1, pr = n & 1, o = j & 127; row = ((j >> 7) << 8) + (((o >> 2) & 1) << 7) + ((o >> 5) << 5) + (pr << 4) + (((o >> 3) & 3) << 2) + (o & 3); }
;     if (!PERMGL) { const int o = n & 255; row = ((n >> 8) << 8) + (((o >> 3) & 1) << 7) + ((o >> 6) << 5) + (((o >> 4) & 3) << 3) + (o & 7); }
;     auto xq = [](unsigned x) { return (unsigned)__builtin_amdgcn_update_dpp(0, (int)x, 0xB1, 0xf, 0xf, true); };
;     const bool odd = lane & 1;
;     const int rowp = (int)xq((unsigned)row);
;     unsigned char* plo = Bq + (size_t)(odd ? rowp : row) * 1024 + 128 * wave + (odd ? 16 : 0);
;     unsigned char* phi = Bq + (size_t)(odd ? row : rowp) * 1024 + 128 * wave + (odd ? 16 : 0);
;     auto packc = [&](int c) { u32x4 o;
;         if (FP8) { o.x = f8x4(v[16 * c], v[16 * c + 1], v[16 * c + 2], v[16 * c + 3], inv); o.y = f8x4(v[16 * c + 4], v[16 * c + 5], v[16 * c + 6], v[16 * c + 7], inv);
;                    o.z = f8x4(v[16 * c + 8], v[16 * c + 9], v[16 * c + 10], v[16 * c + 11], inv); o.w = f8x4(v[16 * c + 12], v[16 * c + 13], v[16 * c + 14], v[16 * c + 15], inv); }
;         else { o.x = q8x4(v[16 * c], v[16 * c + 1], v[16 * c + 2], v[16 * c + 3], inv); o.y = q8x4(v[16 * c + 4], v[16 * c + 5], v[16 * c + 6], v[16 * c + 7], inv);
;                o.z = q8x4(v[16 * c + 8], v[16 * c + 9], v[16 * c + 10], v[16 * c + 11], inv); o.w = q8x4(v[16 * c + 12], v[16 * c + 13], v[16 * c + 14], v[16 * c + 15], inv); }
;         return o; };
; #pragma unroll
;     for (int j = 0; j < 4; ++j) { const u32x4 p0 = packc(2 * j), p1 = packc(2 * j + 1);
;         u32x4 snd, rcv;
; #pragma unroll
;         for (int q = 0; q < 4; ++q) { snd[q] = odd ? p0[q] : p1[q]; rcv[q] = xq(snd[q]); }
;         u32x4 a, b;
; #pragma unroll
;         for (int q = 0; q < 4; ++q) { a[q] = odd ? rcv[q] : p0[q]; b[q] = odd ? p1[q] : rcv[q]; }
;         *(u32x4*)(plo + 32 * j) = a; *(u32x4*)(phi + 32 * j) = b; }
	ds_read2st64_b32 v[2:3], v139 offset1:1
	s_waitcnt lgkmcnt(0)
	v_max3_f32 v5, v5, v2, v3
	ds_read2st64_b32 v[2:3], v139 offset0:2 offset1:3
	s_waitcnt lgkmcnt(0)
	v_max3_f32 v5, v5, v2, v3
	ds_read2st64_b32 v[2:3], v139 offset0:4 offset1:5
	s_waitcnt lgkmcnt(0)
	v_max3_f32 v5, v5, v2, v3
	ds_read2st64_b32 v[2:3], v139 offset0:6 offset1:7
	s_waitcnt lgkmcnt(0)
	v_max3_f32 v2, v5, v2, v3
	v_cmp_lt_f32_e32 vcc, 0, v2
	v_mul_f32_e32 v2, 0x3c010204, v2
	s_nop 0
	v_cndmask_b32_e32 v139, 1.0, v2, vcc
	v_div_scale_f32 v2, s[42:43], v139, v139, 1.0
	v_rcp_f32_e32 v3, v2
	s_nop 0
	v_fma_f32 v5, -v2, v3, 1.0
	v_fmac_f32_e32 v3, v5, v3
	v_div_scale_f32 v5, vcc, 1.0, v139, 1.0
	v_mul_f32_e32 v140, v5, v3
	v_fma_f32 v142, -v2, v140, v5
	v_fmac_f32_e32 v140, v142, v3
	v_fma_f32 v2, -v2, v140, v5
	v_div_fmas_f32 v2, v2, v3, v140
	v_div_fixup_f32 v142, v2, v139, 1.0
	v_fmaak_f32 v11, v11, v142, 0x4b400000
	v_fmaak_f32 v12, v12, v142, 0x4b400000
	v_fmaak_f32 v13, v13, v142, 0x4b400000
	v_fmaak_f32 v14, v14, v142, 0x4b400000
	v_perm_b32 v13, v14, v13, s61
	v_perm_b32 v11, v12, v11, s61
	v_perm_b32 v11, v13, v11, s79
	v_fmaak_f32 v12, v15, v142, 0x4b400000
	v_fmaak_f32 v13, v16, v142, 0x4b400000
	v_fmaak_f32 v14, v17, v142, 0x4b400000
	v_fmaak_f32 v15, v18, v142, 0x4b400000
	v_perm_b32 v14, v15, v14, s61
	v_perm_b32 v12, v13, v12, s61
	v_perm_b32 v13, v14, v12, s79
	v_fmaak_f32 v12, v19, v142, 0x4b400000
	v_fmaak_f32 v14, v20, v142, 0x4b400000
	v_fmaak_f32 v15, v21, v142, 0x4b400000
	v_fmaak_f32 v16, v22, v142, 0x4b400000
	v_perm_b32 v15, v16, v15, s61
	v_perm_b32 v12, v14, v12, s61
	v_perm_b32 v14, v15, v12, s79
	v_fmaak_f32 v12, v23, v142, 0x4b400000
	v_fmaak_f32 v15, v24, v142, 0x4b400000
	v_fmaak_f32 v16, v25, v142, 0x4b400000
	v_fmaak_f32 v17, v26, v142, 0x4b400000
	v_perm_b32 v16, v17, v16, s61
	v_perm_b32 v12, v15, v12, s61
	v_perm_b32 v15, v16, v12, s79
	v_fmaak_f32 v12, v27, v142, 0x4b400000
	v_fmaak_f32 v16, v28, v142, 0x4b400000
	v_fmaak_f32 v17, v29, v142, 0x4b400000
	v_fmaak_f32 v18, v30, v142, 0x4b400000
	v_perm_b32 v17, v18, v17, s61
	v_perm_b32 v12, v16, v12, s61
	v_add_u16_e32 v2, s18, v6
	v_perm_b32 v16, v17, v12, s79
	v_fmaak_f32 v12, v31, v142, 0x4b400000
	v_fmaak_f32 v17, v32, v142, 0x4b400000
	v_fmaak_f32 v18, v34, v142, 0x4b400000
	v_fmaak_f32 v19, v35, v142, 0x4b400000
	v_lshrrev_b16_e32 v2, 1, v2
	v_lshlrev_b32_e32 v3, 4, v4
	v_perm_b32 v18, v19, v18, s61
	v_perm_b32 v12, v17, v12, s61
	v_and_b32_e32 v5, 0x80, v3
	v_and_b32_e32 v140, 0x60, v2
	v_and_or_b32 v4, v4, s73, v9
	v_perm_b32 v17, v18, v12, s79
	v_fmaak_f32 v12, v36, v142, 0x4b400000
	v_fmaak_f32 v18, v37, v142, 0x4b400000
	v_fmaak_f32 v19, v38, v142, 0x4b400000
	v_fmaak_f32 v20, v39, v142, 0x4b400000
	v_and_b32_e32 v3, 16, v3
	v_and_b32_e32 v2, 3, v2
	v_or3_b32 v4, v4, v5, v140
	v_perm_b32 v19, v20, v19, s61
	v_perm_b32 v12, v18, v12, s61
	v_or3_b32 v140, v4, v3, v2
	v_perm_b32 v18, v19, v12, s79
	v_fmaak_f32 v12, v40, v142, 0x4b400000
	v_fmaak_f32 v19, v42, v142, 0x4b400000
	v_fmaak_f32 v20, v44, v142, 0x4b400000
	v_fmaak_f32 v21, v46, v142, 0x4b400000
	v_mov_b32_dpp v4, v140 quad_perm:[1,0,3,2] row_mask:0xf bank_mask:0xf bound_ctrl:1
	v_perm_b32 v20, v21, v20, s61
	v_perm_b32 v12, v19, v12, s61
	v_cndmask_b32_e64 v2, v4, v140, s[4:5]
	v_perm_b32 v19, v20, v12, s79
	v_cndmask_b32_e64 v12, v11, v16, s[4:5]
	v_ashrrev_i32_e32 v3, 31, v2
	v_cndmask_b32_e64 v4, v140, v4, s[4:5]
	v_mov_b32_dpp v20, v12 quad_perm:[1,0,3,2] row_mask:0xf bank_mask:0xf bound_ctrl:1
	v_cndmask_b32_e64 v12, v13, v17, s[4:5]
	v_lshlrev_b64 v[2:3], 10, v[2:3]
	v_readlane_b32 s18, v252, 31
	v_ashrrev_i32_e32 v5, 31, v4
	v_mov_b32_dpp v21, v12 quad_perm:[1,0,3,2] row_mask:0xf bank_mask:0xf bound_ctrl:1
	v_cndmask_b32_e64 v12, v14, v18, s[4:5]
	v_lshl_add_u64 v[2:3], s[46:47], 0, v[2:3]
	v_readlane_b32 s19, v252, 32
	v_lshlrev_b64 v[4:5], 10, v[4:5]
	v_mov_b32_dpp v22, v12 quad_perm:[1,0,3,2] row_mask:0xf bank_mask:0xf bound_ctrl:1
	v_cndmask_b32_e64 v12, v15, v19, s[4:5]
	v_lshl_add_u64 v[2:3], v[2:3], 0, s[18:19]
	v_lshl_add_u64 v[4:5], s[46:47], 0, v[4:5]
	v_mov_b32_dpp v23, v12 quad_perm:[1,0,3,2] row_mask:0xf bank_mask:0xf bound_ctrl:1
	v_lshl_add_u64 v[2:3], v[2:3], 0, v[0:1]
	v_lshl_add_u64 v[4:5], v[4:5], 0, s[18:19]
	v_cndmask_b32_e64 v12, v20, v11, s[4:5]
	v_cndmask_b32_e64 v13, v21, v13, s[4:5]
	v_cndmask_b32_e64 v14, v22, v14, s[4:5]
	v_cndmask_b32_e64 v15, v23, v15, s[4:5]
	v_lshl_add_u64 v[4:5], v[4:5], 0, v[0:1]
	v_cndmask_b32_e64 v16, v16, v20, s[4:5]
	v_cndmask_b32_e64 v17, v17, v21, s[4:5]
	v_cndmask_b32_e64 v18, v18, v22, s[4:5]
	v_cndmask_b32_e64 v19, v19, v23, s[4:5]
	global_store_dwordx4 v[2:3], v[12:15], off
	global_store_dwordx4 v[4:5], v[16:19], off
	v_fmaak_f32 v11, v41, v142, 0x4b400000
	v_fmaak_f32 v12, v43, v142, 0x4b400000
	v_fmaak_f32 v13, v45, v142, 0x4b400000
	v_fmaak_f32 v14, v47, v142, 0x4b400000
	v_perm_b32 v13, v14, v13, s61
	v_perm_b32 v11, v12, v11, s61
	v_perm_b32 v11, v13, v11, s79
	v_fmaak_f32 v12, v48, v142, 0x4b400000
	v_fmaak_f32 v13, v49, v142, 0x4b400000
	v_fmaak_f32 v14, v50, v142, 0x4b400000
	v_fmaak_f32 v15, v51, v142, 0x4b400000
	v_perm_b32 v14, v15, v14, s61
	v_perm_b32 v12, v13, v12, s61
	v_perm_b32 v13, v14, v12, s79
	v_fmaak_f32 v12, v52, v142, 0x4b400000
	v_fmaak_f32 v14, v53, v142, 0x4b400000
	v_fmaak_f32 v15, v54, v142, 0x4b400000
	v_fmaak_f32 v16, v55, v142, 0x4b400000
	v_perm_b32 v15, v16, v15, s61
	v_perm_b32 v12, v14, v12, s61
	v_perm_b32 v14, v15, v12, s79
	v_fmaak_f32 v12, v56, v142, 0x4b400000
	v_fmaak_f32 v15, v57, v142, 0x4b400000
	v_fmaak_f32 v16, v58, v142, 0x4b400000
	v_fmaak_f32 v17, v59, v142, 0x4b400000
	v_perm_b32 v16, v17, v16, s61
; template <bool PERMGL, bool FP8>
; __device__ __forceinline__ void q8_cols_item(const float* W, int N, int n0, unsigned char* Bq, float* sc_out, LAS float* AM, int par, int wave, int lane) {
;     ...
;     auto packc = [&](int c) { u32x4 o;
;         if (FP8) { o.x = f8x4(v[16 * c], v[16 * c + 1], v[16 * c + 2], v[16 * c + 3], inv); o.y = f8x4(v[16 * c + 4], v[16 * c + 5], v[16 * c + 6], v[16 * c + 7], inv);
;                    o.z = f8x4(v[16 * c + 8], v[16 * c + 9], v[16 * c + 10], v[16 * c + 11], inv); o.w = f8x4(v[16 * c + 12], v[16 * c + 13], v[16 * c + 14], v[16 * c + 15], inv); }
;         else { o.x = q8x4(v[16 * c], v[16 * c + 1], v[16 * c + 2], v[16 * c + 3], inv); o.y = q8x4(v[16 * c + 4], v[16 * c + 5], v[16 * c + 6], v[16 * c + 7], inv);
;                o.z = q8x4(v[16 * c + 8], v[16 * c + 9], v[16 * c + 10], v[16 * c + 11], inv); o.w = q8x4(v[16 * c + 12], v[16 * c + 13], v[16 * c + 14], v[16 * c + 15], inv); }
;         return o; };
; #pragma unroll
;     for (int j = 0; j < 4; ++j) { const u32x4 p0 = packc(2 * j), p1 = packc(2 * j + 1);
;         u32x4 snd, rcv;
; #pragma unroll
;         for (int q = 0; q < 4; ++q) { snd[q] = odd ? p0[q] : p1[q]; rcv[q] = xq(snd[q]); }
;         u32x4 a, b;
; #pragma unroll
;         for (int q = 0; q < 4; ++q) { a[q] = odd ? rcv[q] : p0[q]; b[q] = odd ? p1[q] : rcv[q]; }
;         *(u32x4*)(plo + 32 * j) = a; *(u32x4*)(phi + 32 * j) = b; }
	v_perm_b32 v12, v15, v12, s61
	v_perm_b32 v15, v16, v12, s79
	v_fmaak_f32 v12, v60, v142, 0x4b400000
	v_fmaak_f32 v16, v61, v142, 0x4b400000
	v_fmaak_f32 v17, v62, v142, 0x4b400000
	v_fmaak_f32 v18, v63, v142, 0x4b400000
	v_perm_b32 v17, v18, v17, s61
	v_perm_b32 v12, v16, v12, s61
	v_perm_b32 v16, v17, v12, s79
	v_fmaak_f32 v12, v64, v142, 0x4b400000
	v_fmaak_f32 v17, v65, v142, 0x4b400000
	v_fmaak_f32 v18, v66, v142, 0x4b400000
	v_fmaak_f32 v19, v67, v142, 0x4b400000
	v_perm_b32 v18, v19, v18, s61
	v_perm_b32 v12, v17, v12, s61
	v_perm_b32 v17, v18, v12, s79
	v_fmaak_f32 v12, v68, v142, 0x4b400000
	v_fmaak_f32 v18, v69, v142, 0x4b400000
	v_fmaak_f32 v19, v70, v142, 0x4b400000
	v_fmaak_f32 v20, v71, v142, 0x4b400000
	v_perm_b32 v19, v20, v19, s61
	v_perm_b32 v12, v18, v12, s61
	v_perm_b32 v18, v19, v12, s79
	v_fmaak_f32 v12, v72, v142, 0x4b400000
	v_fmaak_f32 v19, v74, v142, 0x4b400000
	v_fmaak_f32 v20, v76, v142, 0x4b400000
	v_fmaak_f32 v21, v78, v142, 0x4b400000
	v_perm_b32 v20, v21, v20, s61
	v_perm_b32 v12, v19, v12, s61
	v_perm_b32 v19, v20, v12, s79
	v_cndmask_b32_e64 v12, v11, v16, s[4:5]
	s_and_b64 vcc, exec, s[0:1]
	s_nop 0
	v_mov_b32_dpp v20, v12 quad_perm:[1,0,3,2] row_mask:0xf bank_mask:0xf bound_ctrl:1
	v_cndmask_b32_e64 v12, v13, v17, s[4:5]
	v_cndmask_b32_e64 v16, v16, v20, s[4:5]
	s_nop 0
	v_mov_b32_dpp v21, v12 quad_perm:[1,0,3,2] row_mask:0xf bank_mask:0xf bound_ctrl:1
	v_cndmask_b32_e64 v12, v14, v18, s[4:5]
	v_cndmask_b32_e64 v13, v21, v13, s[4:5]
	v_cndmask_b32_e64 v17, v17, v21, s[4:5]
	v_mov_b32_dpp v22, v12 quad_perm:[1,0,3,2] row_mask:0xf bank_mask:0xf bound_ctrl:1
	v_cndmask_b32_e64 v12, v15, v19, s[4:5]
	v_cndmask_b32_e64 v14, v22, v14, s[4:5]
	v_cndmask_b32_e64 v18, v18, v22, s[4:5]
	v_mov_b32_dpp v23, v12 quad_perm:[1,0,3,2] row_mask:0xf bank_mask:0xf bound_ctrl:1
	v_cndmask_b32_e64 v12, v20, v11, s[4:5]
	v_cndmask_b32_e64 v15, v23, v15, s[4:5]
	v_cndmask_b32_e64 v19, v19, v23, s[4:5]
	global_store_dwordx4 v[2:3], v[12:15], off offset:32
	global_store_dwordx4 v[4:5], v[16:19], off offset:32
	v_fmaak_f32 v11, v73, v142, 0x4b400000
	v_fmaak_f32 v12, v75, v142, 0x4b400000
	v_fmaak_f32 v13, v77, v142, 0x4b400000
	v_fmaak_f32 v14, v79, v142, 0x4b400000
	v_perm_b32 v13, v14, v13, s61
	v_perm_b32 v11, v12, v11, s61
	v_perm_b32 v11, v13, v11, s79
	v_fmaak_f32 v12, v80, v142, 0x4b400000
	v_fmaak_f32 v13, v81, v142, 0x4b400000
	v_fmaak_f32 v14, v82, v142, 0x4b400000
	v_fmaak_f32 v15, v83, v142, 0x4b400000
	v_perm_b32 v14, v15, v14, s61
	v_perm_b32 v12, v13, v12, s61
	v_perm_b32 v13, v14, v12, s79
	v_fmaak_f32 v12, v84, v142, 0x4b400000
	v_fmaak_f32 v14, v85, v142, 0x4b400000
	v_fmaak_f32 v15, v86, v142, 0x4b400000
	v_fmaak_f32 v16, v87, v142, 0x4b400000
	v_perm_b32 v15, v16, v15, s61
	v_perm_b32 v12, v14, v12, s61
	v_perm_b32 v14, v15, v12, s79
	v_fmaak_f32 v12, v88, v142, 0x4b400000
	v_fmaak_f32 v15, v89, v142, 0x4b400000
	v_fmaak_f32 v16, v90, v142, 0x4b400000
	v_fmaak_f32 v17, v91, v142, 0x4b400000
	v_perm_b32 v16, v17, v16, s61
	v_perm_b32 v12, v15, v12, s61
	v_perm_b32 v15, v16, v12, s79
	v_fmaak_f32 v12, v92, v142, 0x4b400000
	v_fmaak_f32 v16, v93, v142, 0x4b400000
	v_fmaak_f32 v17, v94, v142, 0x4b400000
	v_fmaak_f32 v18, v95, v142, 0x4b400000
	v_perm_b32 v17, v18, v17, s61
	v_perm_b32 v12, v16, v12, s61
	v_perm_b32 v16, v17, v12, s79
	v_fmaak_f32 v12, v96, v142, 0x4b400000
	v_fmaak_f32 v17, v97, v142, 0x4b400000
	v_fmaak_f32 v18, v98, v142, 0x4b400000
	v_fmaak_f32 v19, v99, v142, 0x4b400000
	v_perm_b32 v18, v19, v18, s61
	v_perm_b32 v12, v17, v12, s61
	v_perm_b32 v17, v18, v12, s79
	v_fmaak_f32 v12, v100, v142, 0x4b400000
	v_fmaak_f32 v18, v101, v142, 0x4b400000
	v_fmaak_f32 v19, v102, v142, 0x4b400000
	v_fmaak_f32 v20, v103, v142, 0x4b400000
	v_perm_b32 v19, v20, v19, s61
	v_perm_b32 v12, v18, v12, s61
	v_perm_b32 v18, v19, v12, s79
	v_fmaak_f32 v12, v104, v142, 0x4b400000
	v_fmaak_f32 v19, v106, v142, 0x4b400000
	v_fmaak_f32 v20, v108, v142, 0x4b400000
	v_fmaak_f32 v21, v110, v142, 0x4b400000
	v_perm_b32 v20, v21, v20, s61
	v_perm_b32 v12, v19, v12, s61
	v_perm_b32 v19, v20, v12, s79
	v_cndmask_b32_e64 v12, v11, v16, s[4:5]
	s_nop 1
; template <bool PERMGL, bool FP8>
; __device__ __forceinline__ void q8_cols_item(const float* W, int N, int n0, unsigned char* Bq, float* sc_out, LAS float* AM, int par, int wave, int lane) {
;     ...
;     auto packc = [&](int c) { u32x4 o;
;         if (FP8) { o.x = f8x4(v[16 * c], v[16 * c + 1], v[16 * c + 2], v[16 * c + 3], inv); o.y = f8x4(v[16 * c + 4], v[16 * c + 5], v[16 * c + 6], v[16 * c + 7], inv);
;                    o.z = f8x4(v[16 * c + 8], v[16 * c + 9], v[16 * c + 10], v[16 * c + 11], inv); o.w = f8x4(v[16 * c + 12], v[16 * c + 13], v[16 * c + 14], v[16 * c + 15], inv); }
;         else { o.x = q8x4(v[16 * c], v[16 * c + 1], v[16 * c + 2], v[16 * c + 3], inv); o.y = q8x4(v[16 * c + 4], v[16 * c + 5], v[16 * c + 6], v[16 * c + 7], inv);
;                o.z = q8x4(v[16 * c + 8], v[16 * c + 9], v[16 * c + 10], v[16 * c + 11], inv); o.w = q8x4(v[16 * c + 12], v[16 * c + 13], v[16 * c + 14], v[16 * c + 15], inv); }
;         return o; };
; #pragma unroll
;     for (int j = 0; j < 4; ++j) { const u32x4 p0 = packc(2 * j), p1 = packc(2 * j + 1);
;         u32x4 snd, rcv;
; #pragma unroll
;         for (int q = 0; q < 4; ++q) { snd[q] = odd ? p0[q] : p1[q]; rcv[q] = xq(snd[q]); }
;         u32x4 a, b;
; #pragma unroll
;         for (int q = 0; q < 4; ++q) { a[q] = odd ? rcv[q] : p0[q]; b[q] = odd ? p1[q] : rcv[q]; }
;         *(u32x4*)(plo + 32 * j) = a; *(u32x4*)(phi + 32 * j) = b; }
;     if (wave == 0) sc_out[PERMGL ? row : n] = FP8 ? sc * 16.0f : sc;
	v_mov_b32_dpp v20, v12 quad_perm:[1,0,3,2] row_mask:0xf bank_mask:0xf bound_ctrl:1
	v_cndmask_b32_e64 v12, v13, v17, s[4:5]
	v_cndmask_b32_e64 v16, v16, v20, s[4:5]
	s_nop 0
	v_mov_b32_dpp v21, v12 quad_perm:[1,0,3,2] row_mask:0xf bank_mask:0xf bound_ctrl:1
	v_cndmask_b32_e64 v12, v14, v18, s[4:5]
	v_cndmask_b32_e64 v13, v21, v13, s[4:5]
	v_cndmask_b32_e64 v17, v17, v21, s[4:5]
	v_mov_b32_dpp v22, v12 quad_perm:[1,0,3,2] row_mask:0xf bank_mask:0xf bound_ctrl:1
	v_cndmask_b32_e64 v12, v15, v19, s[4:5]
	v_cndmask_b32_e64 v14, v22, v14, s[4:5]
	v_cndmask_b32_e64 v18, v18, v22, s[4:5]
	v_mov_b32_dpp v23, v12 quad_perm:[1,0,3,2] row_mask:0xf bank_mask:0xf bound_ctrl:1
	v_cndmask_b32_e64 v12, v20, v11, s[4:5]
	v_cndmask_b32_e64 v15, v23, v15, s[4:5]
	v_cndmask_b32_e64 v19, v19, v23, s[4:5]
	global_store_dwordx4 v[2:3], v[12:15], off offset:64
	global_store_dwordx4 v[4:5], v[16:19], off offset:64
	v_fmaak_f32 v11, v105, v142, 0x4b400000
	v_fmaak_f32 v12, v107, v142, 0x4b400000
	v_fmaak_f32 v13, v109, v142, 0x4b400000
	v_fmaak_f32 v14, v111, v142, 0x4b400000
	v_perm_b32 v13, v14, v13, s61
	v_perm_b32 v11, v12, v11, s61
	v_perm_b32 v11, v13, v11, s79
	v_fmaak_f32 v12, v112, v142, 0x4b400000
	v_fmaak_f32 v13, v113, v142, 0x4b400000
	v_fmaak_f32 v14, v114, v142, 0x4b400000
	v_fmaak_f32 v15, v115, v142, 0x4b400000
	v_perm_b32 v14, v15, v14, s61
	v_perm_b32 v12, v13, v12, s61
	v_perm_b32 v13, v14, v12, s79
	v_fmaak_f32 v12, v116, v142, 0x4b400000
	v_fmaak_f32 v14, v117, v142, 0x4b400000
	v_fmaak_f32 v15, v118, v142, 0x4b400000
	v_fmaak_f32 v16, v119, v142, 0x4b400000
	v_perm_b32 v15, v16, v15, s61
	v_perm_b32 v12, v14, v12, s61
	v_perm_b32 v14, v15, v12, s79
	v_fmaak_f32 v12, v120, v142, 0x4b400000
	v_fmaak_f32 v15, v121, v142, 0x4b400000
	v_fmaak_f32 v16, v122, v142, 0x4b400000
	v_fmaak_f32 v17, v123, v142, 0x4b400000
	v_perm_b32 v16, v17, v16, s61
	v_perm_b32 v12, v15, v12, s61
	v_perm_b32 v15, v16, v12, s79
	v_fmaak_f32 v12, v124, v142, 0x4b400000
	v_fmaak_f32 v16, v125, v142, 0x4b400000
	v_fmaak_f32 v17, v126, v142, 0x4b400000
	v_fmaak_f32 v18, v127, v142, 0x4b400000
	v_perm_b32 v17, v18, v17, s61
	v_perm_b32 v12, v16, v12, s61
	v_perm_b32 v16, v17, v12, s79
	v_fmaak_f32 v12, v128, v142, 0x4b400000
	v_fmaak_f32 v17, v129, v142, 0x4b400000
	v_fmaak_f32 v18, v130, v142, 0x4b400000
	v_fmaak_f32 v19, v131, v142, 0x4b400000
	v_perm_b32 v18, v19, v18, s61
	v_perm_b32 v12, v17, v12, s61
	v_perm_b32 v17, v18, v12, s79
	v_fmaak_f32 v12, v132, v142, 0x4b400000
	v_fmaak_f32 v18, v133, v142, 0x4b400000
	v_fmaak_f32 v19, v134, v142, 0x4b400000
	v_fmaak_f32 v20, v135, v142, 0x4b400000
	v_perm_b32 v19, v20, v19, s61
	v_perm_b32 v12, v18, v12, s61
	v_perm_b32 v18, v19, v12, s79
	v_fmaak_f32 v12, v136, v142, 0x4b400000
	v_fmaak_f32 v19, v137, v142, 0x4b400000
	v_fmaak_f32 v20, v138, v142, 0x4b400000
	v_fmaak_f32 v21, v141, v142, 0x4b400000
	v_perm_b32 v20, v21, v20, s61
	v_perm_b32 v12, v19, v12, s61
	v_perm_b32 v19, v20, v12, s79
	v_cndmask_b32_e64 v12, v11, v16, s[4:5]
	s_nop 1
	v_mov_b32_dpp v20, v12 quad_perm:[1,0,3,2] row_mask:0xf bank_mask:0xf bound_ctrl:1
	v_cndmask_b32_e64 v12, v13, v17, s[4:5]
	v_cndmask_b32_e64 v16, v16, v20, s[4:5]
	s_nop 0
	v_mov_b32_dpp v21, v12 quad_perm:[1,0,3,2] row_mask:0xf bank_mask:0xf bound_ctrl:1
	v_cndmask_b32_e64 v12, v14, v18, s[4:5]
	v_cndmask_b32_e64 v13, v21, v13, s[4:5]
	v_cndmask_b32_e64 v17, v17, v21, s[4:5]
	v_mov_b32_dpp v22, v12 quad_perm:[1,0,3,2] row_mask:0xf bank_mask:0xf bound_ctrl:1
	v_cndmask_b32_e64 v12, v15, v19, s[4:5]
	v_cndmask_b32_e64 v14, v22, v14, s[4:5]
	v_cndmask_b32_e64 v18, v18, v22, s[4:5]
	v_mov_b32_dpp v23, v12 quad_perm:[1,0,3,2] row_mask:0xf bank_mask:0xf bound_ctrl:1
	v_cndmask_b32_e64 v12, v20, v11, s[4:5]
	v_cndmask_b32_e64 v15, v23, v15, s[4:5]
	v_cndmask_b32_e64 v19, v19, v23, s[4:5]
	global_store_dwordx4 v[2:3], v[12:15], off offset:96
	global_store_dwordx4 v[4:5], v[16:19], off offset:96
	s_cbranch_vccnz .LBB0_126
	s_lshl_b64 s[18:19], s[76:77], 13
	v_readlane_b32 s29, v253, 2
	s_add_u32 s18, s29, s18
	v_readlane_b32 s29, v253, 3
	s_addc_u32 s19, s29, s19
	v_lshlrev_b32_e32 v2, 2, v140
	global_store_dword v2, v139, s[18:19]
	s_branch .LBB0_126

; template <bool PERMGL, bool FP8>
; __device__ __forceinline__ void q8_cols_item(const float* W, int N, int n0, unsigned char* Bq, float* sc_out, LAS float* AM, int par, int wave, int lane) {
;     const int n = n0 + lane;
;     const float* Wp = W + (size_t)(128 * wave) * N + n;
;     float v[128]; float am = 0.f;
; #pragma unroll
;     for (int i = 0; i < 128; ++i) v[i] = Wp[(size_t)i * N];
; __global__ void __launch_bounds__(NWAVES * 64, 2) mk_fwd(Args args) {
;     ...
;                     else { const int r2 = r - 1024, mi = r2 >> 4, nb = ((r2 & 15) + 8 * ((r2 >> 6) & 1)) & 15;
;                         q8_cols_item<false, true>(args.in[13] + (size_t)mi * D * D, D, nb * 64, ws + WS_WDN + (size_t)mi * D * 1024, (float*)(ws + WS_SBD) + (size_t)mi * D, CAM, par, wave_s, lane_h); } }
.LBB0_143:
	s_lshr_b32 s6, s10, 6
	s_cmpk_gt_i32 s10, 0x3ff
	s_mov_b64 s[4:5], -1
	s_cbranch_scc0 .LBB0_147
	s_lshl_b32 s4, s6, 9
	s_add_i32 s7, s9, s4
	s_add_i32 s4, s10, 0xfffffc00
	s_lshr_b32 s68, s4, 4
	s_lshl_b64 s[4:5], s[68:69], 20
	s_and_b32 s7, s7, 0x3c0
	s_add_u32 s4, s83, s4
	s_addc_u32 s5, s74, s5
	s_lshl_b64 s[12:13], s[68:69], 22
	v_add_u32_e32 v4, s7, v6
	s_add_u32 s12, s48, s12
	s_addc_u32 s13, s51, s13
	v_lshlrev_b32_e32 v32, 2, v4
	v_lshl_add_u64 v[2:3], s[12:13], 0, v[32:33]
	s_movk_i32 s11, 0x2000
	v_add_co_u32_e32 v14, vcc, s11, v2
	s_movk_i32 s11, 0x4000
	s_nop 0
	v_addc_co_u32_e32 v15, vcc, 0, v3, vcc
	global_load_dword v11, v32, s[12:13] nt
	global_load_dword v13, v[14:15], off offset:-4096 nt
	global_load_dword v12, v[14:15], off nt
	v_add_co_u32_e32 v14, vcc, s11, v2
	s_movk_i32 s11, 0x6000
	s_nop 0
	v_addc_co_u32_e32 v15, vcc, 0, v3, vcc
	v_add_co_u32_e32 v18, vcc, s11, v2
	s_mov_b32 s11, 0x8000
	s_nop 0
	v_addc_co_u32_e32 v19, vcc, 0, v3, vcc
	v_add_co_u32_e32 v20, vcc, s11, v2
	s_mov_b32 s11, 0xa000
	s_nop 0
	v_addc_co_u32_e32 v21, vcc, 0, v3, vcc
	v_add_co_u32_e32 v22, vcc, s11, v2
	s_mov_b32 s11, 0xc000
	s_nop 0
	v_addc_co_u32_e32 v23, vcc, 0, v3, vcc
	v_add_co_u32_e32 v24, vcc, s11, v2
	s_mov_b32 s11, 0xe000
	s_nop 0
	v_addc_co_u32_e32 v25, vcc, 0, v3, vcc
	global_load_dword v16, v[14:15], off offset:-4096 nt
	s_nop 0
	global_load_dword v14, v[14:15], off nt
	s_nop 0
	global_load_dword v17, v[18:19], off offset:-4096 nt
	global_load_dword v15, v[18:19], off nt
	s_nop 0
	global_load_dword v19, v[20:21], off offset:-4096 nt
	global_load_dword v18, v[20:21], off nt
	s_nop 0
	global_load_dword v21, v[22:23], off offset:-4096 nt
	global_load_dword v20, v[22:23], off nt
	s_nop 0
	global_load_dword v23, v[24:25], off offset:-4096 nt
	global_load_dword v22, v[24:25], off nt
	v_add_co_u32_e32 v24, vcc, s11, v2
	s_mov_b32 s11, 0x10000
	s_nop 0
	v_addc_co_u32_e32 v25, vcc, 0, v3, vcc
	v_add_co_u32_e32 v28, vcc, s11, v2
	s_mov_b32 s11, 0x12000
	s_nop 0
	v_addc_co_u32_e32 v29, vcc, 0, v3, vcc
	v_add_co_u32_e32 v30, vcc, s11, v2
	s_mov_b32 s11, 0x14000
	s_nop 0
	v_addc_co_u32_e32 v31, vcc, 0, v3, vcc
	v_add_co_u32_e32 v34, vcc, s11, v2
	s_mov_b32 s11, 0x16000
	s_nop 0
	v_addc_co_u32_e32 v35, vcc, 0, v3, vcc
	global_load_dword v27, v[24:25], off offset:-4096 nt
	s_nop 0
	global_load_dword v24, v[24:25], off nt
	s_nop 0
	global_load_dword v26, v[28:29], off offset:-4096 nt
	global_load_dword v25, v[28:29], off nt
	s_nop 0
	global_load_dword v29, v[30:31], off offset:-4096 nt
	global_load_dword v28, v[30:31], off nt
	s_nop 0
	global_load_dword v31, v[34:35], off offset:-4096 nt
	global_load_dword v30, v[34:35], off nt
	v_add_co_u32_e32 v34, vcc, s11, v2
	s_mov_b32 s11, 0x18000
	s_nop 0
	v_addc_co_u32_e32 v35, vcc, 0, v3, vcc
	v_add_co_u32_e32 v38, vcc, s11, v2
	s_mov_b32 s11, 0x1a000
	s_nop 0
	v_addc_co_u32_e32 v39, vcc, 0, v3, vcc
	v_add_co_u32_e32 v40, vcc, s11, v2
	s_mov_b32 s11, 0x1c000
	s_nop 0
	v_addc_co_u32_e32 v41, vcc, 0, v3, vcc
	global_load_dword v37, v[34:35], off offset:-4096 nt
	s_nop 0
	global_load_dword v34, v[34:35], off nt
	s_nop 0
	global_load_dword v36, v[38:39], off offset:-4096 nt
	global_load_dword v35, v[38:39], off nt
	s_nop 0
	global_load_dword v39, v[40:41], off offset:-4096 nt
	global_load_dword v38, v[40:41], off nt
	v_add_co_u32_e32 v40, vcc, s11, v2
	s_mov_b32 s11, 0x1e000
	s_nop 0
	v_addc_co_u32_e32 v41, vcc, 0, v3, vcc
	v_add_co_u32_e32 v44, vcc, s11, v2
	s_mov_b32 s11, 0x20000
	s_nop 0
	v_addc_co_u32_e32 v45, vcc, 0, v3, vcc
	global_load_dword v42, v[40:41], off offset:-4096 nt
	s_nop 0
	global_load_dword v40, v[40:41], off nt
	s_nop 0
	global_load_dword v49, v[44:45], off offset:-4096 nt
	global_load_dword v47, v[44:45], off nt
	v_add_co_u32_e32 v44, vcc, s11, v2
	s_mov_b32 s11, 0x22000
	s_nop 0
	v_addc_co_u32_e32 v45, vcc, 0, v3, vcc
	v_add_co_u32_e32 v50, vcc, s11, v2
	s_mov_b32 s11, 0x24000
	s_nop 0
	v_addc_co_u32_e32 v51, vcc, 0, v3, vcc
	global_load_dword v48, v[44:45], off offset:-4096 nt
	global_load_dword v41, v[44:45], off nt
	s_nop 0
	global_load_dword v44, v[50:51], off offset:-4096 nt
	global_load_dword v43, v[50:51], off nt
	v_add_co_u32_e32 v50, vcc, s11, v2
	s_mov_b32 s11, 0x26000
	s_nop 0
	v_addc_co_u32_e32 v51, vcc, 0, v3, vcc
	global_load_dword v46, v[50:51], off offset:-4096 nt
	global_load_dword v45, v[50:51], off nt
	v_add_co_u32_e32 v50, vcc, s11, v2
	s_mov_b32 s11, 0x28000
	s_nop 0
	v_addc_co_u32_e32 v51, vcc, 0, v3, vcc
	v_add_co_u32_e32 v54, vcc, s11, v2
	s_mov_b32 s11, 0x2a000
	s_nop 0
	v_addc_co_u32_e32 v55, vcc, 0, v3, vcc
	v_add_co_u32_e32 v56, vcc, s11, v2
	s_mov_b32 s11, 0x2c000
	s_nop 0
	v_addc_co_u32_e32 v57, vcc, 0, v3, vcc
	v_add_co_u32_e32 v58, vcc, s11, v2
	s_mov_b32 s11, 0x2e000
	s_nop 0
	v_addc_co_u32_e32 v59, vcc, 0, v3, vcc
	global_load_dword v53, v[50:51], off offset:-4096 nt
	s_nop 0
	global_load_dword v50, v[50:51], off nt
	s_nop 0
	global_load_dword v52, v[54:55], off offset:-4096 nt
	global_load_dword v51, v[54:55], off nt
	s_nop 0
	global_load_dword v55, v[56:57], off offset:-4096 nt
	global_load_dword v54, v[56:57], off nt
	s_nop 0
	global_load_dword v57, v[58:59], off offset:-4096 nt
	global_load_dword v56, v[58:59], off nt
	v_add_co_u32_e32 v58, vcc, s11, v2
	s_mov_b32 s11, 0x30000
	s_nop 0
	v_addc_co_u32_e32 v59, vcc, 0, v3, vcc
	v_add_co_u32_e32 v62, vcc, s11, v2
	s_mov_b32 s11, 0x32000
	s_nop 0
	v_addc_co_u32_e32 v63, vcc, 0, v3, vcc
	v_add_co_u32_e32 v64, vcc, s11, v2
	s_mov_b32 s11, 0x34000
	s_nop 0
	v_addc_co_u32_e32 v65, vcc, 0, v3, vcc
	v_add_co_u32_e32 v66, vcc, s11, v2
	s_mov_b32 s11, 0x36000
	s_nop 0
	v_addc_co_u32_e32 v67, vcc, 0, v3, vcc
; template <bool PERMGL, bool FP8>
; __device__ __forceinline__ void q8_cols_item(const float* W, int N, int n0, unsigned char* Bq, float* sc_out, LAS float* AM, int par, int wave, int lane) {
;     const int n = n0 + lane;
;     const float* Wp = W + (size_t)(128 * wave) * N + n;
;     float v[128]; float am = 0.f;
; #pragma unroll
;     for (int i = 0; i < 128; ++i) v[i] = Wp[(size_t)i * N];
	global_load_dword v61, v[58:59], off offset:-4096 nt
	s_nop 0
	global_load_dword v58, v[58:59], off nt
	s_nop 0
	global_load_dword v60, v[62:63], off offset:-4096 nt
	global_load_dword v59, v[62:63], off nt
	s_nop 0
	global_load_dword v63, v[64:65], off offset:-4096 nt
	global_load_dword v62, v[64:65], off nt
	s_nop 0
	global_load_dword v65, v[66:67], off offset:-4096 nt
	global_load_dword v64, v[66:67], off nt
	v_add_co_u32_e32 v66, vcc, s11, v2
	s_mov_b32 s11, 0x38000
	s_nop 0
	v_addc_co_u32_e32 v67, vcc, 0, v3, vcc
	v_add_co_u32_e32 v70, vcc, s11, v2
	s_mov_b32 s11, 0x3a000
	s_nop 0
	v_addc_co_u32_e32 v71, vcc, 0, v3, vcc
	v_add_co_u32_e32 v72, vcc, s11, v2
	s_mov_b32 s11, 0x3c000
	s_nop 0
	v_addc_co_u32_e32 v73, vcc, 0, v3, vcc
	global_load_dword v69, v[66:67], off offset:-4096 nt
	s_nop 0
	global_load_dword v66, v[66:67], off nt
	s_nop 0
	global_load_dword v68, v[70:71], off offset:-4096 nt
	global_load_dword v67, v[70:71], off nt
	s_nop 0
	global_load_dword v71, v[72:73], off offset:-4096 nt
	global_load_dword v70, v[72:73], off nt
	v_add_co_u32_e32 v72, vcc, s11, v2
	s_mov_b32 s11, 0x3e000
	s_nop 0
	v_addc_co_u32_e32 v73, vcc, 0, v3, vcc
	v_add_co_u32_e32 v76, vcc, s11, v2
	s_mov_b32 s11, 0x40000
	s_nop 0
	v_addc_co_u32_e32 v77, vcc, 0, v3, vcc
	global_load_dword v74, v[72:73], off offset:-4096 nt
	s_nop 0
	global_load_dword v72, v[72:73], off nt
	s_nop 0
	global_load_dword v81, v[76:77], off offset:-4096 nt
	global_load_dword v79, v[76:77], off nt
	v_add_co_u32_e32 v76, vcc, s11, v2
	s_mov_b32 s11, 0x42000
	s_nop 0
	v_addc_co_u32_e32 v77, vcc, 0, v3, vcc
	v_add_co_u32_e32 v82, vcc, s11, v2
	s_mov_b32 s11, 0x44000
	s_nop 0
	v_addc_co_u32_e32 v83, vcc, 0, v3, vcc
	global_load_dword v80, v[76:77], off offset:-4096 nt
	global_load_dword v73, v[76:77], off nt
	s_nop 0
	global_load_dword v76, v[82:83], off offset:-4096 nt
	global_load_dword v75, v[82:83], off nt
	v_add_co_u32_e32 v82, vcc, s11, v2
	s_mov_b32 s11, 0x46000
	s_nop 0
	v_addc_co_u32_e32 v83, vcc, 0, v3, vcc
	global_load_dword v78, v[82:83], off offset:-4096 nt
	global_load_dword v77, v[82:83], off nt
	v_add_co_u32_e32 v82, vcc, s11, v2
	s_mov_b32 s11, 0x48000
	s_nop 0
	v_addc_co_u32_e32 v83, vcc, 0, v3, vcc
	v_add_co_u32_e32 v86, vcc, s11, v2
	s_mov_b32 s11, 0x4a000
	s_nop 0
	v_addc_co_u32_e32 v87, vcc, 0, v3, vcc
	v_add_co_u32_e32 v88, vcc, s11, v2
	s_mov_b32 s11, 0x4c000
	s_nop 0
	v_addc_co_u32_e32 v89, vcc, 0, v3, vcc
	v_add_co_u32_e32 v90, vcc, s11, v2
	s_mov_b32 s11, 0x4e000
	s_nop 0
	v_addc_co_u32_e32 v91, vcc, 0, v3, vcc
	global_load_dword v85, v[82:83], off offset:-4096 nt
	s_nop 0
	global_load_dword v82, v[82:83], off nt
	s_nop 0
	global_load_dword v84, v[86:87], off offset:-4096 nt
	global_load_dword v83, v[86:87], off nt
	s_nop 0
	global_load_dword v87, v[88:89], off offset:-4096 nt
	global_load_dword v86, v[88:89], off nt
	s_nop 0
	global_load_dword v89, v[90:91], off offset:-4096 nt
	global_load_dword v88, v[90:91], off nt
	v_add_co_u32_e32 v90, vcc, s11, v2
	s_mov_b32 s11, 0x50000
	s_nop 0
	v_addc_co_u32_e32 v91, vcc, 0, v3, vcc
	v_add_co_u32_e32 v94, vcc, s11, v2
	s_mov_b32 s11, 0x52000
	s_nop 0
	v_addc_co_u32_e32 v95, vcc, 0, v3, vcc
	v_add_co_u32_e32 v96, vcc, s11, v2
	s_mov_b32 s11, 0x54000
	s_nop 0
	v_addc_co_u32_e32 v97, vcc, 0, v3, vcc
	v_add_co_u32_e32 v98, vcc, s11, v2
	s_mov_b32 s11, 0x56000
	s_nop 0
	v_addc_co_u32_e32 v99, vcc, 0, v3, vcc
	global_load_dword v93, v[90:91], off offset:-4096 nt
	s_nop 0
	global_load_dword v90, v[90:91], off nt
	s_nop 0
	global_load_dword v92, v[94:95], off offset:-4096 nt
	global_load_dword v91, v[94:95], off nt
	s_nop 0
	global_load_dword v95, v[96:97], off offset:-4096 nt
	global_load_dword v94, v[96:97], off nt
	s_nop 0
	global_load_dword v97, v[98:99], off offset:-4096 nt
	global_load_dword v96, v[98:99], off nt
	v_add_co_u32_e32 v98, vcc, s11, v2
	s_mov_b32 s11, 0x58000
	s_nop 0
	v_addc_co_u32_e32 v99, vcc, 0, v3, vcc
	v_add_co_u32_e32 v102, vcc, s11, v2
	s_mov_b32 s11, 0x5a000
	s_nop 0
	v_addc_co_u32_e32 v103, vcc, 0, v3, vcc
	v_add_co_u32_e32 v104, vcc, s11, v2
	s_mov_b32 s11, 0x5c000
	s_nop 0
	v_addc_co_u32_e32 v105, vcc, 0, v3, vcc
	global_load_dword v101, v[98:99], off offset:-4096 nt
	s_nop 0
	global_load_dword v98, v[98:99], off nt
	s_nop 0
	global_load_dword v100, v[102:103], off offset:-4096 nt
	global_load_dword v99, v[102:103], off nt
	s_nop 0
	global_load_dword v103, v[104:105], off offset:-4096 nt
	global_load_dword v102, v[104:105], off nt
	v_add_co_u32_e32 v104, vcc, s11, v2
	s_mov_b32 s11, 0x5e000
	s_nop 0
	v_addc_co_u32_e32 v105, vcc, 0, v3, vcc
	v_add_co_u32_e32 v108, vcc, s11, v2
	s_mov_b32 s11, 0x60000
	s_nop 0
	v_addc_co_u32_e32 v109, vcc, 0, v3, vcc
	global_load_dword v106, v[104:105], off offset:-4096 nt
	s_nop 0
	global_load_dword v104, v[104:105], off nt
	s_nop 0
	global_load_dword v113, v[108:109], off offset:-4096 nt
	global_load_dword v111, v[108:109], off nt
	v_add_co_u32_e32 v108, vcc, s11, v2
	s_mov_b32 s11, 0x62000
	s_nop 0
	v_addc_co_u32_e32 v109, vcc, 0, v3, vcc
	v_add_co_u32_e32 v114, vcc, s11, v2
	s_mov_b32 s11, 0x64000
	s_nop 0
	v_addc_co_u32_e32 v115, vcc, 0, v3, vcc
	global_load_dword v112, v[108:109], off offset:-4096 nt
	global_load_dword v105, v[108:109], off nt
	s_nop 0
	global_load_dword v108, v[114:115], off offset:-4096 nt
	global_load_dword v107, v[114:115], off nt
	v_add_co_u32_e32 v114, vcc, s11, v2
	s_mov_b32 s11, 0x66000
	s_nop 0
	v_addc_co_u32_e32 v115, vcc, 0, v3, vcc
	global_load_dword v110, v[114:115], off offset:-4096 nt
	global_load_dword v109, v[114:115], off nt
	v_add_co_u32_e32 v114, vcc, s11, v2
	s_mov_b32 s11, 0x68000
	s_nop 0
	v_addc_co_u32_e32 v115, vcc, 0, v3, vcc
; template <bool PERMGL, bool FP8>
; __device__ __forceinline__ void q8_cols_item(const float* W, int N, int n0, unsigned char* Bq, float* sc_out, LAS float* AM, int par, int wave, int lane) {
;     ...
;     for (int i = 0; i < 128; ++i) v[i] = Wp[(size_t)i * N];
;     __builtin_amdgcn_sched_barrier(0);
; #pragma unroll
;     for (int i = 0; i < 128; ++i) am = fmaxf(am, fabsf(v[i]));
;     AM[(par * 8 + wave) * 64 + lane] = am;
;     __syncthreads();
	v_add_co_u32_e32 v118, vcc, s11, v2
	s_mov_b32 s11, 0x6a000
	s_nop 0
	v_addc_co_u32_e32 v119, vcc, 0, v3, vcc
	v_add_co_u32_e32 v120, vcc, s11, v2
	s_mov_b32 s11, 0x6c000
	s_nop 0
	v_addc_co_u32_e32 v121, vcc, 0, v3, vcc
	v_add_co_u32_e32 v122, vcc, s11, v2
	s_mov_b32 s11, 0x6e000
	s_nop 0
	v_addc_co_u32_e32 v123, vcc, 0, v3, vcc
	global_load_dword v117, v[114:115], off offset:-4096 nt
	s_nop 0
	global_load_dword v114, v[114:115], off nt
	s_nop 0
	global_load_dword v116, v[118:119], off offset:-4096 nt
	global_load_dword v115, v[118:119], off nt
	s_nop 0
	global_load_dword v119, v[120:121], off offset:-4096 nt
	global_load_dword v118, v[120:121], off nt
	s_nop 0
	global_load_dword v121, v[122:123], off offset:-4096 nt
	global_load_dword v120, v[122:123], off nt
	v_add_co_u32_e32 v122, vcc, s11, v2
	s_mov_b32 s11, 0x70000
	s_nop 0
	v_addc_co_u32_e32 v123, vcc, 0, v3, vcc
	v_add_co_u32_e32 v126, vcc, s11, v2
	s_mov_b32 s11, 0x72000
	s_nop 0
	v_addc_co_u32_e32 v127, vcc, 0, v3, vcc
	v_add_co_u32_e32 v128, vcc, s11, v2
	s_mov_b32 s11, 0x74000
	s_nop 0
	v_addc_co_u32_e32 v129, vcc, 0, v3, vcc
	v_add_co_u32_e32 v130, vcc, s11, v2
	s_mov_b32 s11, 0x76000
	s_nop 0
	v_addc_co_u32_e32 v131, vcc, 0, v3, vcc
	global_load_dword v125, v[122:123], off offset:-4096 nt
	s_nop 0
	global_load_dword v122, v[122:123], off nt
	s_nop 0
	global_load_dword v124, v[126:127], off offset:-4096 nt
	global_load_dword v123, v[126:127], off nt
	s_nop 0
	global_load_dword v127, v[128:129], off offset:-4096 nt
	global_load_dword v126, v[128:129], off nt
	s_nop 0
	global_load_dword v129, v[130:131], off offset:-4096 nt
	global_load_dword v128, v[130:131], off nt
	v_add_co_u32_e32 v130, vcc, s11, v2
	s_mov_b32 s11, 0x78000
	s_nop 0
	v_addc_co_u32_e32 v131, vcc, 0, v3, vcc
	v_add_co_u32_e32 v134, vcc, s11, v2
	s_mov_b32 s11, 0x7a000
	s_nop 0
	v_addc_co_u32_e32 v135, vcc, 0, v3, vcc
	v_add_co_u32_e32 v136, vcc, s11, v2
	s_mov_b32 s11, 0x7c000
	s_nop 0
	v_addc_co_u32_e32 v137, vcc, 0, v3, vcc
	v_add_co_u32_e32 v138, vcc, s11, v2
	s_mov_b32 s11, 0x7e000
	s_nop 0
	v_addc_co_u32_e32 v139, vcc, 0, v3, vcc
	v_add_co_u32_e32 v140, vcc, s11, v2
	s_mov_b32 s11, 0x7f000
	s_nop 0
	v_addc_co_u32_e32 v141, vcc, 0, v3, vcc
	v_add_co_u32_e32 v2, vcc, s11, v2
	global_load_dword v133, v[130:131], off offset:-4096 nt
	s_nop 0
	global_load_dword v130, v[130:131], off nt
	s_nop 0
	global_load_dword v132, v[134:135], off offset:-4096 nt
	global_load_dword v131, v[134:135], off nt
	s_nop 0
	global_load_dword v135, v[136:137], off offset:-4096 nt
	global_load_dword v134, v[136:137], off nt
	s_nop 0
	global_load_dword v137, v[138:139], off offset:-4096 nt
	global_load_dword v136, v[138:139], off nt
	s_nop 0
	global_load_dword v139, v[140:141], off offset:-4096 nt
	global_load_dword v138, v[140:141], off nt
	v_addc_co_u32_e32 v3, vcc, 0, v3, vcc
	global_load_dword v140, v[2:3], off nt
	s_waitcnt vmcnt(0)
	v_max3_f32 v2, |v11|, 0, |v13|
	v_max3_f32 v2, v2, |v12|, |v16|
	v_max3_f32 v2, v2, |v14|, |v17|
	v_max3_f32 v2, v2, |v15|, |v19|
	v_max3_f32 v2, v2, |v18|, |v21|
	v_max3_f32 v2, v2, |v20|, |v23|
	v_max3_f32 v2, v2, |v22|, |v27|
	v_max3_f32 v2, v2, |v24|, |v26|
	v_max3_f32 v2, v2, |v25|, |v29|
	v_max3_f32 v2, v2, |v28|, |v31|
	v_max3_f32 v2, v2, |v30|, |v37|
	v_max3_f32 v2, v2, |v34|, |v36|
	v_max3_f32 v2, v2, |v35|, |v39|
	v_max3_f32 v2, v2, |v38|, |v42|
	v_max3_f32 v2, v2, |v40|, |v49|
	v_max3_f32 v2, v2, |v47|, |v48|
	v_max3_f32 v2, v2, |v41|, |v44|
	v_max3_f32 v2, v2, |v43|, |v46|
	v_max3_f32 v2, v2, |v45|, |v53|
	v_max3_f32 v2, v2, |v50|, |v52|
	v_max3_f32 v2, v2, |v51|, |v55|
	v_max3_f32 v2, v2, |v54|, |v57|
	v_max3_f32 v2, v2, |v56|, |v61|
	v_max3_f32 v2, v2, |v58|, |v60|
	v_max3_f32 v2, v2, |v59|, |v63|
	v_max3_f32 v2, v2, |v62|, |v65|
	v_max3_f32 v2, v2, |v64|, |v69|
	v_max3_f32 v2, v2, |v66|, |v68|
	v_max3_f32 v2, v2, |v67|, |v71|
	v_max3_f32 v2, v2, |v70|, |v74|
	v_max3_f32 v2, v2, |v72|, |v81|
	v_max3_f32 v2, v2, |v79|, |v80|
	v_max3_f32 v2, v2, |v73|, |v76|
	v_max3_f32 v2, v2, |v75|, |v78|
	v_max3_f32 v2, v2, |v77|, |v85|
	v_max3_f32 v2, v2, |v82|, |v84|
	v_max3_f32 v2, v2, |v83|, |v87|
	v_max3_f32 v2, v2, |v86|, |v89|
	v_max3_f32 v2, v2, |v88|, |v93|
	v_max3_f32 v2, v2, |v90|, |v92|
	v_max3_f32 v2, v2, |v91|, |v95|
	v_max3_f32 v2, v2, |v94|, |v97|
	v_max3_f32 v2, v2, |v96|, |v101|
	v_max3_f32 v2, v2, |v98|, |v100|
	v_max3_f32 v2, v2, |v99|, |v103|
	v_max3_f32 v2, v2, |v102|, |v106|
	v_max3_f32 v2, v2, |v104|, |v113|
	v_max3_f32 v2, v2, |v111|, |v112|
	v_max3_f32 v2, v2, |v105|, |v108|
	v_max3_f32 v2, v2, |v107|, |v110|
	v_max3_f32 v2, v2, |v109|, |v117|
	v_max3_f32 v2, v2, |v114|, |v116|
	v_max3_f32 v2, v2, |v115|, |v119|
	v_max3_f32 v2, v2, |v118|, |v121|
	v_max3_f32 v2, v2, |v120|, |v125|
	v_max3_f32 v2, v2, |v122|, |v124|
	v_max3_f32 v2, v2, |v123|, |v127|
	v_max3_f32 v2, v2, |v126|, |v129|
	v_max3_f32 v2, v2, |v128|, |v133|
	v_max3_f32 v2, v2, |v130|, |v132|
	v_max3_f32 v2, v2, |v131|, |v135|
	v_max3_f32 v2, v2, |v134|, |v137|
	v_max3_f32 v2, v2, |v136|, |v139|
	s_lshl_b32 s11, s8, 11
	v_max3_f32 v5, v2, |v138|, |v140|
	v_add_u32_e32 v2, s11, v10
	v_add_u32_e32 v141, s11, v7
	ds_write_b32 v2, v5
	s_waitcnt lgkmcnt(0)
	s_barrier
; template <bool PERMGL, bool FP8>
; __device__ __forceinline__ void q8_cols_item(const float* W, int N, int n0, unsigned char* Bq, float* sc_out, LAS float* AM, int par, int wave, int lane) {
;     ...
;     for (int w = 0; w < 8; ++w) am = fmaxf(am, AM[(par * 8 + w) * 64 + lane]);
;     const float sc = am > 0.f ? am * (FP8 ? (1.0f / 256.0f) : (1.0f / 127.0f)) : 1.0f, inv = 1.0f / sc;
;     int row = n;
;     if (PERMGL) { const int j = n >> 1, pr = n & 1, o = j & 127; row = ((j >> 7) << 8) + (((o >> 2) & 1) << 7) + ((o >> 5) << 5) + (pr << 4) + (((o >> 3) & 3) << 2) + (o & 3); }
;     if (!PERMGL) { const int o = n & 255; row = ((n >> 8) << 8) + (((o >> 3) & 1) << 7) + ((o >> 6) << 5) + (((o >> 4) & 3) << 3) + (o & 7); }
;     auto xq = [](unsigned x) { return (unsigned)__builtin_amdgcn_update_dpp(0, (int)x, 0xB1, 0xf, 0xf, true); };
;     const bool odd = lane & 1;
;     const int rowp = (int)xq((unsigned)row);
;     unsigned char* plo = Bq + (size_t)(odd ? rowp : row) * 1024 + 128 * wave + (odd ? 16 : 0);
;     unsigned char* phi = Bq + (size_t)(odd ? row : rowp) * 1024 + 128 * wave + (odd ? 16 : 0);
;     auto packc = [&](int c) { u32x4 o;
;         if (FP8) { o.x = f8x4(v[16 * c], v[16 * c + 1], v[16 * c + 2], v[16 * c + 3], inv); o.y = f8x4(v[16 * c + 4], v[16 * c + 5], v[16 * c + 6], v[16 * c + 7], inv);
;                    o.z = f8x4(v[16 * c + 8], v[16 * c + 9], v[16 * c + 10], v[16 * c + 11], inv); o.w = f8x4(v[16 * c + 12], v[16 * c + 13], v[16 * c + 14], v[16 * c + 15], inv); }
;         else { o.x = q8x4(v[16 * c], v[16 * c + 1], v[16 * c + 2], v[16 * c + 3], inv); o.y = q8x4(v[16 * c + 4], v[16 * c + 5], v[16 * c + 6], v[16 * c + 7], inv);
;                o.z = q8x4(v[16 * c + 8], v[16 * c + 9], v[16 * c + 10], v[16 * c + 11], inv); o.w = q8x4(v[16 * c + 12], v[16 * c + 13], v[16 * c + 14], v[16 * c + 15], inv); }
;         return o; };
; #pragma unroll
;     for (int j = 0; j < 4; ++j) { const u32x4 p0 = packc(2 * j), p1 = packc(2 * j + 1);
;         u32x4 snd, rcv;
; #pragma unroll
;         for (int q = 0; q < 4; ++q) { snd[q] = odd ? p0[q] : p1[q]; rcv[q] = xq(snd[q]); }
;         u32x4 a, b;
; #pragma unroll
;         for (int q = 0; q < 4; ++q) { a[q] = odd ? rcv[q] : p0[q]; b[q] = odd ? p1[q] : rcv[q]; }
;         *(u32x4*)(plo + 32 * j) = a; *(u32x4*)(phi + 32 * j) = b; }
	ds_read2st64_b32 v[2:3], v141 offset1:1
	s_waitcnt lgkmcnt(0)
	v_max3_f32 v5, v5, v2, v3
	ds_read2st64_b32 v[2:3], v141 offset0:2 offset1:3
	s_waitcnt lgkmcnt(0)
	v_max3_f32 v5, v5, v2, v3
	ds_read2st64_b32 v[2:3], v141 offset0:4 offset1:5
	s_waitcnt lgkmcnt(0)
	v_max3_f32 v5, v5, v2, v3
	ds_read2st64_b32 v[2:3], v141 offset0:6 offset1:7
	s_waitcnt lgkmcnt(0)
	v_max3_f32 v2, v5, v2, v3
	v_cmp_lt_f32_e32 vcc, 0, v2
	v_mul_f32_e32 v2, 0x3b800000, v2
	s_nop 0
	v_cndmask_b32_e32 v141, 1.0, v2, vcc
	v_div_scale_f32 v2, s[12:13], v141, v141, 1.0
	v_rcp_f32_e32 v3, v2
	s_nop 0
	v_fma_f32 v5, -v2, v3, 1.0
	v_fmac_f32_e32 v3, v5, v3
	v_div_scale_f32 v5, vcc, 1.0, v141, 1.0
	v_mul_f32_e32 v142, v5, v3
	v_fma_f32 v143, -v2, v142, v5
	v_fmac_f32_e32 v142, v143, v3
	v_fma_f32 v2, -v2, v142, v5
	v_div_fmas_f32 v2, v2, v3, v142
	v_div_fixup_f32 v142, v2, v141, 1.0
	v_mul_f32_e32 v11, v11, v142
	v_mul_f32_e32 v13, v13, v142
	v_mov_b32_e32 v143, v33
	v_cvt_pk_fp8_f32 v143, v11, v13
	v_mul_f32_e32 v11, v12, v142
	v_mul_f32_e32 v12, v16, v142
	v_mov_b32_e32 v13, v33
	v_cvt_pk_fp8_f32 v143, v11, v12 op_sel:[0,0,1]
	v_mul_f32_e32 v11, v14, v142
	v_mul_f32_e32 v12, v17, v142
	v_cvt_pk_fp8_f32 v13, v11, v12
	v_mul_f32_e32 v11, v15, v142
	v_mul_f32_e32 v12, v19, v142
	v_mov_b32_e32 v14, v33
	v_cvt_pk_fp8_f32 v13, v11, v12 op_sel:[0,0,1]
	v_mul_f32_e32 v11, v18, v142
	v_mul_f32_e32 v12, v21, v142
	v_cvt_pk_fp8_f32 v14, v11, v12
	v_mul_f32_e32 v11, v20, v142
	v_mul_f32_e32 v12, v23, v142
	v_mov_b32_e32 v15, v33
	v_cvt_pk_fp8_f32 v14, v11, v12 op_sel:[0,0,1]
	v_mul_f32_e32 v11, v22, v142
	v_mul_f32_e32 v12, v27, v142
	v_cvt_pk_fp8_f32 v15, v11, v12
	v_mul_f32_e32 v11, v24, v142
	v_mul_f32_e32 v12, v26, v142
	v_mov_b32_e32 v16, v33
	v_cvt_pk_fp8_f32 v15, v11, v12 op_sel:[0,0,1]
	v_mul_f32_e32 v11, v25, v142
	v_mul_f32_e32 v12, v29, v142
	v_cvt_pk_fp8_f32 v16, v11, v12
	v_mul_f32_e32 v11, v28, v142
	v_mul_f32_e32 v12, v31, v142
	v_mov_b32_e32 v17, v33
	v_cvt_pk_fp8_f32 v16, v11, v12 op_sel:[0,0,1]
	v_mul_f32_e32 v11, v30, v142
	v_mul_f32_e32 v12, v37, v142
	v_cvt_pk_fp8_f32 v17, v11, v12
	v_mul_f32_e32 v11, v34, v142
	v_mul_f32_e32 v12, v36, v142
	v_mov_b32_e32 v18, v33
	v_cvt_pk_fp8_f32 v17, v11, v12 op_sel:[0,0,1]
	v_mul_f32_e32 v11, v35, v142
	v_mul_f32_e32 v12, v39, v142
	v_cvt_pk_fp8_f32 v18, v11, v12
	v_mul_f32_e32 v11, v38, v142
	v_mul_f32_e32 v12, v42, v142
	v_mov_b32_e32 v19, v33
	v_cvt_pk_fp8_f32 v18, v11, v12 op_sel:[0,0,1]
	v_mul_f32_e32 v11, v40, v142
	v_mul_f32_e32 v12, v49, v142
	v_add_u16_e32 v2, s7, v6
	v_cvt_pk_fp8_f32 v19, v11, v12
	v_lshrrev_b16_e32 v2, 1, v2
	v_and_b32_e32 v2, 0x78, v2
	v_and_b32_e32 v3, 0x707, v4
	v_or3_b32 v4, v3, v8, v2
	v_mul_f32_e32 v11, v47, v142
	v_mul_f32_e32 v12, v48, v142
	v_mov_b32_dpp v5, v4 quad_perm:[1,0,3,2] row_mask:0xf bank_mask:0xf bound_ctrl:1
	v_cvt_pk_fp8_f32 v19, v11, v12 op_sel:[0,0,1]
	v_cndmask_b32_e64 v2, v5, v4, s[2:3]
	v_ashrrev_i32_e32 v3, 31, v2
	v_cndmask_b32_e64 v4, v4, v5, s[2:3]
	v_cndmask_b32_e64 v12, v13, v17, s[2:3]
	v_lshlrev_b64 v[2:3], 10, v[2:3]
	v_ashrrev_i32_e32 v5, 31, v4
	v_mov_b32_dpp v20, v12 quad_perm:[1,0,3,2] row_mask:0xf bank_mask:0xf bound_ctrl:1
	v_cndmask_b32_e64 v12, v14, v18, s[2:3]
	v_lshl_add_u64 v[2:3], s[4:5], 0, v[2:3]
	v_lshlrev_b64 v[4:5], 10, v[4:5]
	v_cndmask_b32_e64 v11, v143, v16, s[2:3]
	v_mov_b32_dpp v21, v12 quad_perm:[1,0,3,2] row_mask:0xf bank_mask:0xf bound_ctrl:1
	v_cndmask_b32_e64 v12, v15, v19, s[2:3]
	v_lshl_add_u64 v[2:3], v[2:3], 0, s[42:43]
	v_lshl_add_u64 v[4:5], s[4:5], 0, v[4:5]
	v_mov_b32_dpp v11, v11 quad_perm:[1,0,3,2] row_mask:0xf bank_mask:0xf bound_ctrl:1
	v_mov_b32_dpp v22, v12 quad_perm:[1,0,3,2] row_mask:0xf bank_mask:0xf bound_ctrl:1
	v_lshl_add_u64 v[2:3], v[2:3], 0, v[0:1]
	v_lshl_add_u64 v[4:5], v[4:5], 0, s[42:43]
	v_cndmask_b32_e64 v12, v11, v143, s[2:3]
	v_cndmask_b32_e64 v13, v20, v13, s[2:3]
	v_cndmask_b32_e64 v14, v21, v14, s[2:3]
	v_cndmask_b32_e64 v15, v22, v15, s[2:3]
	v_lshl_add_u64 v[4:5], v[4:5], 0, v[0:1]
	v_cndmask_b32_e64 v16, v16, v11, s[2:3]
	v_cndmask_b32_e64 v17, v17, v20, s[2:3]
	v_cndmask_b32_e64 v18, v18, v21, s[2:3]
	v_cndmask_b32_e64 v19, v19, v22, s[2:3]
	global_store_dwordx4 v[2:3], v[12:15], off
	global_store_dwordx4 v[4:5], v[16:19], off
	v_mul_f32_e32 v11, v41, v142
	v_mul_f32_e32 v12, v44, v142
	v_mov_b32_e32 v13, v33
	v_cvt_pk_fp8_f32 v13, v11, v12
	v_mul_f32_e32 v11, v43, v142
	v_mul_f32_e32 v12, v46, v142
	v_mov_b32_e32 v14, v33
	v_cvt_pk_fp8_f32 v13, v11, v12 op_sel:[0,0,1]
	v_mul_f32_e32 v11, v45, v142
	v_mul_f32_e32 v12, v53, v142
	v_cvt_pk_fp8_f32 v14, v11, v12
	v_mul_f32_e32 v11, v50, v142
	v_mul_f32_e32 v12, v52, v142
	v_mov_b32_e32 v15, v33
	v_cvt_pk_fp8_f32 v14, v11, v12 op_sel:[0,0,1]
	v_mul_f32_e32 v11, v51, v142
	v_mul_f32_e32 v12, v55, v142
	v_cvt_pk_fp8_f32 v15, v11, v12
	v_mul_f32_e32 v11, v54, v142
	v_mul_f32_e32 v12, v57, v142
	v_mov_b32_e32 v19, v33
	v_cvt_pk_fp8_f32 v15, v11, v12 op_sel:[0,0,1]
	v_mul_f32_e32 v11, v56, v142
	v_mul_f32_e32 v12, v61, v142
	v_cvt_pk_fp8_f32 v19, v11, v12
	v_mul_f32_e32 v11, v58, v142
	v_mul_f32_e32 v12, v60, v142
	v_mov_b32_e32 v16, v33
	v_cvt_pk_fp8_f32 v19, v11, v12 op_sel:[0,0,1]
	v_mul_f32_e32 v11, v59, v142
	v_mul_f32_e32 v12, v63, v142
	v_cvt_pk_fp8_f32 v16, v11, v12
	v_mul_f32_e32 v11, v62, v142
	v_mul_f32_e32 v12, v65, v142
	v_mov_b32_e32 v17, v33
	v_cvt_pk_fp8_f32 v16, v11, v12 op_sel:[0,0,1]
	v_mul_f32_e32 v11, v64, v142
	v_mul_f32_e32 v12, v69, v142
	v_cvt_pk_fp8_f32 v17, v11, v12
	v_mul_f32_e32 v11, v66, v142
	v_mul_f32_e32 v12, v68, v142
	v_mov_b32_e32 v18, v33
	v_cvt_pk_fp8_f32 v17, v11, v12 op_sel:[0,0,1]
	v_mul_f32_e32 v11, v67, v142
; template <bool PERMGL, bool FP8>
; __device__ __forceinline__ void q8_cols_item(const float* W, int N, int n0, unsigned char* Bq, float* sc_out, LAS float* AM, int par, int wave, int lane) {
;     ...
;     auto packc = [&](int c) { u32x4 o;
;         if (FP8) { o.x = f8x4(v[16 * c], v[16 * c + 1], v[16 * c + 2], v[16 * c + 3], inv); o.y = f8x4(v[16 * c + 4], v[16 * c + 5], v[16 * c + 6], v[16 * c + 7], inv);
;                    o.z = f8x4(v[16 * c + 8], v[16 * c + 9], v[16 * c + 10], v[16 * c + 11], inv); o.w = f8x4(v[16 * c + 12], v[16 * c + 13], v[16 * c + 14], v[16 * c + 15], inv); }
;         else { o.x = q8x4(v[16 * c], v[16 * c + 1], v[16 * c + 2], v[16 * c + 3], inv); o.y = q8x4(v[16 * c + 4], v[16 * c + 5], v[16 * c + 6], v[16 * c + 7], inv);
;                o.z = q8x4(v[16 * c + 8], v[16 * c + 9], v[16 * c + 10], v[16 * c + 11], inv); o.w = q8x4(v[16 * c + 12], v[16 * c + 13], v[16 * c + 14], v[16 * c + 15], inv); }
;         return o; };
; #pragma unroll
;     for (int j = 0; j < 4; ++j) { const u32x4 p0 = packc(2 * j), p1 = packc(2 * j + 1);
;         u32x4 snd, rcv;
; #pragma unroll
;         for (int q = 0; q < 4; ++q) { snd[q] = odd ? p0[q] : p1[q]; rcv[q] = xq(snd[q]); }
;         u32x4 a, b;
; #pragma unroll
;         for (int q = 0; q < 4; ++q) { a[q] = odd ? rcv[q] : p0[q]; b[q] = odd ? p1[q] : rcv[q]; }
;         *(u32x4*)(plo + 32 * j) = a; *(u32x4*)(phi + 32 * j) = b; }
	v_mul_f32_e32 v12, v71, v142
	v_cvt_pk_fp8_f32 v18, v11, v12
	v_mul_f32_e32 v11, v70, v142
	v_mul_f32_e32 v12, v74, v142
	v_mov_b32_e32 v20, v33
	v_cvt_pk_fp8_f32 v18, v11, v12 op_sel:[0,0,1]
	v_mul_f32_e32 v11, v72, v142
	v_mul_f32_e32 v12, v81, v142
	v_cvt_pk_fp8_f32 v20, v11, v12
	v_mul_f32_e32 v11, v79, v142
	v_mul_f32_e32 v12, v80, v142
	s_and_b64 vcc, exec, s[0:1]
	v_cvt_pk_fp8_f32 v20, v11, v12 op_sel:[0,0,1]
	v_cndmask_b32_e64 v12, v14, v17, s[2:3]
	v_cndmask_b32_e64 v11, v13, v16, s[2:3]
	s_nop 0
	v_mov_b32_dpp v21, v12 quad_perm:[1,0,3,2] row_mask:0xf bank_mask:0xf bound_ctrl:1
	v_cndmask_b32_e64 v12, v15, v18, s[2:3]
	v_mov_b32_dpp v11, v11 quad_perm:[1,0,3,2] row_mask:0xf bank_mask:0xf bound_ctrl:1
	v_cndmask_b32_e64 v16, v16, v11, s[2:3]
	v_mov_b32_dpp v22, v12 quad_perm:[1,0,3,2] row_mask:0xf bank_mask:0xf bound_ctrl:1
	v_cndmask_b32_e64 v12, v19, v20, s[2:3]
	v_cndmask_b32_e64 v17, v17, v21, s[2:3]
	v_cndmask_b32_e64 v18, v18, v22, s[2:3]
	v_mov_b32_dpp v23, v12 quad_perm:[1,0,3,2] row_mask:0xf bank_mask:0xf bound_ctrl:1
	v_cndmask_b32_e64 v12, v11, v13, s[2:3]
	v_cndmask_b32_e64 v13, v21, v14, s[2:3]
	v_cndmask_b32_e64 v14, v22, v15, s[2:3]
	v_cndmask_b32_e64 v15, v23, v19, s[2:3]
	v_cndmask_b32_e64 v19, v20, v23, s[2:3]
	global_store_dwordx4 v[2:3], v[12:15], off offset:32
	global_store_dwordx4 v[4:5], v[16:19], off offset:32
	v_mul_f32_e32 v11, v73, v142
	v_mul_f32_e32 v12, v76, v142
	v_mov_b32_e32 v13, v33
	v_cvt_pk_fp8_f32 v13, v11, v12
	v_mul_f32_e32 v11, v75, v142
	v_mul_f32_e32 v12, v78, v142
	v_mov_b32_e32 v14, v33
	v_cvt_pk_fp8_f32 v13, v11, v12 op_sel:[0,0,1]
	v_mul_f32_e32 v11, v77, v142
	v_mul_f32_e32 v12, v85, v142
	v_cvt_pk_fp8_f32 v14, v11, v12
	v_mul_f32_e32 v11, v82, v142
	v_mul_f32_e32 v12, v84, v142
	v_mov_b32_e32 v15, v33
	v_cvt_pk_fp8_f32 v14, v11, v12 op_sel:[0,0,1]
	v_mul_f32_e32 v11, v83, v142
	v_mul_f32_e32 v12, v87, v142
	v_cvt_pk_fp8_f32 v15, v11, v12
	v_mul_f32_e32 v11, v86, v142
	v_mul_f32_e32 v12, v89, v142
	v_mov_b32_e32 v19, v33
	v_cvt_pk_fp8_f32 v15, v11, v12 op_sel:[0,0,1]
	v_mul_f32_e32 v11, v88, v142
	v_mul_f32_e32 v12, v93, v142
	v_cvt_pk_fp8_f32 v19, v11, v12
	v_mul_f32_e32 v11, v90, v142
	v_mul_f32_e32 v12, v92, v142
	v_mov_b32_e32 v16, v33
	v_cvt_pk_fp8_f32 v19, v11, v12 op_sel:[0,0,1]
	v_mul_f32_e32 v11, v91, v142
	v_mul_f32_e32 v12, v95, v142
	v_cvt_pk_fp8_f32 v16, v11, v12
	v_mul_f32_e32 v11, v94, v142
	v_mul_f32_e32 v12, v97, v142
	v_mov_b32_e32 v17, v33
	v_cvt_pk_fp8_f32 v16, v11, v12 op_sel:[0,0,1]
	v_mul_f32_e32 v11, v96, v142
	v_mul_f32_e32 v12, v101, v142
	v_cvt_pk_fp8_f32 v17, v11, v12
	v_mul_f32_e32 v11, v98, v142
	v_mul_f32_e32 v12, v100, v142
	v_mov_b32_e32 v18, v33
	v_cvt_pk_fp8_f32 v17, v11, v12 op_sel:[0,0,1]
	v_mul_f32_e32 v11, v99, v142
	v_mul_f32_e32 v12, v103, v142
	v_cvt_pk_fp8_f32 v18, v11, v12
	v_mul_f32_e32 v11, v102, v142
	v_mul_f32_e32 v12, v106, v142
	v_mov_b32_e32 v20, v33
	v_cvt_pk_fp8_f32 v18, v11, v12 op_sel:[0,0,1]
	v_mul_f32_e32 v11, v104, v142
	v_mul_f32_e32 v12, v113, v142
	v_cvt_pk_fp8_f32 v20, v11, v12
	v_mul_f32_e32 v11, v111, v142
	v_mul_f32_e32 v12, v112, v142
	v_cvt_pk_fp8_f32 v20, v11, v12 op_sel:[0,0,1]
	v_cndmask_b32_e64 v12, v14, v17, s[2:3]
	v_cndmask_b32_e64 v11, v13, v16, s[2:3]
	s_nop 0
	v_mov_b32_dpp v21, v12 quad_perm:[1,0,3,2] row_mask:0xf bank_mask:0xf bound_ctrl:1
	v_cndmask_b32_e64 v12, v15, v18, s[2:3]
	v_mov_b32_dpp v11, v11 quad_perm:[1,0,3,2] row_mask:0xf bank_mask:0xf bound_ctrl:1
	v_cndmask_b32_e64 v16, v16, v11, s[2:3]
	v_mov_b32_dpp v22, v12 quad_perm:[1,0,3,2] row_mask:0xf bank_mask:0xf bound_ctrl:1
	v_cndmask_b32_e64 v12, v19, v20, s[2:3]
	v_cndmask_b32_e64 v17, v17, v21, s[2:3]
	v_cndmask_b32_e64 v18, v18, v22, s[2:3]
	v_mov_b32_dpp v23, v12 quad_perm:[1,0,3,2] row_mask:0xf bank_mask:0xf bound_ctrl:1
	v_cndmask_b32_e64 v12, v11, v13, s[2:3]
	v_cndmask_b32_e64 v13, v21, v14, s[2:3]
	v_cndmask_b32_e64 v14, v22, v15, s[2:3]
	v_cndmask_b32_e64 v15, v23, v19, s[2:3]
	v_cndmask_b32_e64 v19, v20, v23, s[2:3]
	global_store_dwordx4 v[2:3], v[12:15], off offset:64
	global_store_dwordx4 v[4:5], v[16:19], off offset:64
	v_mul_f32_e32 v11, v105, v142
	v_mul_f32_e32 v12, v108, v142
	v_mov_b32_e32 v13, v33
	v_cvt_pk_fp8_f32 v13, v11, v12
	v_mul_f32_e32 v11, v107, v142
	v_mul_f32_e32 v12, v110, v142
	v_mov_b32_e32 v14, v33
	v_cvt_pk_fp8_f32 v13, v11, v12 op_sel:[0,0,1]
	v_mul_f32_e32 v11, v109, v142
	v_mul_f32_e32 v12, v117, v142
	v_cvt_pk_fp8_f32 v14, v11, v12
	v_mul_f32_e32 v11, v114, v142
	v_mul_f32_e32 v12, v116, v142
	v_mov_b32_e32 v15, v33
	v_cvt_pk_fp8_f32 v14, v11, v12 op_sel:[0,0,1]
	v_mul_f32_e32 v11, v115, v142
	v_mul_f32_e32 v12, v119, v142
	v_cvt_pk_fp8_f32 v15, v11, v12
	v_mul_f32_e32 v11, v118, v142
	v_mul_f32_e32 v12, v121, v142
	v_mov_b32_e32 v19, v33
	v_cvt_pk_fp8_f32 v15, v11, v12 op_sel:[0,0,1]
	v_mul_f32_e32 v11, v120, v142
	v_mul_f32_e32 v12, v125, v142
	v_cvt_pk_fp8_f32 v19, v11, v12
	v_mul_f32_e32 v11, v122, v142
	v_mul_f32_e32 v12, v124, v142
	v_mov_b32_e32 v16, v33
	v_cvt_pk_fp8_f32 v19, v11, v12 op_sel:[0,0,1]
	v_mul_f32_e32 v11, v123, v142
	v_mul_f32_e32 v12, v127, v142
	v_cvt_pk_fp8_f32 v16, v11, v12
	v_mul_f32_e32 v11, v126, v142
	v_mul_f32_e32 v12, v129, v142
	v_mov_b32_e32 v17, v33
	v_cvt_pk_fp8_f32 v16, v11, v12 op_sel:[0,0,1]
	v_mul_f32_e32 v11, v128, v142
	v_mul_f32_e32 v12, v133, v142
	v_cvt_pk_fp8_f32 v17, v11, v12
	v_mul_f32_e32 v11, v130, v142
	v_mul_f32_e32 v12, v132, v142
	v_mov_b32_e32 v18, v33
	v_cvt_pk_fp8_f32 v17, v11, v12 op_sel:[0,0,1]
	v_mul_f32_e32 v11, v131, v142
	v_mul_f32_e32 v12, v135, v142
	v_cvt_pk_fp8_f32 v18, v11, v12
	v_mul_f32_e32 v11, v134, v142
	v_mul_f32_e32 v12, v137, v142
	v_mov_b32_e32 v20, v33
	v_cvt_pk_fp8_f32 v18, v11, v12 op_sel:[0,0,1]
	v_mul_f32_e32 v11, v136, v142
	v_mul_f32_e32 v12, v139, v142
	v_cvt_pk_fp8_f32 v20, v11, v12
	v_mul_f32_e32 v11, v138, v142
	v_mul_f32_e32 v12, v140, v142
	v_cvt_pk_fp8_f32 v20, v11, v12 op_sel:[0,0,1]
	v_cndmask_b32_e64 v12, v14, v17, s[2:3]
	v_cndmask_b32_e64 v11, v13, v16, s[2:3]
	s_nop 0
	v_mov_b32_dpp v21, v12 quad_perm:[1,0,3,2] row_mask:0xf bank_mask:0xf bound_ctrl:1
	v_cndmask_b32_e64 v12, v15, v18, s[2:3]
	v_mov_b32_dpp v11, v11 quad_perm:[1,0,3,2] row_mask:0xf bank_mask:0xf bound_ctrl:1
	v_cndmask_b32_e64 v16, v16, v11, s[2:3]
	v_mov_b32_dpp v22, v12 quad_perm:[1,0,3,2] row_mask:0xf bank_mask:0xf bound_ctrl:1
	v_cndmask_b32_e64 v12, v19, v20, s[2:3]
	v_cndmask_b32_e64 v17, v17, v21, s[2:3]
	v_cndmask_b32_e64 v18, v18, v22, s[2:3]
	v_mov_b32_dpp v23, v12 quad_perm:[1,0,3,2] row_mask:0xf bank_mask:0xf bound_ctrl:1
	v_cndmask_b32_e64 v12, v11, v13, s[2:3]
	v_cndmask_b32_e64 v13, v21, v14, s[2:3]
	v_cndmask_b32_e64 v14, v22, v15, s[2:3]
	v_cndmask_b32_e64 v15, v23, v19, s[2:3]
	v_cndmask_b32_e64 v19, v20, v23, s[2:3]
	global_store_dwordx4 v[2:3], v[12:15], off offset:96
	global_store_dwordx4 v[4:5], v[16:19], off offset:96
	s_cbranch_vccnz .LBB0_146
; template <bool PERMGL, bool FP8>
; __device__ __forceinline__ void q8_cols_item(const float* W, int N, int n0, unsigned char* Bq, float* sc_out, LAS float* AM, int par, int wave, int lane) {
;     ...
;     if (wave == 0) sc_out[PERMGL ? row : n] = FP8 ? sc * 16.0f : sc;
	s_lshl_b64 s[4:5], s[68:69], 12
	v_readlane_b32 s7, v252, 60
	s_add_u32 s4, s7, s4
	v_readlane_b32 s7, v252, 61
	s_addc_u32 s5, s7, s5
	v_mul_f32_e32 v2, 0x41800000, v141
	global_store_dword v32, v2, s[4:5]

; template <bool PERMGL, bool FP8>
; __device__ __forceinline__ void q8_cols_item(const float* W, int N, int n0, unsigned char* Bq, float* sc_out, LAS float* AM, int par, int wave, int lane) {
;     const int n = n0 + lane;
;     const float* Wp = W + (size_t)(128 * wave) * N + n;
;     float v[128]; float am = 0.f;
; #pragma unroll
;     for (int i = 0; i < 128; ++i) v[i] = Wp[(size_t)i * N];
; __global__ void __launch_bounds__(NWAVES * 64, 2) mk_fwd(Args args) {
;     ...
;                     if (r < 1024) { const int mi = r >> 5, nb = ((r & 31) + 8 * ((r >> 6) & 3)) & 31;
;                         q8_cols_item<true, false>(args.in[11] + (size_t)mi * D * 2048, 2048, nb * 64, ws + WS_WGU + (size_t)mi * 2048 * 1024, (float*)(ws + WS_SB) + (size_t)mi * 2048, CAM, par, wave_s, lane_h); }
.LBB0_147:
	s_andn2_b64 vcc, exec, s[4:5]
	s_cbranch_vccnz .LBB0_142
	s_lshl_b32 s4, s6, 9
	s_add_i32 s6, s9, s4
	s_ashr_i32 s4, s10, 5
	s_ashr_i32 s5, s4, 31
	s_lshl_b64 s[12:13], s[4:5], 23
	s_and_b32 s11, s6, 0x7c0
	s_lshl_b64 s[6:7], s[4:5], 21
	s_add_u32 s6, s57, s6
	s_addc_u32 s7, s65, s7
	v_readlane_b32 s14, v252, 62
	v_add_u32_e32 v4, s11, v6
	s_add_u32 s12, s14, s12
	v_readlane_b32 s14, v253, 0
	s_addc_u32 s13, s14, s13
	v_lshlrev_b32_e32 v32, 2, v4
	v_lshl_add_u64 v[2:3], s[12:13], 0, v[32:33]
	global_load_dword v11, v32, s[12:13] nt
	s_movk_i32 s12, 0x2000
	v_add_co_u32_e32 v12, vcc, s12, v2
	s_movk_i32 s12, 0x4000
	s_nop 0
	v_addc_co_u32_e32 v13, vcc, 0, v3, vcc
	v_add_co_u32_e32 v14, vcc, s12, v2
	s_movk_i32 s12, 0x6000
	s_nop 0
	v_addc_co_u32_e32 v15, vcc, 0, v3, vcc
	global_load_dword v12, v[12:13], off nt
	s_nop 0
	global_load_dword v13, v[14:15], off nt
	v_add_co_u32_e32 v14, vcc, s12, v2
	s_mov_b32 s12, 0x8000
	s_nop 0
	v_addc_co_u32_e32 v15, vcc, 0, v3, vcc
	v_add_co_u32_e32 v16, vcc, s12, v2
	s_mov_b32 s12, 0xa000
	s_nop 0
	v_addc_co_u32_e32 v17, vcc, 0, v3, vcc
	global_load_dword v14, v[14:15], off nt
	s_nop 0
	global_load_dword v15, v[16:17], off nt
	v_add_co_u32_e32 v16, vcc, s12, v2
	s_mov_b32 s12, 0xc000
	s_nop 0
	v_addc_co_u32_e32 v17, vcc, 0, v3, vcc
	v_add_co_u32_e32 v18, vcc, s12, v2
	s_mov_b32 s12, 0xe000
	s_nop 0
	v_addc_co_u32_e32 v19, vcc, 0, v3, vcc
	global_load_dword v16, v[16:17], off nt
	s_nop 0
	global_load_dword v17, v[18:19], off nt
	v_add_co_u32_e32 v18, vcc, s12, v2
	s_mov_b32 s12, 0x10000
	s_nop 0
	v_addc_co_u32_e32 v19, vcc, 0, v3, vcc
	v_add_co_u32_e32 v20, vcc, s12, v2
	s_mov_b32 s12, 0x12000
	s_nop 0
	v_addc_co_u32_e32 v21, vcc, 0, v3, vcc
	global_load_dword v18, v[18:19], off nt
	s_nop 0
	global_load_dword v19, v[20:21], off nt
	v_add_co_u32_e32 v20, vcc, s12, v2
	s_mov_b32 s12, 0x14000
	s_nop 0
	v_addc_co_u32_e32 v21, vcc, 0, v3, vcc
	v_add_co_u32_e32 v22, vcc, s12, v2
	s_mov_b32 s12, 0x16000
	s_nop 0
	v_addc_co_u32_e32 v23, vcc, 0, v3, vcc
	global_load_dword v20, v[20:21], off nt
	s_nop 0
	global_load_dword v21, v[22:23], off nt
	v_add_co_u32_e32 v22, vcc, s12, v2
	s_mov_b32 s12, 0x18000
	s_nop 0
	v_addc_co_u32_e32 v23, vcc, 0, v3, vcc
	v_add_co_u32_e32 v24, vcc, s12, v2
	s_mov_b32 s12, 0x1a000
	s_nop 0
	v_addc_co_u32_e32 v25, vcc, 0, v3, vcc
	global_load_dword v22, v[22:23], off nt
	s_nop 0
	global_load_dword v23, v[24:25], off nt
	v_add_co_u32_e32 v24, vcc, s12, v2
	s_mov_b32 s12, 0x1c000
	s_nop 0
	v_addc_co_u32_e32 v25, vcc, 0, v3, vcc
	v_add_co_u32_e32 v26, vcc, s12, v2
	s_mov_b32 s12, 0x1e000
	s_nop 0
	v_addc_co_u32_e32 v27, vcc, 0, v3, vcc
	global_load_dword v24, v[24:25], off nt
	s_nop 0
	global_load_dword v25, v[26:27], off nt
	v_add_co_u32_e32 v26, vcc, s12, v2
	s_mov_b32 s12, 0x20000
	s_nop 0
	v_addc_co_u32_e32 v27, vcc, 0, v3, vcc
	v_add_co_u32_e32 v28, vcc, s12, v2
	s_mov_b32 s12, 0x22000
	s_nop 0
	v_addc_co_u32_e32 v29, vcc, 0, v3, vcc
	global_load_dword v26, v[26:27], off nt
	s_nop 0
	global_load_dword v27, v[28:29], off nt
	v_add_co_u32_e32 v28, vcc, s12, v2
	s_mov_b32 s12, 0x24000
	s_nop 0
	v_addc_co_u32_e32 v29, vcc, 0, v3, vcc
	v_add_co_u32_e32 v30, vcc, s12, v2
	s_mov_b32 s12, 0x26000
	s_nop 0
	v_addc_co_u32_e32 v31, vcc, 0, v3, vcc
	global_load_dword v28, v[28:29], off nt
	s_nop 0
	global_load_dword v29, v[30:31], off nt
	v_add_co_u32_e32 v30, vcc, s12, v2
	s_mov_b32 s12, 0x28000
	s_nop 0
	v_addc_co_u32_e32 v31, vcc, 0, v3, vcc
	v_add_co_u32_e32 v34, vcc, s12, v2
	s_mov_b32 s12, 0x2a000
	s_nop 0
	v_addc_co_u32_e32 v35, vcc, 0, v3, vcc
	global_load_dword v30, v[30:31], off nt
	s_nop 0
	global_load_dword v31, v[34:35], off nt
	v_add_co_u32_e32 v34, vcc, s12, v2
	s_mov_b32 s12, 0x2c000
	s_nop 0
	v_addc_co_u32_e32 v35, vcc, 0, v3, vcc
	global_load_dword v32, v[34:35], off nt
	v_add_co_u32_e32 v34, vcc, s12, v2
	s_mov_b32 s12, 0x2e000
	s_nop 0
	v_addc_co_u32_e32 v35, vcc, 0, v3, vcc
	v_add_co_u32_e32 v36, vcc, s12, v2
	s_mov_b32 s12, 0x30000
	s_nop 0
	v_addc_co_u32_e32 v37, vcc, 0, v3, vcc
	global_load_dword v34, v[34:35], off nt
	s_nop 0
	global_load_dword v35, v[36:37], off nt
	v_add_co_u32_e32 v36, vcc, s12, v2
	s_mov_b32 s12, 0x32000
	s_nop 0
	v_addc_co_u32_e32 v37, vcc, 0, v3, vcc
	v_add_co_u32_e32 v38, vcc, s12, v2
	s_mov_b32 s12, 0x34000
	s_nop 0
	v_addc_co_u32_e32 v39, vcc, 0, v3, vcc
	global_load_dword v36, v[36:37], off nt
	s_nop 0
	global_load_dword v37, v[38:39], off nt
	v_add_co_u32_e32 v38, vcc, s12, v2
	s_mov_b32 s12, 0x36000
	s_nop 0
	v_addc_co_u32_e32 v39, vcc, 0, v3, vcc
	v_add_co_u32_e32 v40, vcc, s12, v2
	s_mov_b32 s12, 0x38000
	s_nop 0
	v_addc_co_u32_e32 v41, vcc, 0, v3, vcc
	global_load_dword v38, v[38:39], off nt
	s_nop 0
	global_load_dword v39, v[40:41], off nt
	v_add_co_u32_e32 v40, vcc, s12, v2
	s_mov_b32 s12, 0x3a000
	s_nop 0
	v_addc_co_u32_e32 v41, vcc, 0, v3, vcc
	v_add_co_u32_e32 v42, vcc, s12, v2
	s_mov_b32 s12, 0x3c000
	s_nop 0
	v_addc_co_u32_e32 v43, vcc, 0, v3, vcc
	v_add_co_u32_e32 v44, vcc, s12, v2
	s_mov_b32 s12, 0x3e000
	s_nop 0
	v_addc_co_u32_e32 v45, vcc, 0, v3, vcc
	v_add_co_u32_e32 v46, vcc, s12, v2
	s_mov_b32 s12, 0x40000
	s_nop 0
	v_addc_co_u32_e32 v47, vcc, 0, v3, vcc
	v_add_co_u32_e32 v48, vcc, s12, v2
	s_mov_b32 s12, 0x42000
	s_nop 0
	v_addc_co_u32_e32 v49, vcc, 0, v3, vcc
	global_load_dword v40, v[40:41], off nt
	s_nop 0
	global_load_dword v42, v[42:43], off nt
	s_nop 0
	global_load_dword v44, v[44:45], off nt
	s_nop 0
	global_load_dword v46, v[46:47], off nt
	s_nop 0
	global_load_dword v41, v[48:49], off nt
	v_add_co_u32_e32 v48, vcc, s12, v2
	s_mov_b32 s12, 0x44000
	s_nop 0
	v_addc_co_u32_e32 v49, vcc, 0, v3, vcc
; template <bool PERMGL, bool FP8>
; __device__ __forceinline__ void q8_cols_item(const float* W, int N, int n0, unsigned char* Bq, float* sc_out, LAS float* AM, int par, int wave, int lane) {
;     ...
;     for (int i = 0; i < 128; ++i) v[i] = Wp[(size_t)i * N];
	global_load_dword v43, v[48:49], off nt
	v_add_co_u32_e32 v48, vcc, s12, v2
	s_mov_b32 s12, 0x46000
	s_nop 0
	v_addc_co_u32_e32 v49, vcc, 0, v3, vcc
	global_load_dword v45, v[48:49], off nt
	v_add_co_u32_e32 v48, vcc, s12, v2
	s_mov_b32 s12, 0x48000
	s_nop 0
	v_addc_co_u32_e32 v49, vcc, 0, v3, vcc
	global_load_dword v47, v[48:49], off nt
	v_add_co_u32_e32 v48, vcc, s12, v2
	s_mov_b32 s12, 0x4a000
	s_nop 0
	v_addc_co_u32_e32 v49, vcc, 0, v3, vcc
	v_add_co_u32_e32 v50, vcc, s12, v2
	s_mov_b32 s12, 0x4c000
	s_nop 0
	v_addc_co_u32_e32 v51, vcc, 0, v3, vcc
	global_load_dword v48, v[48:49], off nt
	s_nop 0
	global_load_dword v49, v[50:51], off nt
	v_add_co_u32_e32 v50, vcc, s12, v2
	s_mov_b32 s12, 0x4e000
	s_nop 0
	v_addc_co_u32_e32 v51, vcc, 0, v3, vcc
	v_add_co_u32_e32 v52, vcc, s12, v2
	s_mov_b32 s12, 0x50000
	s_nop 0
	v_addc_co_u32_e32 v53, vcc, 0, v3, vcc
	global_load_dword v50, v[50:51], off nt
	s_nop 0
	global_load_dword v51, v[52:53], off nt
	v_add_co_u32_e32 v52, vcc, s12, v2
	s_mov_b32 s12, 0x52000
	s_nop 0
	v_addc_co_u32_e32 v53, vcc, 0, v3, vcc
	v_add_co_u32_e32 v54, vcc, s12, v2
	s_mov_b32 s12, 0x54000
	s_nop 0
	v_addc_co_u32_e32 v55, vcc, 0, v3, vcc
	global_load_dword v52, v[52:53], off nt
	s_nop 0
	global_load_dword v53, v[54:55], off nt
	v_add_co_u32_e32 v54, vcc, s12, v2
	s_mov_b32 s12, 0x56000
	s_nop 0
	v_addc_co_u32_e32 v55, vcc, 0, v3, vcc
	v_add_co_u32_e32 v56, vcc, s12, v2
	s_mov_b32 s12, 0x58000
	s_nop 0
	v_addc_co_u32_e32 v57, vcc, 0, v3, vcc
	global_load_dword v54, v[54:55], off nt
	s_nop 0
	global_load_dword v55, v[56:57], off nt
	v_add_co_u32_e32 v56, vcc, s12, v2
	s_mov_b32 s12, 0x5a000
	s_nop 0
	v_addc_co_u32_e32 v57, vcc, 0, v3, vcc
	v_add_co_u32_e32 v58, vcc, s12, v2
	s_mov_b32 s12, 0x5c000
	s_nop 0
	v_addc_co_u32_e32 v59, vcc, 0, v3, vcc
	global_load_dword v56, v[56:57], off nt
	s_nop 0
	global_load_dword v57, v[58:59], off nt
	v_add_co_u32_e32 v58, vcc, s12, v2
	s_mov_b32 s12, 0x5e000
	s_nop 0
	v_addc_co_u32_e32 v59, vcc, 0, v3, vcc
	v_add_co_u32_e32 v60, vcc, s12, v2
	s_mov_b32 s12, 0x60000
	s_nop 0
	v_addc_co_u32_e32 v61, vcc, 0, v3, vcc
	global_load_dword v58, v[58:59], off nt
	s_nop 0
	global_load_dword v59, v[60:61], off nt
	v_add_co_u32_e32 v60, vcc, s12, v2
	s_mov_b32 s12, 0x62000
	s_nop 0
	v_addc_co_u32_e32 v61, vcc, 0, v3, vcc
	v_add_co_u32_e32 v62, vcc, s12, v2
	s_mov_b32 s12, 0x64000
	s_nop 0
	v_addc_co_u32_e32 v63, vcc, 0, v3, vcc
	global_load_dword v60, v[60:61], off nt
	s_nop 0
	global_load_dword v61, v[62:63], off nt
	v_add_co_u32_e32 v62, vcc, s12, v2
	s_mov_b32 s12, 0x66000
	s_nop 0
	v_addc_co_u32_e32 v63, vcc, 0, v3, vcc
	v_add_co_u32_e32 v64, vcc, s12, v2
	s_mov_b32 s12, 0x68000
	s_nop 0
	v_addc_co_u32_e32 v65, vcc, 0, v3, vcc
	global_load_dword v62, v[62:63], off nt
	s_nop 0
	global_load_dword v63, v[64:65], off nt
	v_add_co_u32_e32 v64, vcc, s12, v2
	s_mov_b32 s12, 0x6a000
	s_nop 0
	v_addc_co_u32_e32 v65, vcc, 0, v3, vcc
	v_add_co_u32_e32 v66, vcc, s12, v2
	s_mov_b32 s12, 0x6c000
	s_nop 0
	v_addc_co_u32_e32 v67, vcc, 0, v3, vcc
	global_load_dword v64, v[64:65], off nt
	s_nop 0
	global_load_dword v65, v[66:67], off nt
	v_add_co_u32_e32 v66, vcc, s12, v2
	s_mov_b32 s12, 0x6e000
	s_nop 0
	v_addc_co_u32_e32 v67, vcc, 0, v3, vcc
	v_add_co_u32_e32 v68, vcc, s12, v2
	s_mov_b32 s12, 0x70000
	s_nop 0
	v_addc_co_u32_e32 v69, vcc, 0, v3, vcc
	global_load_dword v66, v[66:67], off nt
	s_nop 0
	global_load_dword v67, v[68:69], off nt
	v_add_co_u32_e32 v68, vcc, s12, v2
	s_mov_b32 s12, 0x72000
	s_nop 0
	v_addc_co_u32_e32 v69, vcc, 0, v3, vcc
	v_add_co_u32_e32 v70, vcc, s12, v2
	s_mov_b32 s12, 0x74000
	s_nop 0
	v_addc_co_u32_e32 v71, vcc, 0, v3, vcc
	global_load_dword v68, v[68:69], off nt
	s_nop 0
	global_load_dword v69, v[70:71], off nt
	v_add_co_u32_e32 v70, vcc, s12, v2
	s_mov_b32 s12, 0x76000
	s_nop 0
	v_addc_co_u32_e32 v71, vcc, 0, v3, vcc
	v_add_co_u32_e32 v72, vcc, s12, v2
	s_mov_b32 s12, 0x78000
	s_nop 0
	v_addc_co_u32_e32 v73, vcc, 0, v3, vcc
	global_load_dword v70, v[70:71], off nt
	s_nop 0
	global_load_dword v71, v[72:73], off nt
	v_add_co_u32_e32 v72, vcc, s12, v2
	s_mov_b32 s12, 0x7a000
	s_nop 0
	v_addc_co_u32_e32 v73, vcc, 0, v3, vcc
	v_add_co_u32_e32 v74, vcc, s12, v2
	s_mov_b32 s12, 0x7c000
	s_nop 0
	v_addc_co_u32_e32 v75, vcc, 0, v3, vcc
	v_add_co_u32_e32 v76, vcc, s12, v2
	s_mov_b32 s12, 0x7e000
	s_nop 0
	v_addc_co_u32_e32 v77, vcc, 0, v3, vcc
	v_add_co_u32_e32 v78, vcc, s12, v2
	s_mov_b32 s12, 0x80000
	s_nop 0
	v_addc_co_u32_e32 v79, vcc, 0, v3, vcc
	v_add_co_u32_e32 v80, vcc, s12, v2
	s_mov_b32 s12, 0x82000
	s_nop 0
	v_addc_co_u32_e32 v81, vcc, 0, v3, vcc
	global_load_dword v72, v[72:73], off nt
	s_nop 0
	global_load_dword v74, v[74:75], off nt
	s_nop 0
	global_load_dword v76, v[76:77], off nt
	s_nop 0
	global_load_dword v78, v[78:79], off nt
	s_nop 0
	global_load_dword v73, v[80:81], off nt
	v_add_co_u32_e32 v80, vcc, s12, v2
	s_mov_b32 s12, 0x84000
	s_nop 0
	v_addc_co_u32_e32 v81, vcc, 0, v3, vcc
	global_load_dword v75, v[80:81], off nt
	v_add_co_u32_e32 v80, vcc, s12, v2
	s_mov_b32 s12, 0x86000
	s_nop 0
	v_addc_co_u32_e32 v81, vcc, 0, v3, vcc
	global_load_dword v77, v[80:81], off nt
	v_add_co_u32_e32 v80, vcc, s12, v2
	s_mov_b32 s12, 0x88000
	s_nop 0
	v_addc_co_u32_e32 v81, vcc, 0, v3, vcc
	global_load_dword v79, v[80:81], off nt
	v_add_co_u32_e32 v80, vcc, s12, v2
	s_mov_b32 s12, 0x8a000
	s_nop 0
	v_addc_co_u32_e32 v81, vcc, 0, v3, vcc
	v_add_co_u32_e32 v82, vcc, s12, v2
	s_mov_b32 s12, 0x8c000
	s_nop 0
	v_addc_co_u32_e32 v83, vcc, 0, v3, vcc
	global_load_dword v80, v[80:81], off nt
	s_nop 0
	global_load_dword v81, v[82:83], off nt
	v_add_co_u32_e32 v82, vcc, s12, v2
; template <bool PERMGL, bool FP8>
; __device__ __forceinline__ void q8_cols_item(const float* W, int N, int n0, unsigned char* Bq, float* sc_out, LAS float* AM, int par, int wave, int lane) {
;     ...
;     for (int i = 0; i < 128; ++i) v[i] = Wp[(size_t)i * N];
	s_mov_b32 s12, 0x8e000
	s_nop 0
	v_addc_co_u32_e32 v83, vcc, 0, v3, vcc
	v_add_co_u32_e32 v84, vcc, s12, v2
	s_mov_b32 s12, 0x90000
	s_nop 0
	v_addc_co_u32_e32 v85, vcc, 0, v3, vcc
	global_load_dword v82, v[82:83], off nt
	s_nop 0
	global_load_dword v83, v[84:85], off nt
	v_add_co_u32_e32 v84, vcc, s12, v2
	s_mov_b32 s12, 0x92000
	s_nop 0
	v_addc_co_u32_e32 v85, vcc, 0, v3, vcc
	v_add_co_u32_e32 v86, vcc, s12, v2
	s_mov_b32 s12, 0x94000
	s_nop 0
	v_addc_co_u32_e32 v87, vcc, 0, v3, vcc
	global_load_dword v84, v[84:85], off nt
	s_nop 0
	global_load_dword v85, v[86:87], off nt
	v_add_co_u32_e32 v86, vcc, s12, v2
	s_mov_b32 s12, 0x96000
	s_nop 0
	v_addc_co_u32_e32 v87, vcc, 0, v3, vcc
	v_add_co_u32_e32 v88, vcc, s12, v2
	s_mov_b32 s12, 0x98000
	s_nop 0
	v_addc_co_u32_e32 v89, vcc, 0, v3, vcc
	global_load_dword v86, v[86:87], off nt
	s_nop 0
	global_load_dword v87, v[88:89], off nt
	v_add_co_u32_e32 v88, vcc, s12, v2
	s_mov_b32 s12, 0x9a000
	s_nop 0
	v_addc_co_u32_e32 v89, vcc, 0, v3, vcc
	v_add_co_u32_e32 v90, vcc, s12, v2
	s_mov_b32 s12, 0x9c000
	s_nop 0
	v_addc_co_u32_e32 v91, vcc, 0, v3, vcc
	global_load_dword v88, v[88:89], off nt
	s_nop 0
	global_load_dword v89, v[90:91], off nt
	v_add_co_u32_e32 v90, vcc, s12, v2
	s_mov_b32 s12, 0x9e000
	s_nop 0
	v_addc_co_u32_e32 v91, vcc, 0, v3, vcc
	v_add_co_u32_e32 v92, vcc, s12, v2
	s_mov_b32 s12, 0xa0000
	s_nop 0
	v_addc_co_u32_e32 v93, vcc, 0, v3, vcc
	global_load_dword v90, v[90:91], off nt
	s_nop 0
	global_load_dword v91, v[92:93], off nt
	v_add_co_u32_e32 v92, vcc, s12, v2
	s_mov_b32 s12, 0xa2000
	s_nop 0
	v_addc_co_u32_e32 v93, vcc, 0, v3, vcc
	v_add_co_u32_e32 v94, vcc, s12, v2
	s_mov_b32 s12, 0xa4000
	s_nop 0
	v_addc_co_u32_e32 v95, vcc, 0, v3, vcc
	global_load_dword v92, v[92:93], off nt
	s_nop 0
	global_load_dword v93, v[94:95], off nt
	v_add_co_u32_e32 v94, vcc, s12, v2
	s_mov_b32 s12, 0xa6000
	s_nop 0
	v_addc_co_u32_e32 v95, vcc, 0, v3, vcc
	v_add_co_u32_e32 v96, vcc, s12, v2
	s_mov_b32 s12, 0xa8000
	s_nop 0
	v_addc_co_u32_e32 v97, vcc, 0, v3, vcc
	global_load_dword v94, v[94:95], off nt
	s_nop 0
	global_load_dword v95, v[96:97], off nt
	v_add_co_u32_e32 v96, vcc, s12, v2
	s_mov_b32 s12, 0xaa000
	s_nop 0
	v_addc_co_u32_e32 v97, vcc, 0, v3, vcc
	v_add_co_u32_e32 v98, vcc, s12, v2
	s_mov_b32 s12, 0xac000
	s_nop 0
	v_addc_co_u32_e32 v99, vcc, 0, v3, vcc
	global_load_dword v96, v[96:97], off nt
	s_nop 0
	global_load_dword v97, v[98:99], off nt
	v_add_co_u32_e32 v98, vcc, s12, v2
	s_mov_b32 s12, 0xae000
	s_nop 0
	v_addc_co_u32_e32 v99, vcc, 0, v3, vcc
	v_add_co_u32_e32 v100, vcc, s12, v2
	s_mov_b32 s12, 0xb0000
	s_nop 0
	v_addc_co_u32_e32 v101, vcc, 0, v3, vcc
	global_load_dword v98, v[98:99], off nt
	s_nop 0
	global_load_dword v99, v[100:101], off nt
	v_add_co_u32_e32 v100, vcc, s12, v2
	s_mov_b32 s12, 0xb2000
	s_nop 0
	v_addc_co_u32_e32 v101, vcc, 0, v3, vcc
	v_add_co_u32_e32 v102, vcc, s12, v2
	s_mov_b32 s12, 0xb4000
	s_nop 0
	v_addc_co_u32_e32 v103, vcc, 0, v3, vcc
	global_load_dword v100, v[100:101], off nt
	s_nop 0
	global_load_dword v101, v[102:103], off nt
	v_add_co_u32_e32 v102, vcc, s12, v2
	s_mov_b32 s12, 0xb6000
	s_nop 0
	v_addc_co_u32_e32 v103, vcc, 0, v3, vcc
	v_add_co_u32_e32 v104, vcc, s12, v2
	s_mov_b32 s12, 0xb8000
	s_nop 0
	v_addc_co_u32_e32 v105, vcc, 0, v3, vcc
	global_load_dword v102, v[102:103], off nt
	s_nop 0
	global_load_dword v103, v[104:105], off nt
	v_add_co_u32_e32 v104, vcc, s12, v2
	s_mov_b32 s12, 0xba000
	s_nop 0
	v_addc_co_u32_e32 v105, vcc, 0, v3, vcc
	v_add_co_u32_e32 v106, vcc, s12, v2
	s_mov_b32 s12, 0xbc000
	s_nop 0
	v_addc_co_u32_e32 v107, vcc, 0, v3, vcc
	v_add_co_u32_e32 v108, vcc, s12, v2
	s_mov_b32 s12, 0xbe000
	s_nop 0
	v_addc_co_u32_e32 v109, vcc, 0, v3, vcc
	v_add_co_u32_e32 v110, vcc, s12, v2
	s_mov_b32 s12, 0xc0000
	s_nop 0
	v_addc_co_u32_e32 v111, vcc, 0, v3, vcc
	v_add_co_u32_e32 v112, vcc, s12, v2
	s_mov_b32 s12, 0xc2000
	s_nop 0
	v_addc_co_u32_e32 v113, vcc, 0, v3, vcc
	global_load_dword v104, v[104:105], off nt
	s_nop 0
	global_load_dword v106, v[106:107], off nt
	s_nop 0
	global_load_dword v108, v[108:109], off nt
	s_nop 0
	global_load_dword v110, v[110:111], off nt
	s_nop 0
	global_load_dword v105, v[112:113], off nt
	v_add_co_u32_e32 v112, vcc, s12, v2
	s_mov_b32 s12, 0xc4000
	s_nop 0
	v_addc_co_u32_e32 v113, vcc, 0, v3, vcc
	global_load_dword v107, v[112:113], off nt
	v_add_co_u32_e32 v112, vcc, s12, v2
	s_mov_b32 s12, 0xc6000
	s_nop 0
	v_addc_co_u32_e32 v113, vcc, 0, v3, vcc
	global_load_dword v109, v[112:113], off nt
	v_add_co_u32_e32 v112, vcc, s12, v2
	s_mov_b32 s12, 0xc8000
	s_nop 0
	v_addc_co_u32_e32 v113, vcc, 0, v3, vcc
	global_load_dword v111, v[112:113], off nt
	v_add_co_u32_e32 v112, vcc, s12, v2
	s_mov_b32 s12, 0xca000
	s_nop 0
	v_addc_co_u32_e32 v113, vcc, 0, v3, vcc
	v_add_co_u32_e32 v114, vcc, s12, v2
	s_mov_b32 s12, 0xcc000
	s_nop 0
	v_addc_co_u32_e32 v115, vcc, 0, v3, vcc
	global_load_dword v112, v[112:113], off nt
	s_nop 0
	global_load_dword v113, v[114:115], off nt
	v_add_co_u32_e32 v114, vcc, s12, v2
	s_mov_b32 s12, 0xce000
	s_nop 0
	v_addc_co_u32_e32 v115, vcc, 0, v3, vcc
	v_add_co_u32_e32 v116, vcc, s12, v2
	s_mov_b32 s12, 0xd0000
	s_nop 0
	v_addc_co_u32_e32 v117, vcc, 0, v3, vcc
	global_load_dword v114, v[114:115], off nt
	s_nop 0
	global_load_dword v115, v[116:117], off nt
	v_add_co_u32_e32 v116, vcc, s12, v2
	s_mov_b32 s12, 0xd2000
	s_nop 0
	v_addc_co_u32_e32 v117, vcc, 0, v3, vcc
	v_add_co_u32_e32 v118, vcc, s12, v2
	s_mov_b32 s12, 0xd4000
	s_nop 0
	v_addc_co_u32_e32 v119, vcc, 0, v3, vcc
	global_load_dword v116, v[116:117], off nt
	s_nop 0
	global_load_dword v117, v[118:119], off nt
	v_add_co_u32_e32 v118, vcc, s12, v2
; template <bool PERMGL, bool FP8>
; __device__ __forceinline__ void q8_cols_item(const float* W, int N, int n0, unsigned char* Bq, float* sc_out, LAS float* AM, int par, int wave, int lane) {
;     ...
;     for (int i = 0; i < 128; ++i) v[i] = Wp[(size_t)i * N];
;     __builtin_amdgcn_sched_barrier(0);
; #pragma unroll
;     for (int i = 0; i < 128; ++i) am = fmaxf(am, fabsf(v[i]));
;     AM[(par * 8 + wave) * 64 + lane] = am;
;     __syncthreads();
	s_mov_b32 s12, 0xd6000
	s_nop 0
	v_addc_co_u32_e32 v119, vcc, 0, v3, vcc
	v_add_co_u32_e32 v120, vcc, s12, v2
	s_mov_b32 s12, 0xd8000
	s_nop 0
	v_addc_co_u32_e32 v121, vcc, 0, v3, vcc
	global_load_dword v118, v[118:119], off nt
	s_nop 0
	global_load_dword v119, v[120:121], off nt
	v_add_co_u32_e32 v120, vcc, s12, v2
	s_mov_b32 s12, 0xda000
	s_nop 0
	v_addc_co_u32_e32 v121, vcc, 0, v3, vcc
	v_add_co_u32_e32 v122, vcc, s12, v2
	s_mov_b32 s12, 0xdc000
	s_nop 0
	v_addc_co_u32_e32 v123, vcc, 0, v3, vcc
	global_load_dword v120, v[120:121], off nt
	s_nop 0
	global_load_dword v121, v[122:123], off nt
	v_add_co_u32_e32 v122, vcc, s12, v2
	s_mov_b32 s12, 0xde000
	s_nop 0
	v_addc_co_u32_e32 v123, vcc, 0, v3, vcc
	v_add_co_u32_e32 v124, vcc, s12, v2
	s_mov_b32 s12, 0xe0000
	s_nop 0
	v_addc_co_u32_e32 v125, vcc, 0, v3, vcc
	global_load_dword v122, v[122:123], off nt
	s_nop 0
	global_load_dword v123, v[124:125], off nt
	v_add_co_u32_e32 v124, vcc, s12, v2
	s_mov_b32 s12, 0xe2000
	s_nop 0
	v_addc_co_u32_e32 v125, vcc, 0, v3, vcc
	v_add_co_u32_e32 v126, vcc, s12, v2
	s_mov_b32 s12, 0xe4000
	s_nop 0
	v_addc_co_u32_e32 v127, vcc, 0, v3, vcc
	global_load_dword v124, v[124:125], off nt
	s_nop 0
	global_load_dword v125, v[126:127], off nt
	v_add_co_u32_e32 v126, vcc, s12, v2
	s_mov_b32 s12, 0xe6000
	s_nop 0
	v_addc_co_u32_e32 v127, vcc, 0, v3, vcc
	v_add_co_u32_e32 v128, vcc, s12, v2
	s_mov_b32 s12, 0xe8000
	s_nop 0
	v_addc_co_u32_e32 v129, vcc, 0, v3, vcc
	global_load_dword v126, v[126:127], off nt
	s_nop 0
	global_load_dword v127, v[128:129], off nt
	v_add_co_u32_e32 v128, vcc, s12, v2
	s_mov_b32 s12, 0xea000
	s_nop 0
	v_addc_co_u32_e32 v129, vcc, 0, v3, vcc
	v_add_co_u32_e32 v130, vcc, s12, v2
	s_mov_b32 s12, 0xec000
	s_nop 0
	v_addc_co_u32_e32 v131, vcc, 0, v3, vcc
	global_load_dword v128, v[128:129], off nt
	s_nop 0
	global_load_dword v129, v[130:131], off nt
	v_add_co_u32_e32 v130, vcc, s12, v2
	s_mov_b32 s12, 0xee000
	s_nop 0
	v_addc_co_u32_e32 v131, vcc, 0, v3, vcc
	v_add_co_u32_e32 v132, vcc, s12, v2
	s_mov_b32 s12, 0xf0000
	s_nop 0
	v_addc_co_u32_e32 v133, vcc, 0, v3, vcc
	global_load_dword v130, v[130:131], off nt
	s_nop 0
	global_load_dword v131, v[132:133], off nt
	v_add_co_u32_e32 v132, vcc, s12, v2
	s_mov_b32 s12, 0xf2000
	s_nop 0
	v_addc_co_u32_e32 v133, vcc, 0, v3, vcc
	v_add_co_u32_e32 v134, vcc, s12, v2
	s_mov_b32 s12, 0xf4000
	s_nop 0
	v_addc_co_u32_e32 v135, vcc, 0, v3, vcc
	global_load_dword v132, v[132:133], off nt
	s_nop 0
	global_load_dword v133, v[134:135], off nt
	v_add_co_u32_e32 v134, vcc, s12, v2
	s_mov_b32 s12, 0xf6000
	s_nop 0
	v_addc_co_u32_e32 v135, vcc, 0, v3, vcc
	v_add_co_u32_e32 v136, vcc, s12, v2
	s_mov_b32 s12, 0xf8000
	s_nop 0
	v_addc_co_u32_e32 v137, vcc, 0, v3, vcc
	global_load_dword v134, v[134:135], off nt
	s_nop 0
	global_load_dword v135, v[136:137], off nt
	v_add_co_u32_e32 v136, vcc, s12, v2
	s_mov_b32 s12, 0xfa000
	s_nop 0
	v_addc_co_u32_e32 v137, vcc, 0, v3, vcc
	v_add_co_u32_e32 v138, vcc, s12, v2
	s_mov_b32 s12, 0xfc000
	s_nop 0
	v_addc_co_u32_e32 v139, vcc, 0, v3, vcc
	global_load_dword v136, v[136:137], off nt
	s_nop 0
	global_load_dword v137, v[138:139], off nt
	v_add_co_u32_e32 v138, vcc, s12, v2
	s_mov_b32 s12, 0xfe000
	s_nop 0
	v_addc_co_u32_e32 v139, vcc, 0, v3, vcc
	v_add_co_u32_e32 v2, vcc, s12, v2
	global_load_dword v138, v[138:139], off nt
	s_nop 0
	v_addc_co_u32_e32 v3, vcc, 0, v3, vcc
	global_load_dword v141, v[2:3], off nt
	s_waitcnt vmcnt(0)
	v_max3_f32 v2, |v11|, 0, |v12|
	v_max3_f32 v2, v2, |v13|, |v14|
	v_max3_f32 v2, v2, |v15|, |v16|
	v_max3_f32 v2, v2, |v17|, |v18|
	v_max3_f32 v2, v2, |v19|, |v20|
	v_max3_f32 v2, v2, |v21|, |v22|
	v_max3_f32 v2, v2, |v23|, |v24|
	v_max3_f32 v2, v2, |v25|, |v26|
	v_max3_f32 v2, v2, |v27|, |v28|
	v_max3_f32 v2, v2, |v29|, |v30|
	v_max3_f32 v2, v2, |v31|, |v32|
	v_max3_f32 v2, v2, |v34|, |v35|
	v_max3_f32 v2, v2, |v36|, |v37|
	v_max3_f32 v2, v2, |v38|, |v39|
	v_max3_f32 v2, v2, |v40|, |v42|
	v_max3_f32 v2, v2, |v44|, |v46|
	v_max3_f32 v2, v2, |v41|, |v43|
	v_max3_f32 v2, v2, |v45|, |v47|
	v_max3_f32 v2, v2, |v48|, |v49|
	v_max3_f32 v2, v2, |v50|, |v51|
	v_max3_f32 v2, v2, |v52|, |v53|
	v_max3_f32 v2, v2, |v54|, |v55|
	v_max3_f32 v2, v2, |v56|, |v57|
	v_max3_f32 v2, v2, |v58|, |v59|
	v_max3_f32 v2, v2, |v60|, |v61|
	v_max3_f32 v2, v2, |v62|, |v63|
	v_max3_f32 v2, v2, |v64|, |v65|
	v_max3_f32 v2, v2, |v66|, |v67|
	v_max3_f32 v2, v2, |v68|, |v69|
	v_max3_f32 v2, v2, |v70|, |v71|
	v_max3_f32 v2, v2, |v72|, |v74|
	v_max3_f32 v2, v2, |v76|, |v78|
	v_max3_f32 v2, v2, |v73|, |v75|
	v_max3_f32 v2, v2, |v77|, |v79|
	v_max3_f32 v2, v2, |v80|, |v81|
	v_max3_f32 v2, v2, |v82|, |v83|
	v_max3_f32 v2, v2, |v84|, |v85|
	v_max3_f32 v2, v2, |v86|, |v87|
	v_max3_f32 v2, v2, |v88|, |v89|
	v_max3_f32 v2, v2, |v90|, |v91|
	v_max3_f32 v2, v2, |v92|, |v93|
	v_max3_f32 v2, v2, |v94|, |v95|
	v_max3_f32 v2, v2, |v96|, |v97|
	v_max3_f32 v2, v2, |v98|, |v99|
	v_max3_f32 v2, v2, |v100|, |v101|
	v_max3_f32 v2, v2, |v102|, |v103|
	v_max3_f32 v2, v2, |v104|, |v106|
	v_max3_f32 v2, v2, |v108|, |v110|
	v_max3_f32 v2, v2, |v105|, |v107|
	v_max3_f32 v2, v2, |v109|, |v111|
	v_max3_f32 v2, v2, |v112|, |v113|
	v_max3_f32 v2, v2, |v114|, |v115|
	v_max3_f32 v2, v2, |v116|, |v117|
	v_max3_f32 v2, v2, |v118|, |v119|
	v_max3_f32 v2, v2, |v120|, |v121|
	v_max3_f32 v2, v2, |v122|, |v123|
	v_max3_f32 v2, v2, |v124|, |v125|
	v_max3_f32 v2, v2, |v126|, |v127|
	v_max3_f32 v2, v2, |v128|, |v129|
	v_max3_f32 v2, v2, |v130|, |v131|
	v_max3_f32 v2, v2, |v132|, |v133|
	v_max3_f32 v2, v2, |v134|, |v135|
	v_max3_f32 v2, v2, |v136|, |v137|
	s_lshl_b32 s12, s8, 11
	v_max3_f32 v5, v2, |v138|, |v141|
	v_add_u32_e32 v2, s12, v10
	v_add_u32_e32 v139, s12, v7
	ds_write_b32 v2, v5
	s_waitcnt lgkmcnt(0)
	s_barrier
; template <bool PERMGL, bool FP8>
; __device__ __forceinline__ void q8_cols_item(const float* W, int N, int n0, unsigned char* Bq, float* sc_out, LAS float* AM, int par, int wave, int lane) {
;     ...
;     for (int w = 0; w < 8; ++w) am = fmaxf(am, AM[(par * 8 + w) * 64 + lane]);
;     const float sc = am > 0.f ? am * (FP8 ? (1.0f / 256.0f) : (1.0f / 127.0f)) : 1.0f, inv = 1.0f / sc;
;     int row = n;
;     if (PERMGL) { const int j = n >> 1, pr = n & 1, o = j & 127; row = ((j >> 7) << 8) + (((o >> 2) & 1) << 7) + ((o >> 5) << 5) + (pr << 4) + (((o >> 3) & 3) << 2) + (o & 3); }
;     if (!PERMGL) { const int o = n & 255; row = ((n >> 8) << 8) + (((o >> 3) & 1) << 7) + ((o >> 6) << 5) + (((o >> 4) & 3) << 3) + (o & 7); }
;     auto xq = [](unsigned x) { return (unsigned)__builtin_amdgcn_update_dpp(0, (int)x, 0xB1, 0xf, 0xf, true); };
;     const bool odd = lane & 1;
;     const int rowp = (int)xq((unsigned)row);
;     unsigned char* plo = Bq + (size_t)(odd ? rowp : row) * 1024 + 128 * wave + (odd ? 16 : 0);
;     unsigned char* phi = Bq + (size_t)(odd ? row : rowp) * 1024 + 128 * wave + (odd ? 16 : 0);
;     auto packc = [&](int c) { u32x4 o;
;         if (FP8) { o.x = f8x4(v[16 * c], v[16 * c + 1], v[16 * c + 2], v[16 * c + 3], inv); o.y = f8x4(v[16 * c + 4], v[16 * c + 5], v[16 * c + 6], v[16 * c + 7], inv);
;                    o.z = f8x4(v[16 * c + 8], v[16 * c + 9], v[16 * c + 10], v[16 * c + 11], inv); o.w = f8x4(v[16 * c + 12], v[16 * c + 13], v[16 * c + 14], v[16 * c + 15], inv); }
;         else { o.x = q8x4(v[16 * c], v[16 * c + 1], v[16 * c + 2], v[16 * c + 3], inv); o.y = q8x4(v[16 * c + 4], v[16 * c + 5], v[16 * c + 6], v[16 * c + 7], inv);
;                o.z = q8x4(v[16 * c + 8], v[16 * c + 9], v[16 * c + 10], v[16 * c + 11], inv); o.w = q8x4(v[16 * c + 12], v[16 * c + 13], v[16 * c + 14], v[16 * c + 15], inv); }
;         return o; };
; #pragma unroll
;     for (int j = 0; j < 4; ++j) { const u32x4 p0 = packc(2 * j), p1 = packc(2 * j + 1);
;         u32x4 snd, rcv;
; #pragma unroll
;         for (int q = 0; q < 4; ++q) { snd[q] = odd ? p0[q] : p1[q]; rcv[q] = xq(snd[q]); }
;         u32x4 a, b;
; #pragma unroll
;         for (int q = 0; q < 4; ++q) { a[q] = odd ? rcv[q] : p0[q]; b[q] = odd ? p1[q] : rcv[q]; }
;         *(u32x4*)(plo + 32 * j) = a; *(u32x4*)(phi + 32 * j) = b; }
	ds_read2st64_b32 v[2:3], v139 offset1:1
	s_waitcnt lgkmcnt(0)
	v_max3_f32 v5, v5, v2, v3
	ds_read2st64_b32 v[2:3], v139 offset0:2 offset1:3
	s_waitcnt lgkmcnt(0)
	v_max3_f32 v5, v5, v2, v3
	ds_read2st64_b32 v[2:3], v139 offset0:4 offset1:5
	s_waitcnt lgkmcnt(0)
	v_max3_f32 v5, v5, v2, v3
	ds_read2st64_b32 v[2:3], v139 offset0:6 offset1:7
	s_waitcnt lgkmcnt(0)
	v_max3_f32 v2, v5, v2, v3
	v_cmp_lt_f32_e32 vcc, 0, v2
	v_mul_f32_e32 v2, 0x3c010204, v2
	s_nop 0
	v_cndmask_b32_e32 v139, 1.0, v2, vcc
	v_div_scale_f32 v2, s[12:13], v139, v139, 1.0
	v_rcp_f32_e32 v3, v2
	s_nop 0
	v_fma_f32 v5, -v2, v3, 1.0
	v_fmac_f32_e32 v3, v5, v3
	v_div_scale_f32 v5, vcc, 1.0, v139, 1.0
	v_mul_f32_e32 v140, v5, v3
	v_fma_f32 v142, -v2, v140, v5
	v_fmac_f32_e32 v140, v142, v3
	v_fma_f32 v2, -v2, v140, v5
	v_div_fmas_f32 v2, v2, v3, v140
	v_div_fixup_f32 v142, v2, v139, 1.0
	v_fmaak_f32 v11, v11, v142, 0x4b400000
	v_fmaak_f32 v12, v12, v142, 0x4b400000
	v_fmaak_f32 v13, v13, v142, 0x4b400000
	v_fmaak_f32 v14, v14, v142, 0x4b400000
	v_perm_b32 v13, v14, v13, s61
	v_perm_b32 v11, v12, v11, s61
	v_perm_b32 v11, v13, v11, s79
	v_fmaak_f32 v12, v15, v142, 0x4b400000
	v_fmaak_f32 v13, v16, v142, 0x4b400000
	v_fmaak_f32 v14, v17, v142, 0x4b400000
	v_fmaak_f32 v15, v18, v142, 0x4b400000
	v_perm_b32 v14, v15, v14, s61
	v_perm_b32 v12, v13, v12, s61
	v_perm_b32 v13, v14, v12, s79
	v_fmaak_f32 v12, v19, v142, 0x4b400000
	v_fmaak_f32 v14, v20, v142, 0x4b400000
	v_fmaak_f32 v15, v21, v142, 0x4b400000
	v_fmaak_f32 v16, v22, v142, 0x4b400000
	v_perm_b32 v15, v16, v15, s61
	v_perm_b32 v12, v14, v12, s61
	v_perm_b32 v14, v15, v12, s79
	v_fmaak_f32 v12, v23, v142, 0x4b400000
	v_fmaak_f32 v15, v24, v142, 0x4b400000
	v_fmaak_f32 v16, v25, v142, 0x4b400000
	v_fmaak_f32 v17, v26, v142, 0x4b400000
	v_perm_b32 v16, v17, v16, s61
	v_perm_b32 v12, v15, v12, s61
	v_perm_b32 v15, v16, v12, s79
	v_fmaak_f32 v12, v27, v142, 0x4b400000
	v_fmaak_f32 v16, v28, v142, 0x4b400000
	v_fmaak_f32 v17, v29, v142, 0x4b400000
	v_fmaak_f32 v18, v30, v142, 0x4b400000
	v_perm_b32 v17, v18, v17, s61
	v_perm_b32 v12, v16, v12, s61
	v_add_u16_e32 v2, s11, v6
	v_perm_b32 v16, v17, v12, s79
	v_fmaak_f32 v12, v31, v142, 0x4b400000
	v_fmaak_f32 v17, v32, v142, 0x4b400000
	v_fmaak_f32 v18, v34, v142, 0x4b400000
	v_fmaak_f32 v19, v35, v142, 0x4b400000
	v_lshrrev_b16_e32 v2, 1, v2
	v_lshlrev_b32_e32 v3, 4, v4
	s_movk_i32 s11, 0xf00
	v_perm_b32 v18, v19, v18, s61
	v_perm_b32 v12, v17, v12, s61
	v_and_b32_e32 v5, 0x80, v3
	v_and_b32_e32 v140, 0x60, v2
	v_and_or_b32 v4, v4, s11, v9
	v_perm_b32 v17, v18, v12, s79
	v_fmaak_f32 v12, v36, v142, 0x4b400000
	v_fmaak_f32 v18, v37, v142, 0x4b400000
	v_fmaak_f32 v19, v38, v142, 0x4b400000
	v_fmaak_f32 v20, v39, v142, 0x4b400000
	v_and_b32_e32 v3, 16, v3
	v_and_b32_e32 v2, 3, v2
	v_or3_b32 v4, v4, v5, v140
	v_perm_b32 v19, v20, v19, s61
	v_perm_b32 v12, v18, v12, s61
	v_or3_b32 v140, v4, v3, v2
	v_perm_b32 v18, v19, v12, s79
	v_fmaak_f32 v12, v40, v142, 0x4b400000
	v_fmaak_f32 v19, v42, v142, 0x4b400000
	v_fmaak_f32 v20, v44, v142, 0x4b400000
	v_fmaak_f32 v21, v46, v142, 0x4b400000
	v_mov_b32_dpp v4, v140 quad_perm:[1,0,3,2] row_mask:0xf bank_mask:0xf bound_ctrl:1
	v_perm_b32 v20, v21, v20, s61
	v_perm_b32 v12, v19, v12, s61
	v_cndmask_b32_e64 v2, v4, v140, s[2:3]
	v_perm_b32 v19, v20, v12, s79
	v_cndmask_b32_e64 v12, v11, v16, s[2:3]
	v_ashrrev_i32_e32 v3, 31, v2
	v_cndmask_b32_e64 v4, v140, v4, s[2:3]
	v_mov_b32_dpp v20, v12 quad_perm:[1,0,3,2] row_mask:0xf bank_mask:0xf bound_ctrl:1
	v_cndmask_b32_e64 v12, v13, v17, s[2:3]
	v_lshlrev_b64 v[2:3], 10, v[2:3]
	v_ashrrev_i32_e32 v5, 31, v4
	v_mov_b32_dpp v21, v12 quad_perm:[1,0,3,2] row_mask:0xf bank_mask:0xf bound_ctrl:1
	v_cndmask_b32_e64 v12, v14, v18, s[2:3]
	v_lshl_add_u64 v[2:3], s[6:7], 0, v[2:3]
	v_lshlrev_b64 v[4:5], 10, v[4:5]
	v_mov_b32_dpp v22, v12 quad_perm:[1,0,3,2] row_mask:0xf bank_mask:0xf bound_ctrl:1
	v_cndmask_b32_e64 v12, v15, v19, s[2:3]
	v_lshl_add_u64 v[2:3], v[2:3], 0, s[42:43]
	v_lshl_add_u64 v[4:5], s[6:7], 0, v[4:5]
	v_mov_b32_dpp v23, v12 quad_perm:[1,0,3,2] row_mask:0xf bank_mask:0xf bound_ctrl:1
	v_lshl_add_u64 v[2:3], v[2:3], 0, v[0:1]
	v_lshl_add_u64 v[4:5], v[4:5], 0, s[42:43]
	v_cndmask_b32_e64 v12, v20, v11, s[2:3]
	v_cndmask_b32_e64 v13, v21, v13, s[2:3]
	v_cndmask_b32_e64 v14, v22, v14, s[2:3]
	v_cndmask_b32_e64 v15, v23, v15, s[2:3]
	v_lshl_add_u64 v[4:5], v[4:5], 0, v[0:1]
	v_cndmask_b32_e64 v16, v16, v20, s[2:3]
	v_cndmask_b32_e64 v17, v17, v21, s[2:3]
	v_cndmask_b32_e64 v18, v18, v22, s[2:3]
	v_cndmask_b32_e64 v19, v19, v23, s[2:3]
	global_store_dwordx4 v[2:3], v[12:15], off
	global_store_dwordx4 v[4:5], v[16:19], off
	v_fmaak_f32 v11, v41, v142, 0x4b400000
	v_fmaak_f32 v12, v43, v142, 0x4b400000
	v_fmaak_f32 v13, v45, v142, 0x4b400000
	v_fmaak_f32 v14, v47, v142, 0x4b400000
	v_perm_b32 v13, v14, v13, s61
	v_perm_b32 v11, v12, v11, s61
	v_perm_b32 v11, v13, v11, s79
	v_fmaak_f32 v12, v48, v142, 0x4b400000
	v_fmaak_f32 v13, v49, v142, 0x4b400000
	v_fmaak_f32 v14, v50, v142, 0x4b400000
	v_fmaak_f32 v15, v51, v142, 0x4b400000
	v_perm_b32 v14, v15, v14, s61
	v_perm_b32 v12, v13, v12, s61
	v_perm_b32 v13, v14, v12, s79
	v_fmaak_f32 v12, v52, v142, 0x4b400000
	v_fmaak_f32 v14, v53, v142, 0x4b400000
	v_fmaak_f32 v15, v54, v142, 0x4b400000
	v_fmaak_f32 v16, v55, v142, 0x4b400000
	v_perm_b32 v15, v16, v15, s61
	v_perm_b32 v12, v14, v12, s61
	v_perm_b32 v14, v15, v12, s79
	v_fmaak_f32 v12, v56, v142, 0x4b400000
	v_fmaak_f32 v15, v57, v142, 0x4b400000
	v_fmaak_f32 v16, v58, v142, 0x4b400000
	v_fmaak_f32 v17, v59, v142, 0x4b400000
	v_perm_b32 v16, v17, v16, s61
	v_perm_b32 v12, v15, v12, s61
; template <bool PERMGL, bool FP8>
; __device__ __forceinline__ void q8_cols_item(const float* W, int N, int n0, unsigned char* Bq, float* sc_out, LAS float* AM, int par, int wave, int lane) {
;     ...
;     auto packc = [&](int c) { u32x4 o;
;         if (FP8) { o.x = f8x4(v[16 * c], v[16 * c + 1], v[16 * c + 2], v[16 * c + 3], inv); o.y = f8x4(v[16 * c + 4], v[16 * c + 5], v[16 * c + 6], v[16 * c + 7], inv);
;                    o.z = f8x4(v[16 * c + 8], v[16 * c + 9], v[16 * c + 10], v[16 * c + 11], inv); o.w = f8x4(v[16 * c + 12], v[16 * c + 13], v[16 * c + 14], v[16 * c + 15], inv); }
;         else { o.x = q8x4(v[16 * c], v[16 * c + 1], v[16 * c + 2], v[16 * c + 3], inv); o.y = q8x4(v[16 * c + 4], v[16 * c + 5], v[16 * c + 6], v[16 * c + 7], inv);
;                o.z = q8x4(v[16 * c + 8], v[16 * c + 9], v[16 * c + 10], v[16 * c + 11], inv); o.w = q8x4(v[16 * c + 12], v[16 * c + 13], v[16 * c + 14], v[16 * c + 15], inv); }
;         return o; };
; #pragma unroll
;     for (int j = 0; j < 4; ++j) { const u32x4 p0 = packc(2 * j), p1 = packc(2 * j + 1);
;         u32x4 snd, rcv;
; #pragma unroll
;         for (int q = 0; q < 4; ++q) { snd[q] = odd ? p0[q] : p1[q]; rcv[q] = xq(snd[q]); }
;         u32x4 a, b;
; #pragma unroll
;         for (int q = 0; q < 4; ++q) { a[q] = odd ? rcv[q] : p0[q]; b[q] = odd ? p1[q] : rcv[q]; }
;         *(u32x4*)(plo + 32 * j) = a; *(u32x4*)(phi + 32 * j) = b; }
	v_perm_b32 v15, v16, v12, s79
	v_fmaak_f32 v12, v60, v142, 0x4b400000
	v_fmaak_f32 v16, v61, v142, 0x4b400000
	v_fmaak_f32 v17, v62, v142, 0x4b400000
	v_fmaak_f32 v18, v63, v142, 0x4b400000
	v_perm_b32 v17, v18, v17, s61
	v_perm_b32 v12, v16, v12, s61
	v_perm_b32 v16, v17, v12, s79
	v_fmaak_f32 v12, v64, v142, 0x4b400000
	v_fmaak_f32 v17, v65, v142, 0x4b400000
	v_fmaak_f32 v18, v66, v142, 0x4b400000
	v_fmaak_f32 v19, v67, v142, 0x4b400000
	v_perm_b32 v18, v19, v18, s61
	v_perm_b32 v12, v17, v12, s61
	v_perm_b32 v17, v18, v12, s79
	v_fmaak_f32 v12, v68, v142, 0x4b400000
	v_fmaak_f32 v18, v69, v142, 0x4b400000
	v_fmaak_f32 v19, v70, v142, 0x4b400000
	v_fmaak_f32 v20, v71, v142, 0x4b400000
	v_perm_b32 v19, v20, v19, s61
	v_perm_b32 v12, v18, v12, s61
	v_perm_b32 v18, v19, v12, s79
	v_fmaak_f32 v12, v72, v142, 0x4b400000
	v_fmaak_f32 v19, v74, v142, 0x4b400000
	v_fmaak_f32 v20, v76, v142, 0x4b400000
	v_fmaak_f32 v21, v78, v142, 0x4b400000
	v_perm_b32 v20, v21, v20, s61
	v_perm_b32 v12, v19, v12, s61
	v_perm_b32 v19, v20, v12, s79
	v_cndmask_b32_e64 v12, v11, v16, s[2:3]
	s_and_b64 vcc, exec, s[0:1]
	s_nop 0
	v_mov_b32_dpp v20, v12 quad_perm:[1,0,3,2] row_mask:0xf bank_mask:0xf bound_ctrl:1
	v_cndmask_b32_e64 v12, v13, v17, s[2:3]
	v_cndmask_b32_e64 v16, v16, v20, s[2:3]
	s_nop 0
	v_mov_b32_dpp v21, v12 quad_perm:[1,0,3,2] row_mask:0xf bank_mask:0xf bound_ctrl:1
	v_cndmask_b32_e64 v12, v14, v18, s[2:3]
	v_cndmask_b32_e64 v13, v21, v13, s[2:3]
	v_cndmask_b32_e64 v17, v17, v21, s[2:3]
	v_mov_b32_dpp v22, v12 quad_perm:[1,0,3,2] row_mask:0xf bank_mask:0xf bound_ctrl:1
	v_cndmask_b32_e64 v12, v15, v19, s[2:3]
	v_cndmask_b32_e64 v14, v22, v14, s[2:3]
	v_cndmask_b32_e64 v18, v18, v22, s[2:3]
	v_mov_b32_dpp v23, v12 quad_perm:[1,0,3,2] row_mask:0xf bank_mask:0xf bound_ctrl:1
	v_cndmask_b32_e64 v12, v20, v11, s[2:3]
	v_cndmask_b32_e64 v15, v23, v15, s[2:3]
	v_cndmask_b32_e64 v19, v19, v23, s[2:3]
	global_store_dwordx4 v[2:3], v[12:15], off offset:32
	global_store_dwordx4 v[4:5], v[16:19], off offset:32
	v_fmaak_f32 v11, v73, v142, 0x4b400000
	v_fmaak_f32 v12, v75, v142, 0x4b400000
	v_fmaak_f32 v13, v77, v142, 0x4b400000
	v_fmaak_f32 v14, v79, v142, 0x4b400000
	v_perm_b32 v13, v14, v13, s61
	v_perm_b32 v11, v12, v11, s61
	v_perm_b32 v11, v13, v11, s79
	v_fmaak_f32 v12, v80, v142, 0x4b400000
	v_fmaak_f32 v13, v81, v142, 0x4b400000
	v_fmaak_f32 v14, v82, v142, 0x4b400000
	v_fmaak_f32 v15, v83, v142, 0x4b400000
	v_perm_b32 v14, v15, v14, s61
	v_perm_b32 v12, v13, v12, s61
	v_perm_b32 v13, v14, v12, s79
	v_fmaak_f32 v12, v84, v142, 0x4b400000
	v_fmaak_f32 v14, v85, v142, 0x4b400000
	v_fmaak_f32 v15, v86, v142, 0x4b400000
	v_fmaak_f32 v16, v87, v142, 0x4b400000
	v_perm_b32 v15, v16, v15, s61
	v_perm_b32 v12, v14, v12, s61
	v_perm_b32 v14, v15, v12, s79
	v_fmaak_f32 v12, v88, v142, 0x4b400000
	v_fmaak_f32 v15, v89, v142, 0x4b400000
	v_fmaak_f32 v16, v90, v142, 0x4b400000
	v_fmaak_f32 v17, v91, v142, 0x4b400000
	v_perm_b32 v16, v17, v16, s61
	v_perm_b32 v12, v15, v12, s61
	v_perm_b32 v15, v16, v12, s79
	v_fmaak_f32 v12, v92, v142, 0x4b400000
	v_fmaak_f32 v16, v93, v142, 0x4b400000
	v_fmaak_f32 v17, v94, v142, 0x4b400000
	v_fmaak_f32 v18, v95, v142, 0x4b400000
	v_perm_b32 v17, v18, v17, s61
	v_perm_b32 v12, v16, v12, s61
	v_perm_b32 v16, v17, v12, s79
	v_fmaak_f32 v12, v96, v142, 0x4b400000
	v_fmaak_f32 v17, v97, v142, 0x4b400000
	v_fmaak_f32 v18, v98, v142, 0x4b400000
	v_fmaak_f32 v19, v99, v142, 0x4b400000
	v_perm_b32 v18, v19, v18, s61
	v_perm_b32 v12, v17, v12, s61
	v_perm_b32 v17, v18, v12, s79
	v_fmaak_f32 v12, v100, v142, 0x4b400000
	v_fmaak_f32 v18, v101, v142, 0x4b400000
	v_fmaak_f32 v19, v102, v142, 0x4b400000
	v_fmaak_f32 v20, v103, v142, 0x4b400000
	v_perm_b32 v19, v20, v19, s61
	v_perm_b32 v12, v18, v12, s61
	v_perm_b32 v18, v19, v12, s79
	v_fmaak_f32 v12, v104, v142, 0x4b400000
	v_fmaak_f32 v19, v106, v142, 0x4b400000
	v_fmaak_f32 v20, v108, v142, 0x4b400000
	v_fmaak_f32 v21, v110, v142, 0x4b400000
	v_perm_b32 v20, v21, v20, s61
	v_perm_b32 v12, v19, v12, s61
	v_perm_b32 v19, v20, v12, s79
	v_cndmask_b32_e64 v12, v11, v16, s[2:3]
	s_nop 1
; template <bool PERMGL, bool FP8>
; __device__ __forceinline__ void q8_cols_item(const float* W, int N, int n0, unsigned char* Bq, float* sc_out, LAS float* AM, int par, int wave, int lane) {
;     ...
;     for (int j = 0; j < 4; ++j) { const u32x4 p0 = packc(2 * j), p1 = packc(2 * j + 1);
;         u32x4 snd, rcv;
; #pragma unroll
;         for (int q = 0; q < 4; ++q) { snd[q] = odd ? p0[q] : p1[q]; rcv[q] = xq(snd[q]); }
;         u32x4 a, b;
; #pragma unroll
;         for (int q = 0; q < 4; ++q) { a[q] = odd ? rcv[q] : p0[q]; b[q] = odd ? p1[q] : rcv[q]; }
;         *(u32x4*)(plo + 32 * j) = a; *(u32x4*)(phi + 32 * j) = b; }
;     if (wave == 0) sc_out[PERMGL ? row : n] = FP8 ? sc * 16.0f : sc;
	v_mov_b32_dpp v20, v12 quad_perm:[1,0,3,2] row_mask:0xf bank_mask:0xf bound_ctrl:1
	v_cndmask_b32_e64 v12, v13, v17, s[2:3]
	v_cndmask_b32_e64 v16, v16, v20, s[2:3]
	s_nop 0
	v_mov_b32_dpp v21, v12 quad_perm:[1,0,3,2] row_mask:0xf bank_mask:0xf bound_ctrl:1
	v_cndmask_b32_e64 v12, v14, v18, s[2:3]
	v_cndmask_b32_e64 v13, v21, v13, s[2:3]
	v_cndmask_b32_e64 v17, v17, v21, s[2:3]
	v_mov_b32_dpp v22, v12 quad_perm:[1,0,3,2] row_mask:0xf bank_mask:0xf bound_ctrl:1
	v_cndmask_b32_e64 v12, v15, v19, s[2:3]
	v_cndmask_b32_e64 v14, v22, v14, s[2:3]
	v_cndmask_b32_e64 v18, v18, v22, s[2:3]
	v_mov_b32_dpp v23, v12 quad_perm:[1,0,3,2] row_mask:0xf bank_mask:0xf bound_ctrl:1
	v_cndmask_b32_e64 v12, v20, v11, s[2:3]
	v_cndmask_b32_e64 v15, v23, v15, s[2:3]
	v_cndmask_b32_e64 v19, v19, v23, s[2:3]
	global_store_dwordx4 v[2:3], v[12:15], off offset:64
	global_store_dwordx4 v[4:5], v[16:19], off offset:64
	v_fmaak_f32 v11, v105, v142, 0x4b400000
	v_fmaak_f32 v12, v107, v142, 0x4b400000
	v_fmaak_f32 v13, v109, v142, 0x4b400000
	v_fmaak_f32 v14, v111, v142, 0x4b400000
	v_perm_b32 v13, v14, v13, s61
	v_perm_b32 v11, v12, v11, s61
	v_perm_b32 v11, v13, v11, s79
	v_fmaak_f32 v12, v112, v142, 0x4b400000
	v_fmaak_f32 v13, v113, v142, 0x4b400000
	v_fmaak_f32 v14, v114, v142, 0x4b400000
	v_fmaak_f32 v15, v115, v142, 0x4b400000
	v_perm_b32 v14, v15, v14, s61
	v_perm_b32 v12, v13, v12, s61
	v_perm_b32 v13, v14, v12, s79
	v_fmaak_f32 v12, v116, v142, 0x4b400000
	v_fmaak_f32 v14, v117, v142, 0x4b400000
	v_fmaak_f32 v15, v118, v142, 0x4b400000
	v_fmaak_f32 v16, v119, v142, 0x4b400000
	v_perm_b32 v15, v16, v15, s61
	v_perm_b32 v12, v14, v12, s61
	v_perm_b32 v14, v15, v12, s79
	v_fmaak_f32 v12, v120, v142, 0x4b400000
	v_fmaak_f32 v15, v121, v142, 0x4b400000
	v_fmaak_f32 v16, v122, v142, 0x4b400000
	v_fmaak_f32 v17, v123, v142, 0x4b400000
	v_perm_b32 v16, v17, v16, s61
	v_perm_b32 v12, v15, v12, s61
	v_perm_b32 v15, v16, v12, s79
	v_fmaak_f32 v12, v124, v142, 0x4b400000
	v_fmaak_f32 v16, v125, v142, 0x4b400000
	v_fmaak_f32 v17, v126, v142, 0x4b400000
	v_fmaak_f32 v18, v127, v142, 0x4b400000
	v_perm_b32 v17, v18, v17, s61
	v_perm_b32 v12, v16, v12, s61
	v_perm_b32 v16, v17, v12, s79
	v_fmaak_f32 v12, v128, v142, 0x4b400000
	v_fmaak_f32 v17, v129, v142, 0x4b400000
	v_fmaak_f32 v18, v130, v142, 0x4b400000
	v_fmaak_f32 v19, v131, v142, 0x4b400000
	v_perm_b32 v18, v19, v18, s61
	v_perm_b32 v12, v17, v12, s61
	v_perm_b32 v17, v18, v12, s79
	v_fmaak_f32 v12, v132, v142, 0x4b400000
	v_fmaak_f32 v18, v133, v142, 0x4b400000
	v_fmaak_f32 v19, v134, v142, 0x4b400000
	v_fmaak_f32 v20, v135, v142, 0x4b400000
	v_perm_b32 v19, v20, v19, s61
	v_perm_b32 v12, v18, v12, s61
	v_perm_b32 v18, v19, v12, s79
	v_fmaak_f32 v12, v136, v142, 0x4b400000
	v_fmaak_f32 v19, v137, v142, 0x4b400000
	v_fmaak_f32 v20, v138, v142, 0x4b400000
	v_fmaak_f32 v21, v141, v142, 0x4b400000
	v_perm_b32 v20, v21, v20, s61
	v_perm_b32 v12, v19, v12, s61
	v_perm_b32 v19, v20, v12, s79
	v_cndmask_b32_e64 v12, v11, v16, s[2:3]
	s_nop 1
	v_mov_b32_dpp v20, v12 quad_perm:[1,0,3,2] row_mask:0xf bank_mask:0xf bound_ctrl:1
	v_cndmask_b32_e64 v12, v13, v17, s[2:3]
	v_cndmask_b32_e64 v16, v16, v20, s[2:3]
	s_nop 0
	v_mov_b32_dpp v21, v12 quad_perm:[1,0,3,2] row_mask:0xf bank_mask:0xf bound_ctrl:1
	v_cndmask_b32_e64 v12, v14, v18, s[2:3]
	v_cndmask_b32_e64 v13, v21, v13, s[2:3]
	v_cndmask_b32_e64 v17, v17, v21, s[2:3]
	v_mov_b32_dpp v22, v12 quad_perm:[1,0,3,2] row_mask:0xf bank_mask:0xf bound_ctrl:1
	v_cndmask_b32_e64 v12, v15, v19, s[2:3]
	v_cndmask_b32_e64 v14, v22, v14, s[2:3]
	v_cndmask_b32_e64 v18, v18, v22, s[2:3]
	v_mov_b32_dpp v23, v12 quad_perm:[1,0,3,2] row_mask:0xf bank_mask:0xf bound_ctrl:1
	v_cndmask_b32_e64 v12, v20, v11, s[2:3]
	v_cndmask_b32_e64 v15, v23, v15, s[2:3]
	v_cndmask_b32_e64 v19, v19, v23, s[2:3]
	global_store_dwordx4 v[2:3], v[12:15], off offset:96
	global_store_dwordx4 v[4:5], v[16:19], off offset:96
	s_cbranch_vccnz .LBB0_142
	s_lshl_b64 s[4:5], s[4:5], 13
	v_readlane_b32 s6, v253, 2
	s_add_u32 s4, s6, s4
	v_readlane_b32 s6, v253, 3
	s_addc_u32 s5, s6, s5
	v_lshlrev_b32_e32 v2, 2, v140
	global_store_dword v2, v139, s[4:5]
	s_branch .LBB0_142

; template <bool PERMGL, bool FP8>
; __device__ __forceinline__ void q8_cols_item(const float* W, int N, int n0, unsigned char* Bq, float* sc_out, LAS float* AM, int par, int wave, int lane) {
;     ...
;     for (int i = 0; i < 128; ++i) v[i] = Wp[(size_t)i * N];
; __global__ void __launch_bounds__(NWAVES * 64, 2) mk_fwd(Args args) {
;     ...
;                             const int lyr = cv_first + cv_it / 1536, r = cv_it % 1536;
;                             if (r < 1024) { const int mi = lyr * 32 + (r >> 5), nb = ((r & 31) + 8 * ((r >> 6) & 3)) & 31;
;                                 q8_cols_item<true, false>(args.in[11] + (size_t)mi * D * 2048, 2048, nb * 64, ws + WS_WGU + (size_t)mi * 2048 * 1024, (float*)(ws + WS_SB) + (size_t)mi * 2048, CAM, cv_par, wave, lane); }
;                             else { const int r2 = r - 1024, mi = lyr * 32 + (r2 >> 4), nb = ((r2 & 15) + 8 * ((r2 >> 6) & 1)) & 15;
;                                 q8_cols_item<false, true>(args.in[13] + (size_t)mi * D * D, D, nb * 64, ws + WS_WDN + (size_t)mi * D * 1024, (float*)(ws + WS_SBD) + (size_t)mi * D, CAM, cv_par, wave, lane); }
.LBB0_233:
	s_mul_hi_i32 s8, s24, 0x2aaaaaab
	s_lshr_b32 s9, s8, 31
	s_ashr_i32 s8, s8, 8
	s_add_i32 s13, s8, s9
	s_add_i32 s15, s13, s66
	s_mul_i32 s14, s13, 0x600
	s_mulk_i32 s13, 0xfa00
	s_add_i32 s16, s24, s13
	s_cmpk_gt_i32 s16, 0x3ff
	s_mov_b64 s[8:9], -1
	s_cbranch_scc0 .LBB0_237
	s_add_i32 s8, s16, 0xfffffc00
	s_lshl_b32 s9, s15, 5
	s_lshr_b32 s8, s8, 4
	s_add_i32 s8, s9, s8
	s_sub_i32 s9, s24, s14
	s_lshr_b32 s9, s9, 3
	s_and_b32 s9, s9, 8
	s_add_i32 s9, s24, s9
	s_add_i32 s17, s9, s13
	s_ashr_i32 s9, s8, 31
	s_lshl_b32 s17, s17, 6
	s_lshl_b64 s[10:11], s[8:9], 20
	s_and_b32 s17, s17, 0x3c0
	s_add_u32 s10, s83, s10
	s_addc_u32 s11, s74, s11
	s_lshl_b64 s[18:19], s[8:9], 22
	v_add_u32_e32 v0, s17, v127
	s_add_u32 s18, s48, s18
	s_addc_u32 s19, s51, s19
	v_ashrrev_i32_e32 v1, 31, v0
	v_lshl_add_u64 v[2:3], v[0:1], 2, s[18:19]
	s_movk_i32 s17, 0x2000
	v_add_co_u32_e32 v4, vcc, s17, v2
	s_movk_i32 s17, 0x4000
	s_nop 0
	v_addc_co_u32_e32 v5, vcc, 0, v3, vcc
	global_load_dword v6, v[2:3], off nt
	global_load_dword v8, v[4:5], off offset:-4096 nt
	global_load_dword v7, v[4:5], off nt
	v_add_co_u32_e32 v4, vcc, s17, v2
	s_movk_i32 s17, 0x6000
	s_nop 0
	v_addc_co_u32_e32 v5, vcc, 0, v3, vcc
	global_load_dword v11, v[4:5], off offset:-4096 nt
	global_load_dword v9, v[4:5], off nt
	v_add_co_u32_e32 v4, vcc, s17, v2
	s_mov_b32 s17, 0x8000
	s_nop 0
	v_addc_co_u32_e32 v5, vcc, 0, v3, vcc
	global_load_dword v12, v[4:5], off offset:-4096 nt
	global_load_dword v10, v[4:5], off nt
	v_add_co_u32_e32 v4, vcc, s17, v2
	s_mov_b32 s17, 0xa000
	s_nop 0
	v_addc_co_u32_e32 v5, vcc, 0, v3, vcc
	global_load_dword v14, v[4:5], off offset:-4096 nt
	global_load_dword v13, v[4:5], off nt
	v_add_co_u32_e32 v4, vcc, s17, v2
	s_mov_b32 s17, 0xc000
	s_nop 0
	v_addc_co_u32_e32 v5, vcc, 0, v3, vcc
	global_load_dword v16, v[4:5], off offset:-4096 nt
	global_load_dword v15, v[4:5], off nt
	v_add_co_u32_e32 v4, vcc, s17, v2
	s_mov_b32 s17, 0xe000
	s_nop 0
	v_addc_co_u32_e32 v5, vcc, 0, v3, vcc
	global_load_dword v18, v[4:5], off offset:-4096 nt
	global_load_dword v17, v[4:5], off nt
	v_add_co_u32_e32 v4, vcc, s17, v2
	s_mov_b32 s17, 0x10000
	s_nop 0
	v_addc_co_u32_e32 v5, vcc, 0, v3, vcc
	global_load_dword v22, v[4:5], off offset:-4096 nt
	global_load_dword v19, v[4:5], off nt
	v_add_co_u32_e32 v4, vcc, s17, v2
	s_mov_b32 s17, 0x12000
	s_nop 0
	v_addc_co_u32_e32 v5, vcc, 0, v3, vcc
	global_load_dword v21, v[4:5], off offset:-4096 nt
	global_load_dword v20, v[4:5], off nt
	v_add_co_u32_e32 v4, vcc, s17, v2
	s_mov_b32 s17, 0x14000
	s_nop 0
	v_addc_co_u32_e32 v5, vcc, 0, v3, vcc
	global_load_dword v24, v[4:5], off offset:-4096 nt
	global_load_dword v23, v[4:5], off nt
	v_add_co_u32_e32 v4, vcc, s17, v2
	s_mov_b32 s17, 0x16000
	s_nop 0
	v_addc_co_u32_e32 v5, vcc, 0, v3, vcc
	global_load_dword v26, v[4:5], off offset:-4096 nt
	global_load_dword v25, v[4:5], off nt
	v_add_co_u32_e32 v4, vcc, s17, v2
	s_mov_b32 s17, 0x18000
	s_nop 0
	v_addc_co_u32_e32 v5, vcc, 0, v3, vcc
	global_load_dword v30, v[4:5], off offset:-4096 nt
	global_load_dword v27, v[4:5], off nt
	v_add_co_u32_e32 v4, vcc, s17, v2
	s_mov_b32 s17, 0x1a000
	s_nop 0
	v_addc_co_u32_e32 v5, vcc, 0, v3, vcc
	global_load_dword v29, v[4:5], off offset:-4096 nt
	global_load_dword v28, v[4:5], off nt
	v_add_co_u32_e32 v4, vcc, s17, v2
	s_mov_b32 s17, 0x1c000
	s_nop 0
	v_addc_co_u32_e32 v5, vcc, 0, v3, vcc
	global_load_dword v32, v[4:5], off offset:-4096 nt
	global_load_dword v31, v[4:5], off nt
	v_add_co_u32_e32 v4, vcc, s17, v2
	s_mov_b32 s17, 0x1e000
	s_nop 0
	v_addc_co_u32_e32 v5, vcc, 0, v3, vcc
	global_load_dword v36, v[4:5], off offset:-4096 nt
	global_load_dword v34, v[4:5], off nt
	v_add_co_u32_e32 v4, vcc, s17, v2
	s_mov_b32 s17, 0x20000
	s_nop 0
	v_addc_co_u32_e32 v5, vcc, 0, v3, vcc
	global_load_dword v43, v[4:5], off offset:-4096 nt
	global_load_dword v41, v[4:5], off nt
	v_add_co_u32_e32 v4, vcc, s17, v2
	s_mov_b32 s17, 0x22000
	s_nop 0
	v_addc_co_u32_e32 v5, vcc, 0, v3, vcc
	global_load_dword v42, v[4:5], off offset:-4096 nt
	global_load_dword v35, v[4:5], off nt
	v_add_co_u32_e32 v4, vcc, s17, v2
	s_mov_b32 s17, 0x24000
	s_nop 0
	v_addc_co_u32_e32 v5, vcc, 0, v3, vcc
	global_load_dword v38, v[4:5], off offset:-4096 nt
	global_load_dword v37, v[4:5], off nt
	v_add_co_u32_e32 v4, vcc, s17, v2
	s_mov_b32 s17, 0x26000
	s_nop 0
	v_addc_co_u32_e32 v5, vcc, 0, v3, vcc
	global_load_dword v40, v[4:5], off offset:-4096 nt
	global_load_dword v39, v[4:5], off nt
	v_add_co_u32_e32 v4, vcc, s17, v2
	s_mov_b32 s17, 0x28000
	s_nop 0
	v_addc_co_u32_e32 v5, vcc, 0, v3, vcc
	global_load_dword v47, v[4:5], off offset:-4096 nt
	global_load_dword v44, v[4:5], off nt
	v_add_co_u32_e32 v4, vcc, s17, v2
	s_mov_b32 s17, 0x2a000
	s_nop 0
	v_addc_co_u32_e32 v5, vcc, 0, v3, vcc
	global_load_dword v46, v[4:5], off offset:-4096 nt
	global_load_dword v45, v[4:5], off nt
	v_add_co_u32_e32 v4, vcc, s17, v2
	s_mov_b32 s17, 0x2c000
	s_nop 0
	v_addc_co_u32_e32 v5, vcc, 0, v3, vcc
	global_load_dword v49, v[4:5], off offset:-4096 nt
	global_load_dword v48, v[4:5], off nt
	v_add_co_u32_e32 v4, vcc, s17, v2
	s_mov_b32 s17, 0x2e000
	s_nop 0
	v_addc_co_u32_e32 v5, vcc, 0, v3, vcc
	global_load_dword v51, v[4:5], off offset:-4096 nt
	global_load_dword v50, v[4:5], off nt
	v_add_co_u32_e32 v4, vcc, s17, v2
	s_mov_b32 s17, 0x30000
	s_nop 0
	v_addc_co_u32_e32 v5, vcc, 0, v3, vcc
	global_load_dword v55, v[4:5], off offset:-4096 nt
	global_load_dword v52, v[4:5], off nt
	v_add_co_u32_e32 v4, vcc, s17, v2
	s_mov_b32 s17, 0x32000
	s_nop 0
	v_addc_co_u32_e32 v5, vcc, 0, v3, vcc
	global_load_dword v54, v[4:5], off offset:-4096 nt
	global_load_dword v53, v[4:5], off nt
; template <bool PERMGL, bool FP8>
; __device__ __forceinline__ void q8_cols_item(const float* W, int N, int n0, unsigned char* Bq, float* sc_out, LAS float* AM, int par, int wave, int lane) {
;     ...
;     for (int i = 0; i < 128; ++i) v[i] = Wp[(size_t)i * N];
	v_add_co_u32_e32 v4, vcc, s17, v2
	s_mov_b32 s17, 0x34000
	s_nop 0
	v_addc_co_u32_e32 v5, vcc, 0, v3, vcc
	global_load_dword v57, v[4:5], off offset:-4096 nt
	global_load_dword v56, v[4:5], off nt
	v_add_co_u32_e32 v4, vcc, s17, v2
	s_mov_b32 s17, 0x36000
	s_nop 0
	v_addc_co_u32_e32 v5, vcc, 0, v3, vcc
	global_load_dword v59, v[4:5], off offset:-4096 nt
	global_load_dword v58, v[4:5], off nt
	v_add_co_u32_e32 v4, vcc, s17, v2
	s_mov_b32 s17, 0x38000
	s_nop 0
	v_addc_co_u32_e32 v5, vcc, 0, v3, vcc
	global_load_dword v63, v[4:5], off offset:-4096 nt
	global_load_dword v60, v[4:5], off nt
	v_add_co_u32_e32 v4, vcc, s17, v2
	s_mov_b32 s17, 0x3a000
	s_nop 0
	v_addc_co_u32_e32 v5, vcc, 0, v3, vcc
	global_load_dword v62, v[4:5], off offset:-4096 nt
	global_load_dword v61, v[4:5], off nt
	v_add_co_u32_e32 v4, vcc, s17, v2
	s_mov_b32 s17, 0x3c000
	s_nop 0
	v_addc_co_u32_e32 v5, vcc, 0, v3, vcc
	global_load_dword v65, v[4:5], off offset:-4096 nt
	global_load_dword v64, v[4:5], off nt
	v_add_co_u32_e32 v4, vcc, s17, v2
	s_mov_b32 s17, 0x3e000
	s_nop 0
	v_addc_co_u32_e32 v5, vcc, 0, v3, vcc
	global_load_dword v68, v[4:5], off offset:-4096 nt
	global_load_dword v66, v[4:5], off nt
	v_add_co_u32_e32 v4, vcc, s17, v2
	s_mov_b32 s17, 0x40000
	s_nop 0
	v_addc_co_u32_e32 v5, vcc, 0, v3, vcc
	global_load_dword v75, v[4:5], off offset:-4096 nt
	global_load_dword v73, v[4:5], off nt
	v_add_co_u32_e32 v4, vcc, s17, v2
	s_mov_b32 s17, 0x42000
	s_nop 0
	v_addc_co_u32_e32 v5, vcc, 0, v3, vcc
	global_load_dword v74, v[4:5], off offset:-4096 nt
	global_load_dword v67, v[4:5], off nt
	v_add_co_u32_e32 v4, vcc, s17, v2
	s_mov_b32 s17, 0x44000
	s_nop 0
	v_addc_co_u32_e32 v5, vcc, 0, v3, vcc
	global_load_dword v70, v[4:5], off offset:-4096 nt
	global_load_dword v69, v[4:5], off nt
	v_add_co_u32_e32 v4, vcc, s17, v2
	s_mov_b32 s17, 0x46000
	s_nop 0
	v_addc_co_u32_e32 v5, vcc, 0, v3, vcc
	global_load_dword v72, v[4:5], off offset:-4096 nt
	global_load_dword v71, v[4:5], off nt
	v_add_co_u32_e32 v4, vcc, s17, v2
	s_mov_b32 s17, 0x48000
	s_nop 0
	v_addc_co_u32_e32 v5, vcc, 0, v3, vcc
	global_load_dword v79, v[4:5], off offset:-4096 nt
	global_load_dword v76, v[4:5], off nt
	v_add_co_u32_e32 v4, vcc, s17, v2
	s_mov_b32 s17, 0x4a000
	s_nop 0
	v_addc_co_u32_e32 v5, vcc, 0, v3, vcc
	global_load_dword v78, v[4:5], off offset:-4096 nt
	global_load_dword v77, v[4:5], off nt
	v_add_co_u32_e32 v4, vcc, s17, v2
	s_mov_b32 s17, 0x4c000
	s_nop 0
	v_addc_co_u32_e32 v5, vcc, 0, v3, vcc
	global_load_dword v81, v[4:5], off offset:-4096 nt
	global_load_dword v80, v[4:5], off nt
	v_add_co_u32_e32 v4, vcc, s17, v2
	s_mov_b32 s17, 0x4e000
	s_nop 0
	v_addc_co_u32_e32 v5, vcc, 0, v3, vcc
	global_load_dword v83, v[4:5], off offset:-4096 nt
	global_load_dword v82, v[4:5], off nt
	v_add_co_u32_e32 v4, vcc, s17, v2
	s_mov_b32 s17, 0x50000
	s_nop 0
	v_addc_co_u32_e32 v5, vcc, 0, v3, vcc
	global_load_dword v87, v[4:5], off offset:-4096 nt
	global_load_dword v84, v[4:5], off nt
	v_add_co_u32_e32 v4, vcc, s17, v2
	s_mov_b32 s17, 0x52000
	s_nop 0
	v_addc_co_u32_e32 v5, vcc, 0, v3, vcc
	global_load_dword v86, v[4:5], off offset:-4096 nt
	global_load_dword v85, v[4:5], off nt
	v_add_co_u32_e32 v4, vcc, s17, v2
	s_mov_b32 s17, 0x54000
	s_nop 0
	v_addc_co_u32_e32 v5, vcc, 0, v3, vcc
	global_load_dword v89, v[4:5], off offset:-4096 nt
	global_load_dword v88, v[4:5], off nt
	v_add_co_u32_e32 v4, vcc, s17, v2
	s_mov_b32 s17, 0x56000
	s_nop 0
	v_addc_co_u32_e32 v5, vcc, 0, v3, vcc
	global_load_dword v91, v[4:5], off offset:-4096 nt
	global_load_dword v90, v[4:5], off nt
	v_add_co_u32_e32 v4, vcc, s17, v2
	s_mov_b32 s17, 0x58000
	s_nop 0
	v_addc_co_u32_e32 v5, vcc, 0, v3, vcc
	global_load_dword v95, v[4:5], off offset:-4096 nt
	global_load_dword v92, v[4:5], off nt
	v_add_co_u32_e32 v4, vcc, s17, v2
	s_mov_b32 s17, 0x5a000
	s_nop 0
	v_addc_co_u32_e32 v5, vcc, 0, v3, vcc
	global_load_dword v94, v[4:5], off offset:-4096 nt
	global_load_dword v93, v[4:5], off nt
	v_add_co_u32_e32 v4, vcc, s17, v2
	s_mov_b32 s17, 0x5c000
	s_nop 0
	v_addc_co_u32_e32 v5, vcc, 0, v3, vcc
	global_load_dword v97, v[4:5], off offset:-4096 nt
	global_load_dword v96, v[4:5], off nt
	v_add_co_u32_e32 v4, vcc, s17, v2
	s_mov_b32 s17, 0x5e000
	s_nop 0
	v_addc_co_u32_e32 v5, vcc, 0, v3, vcc
	global_load_dword v100, v[4:5], off offset:-4096 nt
	global_load_dword v98, v[4:5], off nt
	v_add_co_u32_e32 v4, vcc, s17, v2
	s_mov_b32 s17, 0x60000
	s_nop 0
	v_addc_co_u32_e32 v5, vcc, 0, v3, vcc
	global_load_dword v107, v[4:5], off offset:-4096 nt
	global_load_dword v105, v[4:5], off nt
	v_add_co_u32_e32 v4, vcc, s17, v2
	s_mov_b32 s17, 0x62000
	s_nop 0
	v_addc_co_u32_e32 v5, vcc, 0, v3, vcc
	global_load_dword v106, v[4:5], off offset:-4096 nt
	global_load_dword v99, v[4:5], off nt
	v_add_co_u32_e32 v4, vcc, s17, v2
	s_mov_b32 s17, 0x64000
	s_nop 0
	v_addc_co_u32_e32 v5, vcc, 0, v3, vcc
	global_load_dword v102, v[4:5], off offset:-4096 nt
	global_load_dword v101, v[4:5], off nt
	v_add_co_u32_e32 v4, vcc, s17, v2
	s_mov_b32 s17, 0x66000
	s_nop 0
	v_addc_co_u32_e32 v5, vcc, 0, v3, vcc
	global_load_dword v104, v[4:5], off offset:-4096 nt
	global_load_dword v103, v[4:5], off nt
	v_add_co_u32_e32 v4, vcc, s17, v2
	s_mov_b32 s17, 0x68000
	s_nop 0
	v_addc_co_u32_e32 v5, vcc, 0, v3, vcc
	global_load_dword v111, v[4:5], off offset:-4096 nt
	global_load_dword v108, v[4:5], off nt
	v_add_co_u32_e32 v4, vcc, s17, v2
	s_mov_b32 s17, 0x6a000
	s_nop 0
	v_addc_co_u32_e32 v5, vcc, 0, v3, vcc
	global_load_dword v110, v[4:5], off offset:-4096 nt
	global_load_dword v109, v[4:5], off nt
	v_add_co_u32_e32 v4, vcc, s17, v2
	s_mov_b32 s17, 0x6c000
	s_nop 0
; template <bool PERMGL, bool FP8>
; __device__ __forceinline__ void q8_cols_item(const float* W, int N, int n0, unsigned char* Bq, float* sc_out, LAS float* AM, int par, int wave, int lane) {
;     ...
;     for (int i = 0; i < 128; ++i) v[i] = Wp[(size_t)i * N];
;     __builtin_amdgcn_sched_barrier(0);
; #pragma unroll
;     for (int i = 0; i < 128; ++i) am = fmaxf(am, fabsf(v[i]));
;     AM[(par * 8 + wave) * 64 + lane] = am;
;     __syncthreads();
	v_addc_co_u32_e32 v5, vcc, 0, v3, vcc
	global_load_dword v113, v[4:5], off offset:-4096 nt
	global_load_dword v112, v[4:5], off nt
	v_add_co_u32_e32 v4, vcc, s17, v2
	s_mov_b32 s17, 0x6e000
	s_nop 0
	v_addc_co_u32_e32 v5, vcc, 0, v3, vcc
	global_load_dword v115, v[4:5], off offset:-4096 nt
	global_load_dword v114, v[4:5], off nt
	v_add_co_u32_e32 v4, vcc, s17, v2
	s_mov_b32 s17, 0x70000
	s_nop 0
	v_addc_co_u32_e32 v5, vcc, 0, v3, vcc
	global_load_dword v119, v[4:5], off offset:-4096 nt
	global_load_dword v116, v[4:5], off nt
	v_add_co_u32_e32 v4, vcc, s17, v2
	s_mov_b32 s17, 0x72000
	s_nop 0
	v_addc_co_u32_e32 v5, vcc, 0, v3, vcc
	global_load_dword v118, v[4:5], off offset:-4096 nt
	global_load_dword v117, v[4:5], off nt
	v_add_co_u32_e32 v4, vcc, s17, v2
	s_mov_b32 s17, 0x74000
	s_nop 0
	v_addc_co_u32_e32 v5, vcc, 0, v3, vcc
	global_load_dword v121, v[4:5], off offset:-4096 nt
	global_load_dword v120, v[4:5], off nt
	v_add_co_u32_e32 v4, vcc, s17, v2
	s_mov_b32 s17, 0x76000
	s_nop 0
	v_addc_co_u32_e32 v5, vcc, 0, v3, vcc
	global_load_dword v131, v[4:5], off offset:-4096 nt
	global_load_dword v130, v[4:5], off nt
	v_add_co_u32_e32 v4, vcc, s17, v2
	s_mov_b32 s17, 0x78000
	s_nop 0
	v_addc_co_u32_e32 v5, vcc, 0, v3, vcc
	global_load_dword v135, v[4:5], off offset:-4096 nt
	global_load_dword v132, v[4:5], off nt
	v_add_co_u32_e32 v4, vcc, s17, v2
	s_mov_b32 s17, 0x7a000
	s_nop 0
	v_addc_co_u32_e32 v5, vcc, 0, v3, vcc
	global_load_dword v134, v[4:5], off offset:-4096 nt
	global_load_dword v133, v[4:5], off nt
	v_add_co_u32_e32 v4, vcc, s17, v2
	s_mov_b32 s17, 0x7c000
	s_nop 0
	v_addc_co_u32_e32 v5, vcc, 0, v3, vcc
	global_load_dword v137, v[4:5], off offset:-4096 nt
	global_load_dword v136, v[4:5], off nt
	v_add_co_u32_e32 v4, vcc, s17, v2
	s_mov_b32 s17, 0x7e000
	s_nop 0
	v_addc_co_u32_e32 v5, vcc, 0, v3, vcc
	global_load_dword v139, v[4:5], off offset:-4096 nt
	global_load_dword v138, v[4:5], off nt
	v_add_co_u32_e32 v4, vcc, s17, v2
	s_mov_b32 s17, 0x7f000
	s_nop 0
	v_addc_co_u32_e32 v5, vcc, 0, v3, vcc
	v_add_co_u32_e32 v2, vcc, s17, v2
	global_load_dword v141, v[4:5], off offset:-4096 nt
	global_load_dword v140, v[4:5], off nt
	v_addc_co_u32_e32 v3, vcc, 0, v3, vcc
	global_load_dword v142, v[2:3], off nt
	s_waitcnt vmcnt(0)
	v_max3_f32 v2, |v6|, 0, |v8|
	v_max3_f32 v2, v2, |v7|, |v11|
	v_max3_f32 v2, v2, |v9|, |v12|
	v_max3_f32 v2, v2, |v10|, |v14|
	v_max3_f32 v2, v2, |v13|, |v16|
	v_max3_f32 v2, v2, |v15|, |v18|
	v_max3_f32 v2, v2, |v17|, |v22|
	v_max3_f32 v2, v2, |v19|, |v21|
	v_max3_f32 v2, v2, |v20|, |v24|
	v_max3_f32 v2, v2, |v23|, |v26|
	v_max3_f32 v2, v2, |v25|, |v30|
	v_max3_f32 v2, v2, |v27|, |v29|
	v_max3_f32 v2, v2, |v28|, |v32|
	v_max3_f32 v2, v2, |v31|, |v36|
	v_max3_f32 v2, v2, |v34|, |v43|
	v_max3_f32 v2, v2, |v41|, |v42|
	v_max3_f32 v2, v2, |v35|, |v38|
	v_max3_f32 v2, v2, |v37|, |v40|
	v_max3_f32 v2, v2, |v39|, |v47|
	v_max3_f32 v2, v2, |v44|, |v46|
	v_max3_f32 v2, v2, |v45|, |v49|
	v_max3_f32 v2, v2, |v48|, |v51|
	v_max3_f32 v2, v2, |v50|, |v55|
	v_max3_f32 v2, v2, |v52|, |v54|
	v_max3_f32 v2, v2, |v53|, |v57|
	v_max3_f32 v2, v2, |v56|, |v59|
	v_max3_f32 v2, v2, |v58|, |v63|
	v_max3_f32 v2, v2, |v60|, |v62|
	v_max3_f32 v2, v2, |v61|, |v65|
	v_max3_f32 v2, v2, |v64|, |v68|
	v_max3_f32 v2, v2, |v66|, |v75|
	v_max3_f32 v2, v2, |v73|, |v74|
	v_max3_f32 v2, v2, |v67|, |v70|
	v_max3_f32 v2, v2, |v69|, |v72|
	v_max3_f32 v2, v2, |v71|, |v79|
	v_max3_f32 v2, v2, |v76|, |v78|
	v_max3_f32 v2, v2, |v77|, |v81|
	v_max3_f32 v2, v2, |v80|, |v83|
	v_max3_f32 v2, v2, |v82|, |v87|
	v_max3_f32 v2, v2, |v84|, |v86|
	v_max3_f32 v2, v2, |v85|, |v89|
	v_max3_f32 v2, v2, |v88|, |v91|
	v_max3_f32 v2, v2, |v90|, |v95|
	v_max3_f32 v2, v2, |v92|, |v94|
	v_max3_f32 v2, v2, |v93|, |v97|
	v_max3_f32 v2, v2, |v96|, |v100|
	v_max3_f32 v2, v2, |v98|, |v107|
	v_max3_f32 v2, v2, |v105|, |v106|
	v_max3_f32 v2, v2, |v99|, |v102|
	v_max3_f32 v2, v2, |v101|, |v104|
	v_max3_f32 v2, v2, |v103|, |v111|
	v_max3_f32 v2, v2, |v108|, |v110|
	v_max3_f32 v2, v2, |v109|, |v113|
	v_max3_f32 v2, v2, |v112|, |v115|
	v_max3_f32 v2, v2, |v114|, |v119|
	v_max3_f32 v2, v2, |v116|, |v118|
	v_max3_f32 v2, v2, |v117|, |v121|
	v_max3_f32 v2, v2, |v120|, |v131|
	v_max3_f32 v2, v2, |v130|, |v135|
	v_max3_f32 v2, v2, |v132|, |v134|
	v_max3_f32 v2, v2, |v133|, |v137|
	v_max3_f32 v2, v2, |v136|, |v139|
	v_max3_f32 v2, v2, |v138|, |v141|
	s_lshl_b32 s17, s21, 11
	v_max3_f32 v4, v2, |v140|, |v142|
	v_add_u32_e32 v2, s17, v150
	v_add_u32_e32 v5, s17, v151
	ds_write_b32 v2, v4
	s_waitcnt lgkmcnt(0)
	s_barrier
; template <bool PERMGL, bool FP8>
; __device__ __forceinline__ void q8_cols_item(const float* W, int N, int n0, unsigned char* Bq, float* sc_out, LAS float* AM, int par, int wave, int lane) {
;     ...
;     for (int w = 0; w < 8; ++w) am = fmaxf(am, AM[(par * 8 + w) * 64 + lane]);
;     const float sc = am > 0.f ? am * (FP8 ? (1.0f / 256.0f) : (1.0f / 127.0f)) : 1.0f, inv = 1.0f / sc;
;     int row = n;
;     if (PERMGL) { const int j = n >> 1, pr = n & 1, o = j & 127; row = ((j >> 7) << 8) + (((o >> 2) & 1) << 7) + ((o >> 5) << 5) + (pr << 4) + (((o >> 3) & 3) << 2) + (o & 3); }
;     if (!PERMGL) { const int o = n & 255; row = ((n >> 8) << 8) + (((o >> 3) & 1) << 7) + ((o >> 6) << 5) + (((o >> 4) & 3) << 3) + (o & 7); }
;     auto xq = [](unsigned x) { return (unsigned)__builtin_amdgcn_update_dpp(0, (int)x, 0xB1, 0xf, 0xf, true); };
;     const bool odd = lane & 1;
;     const int rowp = (int)xq((unsigned)row);
;     unsigned char* plo = Bq + (size_t)(odd ? rowp : row) * 1024 + 128 * wave + (odd ? 16 : 0);
;     unsigned char* phi = Bq + (size_t)(odd ? row : rowp) * 1024 + 128 * wave + (odd ? 16 : 0);
;     auto packc = [&](int c) { u32x4 o;
;         if (FP8) { o.x = f8x4(v[16 * c], v[16 * c + 1], v[16 * c + 2], v[16 * c + 3], inv); o.y = f8x4(v[16 * c + 4], v[16 * c + 5], v[16 * c + 6], v[16 * c + 7], inv);
;                    o.z = f8x4(v[16 * c + 8], v[16 * c + 9], v[16 * c + 10], v[16 * c + 11], inv); o.w = f8x4(v[16 * c + 12], v[16 * c + 13], v[16 * c + 14], v[16 * c + 15], inv); }
;         else { o.x = q8x4(v[16 * c], v[16 * c + 1], v[16 * c + 2], v[16 * c + 3], inv); o.y = q8x4(v[16 * c + 4], v[16 * c + 5], v[16 * c + 6], v[16 * c + 7], inv);
;                o.z = q8x4(v[16 * c + 8], v[16 * c + 9], v[16 * c + 10], v[16 * c + 11], inv); o.w = q8x4(v[16 * c + 12], v[16 * c + 13], v[16 * c + 14], v[16 * c + 15], inv); }
;         return o; };
; #pragma unroll
;     for (int j = 0; j < 4; ++j) { const u32x4 p0 = packc(2 * j), p1 = packc(2 * j + 1);
;         u32x4 snd, rcv;
; #pragma unroll
;         for (int q = 0; q < 4; ++q) { snd[q] = odd ? p0[q] : p1[q]; rcv[q] = xq(snd[q]); }
;         u32x4 a, b;
; #pragma unroll
;         for (int q = 0; q < 4; ++q) { a[q] = odd ? rcv[q] : p0[q]; b[q] = odd ? p1[q] : rcv[q]; }
;         *(u32x4*)(plo + 32 * j) = a; *(u32x4*)(phi + 32 * j) = b; }
	ds_read2st64_b32 v[2:3], v5 offset1:1
	v_mov_b32_e32 v145, v33
	s_waitcnt lgkmcnt(0)
	v_max3_f32 v4, v4, v2, v3
	ds_read2st64_b32 v[2:3], v5 offset0:2 offset1:3
	s_waitcnt lgkmcnt(0)
	v_max3_f32 v4, v4, v2, v3
	ds_read2st64_b32 v[2:3], v5 offset0:4 offset1:5
	s_waitcnt lgkmcnt(0)
	v_max3_f32 v4, v4, v2, v3
	ds_read2st64_b32 v[2:3], v5 offset0:6 offset1:7
	s_waitcnt lgkmcnt(0)
	v_max3_f32 v2, v4, v2, v3
	v_cmp_lt_f32_e32 vcc, 0, v2
	v_mul_f32_e32 v2, 0x3b800000, v2
	s_nop 0
	v_cndmask_b32_e32 v143, 1.0, v2, vcc
	v_div_scale_f32 v2, s[18:19], v143, v143, 1.0
	v_rcp_f32_e32 v3, v2
	s_nop 0
	v_fma_f32 v4, -v2, v3, 1.0
	v_fmac_f32_e32 v3, v4, v3
	v_div_scale_f32 v4, vcc, 1.0, v143, 1.0
	v_mul_f32_e32 v5, v4, v3
	v_fma_f32 v144, -v2, v5, v4
	v_fmac_f32_e32 v5, v144, v3
	v_fma_f32 v2, -v2, v5, v4
	v_div_fmas_f32 v2, v2, v3, v5
	v_div_fixup_f32 v144, v2, v143, 1.0
	v_mul_f32_e32 v6, v6, v144
	v_mul_f32_e32 v8, v8, v144
	v_cvt_pk_fp8_f32 v145, v6, v8
	v_mul_f32_e32 v6, v7, v144
	v_mul_f32_e32 v7, v11, v144
	v_mov_b32_e32 v8, v33
	v_cvt_pk_fp8_f32 v145, v6, v7 op_sel:[0,0,1]
	v_mul_f32_e32 v6, v9, v144
	v_mul_f32_e32 v7, v12, v144
	v_cvt_pk_fp8_f32 v8, v6, v7
	v_mul_f32_e32 v6, v10, v144
	v_mul_f32_e32 v7, v14, v144
	v_mov_b32_e32 v9, v33
	v_cvt_pk_fp8_f32 v8, v6, v7 op_sel:[0,0,1]
	v_mul_f32_e32 v6, v13, v144
	v_mul_f32_e32 v7, v16, v144
	v_cvt_pk_fp8_f32 v9, v6, v7
	v_mul_f32_e32 v6, v15, v144
	v_mul_f32_e32 v7, v18, v144
	v_mov_b32_e32 v13, v33
	v_cvt_pk_fp8_f32 v9, v6, v7 op_sel:[0,0,1]
	v_mul_f32_e32 v6, v17, v144
	v_mul_f32_e32 v7, v22, v144
	v_cvt_pk_fp8_f32 v13, v6, v7
	v_mul_f32_e32 v6, v19, v144
	v_mul_f32_e32 v7, v21, v144
	v_mov_b32_e32 v10, v33
	v_cvt_pk_fp8_f32 v13, v6, v7 op_sel:[0,0,1]
	v_mul_f32_e32 v6, v20, v144
	v_mul_f32_e32 v7, v24, v144
	v_cvt_pk_fp8_f32 v10, v6, v7
	v_mul_f32_e32 v6, v23, v144
	v_mul_f32_e32 v7, v26, v144
	v_mov_b32_e32 v11, v33
	v_cvt_pk_fp8_f32 v10, v6, v7 op_sel:[0,0,1]
	v_mul_f32_e32 v6, v25, v144
	v_mul_f32_e32 v7, v30, v144
	v_cvt_pk_fp8_f32 v11, v6, v7
	v_mul_f32_e32 v6, v27, v144
	v_mul_f32_e32 v7, v29, v144
	v_mov_b32_e32 v12, v33
	v_cvt_pk_fp8_f32 v11, v6, v7 op_sel:[0,0,1]
	v_mul_f32_e32 v6, v28, v144
	v_mul_f32_e32 v7, v32, v144
	v_cvt_pk_fp8_f32 v12, v6, v7
	v_mul_f32_e32 v6, v31, v144
	v_mul_f32_e32 v7, v36, v144
	v_mov_b32_e32 v14, v33
	v_cvt_pk_fp8_f32 v12, v6, v7 op_sel:[0,0,1]
	v_mul_f32_e32 v6, v34, v144
	v_mul_f32_e32 v7, v43, v144
	v_cvt_pk_fp8_f32 v14, v6, v7
	v_lshrrev_b32_e32 v2, 1, v0
	v_and_b32_e32 v2, 0x78, v2
	v_and_b32_e32 v3, 0xffffff07, v0
	v_or3_b32 v4, v3, v152, v2
	v_mul_f32_e32 v6, v41, v144
	v_mul_f32_e32 v7, v42, v144
	v_mov_b32_dpp v5, v4 quad_perm:[1,0,3,2] row_mask:0xf bank_mask:0xf bound_ctrl:1
	v_cvt_pk_fp8_f32 v14, v6, v7 op_sel:[0,0,1]
	v_cndmask_b32_e64 v2, v5, v4, s[2:3]
	v_cndmask_b32_e64 v6, v145, v10, s[2:3]
	v_ashrrev_i32_e32 v3, 31, v2
	v_cndmask_b32_e64 v4, v4, v5, s[2:3]
	v_mov_b32_dpp v7, v6 quad_perm:[1,0,3,2] row_mask:0xf bank_mask:0xf bound_ctrl:1
	v_cndmask_b32_e64 v6, v8, v11, s[2:3]
	v_lshlrev_b64 v[2:3], 10, v[2:3]
	v_ashrrev_i32_e32 v5, 31, v4
	v_mov_b32_dpp v15, v6 quad_perm:[1,0,3,2] row_mask:0xf bank_mask:0xf bound_ctrl:1
	v_cndmask_b32_e64 v6, v9, v12, s[2:3]
	v_lshl_add_u64 v[2:3], s[10:11], 0, v[2:3]
	v_lshlrev_b64 v[4:5], 10, v[4:5]
	v_mov_b32_dpp v16, v6 quad_perm:[1,0,3,2] row_mask:0xf bank_mask:0xf bound_ctrl:1
	v_cndmask_b32_e64 v6, v13, v14, s[2:3]
	v_lshl_add_u64 v[2:3], v[2:3], 0, s[42:43]
	v_lshl_add_u64 v[4:5], s[10:11], 0, v[4:5]
	v_mov_b32_dpp v17, v6 quad_perm:[1,0,3,2] row_mask:0xf bank_mask:0xf bound_ctrl:1
	v_lshl_add_u64 v[2:3], v[2:3], 0, v[122:123]
	v_lshl_add_u64 v[4:5], v[4:5], 0, s[42:43]
	v_cndmask_b32_e64 v6, v7, v145, s[2:3]
	v_cndmask_b32_e64 v10, v10, v7, s[2:3]
	v_cndmask_b32_e64 v7, v15, v8, s[2:3]
	v_cndmask_b32_e64 v8, v16, v9, s[2:3]
	v_cndmask_b32_e64 v9, v17, v13, s[2:3]
	v_lshl_add_u64 v[4:5], v[4:5], 0, v[122:123]
	v_cndmask_b32_e64 v11, v11, v15, s[2:3]
	v_cndmask_b32_e64 v12, v12, v16, s[2:3]
	v_cndmask_b32_e64 v13, v14, v17, s[2:3]
	global_store_dwordx4 v[2:3], v[6:9], off
	global_store_dwordx4 v[4:5], v[10:13], off
	v_mov_b32_e32 v14, v33
	v_mul_f32_e32 v6, v35, v144
	v_mul_f32_e32 v7, v38, v144
	v_mov_b32_e32 v8, v33
	v_cvt_pk_fp8_f32 v8, v6, v7
	v_mul_f32_e32 v6, v37, v144
	v_mul_f32_e32 v7, v40, v144
	v_mov_b32_e32 v9, v33
	v_cvt_pk_fp8_f32 v8, v6, v7 op_sel:[0,0,1]
	v_mul_f32_e32 v6, v39, v144
	v_mul_f32_e32 v7, v47, v144
	v_cvt_pk_fp8_f32 v9, v6, v7
	v_mul_f32_e32 v6, v44, v144
	v_mul_f32_e32 v7, v46, v144
	v_mov_b32_e32 v12, v33
	v_cvt_pk_fp8_f32 v9, v6, v7 op_sel:[0,0,1]
	v_mul_f32_e32 v6, v45, v144
	v_mul_f32_e32 v7, v49, v144
	v_cvt_pk_fp8_f32 v12, v6, v7
	v_mul_f32_e32 v6, v48, v144
	v_mul_f32_e32 v7, v51, v144
	v_mov_b32_e32 v13, v33
	v_cvt_pk_fp8_f32 v12, v6, v7 op_sel:[0,0,1]
	v_mul_f32_e32 v6, v50, v144
	v_mul_f32_e32 v7, v55, v144
	v_cvt_pk_fp8_f32 v13, v6, v7
	v_mul_f32_e32 v6, v52, v144
	v_mul_f32_e32 v7, v54, v144
	v_mov_b32_e32 v10, v33
	v_cvt_pk_fp8_f32 v13, v6, v7 op_sel:[0,0,1]
	v_mul_f32_e32 v6, v53, v144
	v_mul_f32_e32 v7, v57, v144
	v_cvt_pk_fp8_f32 v10, v6, v7
	v_mul_f32_e32 v6, v56, v144
	v_mul_f32_e32 v7, v59, v144
	v_mov_b32_e32 v11, v33
	v_cvt_pk_fp8_f32 v10, v6, v7 op_sel:[0,0,1]
	v_mul_f32_e32 v6, v58, v144
	v_mul_f32_e32 v7, v63, v144
	v_cvt_pk_fp8_f32 v11, v6, v7
	v_mul_f32_e32 v6, v60, v144
	v_mul_f32_e32 v7, v62, v144
	v_mov_b32_e32 v15, v33
	v_cvt_pk_fp8_f32 v11, v6, v7 op_sel:[0,0,1]
	v_mul_f32_e32 v6, v61, v144
	v_mul_f32_e32 v7, v65, v144
	v_cvt_pk_fp8_f32 v14, v6, v7
	v_mul_f32_e32 v6, v64, v144
	v_mul_f32_e32 v7, v68, v144
	s_and_b64 vcc, exec, s[0:1]
; template <bool PERMGL, bool FP8>
; __device__ __forceinline__ void q8_cols_item(const float* W, int N, int n0, unsigned char* Bq, float* sc_out, LAS float* AM, int par, int wave, int lane) {
;     ...
;     for (int j = 0; j < 4; ++j) { const u32x4 p0 = packc(2 * j), p1 = packc(2 * j + 1);
;         u32x4 snd, rcv;
; #pragma unroll
;         for (int q = 0; q < 4; ++q) { snd[q] = odd ? p0[q] : p1[q]; rcv[q] = xq(snd[q]); }
;         u32x4 a, b;
; #pragma unroll
;         for (int q = 0; q < 4; ++q) { a[q] = odd ? rcv[q] : p0[q]; b[q] = odd ? p1[q] : rcv[q]; }
;         *(u32x4*)(plo + 32 * j) = a; *(u32x4*)(phi + 32 * j) = b; }
;     if (wave == 0) sc_out[PERMGL ? row : n] = FP8 ? sc * 16.0f : sc;
	v_cvt_pk_fp8_f32 v14, v6, v7 op_sel:[0,0,1]
	v_mul_f32_e32 v6, v66, v144
	v_mul_f32_e32 v7, v75, v144
	v_cvt_pk_fp8_f32 v15, v6, v7
	v_mul_f32_e32 v6, v73, v144
	v_mul_f32_e32 v7, v74, v144
	v_cvt_pk_fp8_f32 v15, v6, v7 op_sel:[0,0,1]
	v_cndmask_b32_e64 v6, v8, v10, s[2:3]
	s_nop 1
	v_mov_b32_dpp v7, v6 quad_perm:[1,0,3,2] row_mask:0xf bank_mask:0xf bound_ctrl:1
	v_cndmask_b32_e64 v6, v9, v11, s[2:3]
	v_cndmask_b32_e64 v10, v10, v7, s[2:3]
	s_nop 0
	v_mov_b32_dpp v16, v6 quad_perm:[1,0,3,2] row_mask:0xf bank_mask:0xf bound_ctrl:1
	v_cndmask_b32_e64 v6, v12, v14, s[2:3]
	v_cndmask_b32_e64 v11, v11, v16, s[2:3]
	s_nop 0
	v_mov_b32_dpp v17, v6 quad_perm:[1,0,3,2] row_mask:0xf bank_mask:0xf bound_ctrl:1
	v_cndmask_b32_e64 v6, v13, v15, s[2:3]
	s_nop 1
	v_mov_b32_dpp v18, v6 quad_perm:[1,0,3,2] row_mask:0xf bank_mask:0xf bound_ctrl:1
	v_cndmask_b32_e64 v6, v7, v8, s[2:3]
	v_cndmask_b32_e64 v7, v16, v9, s[2:3]
	v_cndmask_b32_e64 v8, v17, v12, s[2:3]
	v_cndmask_b32_e64 v9, v18, v13, s[2:3]
	v_cndmask_b32_e64 v12, v14, v17, s[2:3]
	v_cndmask_b32_e64 v13, v15, v18, s[2:3]
	global_store_dwordx4 v[2:3], v[6:9], off offset:32
	global_store_dwordx4 v[4:5], v[10:13], off offset:32
	v_mov_b32_e32 v14, v33
	v_mul_f32_e32 v6, v67, v144
	v_mul_f32_e32 v7, v70, v144
	v_mov_b32_e32 v8, v33
	v_cvt_pk_fp8_f32 v8, v6, v7
	v_mul_f32_e32 v6, v69, v144
	v_mul_f32_e32 v7, v72, v144
	v_mov_b32_e32 v9, v33
	v_cvt_pk_fp8_f32 v8, v6, v7 op_sel:[0,0,1]
	v_mul_f32_e32 v6, v71, v144
	v_mul_f32_e32 v7, v79, v144
	v_cvt_pk_fp8_f32 v9, v6, v7
	v_mul_f32_e32 v6, v76, v144
	v_mul_f32_e32 v7, v78, v144
	v_mov_b32_e32 v12, v33
	v_cvt_pk_fp8_f32 v9, v6, v7 op_sel:[0,0,1]
	v_mul_f32_e32 v6, v77, v144
	v_mul_f32_e32 v7, v81, v144
	v_cvt_pk_fp8_f32 v12, v6, v7
	v_mul_f32_e32 v6, v80, v144
	v_mul_f32_e32 v7, v83, v144
	v_mov_b32_e32 v13, v33
	v_cvt_pk_fp8_f32 v12, v6, v7 op_sel:[0,0,1]
	v_mul_f32_e32 v6, v82, v144
	v_mul_f32_e32 v7, v87, v144
	v_cvt_pk_fp8_f32 v13, v6, v7
	v_mul_f32_e32 v6, v84, v144
	v_mul_f32_e32 v7, v86, v144
	v_mov_b32_e32 v10, v33
	v_cvt_pk_fp8_f32 v13, v6, v7 op_sel:[0,0,1]
	v_mul_f32_e32 v6, v85, v144
	v_mul_f32_e32 v7, v89, v144
	v_cvt_pk_fp8_f32 v10, v6, v7
	v_mul_f32_e32 v6, v88, v144
	v_mul_f32_e32 v7, v91, v144
	v_mov_b32_e32 v11, v33
	v_cvt_pk_fp8_f32 v10, v6, v7 op_sel:[0,0,1]
	v_mul_f32_e32 v6, v90, v144
	v_mul_f32_e32 v7, v95, v144
	v_cvt_pk_fp8_f32 v11, v6, v7
	v_mul_f32_e32 v6, v92, v144
	v_mul_f32_e32 v7, v94, v144
	v_mov_b32_e32 v15, v33
	v_cvt_pk_fp8_f32 v11, v6, v7 op_sel:[0,0,1]
	v_mul_f32_e32 v6, v93, v144
	v_mul_f32_e32 v7, v97, v144
	v_cvt_pk_fp8_f32 v14, v6, v7
	v_mul_f32_e32 v6, v96, v144
	v_mul_f32_e32 v7, v100, v144
	v_cvt_pk_fp8_f32 v14, v6, v7 op_sel:[0,0,1]
	v_mul_f32_e32 v6, v98, v144
	v_mul_f32_e32 v7, v107, v144
	v_cvt_pk_fp8_f32 v15, v6, v7
	v_mul_f32_e32 v6, v105, v144
	v_mul_f32_e32 v7, v106, v144
	v_cvt_pk_fp8_f32 v15, v6, v7 op_sel:[0,0,1]
	v_cndmask_b32_e64 v6, v8, v10, s[2:3]
	s_nop 1
	v_mov_b32_dpp v7, v6 quad_perm:[1,0,3,2] row_mask:0xf bank_mask:0xf bound_ctrl:1
	v_cndmask_b32_e64 v6, v9, v11, s[2:3]
	v_cndmask_b32_e64 v10, v10, v7, s[2:3]
	s_nop 0
	v_mov_b32_dpp v16, v6 quad_perm:[1,0,3,2] row_mask:0xf bank_mask:0xf bound_ctrl:1
	v_cndmask_b32_e64 v6, v12, v14, s[2:3]
	v_cndmask_b32_e64 v11, v11, v16, s[2:3]
	s_nop 0
	v_mov_b32_dpp v17, v6 quad_perm:[1,0,3,2] row_mask:0xf bank_mask:0xf bound_ctrl:1
	v_cndmask_b32_e64 v6, v13, v15, s[2:3]
	s_nop 1
	v_mov_b32_dpp v18, v6 quad_perm:[1,0,3,2] row_mask:0xf bank_mask:0xf bound_ctrl:1
	v_cndmask_b32_e64 v6, v7, v8, s[2:3]
	v_cndmask_b32_e64 v7, v16, v9, s[2:3]
	v_cndmask_b32_e64 v8, v17, v12, s[2:3]
	v_cndmask_b32_e64 v9, v18, v13, s[2:3]
	v_cndmask_b32_e64 v12, v14, v17, s[2:3]
	v_cndmask_b32_e64 v13, v15, v18, s[2:3]
	global_store_dwordx4 v[2:3], v[6:9], off offset:64
	global_store_dwordx4 v[4:5], v[10:13], off offset:64
	v_mov_b32_e32 v14, v33
	v_mul_f32_e32 v6, v99, v144
	v_mul_f32_e32 v7, v102, v144
	v_mov_b32_e32 v8, v33
	v_cvt_pk_fp8_f32 v8, v6, v7
	v_mul_f32_e32 v6, v101, v144
	v_mul_f32_e32 v7, v104, v144
	v_mov_b32_e32 v9, v33
	v_cvt_pk_fp8_f32 v8, v6, v7 op_sel:[0,0,1]
	v_mul_f32_e32 v6, v103, v144
	v_mul_f32_e32 v7, v111, v144
	v_cvt_pk_fp8_f32 v9, v6, v7
	v_mul_f32_e32 v6, v108, v144
	v_mul_f32_e32 v7, v110, v144
	v_mov_b32_e32 v12, v33
	v_cvt_pk_fp8_f32 v9, v6, v7 op_sel:[0,0,1]
	v_mul_f32_e32 v6, v109, v144
	v_mul_f32_e32 v7, v113, v144
	v_cvt_pk_fp8_f32 v12, v6, v7
	v_mul_f32_e32 v6, v112, v144
	v_mul_f32_e32 v7, v115, v144
	v_mov_b32_e32 v13, v33
	v_cvt_pk_fp8_f32 v12, v6, v7 op_sel:[0,0,1]
	v_mul_f32_e32 v6, v114, v144
	v_mul_f32_e32 v7, v119, v144
	v_cvt_pk_fp8_f32 v13, v6, v7
	v_mul_f32_e32 v6, v116, v144
	v_mul_f32_e32 v7, v118, v144
	v_mov_b32_e32 v10, v33
	v_cvt_pk_fp8_f32 v13, v6, v7 op_sel:[0,0,1]
	v_mul_f32_e32 v6, v117, v144
	v_mul_f32_e32 v7, v121, v144
	v_cvt_pk_fp8_f32 v10, v6, v7
	v_mul_f32_e32 v6, v120, v144
	v_mul_f32_e32 v7, v131, v144
	v_mov_b32_e32 v11, v33
	v_cvt_pk_fp8_f32 v10, v6, v7 op_sel:[0,0,1]
	v_mul_f32_e32 v6, v130, v144
	v_mul_f32_e32 v7, v135, v144
	v_cvt_pk_fp8_f32 v11, v6, v7
	v_mul_f32_e32 v6, v132, v144
	v_mul_f32_e32 v7, v134, v144
	v_mov_b32_e32 v15, v33
	v_cvt_pk_fp8_f32 v11, v6, v7 op_sel:[0,0,1]
	v_mul_f32_e32 v6, v133, v144
	v_mul_f32_e32 v7, v137, v144
	v_cvt_pk_fp8_f32 v14, v6, v7
	v_mul_f32_e32 v6, v136, v144
	v_mul_f32_e32 v7, v139, v144
	v_cvt_pk_fp8_f32 v14, v6, v7 op_sel:[0,0,1]
	v_mul_f32_e32 v6, v138, v144
	v_mul_f32_e32 v7, v141, v144
	v_cvt_pk_fp8_f32 v15, v6, v7
	v_mul_f32_e32 v6, v140, v144
	v_mul_f32_e32 v7, v142, v144
	v_cvt_pk_fp8_f32 v15, v6, v7 op_sel:[0,0,1]
	v_cndmask_b32_e64 v6, v8, v10, s[2:3]
	s_nop 1
	v_mov_b32_dpp v7, v6 quad_perm:[1,0,3,2] row_mask:0xf bank_mask:0xf bound_ctrl:1
	v_cndmask_b32_e64 v6, v9, v11, s[2:3]
	v_cndmask_b32_e64 v10, v10, v7, s[2:3]
	s_nop 0
	v_mov_b32_dpp v16, v6 quad_perm:[1,0,3,2] row_mask:0xf bank_mask:0xf bound_ctrl:1
	v_cndmask_b32_e64 v6, v12, v14, s[2:3]
	v_cndmask_b32_e64 v11, v11, v16, s[2:3]
	s_nop 0
	v_mov_b32_dpp v17, v6 quad_perm:[1,0,3,2] row_mask:0xf bank_mask:0xf bound_ctrl:1
	v_cndmask_b32_e64 v6, v13, v15, s[2:3]
	s_nop 1
	v_mov_b32_dpp v18, v6 quad_perm:[1,0,3,2] row_mask:0xf bank_mask:0xf bound_ctrl:1
	v_cndmask_b32_e64 v6, v7, v8, s[2:3]
	v_cndmask_b32_e64 v7, v16, v9, s[2:3]
	v_cndmask_b32_e64 v8, v17, v12, s[2:3]
	v_cndmask_b32_e64 v9, v18, v13, s[2:3]
	v_cndmask_b32_e64 v12, v14, v17, s[2:3]
	v_cndmask_b32_e64 v13, v15, v18, s[2:3]
	global_store_dwordx4 v[2:3], v[6:9], off offset:96
	global_store_dwordx4 v[4:5], v[10:13], off offset:96
	s_cbranch_vccnz .LBB0_236
	s_lshl_b64 s[8:9], s[8:9], 12
	v_readlane_b32 s10, v252, 60
	s_add_u32 s8, s10, s8
	v_readlane_b32 s10, v252, 61
	s_addc_u32 s9, s10, s9
	v_mul_f32_e32 v2, 0x41800000, v143
	v_lshl_add_u64 v[0:1], v[0:1], 2, s[8:9]
	global_store_dword v[0:1], v2, off

; template <bool PERMGL, bool FP8>
; __device__ __forceinline__ void q8_cols_item(const float* W, int N, int n0, unsigned char* Bq, float* sc_out, LAS float* AM, int par, int wave, int lane) {
;     ...
;     for (int i = 0; i < 128; ++i) v[i] = Wp[(size_t)i * N];
; __global__ void __launch_bounds__(NWAVES * 64, 2) mk_fwd(Args args) {
;     ...
;                             if (r < 1024) { const int mi = lyr * 32 + (r >> 5), nb = ((r & 31) + 8 * ((r >> 6) & 3)) & 31;
;                                 q8_cols_item<true, false>(args.in[11] + (size_t)mi * D * 2048, 2048, nb * 64, ws + WS_WGU + (size_t)mi * 2048 * 1024, (float*)(ws + WS_SB) + (size_t)mi * 2048, CAM, cv_par, wave, lane); }
.LBB0_237:
	s_andn2_b64 vcc, exec, s[8:9]
	s_cbranch_vccnz .LBB0_232
	s_lshl_b32 s8, s15, 5
	s_ashr_i32 s9, s16, 5
	s_add_i32 s8, s8, s9
	s_sub_i32 s9, s24, s14
	s_lshr_b32 s9, s9, 3
	s_and_b32 s9, s9, 24
	s_add_i32 s9, s24, s9
	s_add_i32 s10, s9, s13
	s_ashr_i32 s9, s8, 31
	s_lshl_b32 s10, s10, 6
	s_lshl_b64 s[14:15], s[8:9], 23
	s_and_b32 s13, s10, 0x7c0
	s_lshl_b64 s[10:11], s[8:9], 21
	s_add_u32 s10, s57, s10
	s_addc_u32 s11, s65, s11
	v_add_u32_e32 v0, s13, v127
	v_readlane_b32 s13, v252, 62
	s_add_u32 s14, s13, s14
	v_readlane_b32 s13, v253, 0
	s_addc_u32 s15, s13, s15
	v_ashrrev_i32_e32 v1, 31, v0
	v_lshl_add_u64 v[2:3], v[0:1], 2, s[14:15]
	s_movk_i32 s13, 0x2000
	v_add_co_u32_e32 v4, vcc, s13, v2
	s_movk_i32 s13, 0x4000
	s_nop 0
	v_addc_co_u32_e32 v5, vcc, 0, v3, vcc
	global_load_dword v1, v[2:3], off nt
	global_load_dword v6, v[4:5], off nt
	v_add_co_u32_e32 v4, vcc, s13, v2
	s_movk_i32 s13, 0x6000
	s_nop 0
	v_addc_co_u32_e32 v5, vcc, 0, v3, vcc
	global_load_dword v7, v[4:5], off nt
	v_add_co_u32_e32 v4, vcc, s13, v2
	s_mov_b32 s13, 0x8000
	s_nop 0
	v_addc_co_u32_e32 v5, vcc, 0, v3, vcc
	global_load_dword v8, v[4:5], off nt
	v_add_co_u32_e32 v4, vcc, s13, v2
	s_mov_b32 s13, 0xa000
	s_nop 0
	v_addc_co_u32_e32 v5, vcc, 0, v3, vcc
	global_load_dword v9, v[4:5], off nt
	v_add_co_u32_e32 v4, vcc, s13, v2
	s_mov_b32 s13, 0xc000
	s_nop 0
	v_addc_co_u32_e32 v5, vcc, 0, v3, vcc
	global_load_dword v10, v[4:5], off nt
	v_add_co_u32_e32 v4, vcc, s13, v2
	s_mov_b32 s13, 0xe000
	s_nop 0
	v_addc_co_u32_e32 v5, vcc, 0, v3, vcc
	global_load_dword v11, v[4:5], off nt
	v_add_co_u32_e32 v4, vcc, s13, v2
	s_mov_b32 s13, 0x10000
	s_nop 0
	v_addc_co_u32_e32 v5, vcc, 0, v3, vcc
	global_load_dword v12, v[4:5], off nt
	v_add_co_u32_e32 v4, vcc, s13, v2
	s_mov_b32 s13, 0x12000
	s_nop 0
	v_addc_co_u32_e32 v5, vcc, 0, v3, vcc
	global_load_dword v13, v[4:5], off nt
	v_add_co_u32_e32 v4, vcc, s13, v2
	s_mov_b32 s13, 0x14000
	s_nop 0
	v_addc_co_u32_e32 v5, vcc, 0, v3, vcc
	global_load_dword v14, v[4:5], off nt
	v_add_co_u32_e32 v4, vcc, s13, v2
	s_mov_b32 s13, 0x16000
	s_nop 0
	v_addc_co_u32_e32 v5, vcc, 0, v3, vcc
	global_load_dword v15, v[4:5], off nt
	v_add_co_u32_e32 v4, vcc, s13, v2
	s_mov_b32 s13, 0x18000
	s_nop 0
	v_addc_co_u32_e32 v5, vcc, 0, v3, vcc
	global_load_dword v16, v[4:5], off nt
	v_add_co_u32_e32 v4, vcc, s13, v2
	s_mov_b32 s13, 0x1a000
	s_nop 0
	v_addc_co_u32_e32 v5, vcc, 0, v3, vcc
	global_load_dword v17, v[4:5], off nt
	v_add_co_u32_e32 v4, vcc, s13, v2
	s_mov_b32 s13, 0x1c000
	s_nop 0
	v_addc_co_u32_e32 v5, vcc, 0, v3, vcc
	global_load_dword v18, v[4:5], off nt
	v_add_co_u32_e32 v4, vcc, s13, v2
	s_mov_b32 s13, 0x1e000
	s_nop 0
	v_addc_co_u32_e32 v5, vcc, 0, v3, vcc
	global_load_dword v19, v[4:5], off nt
	v_add_co_u32_e32 v4, vcc, s13, v2
	s_mov_b32 s13, 0x20000
	s_nop 0
	v_addc_co_u32_e32 v5, vcc, 0, v3, vcc
	global_load_dword v20, v[4:5], off nt
	v_add_co_u32_e32 v4, vcc, s13, v2
	s_mov_b32 s13, 0x22000
	s_nop 0
	v_addc_co_u32_e32 v5, vcc, 0, v3, vcc
	global_load_dword v21, v[4:5], off nt
	v_add_co_u32_e32 v4, vcc, s13, v2
	s_mov_b32 s13, 0x24000
	s_nop 0
	v_addc_co_u32_e32 v5, vcc, 0, v3, vcc
	global_load_dword v22, v[4:5], off nt
	v_add_co_u32_e32 v4, vcc, s13, v2
	s_mov_b32 s13, 0x26000
	s_nop 0
	v_addc_co_u32_e32 v5, vcc, 0, v3, vcc
	global_load_dword v23, v[4:5], off nt
	v_add_co_u32_e32 v4, vcc, s13, v2
	s_mov_b32 s13, 0x28000
	s_nop 0
	v_addc_co_u32_e32 v5, vcc, 0, v3, vcc
	global_load_dword v24, v[4:5], off nt
	v_add_co_u32_e32 v4, vcc, s13, v2
	s_mov_b32 s13, 0x2a000
	s_nop 0
	v_addc_co_u32_e32 v5, vcc, 0, v3, vcc
	global_load_dword v25, v[4:5], off nt
	v_add_co_u32_e32 v4, vcc, s13, v2
	s_mov_b32 s13, 0x2c000
	s_nop 0
	v_addc_co_u32_e32 v5, vcc, 0, v3, vcc
	global_load_dword v26, v[4:5], off nt
	v_add_co_u32_e32 v4, vcc, s13, v2
	s_mov_b32 s13, 0x2e000
	s_nop 0
	v_addc_co_u32_e32 v5, vcc, 0, v3, vcc
	global_load_dword v27, v[4:5], off nt
	v_add_co_u32_e32 v4, vcc, s13, v2
	s_mov_b32 s13, 0x30000
	s_nop 0
	v_addc_co_u32_e32 v5, vcc, 0, v3, vcc
	global_load_dword v28, v[4:5], off nt
	v_add_co_u32_e32 v4, vcc, s13, v2
	s_mov_b32 s13, 0x32000
	s_nop 0
	v_addc_co_u32_e32 v5, vcc, 0, v3, vcc
	global_load_dword v29, v[4:5], off nt
	v_add_co_u32_e32 v4, vcc, s13, v2
	s_mov_b32 s13, 0x34000
	s_nop 0
	v_addc_co_u32_e32 v5, vcc, 0, v3, vcc
	global_load_dword v30, v[4:5], off nt
	v_add_co_u32_e32 v4, vcc, s13, v2
	s_mov_b32 s13, 0x36000
	s_nop 0
	v_addc_co_u32_e32 v5, vcc, 0, v3, vcc
	global_load_dword v31, v[4:5], off nt
	v_add_co_u32_e32 v4, vcc, s13, v2
	s_mov_b32 s13, 0x38000
	s_nop 0
	v_addc_co_u32_e32 v5, vcc, 0, v3, vcc
	global_load_dword v32, v[4:5], off nt
	v_add_co_u32_e32 v4, vcc, s13, v2
	s_mov_b32 s13, 0x3a000
	s_nop 0
	v_addc_co_u32_e32 v5, vcc, 0, v3, vcc
	global_load_dword v34, v[4:5], off nt
	v_add_co_u32_e32 v4, vcc, s13, v2
	s_mov_b32 s13, 0x3c000
	s_nop 0
	v_addc_co_u32_e32 v5, vcc, 0, v3, vcc
	global_load_dword v36, v[4:5], off nt
	v_add_co_u32_e32 v4, vcc, s13, v2
	s_mov_b32 s13, 0x3e000
	s_nop 0
	v_addc_co_u32_e32 v5, vcc, 0, v3, vcc
	global_load_dword v38, v[4:5], off nt
	v_add_co_u32_e32 v4, vcc, s13, v2
	s_mov_b32 s13, 0x40000
	s_nop 0
	v_addc_co_u32_e32 v5, vcc, 0, v3, vcc
	global_load_dword v40, v[4:5], off nt
	v_add_co_u32_e32 v4, vcc, s13, v2
	s_mov_b32 s13, 0x42000
	s_nop 0
	v_addc_co_u32_e32 v5, vcc, 0, v3, vcc
	global_load_dword v35, v[4:5], off nt
	v_add_co_u32_e32 v4, vcc, s13, v2
	s_mov_b32 s13, 0x44000
	s_nop 0
	v_addc_co_u32_e32 v5, vcc, 0, v3, vcc
	global_load_dword v37, v[4:5], off nt
	v_add_co_u32_e32 v4, vcc, s13, v2
	s_mov_b32 s13, 0x46000
	s_nop 0
	v_addc_co_u32_e32 v5, vcc, 0, v3, vcc
; template <bool PERMGL, bool FP8>
; __device__ __forceinline__ void q8_cols_item(const float* W, int N, int n0, unsigned char* Bq, float* sc_out, LAS float* AM, int par, int wave, int lane) {
;     ...
;     for (int i = 0; i < 128; ++i) v[i] = Wp[(size_t)i * N];
	global_load_dword v39, v[4:5], off nt
	v_add_co_u32_e32 v4, vcc, s13, v2
	s_mov_b32 s13, 0x48000
	s_nop 0
	v_addc_co_u32_e32 v5, vcc, 0, v3, vcc
	global_load_dword v41, v[4:5], off nt
	v_add_co_u32_e32 v4, vcc, s13, v2
	s_mov_b32 s13, 0x4a000
	s_nop 0
	v_addc_co_u32_e32 v5, vcc, 0, v3, vcc
	global_load_dword v42, v[4:5], off nt
	v_add_co_u32_e32 v4, vcc, s13, v2
	s_mov_b32 s13, 0x4c000
	s_nop 0
	v_addc_co_u32_e32 v5, vcc, 0, v3, vcc
	global_load_dword v43, v[4:5], off nt
	v_add_co_u32_e32 v4, vcc, s13, v2
	s_mov_b32 s13, 0x4e000
	s_nop 0
	v_addc_co_u32_e32 v5, vcc, 0, v3, vcc
	global_load_dword v44, v[4:5], off nt
	v_add_co_u32_e32 v4, vcc, s13, v2
	s_mov_b32 s13, 0x50000
	s_nop 0
	v_addc_co_u32_e32 v5, vcc, 0, v3, vcc
	global_load_dword v45, v[4:5], off nt
	v_add_co_u32_e32 v4, vcc, s13, v2
	s_mov_b32 s13, 0x52000
	s_nop 0
	v_addc_co_u32_e32 v5, vcc, 0, v3, vcc
	global_load_dword v46, v[4:5], off nt
	v_add_co_u32_e32 v4, vcc, s13, v2
	s_mov_b32 s13, 0x54000
	s_nop 0
	v_addc_co_u32_e32 v5, vcc, 0, v3, vcc
	global_load_dword v47, v[4:5], off nt
	v_add_co_u32_e32 v4, vcc, s13, v2
	s_mov_b32 s13, 0x56000
	s_nop 0
	v_addc_co_u32_e32 v5, vcc, 0, v3, vcc
	global_load_dword v48, v[4:5], off nt
	v_add_co_u32_e32 v4, vcc, s13, v2
	s_mov_b32 s13, 0x58000
	s_nop 0
	v_addc_co_u32_e32 v5, vcc, 0, v3, vcc
	global_load_dword v49, v[4:5], off nt
	v_add_co_u32_e32 v4, vcc, s13, v2
	s_mov_b32 s13, 0x5a000
	s_nop 0
	v_addc_co_u32_e32 v5, vcc, 0, v3, vcc
	global_load_dword v50, v[4:5], off nt
	v_add_co_u32_e32 v4, vcc, s13, v2
	s_mov_b32 s13, 0x5c000
	s_nop 0
	v_addc_co_u32_e32 v5, vcc, 0, v3, vcc
	global_load_dword v51, v[4:5], off nt
	v_add_co_u32_e32 v4, vcc, s13, v2
	s_mov_b32 s13, 0x5e000
	s_nop 0
	v_addc_co_u32_e32 v5, vcc, 0, v3, vcc
	global_load_dword v52, v[4:5], off nt
	v_add_co_u32_e32 v4, vcc, s13, v2
	s_mov_b32 s13, 0x60000
	s_nop 0
	v_addc_co_u32_e32 v5, vcc, 0, v3, vcc
	global_load_dword v53, v[4:5], off nt
	v_add_co_u32_e32 v4, vcc, s13, v2
	s_mov_b32 s13, 0x62000
	s_nop 0
	v_addc_co_u32_e32 v5, vcc, 0, v3, vcc
	global_load_dword v54, v[4:5], off nt
	v_add_co_u32_e32 v4, vcc, s13, v2
	s_mov_b32 s13, 0x64000
	s_nop 0
	v_addc_co_u32_e32 v5, vcc, 0, v3, vcc
	global_load_dword v55, v[4:5], off nt
	v_add_co_u32_e32 v4, vcc, s13, v2
	s_mov_b32 s13, 0x66000
	s_nop 0
	v_addc_co_u32_e32 v5, vcc, 0, v3, vcc
	global_load_dword v56, v[4:5], off nt
	v_add_co_u32_e32 v4, vcc, s13, v2
	s_mov_b32 s13, 0x68000
	s_nop 0
	v_addc_co_u32_e32 v5, vcc, 0, v3, vcc
	global_load_dword v57, v[4:5], off nt
	v_add_co_u32_e32 v4, vcc, s13, v2
	s_mov_b32 s13, 0x6a000
	s_nop 0
	v_addc_co_u32_e32 v5, vcc, 0, v3, vcc
	global_load_dword v58, v[4:5], off nt
	v_add_co_u32_e32 v4, vcc, s13, v2
	s_mov_b32 s13, 0x6c000
	s_nop 0
	v_addc_co_u32_e32 v5, vcc, 0, v3, vcc
	global_load_dword v59, v[4:5], off nt
	v_add_co_u32_e32 v4, vcc, s13, v2
	s_mov_b32 s13, 0x6e000
	s_nop 0
	v_addc_co_u32_e32 v5, vcc, 0, v3, vcc
	global_load_dword v60, v[4:5], off nt
	v_add_co_u32_e32 v4, vcc, s13, v2
	s_mov_b32 s13, 0x70000
	s_nop 0
	v_addc_co_u32_e32 v5, vcc, 0, v3, vcc
	global_load_dword v61, v[4:5], off nt
	v_add_co_u32_e32 v4, vcc, s13, v2
	s_mov_b32 s13, 0x72000
	s_nop 0
	v_addc_co_u32_e32 v5, vcc, 0, v3, vcc
	global_load_dword v62, v[4:5], off nt
	v_add_co_u32_e32 v4, vcc, s13, v2
	s_mov_b32 s13, 0x74000
	s_nop 0
	v_addc_co_u32_e32 v5, vcc, 0, v3, vcc
	global_load_dword v63, v[4:5], off nt
	v_add_co_u32_e32 v4, vcc, s13, v2
	s_mov_b32 s13, 0x76000
	s_nop 0
	v_addc_co_u32_e32 v5, vcc, 0, v3, vcc
	global_load_dword v64, v[4:5], off nt
	v_add_co_u32_e32 v4, vcc, s13, v2
	s_mov_b32 s13, 0x78000
	s_nop 0
	v_addc_co_u32_e32 v5, vcc, 0, v3, vcc
	global_load_dword v65, v[4:5], off nt
	v_add_co_u32_e32 v4, vcc, s13, v2
	s_mov_b32 s13, 0x7a000
	s_nop 0
	v_addc_co_u32_e32 v5, vcc, 0, v3, vcc
	global_load_dword v66, v[4:5], off nt
	v_add_co_u32_e32 v4, vcc, s13, v2
	s_mov_b32 s13, 0x7c000
	s_nop 0
	v_addc_co_u32_e32 v5, vcc, 0, v3, vcc
	global_load_dword v68, v[4:5], off nt
	v_add_co_u32_e32 v4, vcc, s13, v2
	s_mov_b32 s13, 0x7e000
	s_nop 0
	v_addc_co_u32_e32 v5, vcc, 0, v3, vcc
	global_load_dword v70, v[4:5], off nt
	v_add_co_u32_e32 v4, vcc, s13, v2
	s_mov_b32 s13, 0x80000
	s_nop 0
	v_addc_co_u32_e32 v5, vcc, 0, v3, vcc
	global_load_dword v72, v[4:5], off nt
	v_add_co_u32_e32 v4, vcc, s13, v2
	s_mov_b32 s13, 0x82000
	s_nop 0
	v_addc_co_u32_e32 v5, vcc, 0, v3, vcc
	global_load_dword v67, v[4:5], off nt
	v_add_co_u32_e32 v4, vcc, s13, v2
	s_mov_b32 s13, 0x84000
	s_nop 0
	v_addc_co_u32_e32 v5, vcc, 0, v3, vcc
	global_load_dword v69, v[4:5], off nt
	v_add_co_u32_e32 v4, vcc, s13, v2
	s_mov_b32 s13, 0x86000
	s_nop 0
	v_addc_co_u32_e32 v5, vcc, 0, v3, vcc
	global_load_dword v71, v[4:5], off nt
	v_add_co_u32_e32 v4, vcc, s13, v2
	s_mov_b32 s13, 0x88000
	s_nop 0
	v_addc_co_u32_e32 v5, vcc, 0, v3, vcc
	global_load_dword v73, v[4:5], off nt
	v_add_co_u32_e32 v4, vcc, s13, v2
	s_mov_b32 s13, 0x8a000
	s_nop 0
	v_addc_co_u32_e32 v5, vcc, 0, v3, vcc
	global_load_dword v74, v[4:5], off nt
	v_add_co_u32_e32 v4, vcc, s13, v2
	s_mov_b32 s13, 0x8c000
	s_nop 0
	v_addc_co_u32_e32 v5, vcc, 0, v3, vcc
	global_load_dword v75, v[4:5], off nt
	v_add_co_u32_e32 v4, vcc, s13, v2
	s_mov_b32 s13, 0x8e000
	s_nop 0
	v_addc_co_u32_e32 v5, vcc, 0, v3, vcc
	global_load_dword v76, v[4:5], off nt
	v_add_co_u32_e32 v4, vcc, s13, v2
	s_mov_b32 s13, 0x90000
	s_nop 0
	v_addc_co_u32_e32 v5, vcc, 0, v3, vcc
	global_load_dword v77, v[4:5], off nt
	v_add_co_u32_e32 v4, vcc, s13, v2
	s_mov_b32 s13, 0x92000
	s_nop 0
	v_addc_co_u32_e32 v5, vcc, 0, v3, vcc
	global_load_dword v78, v[4:5], off nt
	v_add_co_u32_e32 v4, vcc, s13, v2
	s_mov_b32 s13, 0x94000
; template <bool PERMGL, bool FP8>
; __device__ __forceinline__ void q8_cols_item(const float* W, int N, int n0, unsigned char* Bq, float* sc_out, LAS float* AM, int par, int wave, int lane) {
;     ...
;     const float* Wp = W + (size_t)(128 * wave) * N + n;
;     float v[128]; float am = 0.f;
; #pragma unroll
;     for (int i = 0; i < 128; ++i) v[i] = Wp[(size_t)i * N];
	s_nop 0
	v_addc_co_u32_e32 v5, vcc, 0, v3, vcc
	global_load_dword v79, v[4:5], off nt
	v_add_co_u32_e32 v4, vcc, s13, v2
	s_mov_b32 s13, 0x96000
	s_nop 0
	v_addc_co_u32_e32 v5, vcc, 0, v3, vcc
	global_load_dword v80, v[4:5], off nt
	v_add_co_u32_e32 v4, vcc, s13, v2
	s_mov_b32 s13, 0x98000
	s_nop 0
	v_addc_co_u32_e32 v5, vcc, 0, v3, vcc
	global_load_dword v81, v[4:5], off nt
	v_add_co_u32_e32 v4, vcc, s13, v2
	s_mov_b32 s13, 0x9a000
	s_nop 0
	v_addc_co_u32_e32 v5, vcc, 0, v3, vcc
	global_load_dword v82, v[4:5], off nt
	v_add_co_u32_e32 v4, vcc, s13, v2
	s_mov_b32 s13, 0x9c000
	s_nop 0
	v_addc_co_u32_e32 v5, vcc, 0, v3, vcc
	global_load_dword v83, v[4:5], off nt
	v_add_co_u32_e32 v4, vcc, s13, v2
	s_mov_b32 s13, 0x9e000
	s_nop 0
	v_addc_co_u32_e32 v5, vcc, 0, v3, vcc
	global_load_dword v84, v[4:5], off nt
	v_add_co_u32_e32 v4, vcc, s13, v2
	s_mov_b32 s13, 0xa0000
	s_nop 0
	v_addc_co_u32_e32 v5, vcc, 0, v3, vcc
	global_load_dword v85, v[4:5], off nt
	v_add_co_u32_e32 v4, vcc, s13, v2
	s_mov_b32 s13, 0xa2000
	s_nop 0
	v_addc_co_u32_e32 v5, vcc, 0, v3, vcc
	global_load_dword v86, v[4:5], off nt
	v_add_co_u32_e32 v4, vcc, s13, v2
	s_mov_b32 s13, 0xa4000
	s_nop 0
	v_addc_co_u32_e32 v5, vcc, 0, v3, vcc
	global_load_dword v87, v[4:5], off nt
	v_add_co_u32_e32 v4, vcc, s13, v2
	s_mov_b32 s13, 0xa6000
	s_nop 0
	v_addc_co_u32_e32 v5, vcc, 0, v3, vcc
	global_load_dword v88, v[4:5], off nt
	v_add_co_u32_e32 v4, vcc, s13, v2
	s_mov_b32 s13, 0xa8000
	s_nop 0
	v_addc_co_u32_e32 v5, vcc, 0, v3, vcc
	global_load_dword v89, v[4:5], off nt
	v_add_co_u32_e32 v4, vcc, s13, v2
	s_mov_b32 s13, 0xaa000
	s_nop 0
	v_addc_co_u32_e32 v5, vcc, 0, v3, vcc
	global_load_dword v90, v[4:5], off nt
	v_add_co_u32_e32 v4, vcc, s13, v2
	s_mov_b32 s13, 0xac000
	s_nop 0
	v_addc_co_u32_e32 v5, vcc, 0, v3, vcc
	global_load_dword v91, v[4:5], off nt
	v_add_co_u32_e32 v4, vcc, s13, v2
	s_mov_b32 s13, 0xae000
	s_nop 0
	v_addc_co_u32_e32 v5, vcc, 0, v3, vcc
	global_load_dword v92, v[4:5], off nt
	v_add_co_u32_e32 v4, vcc, s13, v2
	s_mov_b32 s13, 0xb0000
	s_nop 0
	v_addc_co_u32_e32 v5, vcc, 0, v3, vcc
	global_load_dword v93, v[4:5], off nt
	v_add_co_u32_e32 v4, vcc, s13, v2
	s_mov_b32 s13, 0xb2000
	s_nop 0
	v_addc_co_u32_e32 v5, vcc, 0, v3, vcc
	global_load_dword v94, v[4:5], off nt
	v_add_co_u32_e32 v4, vcc, s13, v2
	s_mov_b32 s13, 0xb4000
	s_nop 0
	v_addc_co_u32_e32 v5, vcc, 0, v3, vcc
	global_load_dword v95, v[4:5], off nt
	v_add_co_u32_e32 v4, vcc, s13, v2
	s_mov_b32 s13, 0xb6000
	s_nop 0
	v_addc_co_u32_e32 v5, vcc, 0, v3, vcc
	global_load_dword v96, v[4:5], off nt
	v_add_co_u32_e32 v4, vcc, s13, v2
	s_mov_b32 s13, 0xb8000
	s_nop 0
	v_addc_co_u32_e32 v5, vcc, 0, v3, vcc
	global_load_dword v97, v[4:5], off nt
	v_add_co_u32_e32 v4, vcc, s13, v2
	s_mov_b32 s13, 0xba000
	s_nop 0
	v_addc_co_u32_e32 v5, vcc, 0, v3, vcc
	global_load_dword v98, v[4:5], off nt
	v_add_co_u32_e32 v4, vcc, s13, v2
	s_mov_b32 s13, 0xbc000
	s_nop 0
	v_addc_co_u32_e32 v5, vcc, 0, v3, vcc
	global_load_dword v100, v[4:5], off nt
	v_add_co_u32_e32 v4, vcc, s13, v2
	s_mov_b32 s13, 0xbe000
	s_nop 0
	v_addc_co_u32_e32 v5, vcc, 0, v3, vcc
	global_load_dword v102, v[4:5], off nt
	v_add_co_u32_e32 v4, vcc, s13, v2
	s_mov_b32 s13, 0xc0000
	s_nop 0
	v_addc_co_u32_e32 v5, vcc, 0, v3, vcc
	global_load_dword v104, v[4:5], off nt
	v_add_co_u32_e32 v4, vcc, s13, v2
	s_mov_b32 s13, 0xc2000
	s_nop 0
	v_addc_co_u32_e32 v5, vcc, 0, v3, vcc
	global_load_dword v99, v[4:5], off nt
	v_add_co_u32_e32 v4, vcc, s13, v2
	s_mov_b32 s13, 0xc4000
	s_nop 0
	v_addc_co_u32_e32 v5, vcc, 0, v3, vcc
	global_load_dword v101, v[4:5], off nt
	v_add_co_u32_e32 v4, vcc, s13, v2
	s_mov_b32 s13, 0xc6000
	s_nop 0
	v_addc_co_u32_e32 v5, vcc, 0, v3, vcc
	global_load_dword v103, v[4:5], off nt
	v_add_co_u32_e32 v4, vcc, s13, v2
	s_mov_b32 s13, 0xc8000
	s_nop 0
	v_addc_co_u32_e32 v5, vcc, 0, v3, vcc
	global_load_dword v105, v[4:5], off nt
	v_add_co_u32_e32 v4, vcc, s13, v2
	s_mov_b32 s13, 0xca000
	s_nop 0
	v_addc_co_u32_e32 v5, vcc, 0, v3, vcc
	global_load_dword v106, v[4:5], off nt
	v_add_co_u32_e32 v4, vcc, s13, v2
	s_mov_b32 s13, 0xcc000
	s_nop 0
	v_addc_co_u32_e32 v5, vcc, 0, v3, vcc
	global_load_dword v107, v[4:5], off nt
	v_add_co_u32_e32 v4, vcc, s13, v2
	s_mov_b32 s13, 0xce000
	s_nop 0
	v_addc_co_u32_e32 v5, vcc, 0, v3, vcc
	global_load_dword v108, v[4:5], off nt
	v_add_co_u32_e32 v4, vcc, s13, v2
	s_mov_b32 s13, 0xd0000
	s_nop 0
	v_addc_co_u32_e32 v5, vcc, 0, v3, vcc
	global_load_dword v109, v[4:5], off nt
	v_add_co_u32_e32 v4, vcc, s13, v2
	s_mov_b32 s13, 0xd2000
	s_nop 0
	v_addc_co_u32_e32 v5, vcc, 0, v3, vcc
	global_load_dword v110, v[4:5], off nt
	v_add_co_u32_e32 v4, vcc, s13, v2
	s_mov_b32 s13, 0xd4000
	s_nop 0
	v_addc_co_u32_e32 v5, vcc, 0, v3, vcc
	global_load_dword v111, v[4:5], off nt
	v_add_co_u32_e32 v4, vcc, s13, v2
	s_mov_b32 s13, 0xd6000
	s_nop 0
	v_addc_co_u32_e32 v5, vcc, 0, v3, vcc
	global_load_dword v112, v[4:5], off nt
	v_add_co_u32_e32 v4, vcc, s13, v2
	s_mov_b32 s13, 0xd8000
	s_nop 0
	v_addc_co_u32_e32 v5, vcc, 0, v3, vcc
	global_load_dword v113, v[4:5], off nt
	v_add_co_u32_e32 v4, vcc, s13, v2
	s_mov_b32 s13, 0xda000
	s_nop 0
	v_addc_co_u32_e32 v5, vcc, 0, v3, vcc
	global_load_dword v114, v[4:5], off nt
	v_add_co_u32_e32 v4, vcc, s13, v2
	s_mov_b32 s13, 0xdc000
	s_nop 0
	v_addc_co_u32_e32 v5, vcc, 0, v3, vcc
	global_load_dword v115, v[4:5], off nt
	v_add_co_u32_e32 v4, vcc, s13, v2
	s_mov_b32 s13, 0xde000
	s_nop 0
	v_addc_co_u32_e32 v5, vcc, 0, v3, vcc
	global_load_dword v116, v[4:5], off nt
	v_add_co_u32_e32 v4, vcc, s13, v2
	s_mov_b32 s13, 0xe0000
	s_nop 0
	v_addc_co_u32_e32 v5, vcc, 0, v3, vcc
	global_load_dword v117, v[4:5], off nt
; template <bool PERMGL, bool FP8>
; __device__ __forceinline__ void q8_cols_item(const float* W, int N, int n0, unsigned char* Bq, float* sc_out, LAS float* AM, int par, int wave, int lane) {
;     ...
;     for (int i = 0; i < 128; ++i) v[i] = Wp[(size_t)i * N];
;     __builtin_amdgcn_sched_barrier(0);
; #pragma unroll
;     for (int i = 0; i < 128; ++i) am = fmaxf(am, fabsf(v[i]));
;     AM[(par * 8 + wave) * 64 + lane] = am;
;     __syncthreads();
	v_add_co_u32_e32 v4, vcc, s13, v2
	s_mov_b32 s13, 0xe2000
	s_nop 0
	v_addc_co_u32_e32 v5, vcc, 0, v3, vcc
	global_load_dword v118, v[4:5], off nt
	v_add_co_u32_e32 v4, vcc, s13, v2
	s_mov_b32 s13, 0xe4000
	s_nop 0
	v_addc_co_u32_e32 v5, vcc, 0, v3, vcc
	global_load_dword v119, v[4:5], off nt
	v_add_co_u32_e32 v4, vcc, s13, v2
	s_mov_b32 s13, 0xe6000
	s_nop 0
	v_addc_co_u32_e32 v5, vcc, 0, v3, vcc
	global_load_dword v120, v[4:5], off nt
	v_add_co_u32_e32 v4, vcc, s13, v2
	s_mov_b32 s13, 0xe8000
	s_nop 0
	v_addc_co_u32_e32 v5, vcc, 0, v3, vcc
	global_load_dword v121, v[4:5], off nt
	v_add_co_u32_e32 v4, vcc, s13, v2
	s_mov_b32 s13, 0xea000
	s_nop 0
	v_addc_co_u32_e32 v5, vcc, 0, v3, vcc
	global_load_dword v130, v[4:5], off nt
	v_add_co_u32_e32 v4, vcc, s13, v2
	s_mov_b32 s13, 0xec000
	s_nop 0
	v_addc_co_u32_e32 v5, vcc, 0, v3, vcc
	global_load_dword v131, v[4:5], off nt
	v_add_co_u32_e32 v4, vcc, s13, v2
	s_mov_b32 s13, 0xee000
	s_nop 0
	v_addc_co_u32_e32 v5, vcc, 0, v3, vcc
	global_load_dword v132, v[4:5], off nt
	v_add_co_u32_e32 v4, vcc, s13, v2
	s_mov_b32 s13, 0xf0000
	s_nop 0
	v_addc_co_u32_e32 v5, vcc, 0, v3, vcc
	global_load_dword v133, v[4:5], off nt
	v_add_co_u32_e32 v4, vcc, s13, v2
	s_mov_b32 s13, 0xf2000
	s_nop 0
	v_addc_co_u32_e32 v5, vcc, 0, v3, vcc
	global_load_dword v134, v[4:5], off nt
	v_add_co_u32_e32 v4, vcc, s13, v2
	s_mov_b32 s13, 0xf4000
	s_nop 0
	v_addc_co_u32_e32 v5, vcc, 0, v3, vcc
	global_load_dword v135, v[4:5], off nt
	v_add_co_u32_e32 v4, vcc, s13, v2
	s_mov_b32 s13, 0xf6000
	s_nop 0
	v_addc_co_u32_e32 v5, vcc, 0, v3, vcc
	global_load_dword v136, v[4:5], off nt
	v_add_co_u32_e32 v4, vcc, s13, v2
	s_mov_b32 s13, 0xf8000
	s_nop 0
	v_addc_co_u32_e32 v5, vcc, 0, v3, vcc
	global_load_dword v137, v[4:5], off nt
	v_add_co_u32_e32 v4, vcc, s13, v2
	s_mov_b32 s13, 0xfa000
	s_nop 0
	v_addc_co_u32_e32 v5, vcc, 0, v3, vcc
	global_load_dword v138, v[4:5], off nt
	v_add_co_u32_e32 v4, vcc, s13, v2
	s_mov_b32 s13, 0xfc000
	s_nop 0
	v_addc_co_u32_e32 v5, vcc, 0, v3, vcc
	global_load_dword v139, v[4:5], off nt
	v_add_co_u32_e32 v4, vcc, s13, v2
	s_mov_b32 s13, 0xfe000
	s_nop 0
	v_addc_co_u32_e32 v5, vcc, 0, v3, vcc
	v_add_co_u32_e32 v2, vcc, s13, v2
	global_load_dword v140, v[4:5], off nt
	s_nop 0
	v_addc_co_u32_e32 v3, vcc, 0, v3, vcc
	global_load_dword v142, v[2:3], off nt
	s_waitcnt vmcnt(0)
	v_max3_f32 v2, |v1|, 0, |v6|
	v_max3_f32 v2, v2, |v7|, |v8|
	v_max3_f32 v2, v2, |v9|, |v10|
	v_max3_f32 v2, v2, |v11|, |v12|
	v_max3_f32 v2, v2, |v13|, |v14|
	v_max3_f32 v2, v2, |v15|, |v16|
	v_max3_f32 v2, v2, |v17|, |v18|
	v_max3_f32 v2, v2, |v19|, |v20|
	v_max3_f32 v2, v2, |v21|, |v22|
	v_max3_f32 v2, v2, |v23|, |v24|
	v_max3_f32 v2, v2, |v25|, |v26|
	v_max3_f32 v2, v2, |v27|, |v28|
	v_max3_f32 v2, v2, |v29|, |v30|
	v_max3_f32 v2, v2, |v31|, |v32|
	v_max3_f32 v2, v2, |v34|, |v36|
	v_max3_f32 v2, v2, |v38|, |v40|
	v_max3_f32 v2, v2, |v35|, |v37|
	v_max3_f32 v2, v2, |v39|, |v41|
	v_max3_f32 v2, v2, |v42|, |v43|
	v_max3_f32 v2, v2, |v44|, |v45|
	v_max3_f32 v2, v2, |v46|, |v47|
	v_max3_f32 v2, v2, |v48|, |v49|
	v_max3_f32 v2, v2, |v50|, |v51|
	v_max3_f32 v2, v2, |v52|, |v53|
	v_max3_f32 v2, v2, |v54|, |v55|
	v_max3_f32 v2, v2, |v56|, |v57|
	v_max3_f32 v2, v2, |v58|, |v59|
	v_max3_f32 v2, v2, |v60|, |v61|
	v_max3_f32 v2, v2, |v62|, |v63|
	v_max3_f32 v2, v2, |v64|, |v65|
	v_max3_f32 v2, v2, |v66|, |v68|
	v_max3_f32 v2, v2, |v70|, |v72|
	v_max3_f32 v2, v2, |v67|, |v69|
	v_max3_f32 v2, v2, |v71|, |v73|
	v_max3_f32 v2, v2, |v74|, |v75|
	v_max3_f32 v2, v2, |v76|, |v77|
	v_max3_f32 v2, v2, |v78|, |v79|
	v_max3_f32 v2, v2, |v80|, |v81|
	v_max3_f32 v2, v2, |v82|, |v83|
	v_max3_f32 v2, v2, |v84|, |v85|
	v_max3_f32 v2, v2, |v86|, |v87|
	v_max3_f32 v2, v2, |v88|, |v89|
	v_max3_f32 v2, v2, |v90|, |v91|
	v_max3_f32 v2, v2, |v92|, |v93|
	v_max3_f32 v2, v2, |v94|, |v95|
	v_max3_f32 v2, v2, |v96|, |v97|
	v_max3_f32 v2, v2, |v98|, |v100|
	v_max3_f32 v2, v2, |v102|, |v104|
	v_max3_f32 v2, v2, |v99|, |v101|
	v_max3_f32 v2, v2, |v103|, |v105|
	v_max3_f32 v2, v2, |v106|, |v107|
	v_max3_f32 v2, v2, |v108|, |v109|
	v_max3_f32 v2, v2, |v110|, |v111|
	v_max3_f32 v2, v2, |v112|, |v113|
	v_max3_f32 v2, v2, |v114|, |v115|
	v_max3_f32 v2, v2, |v116|, |v117|
	v_max3_f32 v2, v2, |v118|, |v119|
	v_max3_f32 v2, v2, |v120|, |v121|
	v_max3_f32 v2, v2, |v130|, |v131|
	v_max3_f32 v2, v2, |v132|, |v133|
	v_max3_f32 v2, v2, |v134|, |v135|
	v_max3_f32 v2, v2, |v136|, |v137|
	v_max3_f32 v2, v2, |v138|, |v139|
	s_lshl_b32 s13, s21, 11
	v_max3_f32 v4, v2, |v140|, |v142|
	v_add_u32_e32 v2, s13, v150
	v_add_u32_e32 v5, s13, v151
	ds_write_b32 v2, v4
	s_waitcnt lgkmcnt(0)
	s_barrier
; template <bool PERMGL, bool FP8>
; __device__ __forceinline__ void q8_cols_item(const float* W, int N, int n0, unsigned char* Bq, float* sc_out, LAS float* AM, int par, int wave, int lane) {
;     ...
;     for (int w = 0; w < 8; ++w) am = fmaxf(am, AM[(par * 8 + w) * 64 + lane]);
;     const float sc = am > 0.f ? am * (FP8 ? (1.0f / 256.0f) : (1.0f / 127.0f)) : 1.0f, inv = 1.0f / sc;
;     int row = n;
;     if (PERMGL) { const int j = n >> 1, pr = n & 1, o = j & 127; row = ((j >> 7) << 8) + (((o >> 2) & 1) << 7) + ((o >> 5) << 5) + (pr << 4) + (((o >> 3) & 3) << 2) + (o & 3); }
;     if (!PERMGL) { const int o = n & 255; row = ((n >> 8) << 8) + (((o >> 3) & 1) << 7) + ((o >> 6) << 5) + (((o >> 4) & 3) << 3) + (o & 7); }
;     auto xq = [](unsigned x) { return (unsigned)__builtin_amdgcn_update_dpp(0, (int)x, 0xB1, 0xf, 0xf, true); };
;     const bool odd = lane & 1;
;     const int rowp = (int)xq((unsigned)row);
;     unsigned char* plo = Bq + (size_t)(odd ? rowp : row) * 1024 + 128 * wave + (odd ? 16 : 0);
;     unsigned char* phi = Bq + (size_t)(odd ? row : rowp) * 1024 + 128 * wave + (odd ? 16 : 0);
;     auto packc = [&](int c) { u32x4 o;
;         if (FP8) { o.x = f8x4(v[16 * c], v[16 * c + 1], v[16 * c + 2], v[16 * c + 3], inv); o.y = f8x4(v[16 * c + 4], v[16 * c + 5], v[16 * c + 6], v[16 * c + 7], inv);
;                    o.z = f8x4(v[16 * c + 8], v[16 * c + 9], v[16 * c + 10], v[16 * c + 11], inv); o.w = f8x4(v[16 * c + 12], v[16 * c + 13], v[16 * c + 14], v[16 * c + 15], inv); }
;         else { o.x = q8x4(v[16 * c], v[16 * c + 1], v[16 * c + 2], v[16 * c + 3], inv); o.y = q8x4(v[16 * c + 4], v[16 * c + 5], v[16 * c + 6], v[16 * c + 7], inv);
;                o.z = q8x4(v[16 * c + 8], v[16 * c + 9], v[16 * c + 10], v[16 * c + 11], inv); o.w = q8x4(v[16 * c + 12], v[16 * c + 13], v[16 * c + 14], v[16 * c + 15], inv); }
;         return o; };
; #pragma unroll
;     for (int j = 0; j < 4; ++j) { const u32x4 p0 = packc(2 * j), p1 = packc(2 * j + 1);
;         u32x4 snd, rcv;
; #pragma unroll
;         for (int q = 0; q < 4; ++q) { snd[q] = odd ? p0[q] : p1[q]; rcv[q] = xq(snd[q]); }
;         u32x4 a, b;
; #pragma unroll
;         for (int q = 0; q < 4; ++q) { a[q] = odd ? rcv[q] : p0[q]; b[q] = odd ? p1[q] : rcv[q]; }
;         *(u32x4*)(plo + 32 * j) = a; *(u32x4*)(phi + 32 * j) = b; }
	ds_read2st64_b32 v[2:3], v5 offset1:1
	s_movk_i32 s13, 0xff00
	s_waitcnt lgkmcnt(0)
	v_max3_f32 v4, v4, v2, v3
	ds_read2st64_b32 v[2:3], v5 offset0:2 offset1:3
	s_waitcnt lgkmcnt(0)
	v_max3_f32 v4, v4, v2, v3
	ds_read2st64_b32 v[2:3], v5 offset0:4 offset1:5
	s_waitcnt lgkmcnt(0)
	v_max3_f32 v4, v4, v2, v3
	ds_read2st64_b32 v[2:3], v5 offset0:6 offset1:7
	s_waitcnt lgkmcnt(0)
	v_max3_f32 v2, v4, v2, v3
	v_cmp_lt_f32_e32 vcc, 0, v2
	v_mul_f32_e32 v2, 0x3c010204, v2
	s_nop 0
	v_cndmask_b32_e32 v141, 1.0, v2, vcc
	v_div_scale_f32 v2, s[14:15], v141, v141, 1.0
	v_rcp_f32_e32 v3, v2
	s_nop 0
	v_fma_f32 v4, -v2, v3, 1.0
	v_fmac_f32_e32 v3, v4, v3
	v_div_scale_f32 v4, vcc, 1.0, v141, 1.0
	v_mul_f32_e32 v5, v4, v3
	v_fma_f32 v143, -v2, v5, v4
	v_fmac_f32_e32 v5, v143, v3
	v_fma_f32 v2, -v2, v5, v4
	v_div_fmas_f32 v2, v2, v3, v5
	v_div_fixup_f32 v143, v2, v141, 1.0
	v_fmaak_f32 v1, v1, v143, 0x4b400000
	v_fmaak_f32 v6, v6, v143, 0x4b400000
	v_fmaak_f32 v7, v7, v143, 0x4b400000
	v_fmaak_f32 v8, v8, v143, 0x4b400000
	v_perm_b32 v7, v8, v7, s61
	v_perm_b32 v1, v6, v1, s61
	v_perm_b32 v1, v7, v1, s79
	v_fmaak_f32 v6, v9, v143, 0x4b400000
	v_fmaak_f32 v7, v10, v143, 0x4b400000
	v_fmaak_f32 v8, v11, v143, 0x4b400000
	v_fmaak_f32 v9, v12, v143, 0x4b400000
	v_perm_b32 v8, v9, v8, s61
	v_perm_b32 v6, v7, v6, s61
	v_perm_b32 v7, v8, v6, s79
	v_fmaak_f32 v6, v13, v143, 0x4b400000
	v_fmaak_f32 v8, v14, v143, 0x4b400000
	v_fmaak_f32 v9, v15, v143, 0x4b400000
	v_fmaak_f32 v10, v16, v143, 0x4b400000
	v_perm_b32 v9, v10, v9, s61
	v_perm_b32 v6, v8, v6, s61
	v_perm_b32 v8, v9, v6, s79
	v_fmaak_f32 v6, v17, v143, 0x4b400000
	v_fmaak_f32 v9, v18, v143, 0x4b400000
	v_fmaak_f32 v10, v19, v143, 0x4b400000
	v_fmaak_f32 v11, v20, v143, 0x4b400000
	v_perm_b32 v10, v11, v10, s61
	v_perm_b32 v6, v9, v6, s61
	v_perm_b32 v9, v10, v6, s79
	v_fmaak_f32 v6, v21, v143, 0x4b400000
	v_fmaak_f32 v10, v22, v143, 0x4b400000
	v_fmaak_f32 v11, v23, v143, 0x4b400000
	v_fmaak_f32 v12, v24, v143, 0x4b400000
	v_perm_b32 v11, v12, v11, s61
	v_perm_b32 v6, v10, v6, s61
	v_perm_b32 v10, v11, v6, s79
	v_fmaak_f32 v6, v25, v143, 0x4b400000
	v_fmaak_f32 v11, v26, v143, 0x4b400000
	v_fmaak_f32 v12, v27, v143, 0x4b400000
	v_fmaak_f32 v13, v28, v143, 0x4b400000
	v_lshrrev_b32_e32 v2, 1, v0
	v_lshlrev_b32_e32 v3, 4, v0
	v_perm_b32 v12, v13, v12, s61
	v_perm_b32 v6, v11, v6, s61
	v_and_b32_e32 v4, 0x80, v3
	v_and_b32_e32 v2, 0x60, v2
	v_bfe_u32 v5, v0, 1, 2
	v_and_or_b32 v0, v0, s13, v153
	v_perm_b32 v11, v12, v6, s79
	v_fmaak_f32 v6, v29, v143, 0x4b400000
	v_fmaak_f32 v12, v30, v143, 0x4b400000
	v_fmaak_f32 v13, v31, v143, 0x4b400000
	v_fmaak_f32 v14, v32, v143, 0x4b400000
	v_and_b32_e32 v3, 16, v3
	v_or3_b32 v0, v0, v4, v2
	v_perm_b32 v13, v14, v13, s61
	v_perm_b32 v6, v12, v6, s61
	v_or3_b32 v0, v0, v3, v5
	v_perm_b32 v12, v13, v6, s79
	v_fmaak_f32 v6, v34, v143, 0x4b400000
	v_fmaak_f32 v13, v36, v143, 0x4b400000
	v_fmaak_f32 v14, v38, v143, 0x4b400000
	v_fmaak_f32 v15, v40, v143, 0x4b400000
	v_mov_b32_dpp v4, v0 quad_perm:[1,0,3,2] row_mask:0xf bank_mask:0xf bound_ctrl:1
	v_perm_b32 v14, v15, v14, s61
	v_perm_b32 v6, v13, v6, s61
	v_cndmask_b32_e64 v2, v4, v0, s[2:3]
	v_perm_b32 v13, v14, v6, s79
	v_cndmask_b32_e64 v6, v1, v10, s[2:3]
	v_ashrrev_i32_e32 v3, 31, v2
	v_cndmask_b32_e64 v4, v0, v4, s[2:3]
	v_mov_b32_dpp v14, v6 quad_perm:[1,0,3,2] row_mask:0xf bank_mask:0xf bound_ctrl:1
	v_cndmask_b32_e64 v6, v7, v11, s[2:3]
	v_lshlrev_b64 v[2:3], 10, v[2:3]
	v_ashrrev_i32_e32 v5, 31, v4
	v_mov_b32_dpp v15, v6 quad_perm:[1,0,3,2] row_mask:0xf bank_mask:0xf bound_ctrl:1
	v_cndmask_b32_e64 v6, v8, v12, s[2:3]
	v_lshl_add_u64 v[2:3], s[10:11], 0, v[2:3]
	v_lshlrev_b64 v[4:5], 10, v[4:5]
	v_mov_b32_dpp v16, v6 quad_perm:[1,0,3,2] row_mask:0xf bank_mask:0xf bound_ctrl:1
	v_cndmask_b32_e64 v6, v9, v13, s[2:3]
	v_lshl_add_u64 v[2:3], v[2:3], 0, s[42:43]
	v_lshl_add_u64 v[4:5], s[10:11], 0, v[4:5]
	v_mov_b32_dpp v17, v6 quad_perm:[1,0,3,2] row_mask:0xf bank_mask:0xf bound_ctrl:1
	v_lshl_add_u64 v[2:3], v[2:3], 0, v[122:123]
	v_lshl_add_u64 v[4:5], v[4:5], 0, s[42:43]
	v_cndmask_b32_e64 v6, v14, v1, s[2:3]
	v_cndmask_b32_e64 v7, v15, v7, s[2:3]
	v_cndmask_b32_e64 v8, v16, v8, s[2:3]
	v_cndmask_b32_e64 v9, v17, v9, s[2:3]
	v_lshl_add_u64 v[4:5], v[4:5], 0, v[122:123]
	v_cndmask_b32_e64 v10, v10, v14, s[2:3]
	v_cndmask_b32_e64 v11, v11, v15, s[2:3]
	v_cndmask_b32_e64 v12, v12, v16, s[2:3]
	v_cndmask_b32_e64 v13, v13, v17, s[2:3]
	global_store_dwordx4 v[2:3], v[6:9], off
	global_store_dwordx4 v[4:5], v[10:13], off
	v_fmaak_f32 v1, v35, v143, 0x4b400000
	v_fmaak_f32 v6, v37, v143, 0x4b400000
	v_fmaak_f32 v7, v39, v143, 0x4b400000
	v_fmaak_f32 v8, v41, v143, 0x4b400000
	v_perm_b32 v7, v8, v7, s61
	v_perm_b32 v1, v6, v1, s61
	v_perm_b32 v1, v7, v1, s79
	v_fmaak_f32 v6, v42, v143, 0x4b400000
	v_fmaak_f32 v7, v43, v143, 0x4b400000
	v_fmaak_f32 v8, v44, v143, 0x4b400000
	v_fmaak_f32 v9, v45, v143, 0x4b400000
	v_perm_b32 v8, v9, v8, s61
	v_perm_b32 v6, v7, v6, s61
	v_perm_b32 v7, v8, v6, s79
	v_fmaak_f32 v6, v46, v143, 0x4b400000
	v_fmaak_f32 v8, v47, v143, 0x4b400000
	v_fmaak_f32 v9, v48, v143, 0x4b400000
	v_fmaak_f32 v10, v49, v143, 0x4b400000
	v_perm_b32 v9, v10, v9, s61
	v_perm_b32 v6, v8, v6, s61
	v_perm_b32 v8, v9, v6, s79
	v_fmaak_f32 v6, v50, v143, 0x4b400000
	v_fmaak_f32 v9, v51, v143, 0x4b400000
	v_fmaak_f32 v10, v52, v143, 0x4b400000
	v_fmaak_f32 v11, v53, v143, 0x4b400000
	v_perm_b32 v10, v11, v10, s61
	v_perm_b32 v6, v9, v6, s61
	v_perm_b32 v9, v10, v6, s79
	v_fmaak_f32 v6, v54, v143, 0x4b400000
	v_fmaak_f32 v10, v55, v143, 0x4b400000
	v_fmaak_f32 v11, v56, v143, 0x4b400000
	v_fmaak_f32 v12, v57, v143, 0x4b400000
; template <bool PERMGL, bool FP8>
; __device__ __forceinline__ void q8_cols_item(const float* W, int N, int n0, unsigned char* Bq, float* sc_out, LAS float* AM, int par, int wave, int lane) {
;     ...
;     auto packc = [&](int c) { u32x4 o;
;         if (FP8) { o.x = f8x4(v[16 * c], v[16 * c + 1], v[16 * c + 2], v[16 * c + 3], inv); o.y = f8x4(v[16 * c + 4], v[16 * c + 5], v[16 * c + 6], v[16 * c + 7], inv);
;                    o.z = f8x4(v[16 * c + 8], v[16 * c + 9], v[16 * c + 10], v[16 * c + 11], inv); o.w = f8x4(v[16 * c + 12], v[16 * c + 13], v[16 * c + 14], v[16 * c + 15], inv); }
;         else { o.x = q8x4(v[16 * c], v[16 * c + 1], v[16 * c + 2], v[16 * c + 3], inv); o.y = q8x4(v[16 * c + 4], v[16 * c + 5], v[16 * c + 6], v[16 * c + 7], inv);
;                o.z = q8x4(v[16 * c + 8], v[16 * c + 9], v[16 * c + 10], v[16 * c + 11], inv); o.w = q8x4(v[16 * c + 12], v[16 * c + 13], v[16 * c + 14], v[16 * c + 15], inv); }
;         return o; };
; #pragma unroll
;     for (int j = 0; j < 4; ++j) { const u32x4 p0 = packc(2 * j), p1 = packc(2 * j + 1);
;         u32x4 snd, rcv;
; #pragma unroll
;         for (int q = 0; q < 4; ++q) { snd[q] = odd ? p0[q] : p1[q]; rcv[q] = xq(snd[q]); }
;         u32x4 a, b;
; #pragma unroll
;         for (int q = 0; q < 4; ++q) { a[q] = odd ? rcv[q] : p0[q]; b[q] = odd ? p1[q] : rcv[q]; }
;         *(u32x4*)(plo + 32 * j) = a; *(u32x4*)(phi + 32 * j) = b; }
	v_perm_b32 v11, v12, v11, s61
	v_perm_b32 v6, v10, v6, s61
	v_perm_b32 v10, v11, v6, s79
	v_fmaak_f32 v6, v58, v143, 0x4b400000
	v_fmaak_f32 v11, v59, v143, 0x4b400000
	v_fmaak_f32 v12, v60, v143, 0x4b400000
	v_fmaak_f32 v13, v61, v143, 0x4b400000
	v_perm_b32 v12, v13, v12, s61
	v_perm_b32 v6, v11, v6, s61
	v_perm_b32 v11, v12, v6, s79
	v_fmaak_f32 v6, v62, v143, 0x4b400000
	v_fmaak_f32 v12, v63, v143, 0x4b400000
	v_fmaak_f32 v13, v64, v143, 0x4b400000
	v_fmaak_f32 v14, v65, v143, 0x4b400000
	v_perm_b32 v13, v14, v13, s61
	v_perm_b32 v6, v12, v6, s61
	v_perm_b32 v12, v13, v6, s79
	v_fmaak_f32 v6, v66, v143, 0x4b400000
	v_fmaak_f32 v13, v68, v143, 0x4b400000
	v_fmaak_f32 v14, v70, v143, 0x4b400000
	v_fmaak_f32 v15, v72, v143, 0x4b400000
	v_perm_b32 v14, v15, v14, s61
	v_perm_b32 v6, v13, v6, s61
	v_perm_b32 v13, v14, v6, s79
	v_cndmask_b32_e64 v6, v1, v10, s[2:3]
	s_and_b64 vcc, exec, s[0:1]
	s_nop 0
	v_mov_b32_dpp v14, v6 quad_perm:[1,0,3,2] row_mask:0xf bank_mask:0xf bound_ctrl:1
	v_cndmask_b32_e64 v6, v7, v11, s[2:3]
	v_cndmask_b32_e64 v10, v10, v14, s[2:3]
	s_nop 0
	v_mov_b32_dpp v15, v6 quad_perm:[1,0,3,2] row_mask:0xf bank_mask:0xf bound_ctrl:1
	v_cndmask_b32_e64 v6, v8, v12, s[2:3]
	v_cndmask_b32_e64 v7, v15, v7, s[2:3]
	v_cndmask_b32_e64 v11, v11, v15, s[2:3]
	v_mov_b32_dpp v16, v6 quad_perm:[1,0,3,2] row_mask:0xf bank_mask:0xf bound_ctrl:1
	v_cndmask_b32_e64 v6, v9, v13, s[2:3]
	v_cndmask_b32_e64 v8, v16, v8, s[2:3]
	v_cndmask_b32_e64 v12, v12, v16, s[2:3]
	v_mov_b32_dpp v17, v6 quad_perm:[1,0,3,2] row_mask:0xf bank_mask:0xf bound_ctrl:1
	v_cndmask_b32_e64 v6, v14, v1, s[2:3]
	v_cndmask_b32_e64 v9, v17, v9, s[2:3]
	v_cndmask_b32_e64 v13, v13, v17, s[2:3]
	global_store_dwordx4 v[2:3], v[6:9], off offset:32
	global_store_dwordx4 v[4:5], v[10:13], off offset:32
	v_fmaak_f32 v1, v67, v143, 0x4b400000
	v_fmaak_f32 v6, v69, v143, 0x4b400000
	v_fmaak_f32 v7, v71, v143, 0x4b400000
	v_fmaak_f32 v8, v73, v143, 0x4b400000
	v_perm_b32 v7, v8, v7, s61
	v_perm_b32 v1, v6, v1, s61
	v_perm_b32 v1, v7, v1, s79
	v_fmaak_f32 v6, v74, v143, 0x4b400000
	v_fmaak_f32 v7, v75, v143, 0x4b400000
	v_fmaak_f32 v8, v76, v143, 0x4b400000
	v_fmaak_f32 v9, v77, v143, 0x4b400000
	v_perm_b32 v8, v9, v8, s61
	v_perm_b32 v6, v7, v6, s61
	v_perm_b32 v7, v8, v6, s79
	v_fmaak_f32 v6, v78, v143, 0x4b400000
	v_fmaak_f32 v8, v79, v143, 0x4b400000
	v_fmaak_f32 v9, v80, v143, 0x4b400000
	v_fmaak_f32 v10, v81, v143, 0x4b400000
	v_perm_b32 v9, v10, v9, s61
	v_perm_b32 v6, v8, v6, s61
	v_perm_b32 v8, v9, v6, s79
	v_fmaak_f32 v6, v82, v143, 0x4b400000
	v_fmaak_f32 v9, v83, v143, 0x4b400000
	v_fmaak_f32 v10, v84, v143, 0x4b400000
	v_fmaak_f32 v11, v85, v143, 0x4b400000
	v_perm_b32 v10, v11, v10, s61
	v_perm_b32 v6, v9, v6, s61
	v_perm_b32 v9, v10, v6, s79
	v_fmaak_f32 v6, v86, v143, 0x4b400000
	v_fmaak_f32 v10, v87, v143, 0x4b400000
	v_fmaak_f32 v11, v88, v143, 0x4b400000
	v_fmaak_f32 v12, v89, v143, 0x4b400000
	v_perm_b32 v11, v12, v11, s61
	v_perm_b32 v6, v10, v6, s61
	v_perm_b32 v10, v11, v6, s79
	v_fmaak_f32 v6, v90, v143, 0x4b400000
	v_fmaak_f32 v11, v91, v143, 0x4b400000
	v_fmaak_f32 v12, v92, v143, 0x4b400000
	v_fmaak_f32 v13, v93, v143, 0x4b400000
	v_perm_b32 v12, v13, v12, s61
	v_perm_b32 v6, v11, v6, s61
	v_perm_b32 v11, v12, v6, s79
	v_fmaak_f32 v6, v94, v143, 0x4b400000
	v_fmaak_f32 v12, v95, v143, 0x4b400000
	v_fmaak_f32 v13, v96, v143, 0x4b400000
	v_fmaak_f32 v14, v97, v143, 0x4b400000
	v_perm_b32 v13, v14, v13, s61
	v_perm_b32 v6, v12, v6, s61
	v_perm_b32 v12, v13, v6, s79
	v_fmaak_f32 v6, v98, v143, 0x4b400000
	v_fmaak_f32 v13, v100, v143, 0x4b400000
	v_fmaak_f32 v14, v102, v143, 0x4b400000
	v_fmaak_f32 v15, v104, v143, 0x4b400000
	v_perm_b32 v14, v15, v14, s61
	v_perm_b32 v6, v13, v6, s61
	v_perm_b32 v13, v14, v6, s79
	v_cndmask_b32_e64 v6, v1, v10, s[2:3]
	s_nop 1
	v_mov_b32_dpp v14, v6 quad_perm:[1,0,3,2] row_mask:0xf bank_mask:0xf bound_ctrl:1
	v_cndmask_b32_e64 v6, v7, v11, s[2:3]
	v_cndmask_b32_e64 v10, v10, v14, s[2:3]
; template <bool PERMGL, bool FP8>
; __device__ __forceinline__ void q8_cols_item(const float* W, int N, int n0, unsigned char* Bq, float* sc_out, LAS float* AM, int par, int wave, int lane) {
;     ...
;     auto packc = [&](int c) { u32x4 o;
;         if (FP8) { o.x = f8x4(v[16 * c], v[16 * c + 1], v[16 * c + 2], v[16 * c + 3], inv); o.y = f8x4(v[16 * c + 4], v[16 * c + 5], v[16 * c + 6], v[16 * c + 7], inv);
;                    o.z = f8x4(v[16 * c + 8], v[16 * c + 9], v[16 * c + 10], v[16 * c + 11], inv); o.w = f8x4(v[16 * c + 12], v[16 * c + 13], v[16 * c + 14], v[16 * c + 15], inv); }
;         else { o.x = q8x4(v[16 * c], v[16 * c + 1], v[16 * c + 2], v[16 * c + 3], inv); o.y = q8x4(v[16 * c + 4], v[16 * c + 5], v[16 * c + 6], v[16 * c + 7], inv);
;                o.z = q8x4(v[16 * c + 8], v[16 * c + 9], v[16 * c + 10], v[16 * c + 11], inv); o.w = q8x4(v[16 * c + 12], v[16 * c + 13], v[16 * c + 14], v[16 * c + 15], inv); }
;         return o; };
; #pragma unroll
;     for (int j = 0; j < 4; ++j) { const u32x4 p0 = packc(2 * j), p1 = packc(2 * j + 1);
;         u32x4 snd, rcv;
; #pragma unroll
;         for (int q = 0; q < 4; ++q) { snd[q] = odd ? p0[q] : p1[q]; rcv[q] = xq(snd[q]); }
;         u32x4 a, b;
; #pragma unroll
;         for (int q = 0; q < 4; ++q) { a[q] = odd ? rcv[q] : p0[q]; b[q] = odd ? p1[q] : rcv[q]; }
;         *(u32x4*)(plo + 32 * j) = a; *(u32x4*)(phi + 32 * j) = b; }
;     if (wave == 0) sc_out[PERMGL ? row : n] = FP8 ? sc * 16.0f : sc;
	s_nop 0
	v_mov_b32_dpp v15, v6 quad_perm:[1,0,3,2] row_mask:0xf bank_mask:0xf bound_ctrl:1
	v_cndmask_b32_e64 v6, v8, v12, s[2:3]
	v_cndmask_b32_e64 v7, v15, v7, s[2:3]
	v_cndmask_b32_e64 v11, v11, v15, s[2:3]
	v_mov_b32_dpp v16, v6 quad_perm:[1,0,3,2] row_mask:0xf bank_mask:0xf bound_ctrl:1
	v_cndmask_b32_e64 v6, v9, v13, s[2:3]
	v_cndmask_b32_e64 v8, v16, v8, s[2:3]
	v_cndmask_b32_e64 v12, v12, v16, s[2:3]
	v_mov_b32_dpp v17, v6 quad_perm:[1,0,3,2] row_mask:0xf bank_mask:0xf bound_ctrl:1
	v_cndmask_b32_e64 v6, v14, v1, s[2:3]
	v_cndmask_b32_e64 v9, v17, v9, s[2:3]
	v_cndmask_b32_e64 v13, v13, v17, s[2:3]
	global_store_dwordx4 v[2:3], v[6:9], off offset:64
	global_store_dwordx4 v[4:5], v[10:13], off offset:64
	v_fmaak_f32 v1, v99, v143, 0x4b400000
	v_fmaak_f32 v6, v101, v143, 0x4b400000
	v_fmaak_f32 v7, v103, v143, 0x4b400000
	v_fmaak_f32 v8, v105, v143, 0x4b400000
	v_perm_b32 v7, v8, v7, s61
	v_perm_b32 v1, v6, v1, s61
	v_perm_b32 v1, v7, v1, s79
	v_fmaak_f32 v6, v106, v143, 0x4b400000
	v_fmaak_f32 v7, v107, v143, 0x4b400000
	v_fmaak_f32 v8, v108, v143, 0x4b400000
	v_fmaak_f32 v9, v109, v143, 0x4b400000
	v_perm_b32 v8, v9, v8, s61
	v_perm_b32 v6, v7, v6, s61
	v_perm_b32 v7, v8, v6, s79
	v_fmaak_f32 v6, v110, v143, 0x4b400000
	v_fmaak_f32 v8, v111, v143, 0x4b400000
	v_fmaak_f32 v9, v112, v143, 0x4b400000
	v_fmaak_f32 v10, v113, v143, 0x4b400000
	v_perm_b32 v9, v10, v9, s61
	v_perm_b32 v6, v8, v6, s61
	v_perm_b32 v8, v9, v6, s79
	v_fmaak_f32 v6, v114, v143, 0x4b400000
	v_fmaak_f32 v9, v115, v143, 0x4b400000
	v_fmaak_f32 v10, v116, v143, 0x4b400000
	v_fmaak_f32 v11, v117, v143, 0x4b400000
	v_perm_b32 v10, v11, v10, s61
	v_perm_b32 v6, v9, v6, s61
	v_perm_b32 v9, v10, v6, s79
	v_fmaak_f32 v6, v118, v143, 0x4b400000
	v_fmaak_f32 v10, v119, v143, 0x4b400000
	v_fmaak_f32 v11, v120, v143, 0x4b400000
	v_fmaak_f32 v12, v121, v143, 0x4b400000
	v_perm_b32 v11, v12, v11, s61
	v_perm_b32 v6, v10, v6, s61
	v_perm_b32 v10, v11, v6, s79
	v_fmaak_f32 v6, v130, v143, 0x4b400000
	v_fmaak_f32 v11, v131, v143, 0x4b400000
	v_fmaak_f32 v12, v132, v143, 0x4b400000
	v_fmaak_f32 v13, v133, v143, 0x4b400000
	v_perm_b32 v12, v13, v12, s61
	v_perm_b32 v6, v11, v6, s61
	v_perm_b32 v11, v12, v6, s79
	v_fmaak_f32 v6, v134, v143, 0x4b400000
	v_fmaak_f32 v12, v135, v143, 0x4b400000
	v_fmaak_f32 v13, v136, v143, 0x4b400000
	v_fmaak_f32 v14, v137, v143, 0x4b400000
	v_perm_b32 v13, v14, v13, s61
	v_perm_b32 v6, v12, v6, s61
	v_perm_b32 v12, v13, v6, s79
	v_fmaak_f32 v6, v138, v143, 0x4b400000
	v_fmaak_f32 v13, v139, v143, 0x4b400000
	v_fmaak_f32 v14, v140, v143, 0x4b400000
	v_fmaak_f32 v15, v142, v143, 0x4b400000
	v_perm_b32 v14, v15, v14, s61
	v_perm_b32 v6, v13, v6, s61
	v_perm_b32 v13, v14, v6, s79
	v_cndmask_b32_e64 v6, v1, v10, s[2:3]
	s_nop 1
	v_mov_b32_dpp v14, v6 quad_perm:[1,0,3,2] row_mask:0xf bank_mask:0xf bound_ctrl:1
	v_cndmask_b32_e64 v6, v7, v11, s[2:3]
	v_cndmask_b32_e64 v10, v10, v14, s[2:3]
	s_nop 0
	v_mov_b32_dpp v15, v6 quad_perm:[1,0,3,2] row_mask:0xf bank_mask:0xf bound_ctrl:1
	v_cndmask_b32_e64 v6, v8, v12, s[2:3]
	v_cndmask_b32_e64 v7, v15, v7, s[2:3]
	v_cndmask_b32_e64 v11, v11, v15, s[2:3]
	v_mov_b32_dpp v16, v6 quad_perm:[1,0,3,2] row_mask:0xf bank_mask:0xf bound_ctrl:1
	v_cndmask_b32_e64 v6, v9, v13, s[2:3]
	v_cndmask_b32_e64 v8, v16, v8, s[2:3]
	v_cndmask_b32_e64 v12, v12, v16, s[2:3]
	v_mov_b32_dpp v17, v6 quad_perm:[1,0,3,2] row_mask:0xf bank_mask:0xf bound_ctrl:1
	v_cndmask_b32_e64 v6, v14, v1, s[2:3]
	v_cndmask_b32_e64 v9, v17, v9, s[2:3]
	v_cndmask_b32_e64 v13, v13, v17, s[2:3]
	global_store_dwordx4 v[2:3], v[6:9], off offset:96
	global_store_dwordx4 v[4:5], v[10:13], off offset:96
	s_cbranch_vccnz .LBB0_232
	s_lshl_b64 s[8:9], s[8:9], 13
	v_readlane_b32 s10, v253, 2
	s_add_u32 s8, s10, s8
	v_readlane_b32 s10, v253, 3
	s_addc_u32 s9, s10, s9
	v_ashrrev_i32_e32 v1, 31, v0
	v_lshl_add_u64 v[0:1], v[0:1], 2, s[8:9]
	global_store_dword v[0:1], v141, off
	s_branch .LBB0_232

; __global__ void __launch_bounds__(NWAVES * 64, 2) mk_fwd(Args args) {
;     ...
;             auto tok_of = [&](int t0, int j) { return (j == 0 || t0 + NGW >= T) ? t0 : t0 + NGW; };
;             auto load_raw = [&](int t0) { return INFO[(size_t)tok_of(t0, (lane >> 2) & 1) * 4 + (lane & 3)]; };
;             auto unpack_raw = [&](const i32x4& raw, int (&e)[2][4], int (&p)[2][4], float (&gq)[2][4]) {
; #pragma unroll
;                 for (int j = 0; j < 2; ++j)
; #pragma unroll
;                     for (int k = 0; k < 4; ++k) { e[j][k] = __builtin_amdgcn_readlane(raw.x, 4 * j + k); p[j][k] = __builtin_amdgcn_readlane(raw.y, 4 * j + k);
;                         gq[j][k] = __int_as_float(__builtin_amdgcn_readlane(raw.z, 4 * j + k)) * (1.0f / 16.0f); } };
;     ...
;             i32x4 raw = load_raw(gw);
;             { int e0[2][4], p0[2][4]; unpack_raw(raw, e0, p0, gt); load_rows(gw, e0, p0, xr, yr); }
.LBB0_704:
	s_mov_b32 s2, -1
	s_waitcnt lgkmcnt(0)
	s_barrier
	v_readlane_b32 s4, v253, 57
	v_mbcnt_lo_u32_b32 v0, s2, 0
	v_mbcnt_hi_u32_b32 v0, s2, v0
	s_nop 0
	v_and_b32_e32 v1, 4, v0
	v_cmp_eq_u32_e64 s[2:3], 0, v1
	v_mov_b32_e32 v1, s4
	v_readlane_b32 s4, v253, 19
	v_readlane_b32 s5, v253, 20
	s_nop 0
	v_mov_b32_e32 v2, s4
	v_readlane_b32 s4, v253, 52
	v_readlane_b32 s5, v253, 53
	s_or_b64 vcc, s[2:3], s[4:5]
	v_cndmask_b32_e32 v2, v1, v2, vcc
	v_ashrrev_i32_e32 v3, 31, v2
	v_readlane_b32 s4, v252, 39
	v_and_b32_e32 v1, 3, v0
	v_lshlrev_b64 v[2:3], 6, v[2:3]
	v_readlane_b32 s5, v252, 40
	v_lshlrev_b32_e32 v32, 4, v1
	s_cmp_lg_u32 s66, 3
	v_lshl_add_u64 v[2:3], s[4:5], 0, v[2:3]
	v_lshl_add_u64 v[2:3], v[2:3], 0, v[32:33]
	global_load_dwordx4 v[2:5], v[2:3], off nt
	v_readlane_b32 s4, v254, 38
	v_readlane_b32 s5, v254, 39
	s_cselect_b64 s[8:9], -1, 0
	s_andn2_b64 vcc, exec, s[4:5]
	s_waitcnt vmcnt(0)
	v_readlane_b32 s7, v2, 0
	v_readlane_b32 s6, v3, 0
	v_readlane_b32 s24, v4, 0
	v_readlane_b32 s11, v2, 1
	v_readlane_b32 s10, v3, 1
	v_readlane_b32 s25, v4, 1
	v_readlane_b32 s13, v2, 2
	v_readlane_b32 s12, v3, 2
	v_readlane_b32 s26, v4, 2
	v_readlane_b32 s15, v2, 3
	v_readlane_b32 s14, v3, 3
	v_readlane_b32 s27, v4, 3
	v_readlane_b32 s17, v2, 4
	v_readlane_b32 s16, v3, 4
	v_readlane_b32 s28, v4, 4
	v_readlane_b32 s19, v2, 5
	v_readlane_b32 s18, v3, 5
	v_readlane_b32 s29, v4, 5
	v_readlane_b32 s21, v2, 6
	v_readlane_b32 s20, v3, 6
	v_readlane_b32 s30, v4, 6
	v_readlane_b32 s23, v2, 7
	v_readlane_b32 s22, v3, 7
	v_readlane_b32 s31, v4, 7
	s_cbranch_vccnz .LBB0_719
; __global__ void __launch_bounds__(NWAVES * 64, 2) mk_fwd(Args args) {
;     ...
;             auto load_rows = [&](int t0, const int (&e)[2][4], const int (&p)[2][4], u32x4 (&xr)[2][2], u32x2 (&yr)[2][4][2]) {
; #pragma unroll
;                 for (int j = 0; j < 2; ++j) { const int t = tok_of(t0, j);
;                     xr[j][0] = *(const u32x4*)(YB + (size_t)t * D + 8 * lane); xr[j][1] = *(const u32x4*)(YB + (size_t)t * D + 512 + 8 * lane);
; #pragma unroll
;                     for (int k = 0; k < 4; ++k) { const unsigned char* yp = (const unsigned char*)YS + ((size_t)TB[e[j][k]] * 256 + p[j][k]) * D;
;                         yr[j][k][0] = *(const u32x2*)(yp + 8 * lane); yr[j][k][1] = *(const u32x2*)(yp + 512 + 8 * lane); } } };
;             u32x4 xr[2][2], xrn[2][2]; u32x2 yr[2][4][2], yrn[2][4][2]; float gt[2][4];
;             i32x4 raw = load_raw(gw);
;             { int e0[2][4], p0[2][4]; unpack_raw(raw, e0, p0, gt); load_rows(gw, e0, p0, xr, yr); }
	v_readlane_b32 s4, v254, 40
	v_readlane_b32 s5, v254, 41
	s_or_b32 s68, s4, 0x400
	s_mov_b64 s[34:35], s[84:85]
	v_readlane_b32 s80, v252, 43
	s_lshl_b64 s[4:5], s[68:69], 2
	v_readlane_b32 s84, v252, 47
	v_readlane_b32 s85, v252, 48
	v_readlane_b32 s94, v252, 57
	v_readlane_b32 s95, v252, 58
	s_mov_b64 s[84:85], s[34:35]
	s_add_u32 s34, s94, s4
	s_addc_u32 s35, s95, s5
	v_readlane_b32 s40, v252, 0
	v_lshlrev_b32_e32 v94, 3, v0
	v_readlane_b32 s41, v252, 1
	s_add_u32 s4, s40, s4
	v_ashrrev_i32_e32 v95, 31, v94
	s_addc_u32 s5, s41, s5
	v_lshlrev_b64 v[2:3], 2, v[94:95]
	v_lshl_add_u64 v[104:105], s[4:5], 0, v[2:3]
	v_readlane_b32 s4, v254, 13
	v_lshl_add_u64 v[102:103], s[34:35], 0, v[2:3]
	v_lshlrev_b64 v[20:21], 1, v[94:95]
	v_readlane_b32 s5, v254, 14
	v_readlane_b32 s34, v253, 60
	v_readlane_b32 s33, v253, 59
	v_lshl_add_u64 v[106:107], s[4:5], 0, v[20:21]
	v_cmp_eq_u32_e64 s[4:5], 0, v0
	v_readlane_b32 s35, v253, 61
	v_mov_b32_e32 v0, s33
	v_readlane_b32 s33, v253, 58
	s_or_b64 vcc, s[2:3], s[34:35]
	v_readlane_b32 s40, v252, 39
	v_mov_b32_e32 v1, s33
	v_cndmask_b32_e32 v0, v0, v1, vcc
	v_readlane_b32 s44, v254, 48
	v_ashrrev_i32_e32 v1, 31, v0
	v_readlane_b32 s41, v252, 40
	v_readlane_b32 s45, v254, 49
	v_lshlrev_b64 v[0:1], 6, v[0:1]
	v_lshl_add_u64 v[0:1], s[40:41], 0, v[0:1]
	v_lshl_add_u64 v[98:99], s[44:45], 0, v[2:3]
	v_readlane_b32 s44, v254, 44
	v_readlane_b32 s42, v252, 2
	v_readlane_b32 s43, v252, 3
	v_readlane_b32 s45, v254, 45
	v_lshl_add_u64 v[0:1], v[0:1], 0, v[32:33]
	s_lshl_b32 s23, s23, 2
	v_lshl_add_u64 v[100:101], s[44:45], 0, v[2:3]
	v_lshl_add_u64 v[110:111], s[42:43], 0, v[2:3]
	global_load_dwordx4 v[0:3], v[0:1], off nt
	s_add_i32 s23, s67, s23
	s_waitcnt vmcnt(0)
	v_mov_b32_e32 v3, s23
	ds_read_b32 v4, v3
	s_ashr_i32 s23, s22, 31
	s_lshl_b64 s[22:23], s[22:23], 10
	s_lshl_b32 s21, s21, 2
	s_add_i32 s21, s67, s21
	s_waitcnt lgkmcnt(0)
	v_ashrrev_i32_e32 v5, 31, v4
	v_lshlrev_b64 v[4:5], 18, v[4:5]
	v_lshl_add_u64 v[4:5], s[52:53], 0, v[4:5]
	v_lshl_add_u64 v[4:5], v[4:5], 0, s[22:23]
	v_lshl_add_u64 v[4:5], v[4:5], 0, v[94:95]
	v_mov_b32_e32 v3, s21
	global_load_dwordx2 v[112:113], v[4:5], off offset:512 nt
	global_load_dwordx2 v[114:115], v[4:5], off nt
	ds_read_b32 v4, v3
	s_ashr_i32 s21, s20, 31
	s_lshl_b64 s[20:21], s[20:21], 10
	s_lshl_b32 s19, s19, 2
	s_add_i32 s19, s67, s19
	s_waitcnt lgkmcnt(0)
	v_ashrrev_i32_e32 v5, 31, v4
	v_lshlrev_b64 v[4:5], 18, v[4:5]
	v_lshl_add_u64 v[4:5], s[52:53], 0, v[4:5]
	v_lshl_add_u64 v[4:5], v[4:5], 0, s[20:21]
	v_lshl_add_u64 v[4:5], v[4:5], 0, v[94:95]
	v_mov_b32_e32 v3, s19
	global_load_dwordx2 v[116:117], v[4:5], off offset:512 nt
	global_load_dwordx2 v[118:119], v[4:5], off nt
	ds_read_b32 v4, v3
	s_ashr_i32 s19, s18, 31
	s_lshl_b64 s[18:19], s[18:19], 10
	s_lshl_b32 s17, s17, 2
	s_add_i32 s17, s67, s17
	s_waitcnt lgkmcnt(0)
	v_ashrrev_i32_e32 v5, 31, v4
	v_lshlrev_b64 v[4:5], 18, v[4:5]
	v_lshl_add_u64 v[4:5], s[52:53], 0, v[4:5]
	v_lshl_add_u64 v[4:5], v[4:5], 0, s[18:19]
	v_lshl_add_u64 v[4:5], v[4:5], 0, v[94:95]
	v_mov_b32_e32 v3, s17
	global_load_dwordx2 v[120:121], v[4:5], off offset:512 nt
	global_load_dwordx2 v[122:123], v[4:5], off nt
	ds_read_b32 v4, v3
	s_ashr_i32 s17, s16, 31
	s_lshl_b64 s[16:17], s[16:17], 10
	s_lshl_b32 s15, s15, 2
	s_add_i32 s15, s67, s15
	s_waitcnt lgkmcnt(0)
	v_ashrrev_i32_e32 v5, 31, v4
	v_lshlrev_b64 v[4:5], 18, v[4:5]
	v_lshl_add_u64 v[4:5], s[52:53], 0, v[4:5]
	v_lshl_add_u64 v[4:5], v[4:5], 0, s[16:17]
	v_readlane_b32 s16, v253, 54
	v_readlane_b32 s17, v253, 55
	v_lshl_add_u64 v[4:5], v[4:5], 0, v[94:95]
	v_mov_b32_e32 v3, s15
	v_lshl_add_u64 v[8:9], s[16:17], 0, v[20:21]
	global_load_dwordx2 v[132:133], v[4:5], off offset:512 nt
	global_load_dwordx2 v[134:135], v[4:5], off nt
	s_nop 0
	global_load_dwordx4 v[4:7], v[8:9], off offset:1024 nt
	s_nop 0
	global_load_dwordx4 v[8:11], v[8:9], off nt
	ds_read_b32 v12, v3
	s_ashr_i32 s15, s14, 31
	s_lshl_b64 s[14:15], s[14:15], 10
	s_lshl_b32 s13, s13, 2
	s_add_i32 s13, s67, s13
	s_waitcnt lgkmcnt(0)
	v_ashrrev_i32_e32 v13, 31, v12
	v_lshlrev_b64 v[12:13], 18, v[12:13]
	v_lshl_add_u64 v[12:13], s[52:53], 0, v[12:13]
	v_lshl_add_u64 v[12:13], v[12:13], 0, s[14:15]
	v_lshl_add_u64 v[12:13], v[12:13], 0, v[94:95]
	v_mov_b32_e32 v3, s13
	global_load_dwordx2 v[124:125], v[12:13], off offset:512 nt
	global_load_dwordx2 v[126:127], v[12:13], off nt
	ds_read_b32 v12, v3
	s_ashr_i32 s13, s12, 31
	s_lshl_b64 s[12:13], s[12:13], 10
	s_lshl_b32 s11, s11, 2
	s_add_i32 s11, s67, s11
	s_waitcnt lgkmcnt(0)
	v_ashrrev_i32_e32 v13, 31, v12
	v_lshlrev_b64 v[12:13], 18, v[12:13]
	v_lshl_add_u64 v[12:13], s[52:53], 0, v[12:13]
	v_lshl_add_u64 v[12:13], v[12:13], 0, s[12:13]
	v_lshl_add_u64 v[12:13], v[12:13], 0, v[94:95]
	v_mov_b32_e32 v3, s11
	global_load_dwordx2 v[128:129], v[12:13], off offset:512 nt
	global_load_dwordx2 v[130:131], v[12:13], off nt
	ds_read_b32 v12, v3
	s_ashr_i32 s11, s10, 31
	s_lshl_b64 s[10:11], s[10:11], 10
	s_lshl_b32 s7, s7, 2
	s_add_i32 s7, s67, s7
	s_waitcnt lgkmcnt(0)
	v_ashrrev_i32_e32 v13, 31, v12
	v_lshlrev_b64 v[12:13], 18, v[12:13]
	v_lshl_add_u64 v[12:13], s[52:53], 0, v[12:13]
	v_lshl_add_u64 v[12:13], v[12:13], 0, s[10:11]
	v_lshl_add_u64 v[12:13], v[12:13], 0, v[94:95]
	v_mov_b32_e32 v3, s7
	global_load_dwordx2 v[136:137], v[12:13], off offset:512 nt
	global_load_dwordx2 v[138:139], v[12:13], off nt
	ds_read_b32 v12, v3
	s_ashr_i32 s7, s6, 31
	s_lshl_b64 s[6:7], s[6:7], 10
	v_readlane_b32 s82, v252, 45
	v_readlane_b32 s83, v252, 46
	s_waitcnt lgkmcnt(0)
	v_ashrrev_i32_e32 v13, 31, v12
	v_lshlrev_b64 v[12:13], 18, v[12:13]
	v_lshl_add_u64 v[12:13], s[52:53], 0, v[12:13]
	v_lshl_add_u64 v[12:13], v[12:13], 0, s[6:7]
	v_readlane_b32 s6, v253, 50
	v_readlane_b32 s7, v253, 51
	v_lshl_add_u64 v[12:13], v[12:13], 0, v[94:95]
	global_load_dwordx2 v[142:143], v[12:13], off offset:512 nt
	global_load_dwordx2 v[144:145], v[12:13], off nt
	v_lshl_add_u64 v[16:17], s[6:7], 0, v[20:21]
	global_load_dwordx4 v[12:15], v[16:17], off offset:1024 nt
	s_nop 0
	global_load_dwordx4 v[16:19], v[16:17], off nt
	v_readlane_b32 s81, v252, 44
	v_readlane_b32 s88, v252, 51
	v_readlane_b32 s89, v252, 52
	v_readlane_b32 s92, v252, 55
	v_readlane_b32 s93, v252, 56
	v_readlane_b32 s82, v254, 9
	v_readlane_b32 s94, v254, 19
	v_readlane_b32 s80, v254, 17
	v_readlane_b32 s88, v254, 21
	v_readlane_b32 s92, v254, 15
	v_readlane_b32 s83, v254, 10
	v_readlane_b32 s95, v254, 20
	v_readlane_b32 s81, v254, 18
	v_readlane_b32 s89, v254, 22
	v_readlane_b32 s93, v254, 16
	v_readlane_b32 s83, v254, 23
	v_lshl_add_u64 v[96:97], s[40:41], 0, v[32:33]
	v_lshl_add_u64 v[108:109], s[36:37], 0, v[94:95]
	v_lshl_add_u64 v[140:141], s[94:95], 0, v[20:21]
	v_readlane_b32 s10, v253, 19
	v_readlane_b32 s86, v252, 49
	v_readlane_b32 s87, v252, 50
	v_readlane_b32 s90, v252, 53
	v_readlane_b32 s91, v252, 54
	v_readlane_b32 s11, v253, 20
	s_branch .LBB0_707

; __global__ void __launch_bounds__(NWAVES * 64, 2) mk_fwd(Args args) {
;     ...
;             auto load_rows = [&](int t0, const int (&e)[2][4], const int (&p)[2][4], u32x4 (&xr)[2][2], u32x2 (&yr)[2][4][2]) {
; #pragma unroll
;                 for (int j = 0; j < 2; ++j) { const int t = tok_of(t0, j);
;                     xr[j][0] = *(const u32x4*)(YB + (size_t)t * D + 8 * lane); xr[j][1] = *(const u32x4*)(YB + (size_t)t * D + 512 + 8 * lane);
; #pragma unroll
;                     for (int k = 0; k < 4; ++k) { const unsigned char* yp = (const unsigned char*)YS + ((size_t)TB[e[j][k]] * 256 + p[j][k]) * D;
;                         yr[j][k][0] = *(const u32x2*)(yp + 8 * lane); yr[j][k][1] = *(const u32x2*)(yp + 512 + 8 * lane); } } };
;     ...
;             for (int t0 = gw; t0 < T; t0 += 2 * NGW) {
;                 int tt[2]; tt[0] = t0; tt[1] = tok_of(t0, 1);
;                 const int t1 = (t0 + 2 * NGW < T) ? t0 + 2 * NGW : t0, t2 = (t1 + 2 * NGW < T) ? t1 + 2 * NGW : t1;
;                 int en[2][4], pn[2][4]; float gn[2][4];
;                 unpack_raw(raw, en, pn, gn);
;                 load_rows(t1, en, pn, xrn, yrn);
;                 raw = load_raw(t2);
.LBB0_707:
	v_readlane_b32 s7, v253, 56
	s_add_i32 s6, s7, s10
	s_cmp_lt_i32 s6, 0x8000
	s_cselect_b32 s18, s6, s10
	s_add_i32 s6, s18, s7
	s_cmp_lt_i32 s6, 0x8000
	s_cselect_b32 s11, s6, s18
	v_readlane_b32 s7, v0, 0
	s_ashr_i32 s19, s18, 31
	s_lshl_b64 s[42:43], s[18:19], 11
	s_lshl_b32 s7, s7, 2
	s_waitcnt vmcnt(0)
	v_mov_b64_e32 v[30:31], v[18:19]
	v_mov_b64_e32 v[36:37], v[14:15]
	v_readlane_b32 s34, v1, 0
	v_readlane_b32 s13, v0, 1
	v_readlane_b32 s40, v1, 1
	v_readlane_b32 s15, v0, 2
	v_readlane_b32 s22, v1, 2
	v_readlane_b32 s17, v0, 3
	v_readlane_b32 s20, v1, 3
	v_readlane_b32 s33, v0, 4
	v_readlane_b32 s16, v1, 4
	v_readlane_b32 s38, v0, 5
	v_readlane_b32 s14, v1, 5
	v_readlane_b32 s44, v0, 6
	v_readlane_b32 s12, v1, 6
	v_readlane_b32 s45, v0, 7
	v_readlane_b32 s6, v1, 7
	v_lshl_add_u64 v[0:1], v[140:141], 0, s[42:43]
	s_add_i32 s7, s67, s7
	v_mov_b64_e32 v[28:29], v[16:17]
	v_mov_b64_e32 v[34:35], v[12:13]
	global_load_dwordx4 v[16:19], v[0:1], off nt
	global_load_dwordx4 v[12:15], v[0:1], off offset:1024 nt
	v_mov_b32_e32 v0, s7
	s_lshl_b32 s7, s13, 2
	s_add_i32 s7, s67, s7
	v_mov_b32_e32 v1, s7
	s_lshl_b32 s7, s15, 2
	ds_read_b32 v0, v0
	s_add_i32 s7, s67, s7
	v_mov_b32_e32 v3, s7
	s_lshl_b32 s7, s17, 2
	v_mov_b64_e32 v[26:27], v[6:7]
	s_add_i32 s7, s67, s7
	v_mov_b64_e32 v[24:25], v[4:5]
	v_mul_f32_e32 v44, s24, v224
	v_mul_f32_e32 v42, s25, v224
	v_mul_f32_e32 v40, s26, v224
	v_mul_f32_e32 v38, s27, v224
	v_mul_f32_e32 v150, s28, v224
	v_mul_f32_e32 v148, s29, v224
	v_mul_f32_e32 v146, s30, v224
	v_mul_f32_e32 v32, s31, v224
	v_readlane_b32 s24, v2, 0
	v_readlane_b32 s25, v2, 1
	v_readlane_b32 s26, v2, 2
	v_readlane_b32 s27, v2, 3
	v_readlane_b32 s28, v2, 4
	v_readlane_b32 s29, v2, 5
	v_readlane_b32 s30, v2, 6
	v_readlane_b32 s31, v2, 7
	v_mov_b32_e32 v5, s7
	ds_read_b32 v2, v1
	ds_read_b32 v4, v3
	ds_read_b32 v6, v5
	s_waitcnt lgkmcnt(3)
	v_ashrrev_i32_e32 v1, 31, v0
	s_ashr_i32 s35, s34, 31
	v_lshlrev_b64 v[0:1], 18, v[0:1]
	s_waitcnt lgkmcnt(2)
	v_ashrrev_i32_e32 v3, 31, v2
	s_lshl_b64 s[34:35], s[34:35], 10
	v_lshl_add_u64 v[0:1], s[52:53], 0, v[0:1]
	s_ashr_i32 s41, s40, 31
	v_lshlrev_b64 v[2:3], 18, v[2:3]
	v_lshl_add_u64 v[0:1], v[0:1], 0, s[34:35]
	s_lshl_b64 s[34:35], s[40:41], 10
	v_lshl_add_u64 v[2:3], s[52:53], 0, v[2:3]
	s_ashr_i32 s23, s22, 31
	s_ashr_i32 s21, s20, 31
	v_lshl_add_u64 v[0:1], v[0:1], 0, v[94:95]
	v_lshl_add_u64 v[2:3], v[2:3], 0, s[34:35]
	s_waitcnt lgkmcnt(1)
	v_ashrrev_i32_e32 v5, 31, v4
	s_lshl_b64 s[22:23], s[22:23], 10
	s_lshl_b64 s[20:21], s[20:21], 10
	s_add_i32 s7, s18, s82
	v_mov_b64_e32 v[60:61], v[144:145]
	v_mov_b64_e32 v[52:53], v[142:143]
	v_mov_b64_e32 v[58:59], v[138:139]
	v_mov_b64_e32 v[50:51], v[136:137]
	v_lshl_add_u64 v[2:3], v[2:3], 0, v[94:95]
	global_load_dwordx2 v[144:145], v[0:1], off nt
	global_load_dwordx2 v[142:143], v[0:1], off offset:512 nt
	global_load_dwordx2 v[138:139], v[2:3], off nt
	global_load_dwordx2 v[136:137], v[2:3], off offset:512 nt
	v_lshlrev_b64 v[0:1], 18, v[4:5]
	s_waitcnt lgkmcnt(0)
	v_ashrrev_i32_e32 v7, 31, v6
	s_cmpk_gt_i32 s7, 0x7fff
	v_lshl_add_u64 v[0:1], s[52:53], 0, v[0:1]
	v_lshlrev_b64 v[2:3], 18, v[6:7]
	s_cselect_b32 s18, s18, s7
	v_lshl_add_u64 v[0:1], v[0:1], 0, s[22:23]
	v_lshl_add_u64 v[2:3], s[52:53], 0, v[2:3]
	s_ashr_i32 s19, s18, 31
	v_lshl_add_u64 v[0:1], v[0:1], 0, v[94:95]
	v_lshl_add_u64 v[2:3], v[2:3], 0, s[20:21]
	s_lshl_b64 s[18:19], s[18:19], 11
	s_lshl_b32 s7, s33, 2
	v_mov_b64_e32 v[56:57], v[130:131]
	v_mov_b64_e32 v[48:49], v[128:129]
	v_mov_b64_e32 v[54:55], v[126:127]
	v_mov_b64_e32 v[46:47], v[124:125]
	v_mov_b64_e32 v[22:23], v[10:11]
	v_lshl_add_u64 v[2:3], v[2:3], 0, v[94:95]
	global_load_dwordx2 v[130:131], v[0:1], off nt
	global_load_dwordx2 v[128:129], v[0:1], off offset:512 nt
	global_load_dwordx2 v[126:127], v[2:3], off nt
	global_load_dwordx2 v[124:125], v[2:3], off offset:512 nt
	v_lshl_add_u64 v[0:1], v[140:141], 0, s[18:19]
	s_add_i32 s7, s67, s7
	v_mov_b64_e32 v[20:21], v[8:9]
	global_load_dwordx4 v[8:11], v[0:1], off nt
	global_load_dwordx4 v[4:7], v[0:1], off offset:1024 nt
	v_mov_b32_e32 v0, s7
	s_lshl_b32 s7, s38, 2
	s_add_i32 s7, s67, s7
	v_mov_b32_e32 v1, s7
	s_lshl_b32 s7, s44, 2
	ds_read_b32 v0, v0
	s_add_i32 s7, s67, s7
	v_mov_b32_e32 v3, s7
	s_lshl_b32 s7, s45, 2
	s_add_i32 s7, s67, s7
	v_mov_b32_e32 v39, s7
	ds_read_b32 v2, v1
	ds_read_b32 v62, v3
	ds_read_b32 v64, v39
	s_waitcnt lgkmcnt(3)
	v_ashrrev_i32_e32 v1, 31, v0
	s_ashr_i32 s17, s16, 31
	v_lshlrev_b64 v[0:1], 18, v[0:1]
	s_waitcnt lgkmcnt(2)
	v_ashrrev_i32_e32 v3, 31, v2
	s_lshl_b64 s[16:17], s[16:17], 10
	v_lshl_add_u64 v[0:1], s[52:53], 0, v[0:1]
	s_ashr_i32 s15, s14, 31
	v_lshlrev_b64 v[2:3], 18, v[2:3]
	v_lshl_add_u64 v[0:1], v[0:1], 0, s[16:17]
	s_lshl_b64 s[14:15], s[14:15], 10
	v_lshl_add_u64 v[2:3], s[52:53], 0, v[2:3]
	v_lshl_add_u64 v[0:1], v[0:1], 0, v[94:95]
	v_lshl_add_u64 v[2:3], v[2:3], 0, s[14:15]
	s_waitcnt lgkmcnt(1)
	v_ashrrev_i32_e32 v63, 31, v62
	v_mov_b64_e32 v[166:167], v[134:135]
	v_mov_b64_e32 v[158:159], v[132:133]
	v_mov_b64_e32 v[164:165], v[122:123]
	v_mov_b64_e32 v[156:157], v[120:121]
	v_lshl_add_u64 v[2:3], v[2:3], 0, v[94:95]
	global_load_dwordx2 v[134:135], v[0:1], off nt
	global_load_dwordx2 v[132:133], v[0:1], off offset:512 nt
	global_load_dwordx2 v[122:123], v[2:3], off nt
	global_load_dwordx2 v[120:121], v[2:3], off offset:512 nt
	s_ashr_i32 s13, s12, 31
	v_lshlrev_b64 v[0:1], 18, v[62:63]
	s_lshl_b64 s[12:13], s[12:13], 10
	v_lshl_add_u64 v[0:1], s[52:53], 0, v[0:1]
	s_waitcnt lgkmcnt(0)
; __device__ __forceinline__ float wave_sum(float v) { v += dpp_f<0xB1>(v); v += dpp_f<0x4E>(v); v += dpp_f<0x141>(v); v += dpp_f<0x140>(v); v += xor_sw<16>(v); return sum_x32(v); }
; __device__ __forceinline__ void ln_row16(float (&v)[16], const float* lng, const float* lnb, int lane, float (&o)[16]) {
;     const float s = ((v[0] + v[1]) + (v[2] + v[3])) + ((v[4] + v[5]) + (v[6] + v[7])) + (((v[8] + v[9]) + (v[10] + v[11])) + ((v[12] + v[13]) + (v[14] + v[15])));
;     const float mean = wave_sum(s) * (1.0f / D);
; #pragma unroll
;     for (int i = 0; i < 16; ++i) v[i] -= mean;
;     const float s2 = ((v[0] * v[0] + v[1] * v[1]) + (v[2] * v[2] + v[3] * v[3])) + ((v[4] * v[4] + v[5] * v[5]) + (v[6] * v[6] + v[7] * v[7]))
;                    + (((v[8] * v[8] + v[9] * v[9]) + (v[10] * v[10] + v[11] * v[11])) + ((v[12] * v[12] + v[13] * v[13]) + (v[14] * v[14] + v[15] * v[15])));
;     const float rstd = 1.0f / sqrtf(wave_sum(s2) * (1.0f / D) + LN_EPS);
; #pragma unroll
;     for (int hf = 0; hf < 2; ++hf) { const int col = 512 * hf + 8 * lane;
;         const f32x4 g0 = *(const f32x4*)(lng + col), g1 = *(const f32x4*)(lng + col + 4), b0 = *(const f32x4*)(lnb + col), b1 = *(const f32x4*)(lnb + col + 4);
; #pragma unroll
;         for (int i = 0; i < 4; ++i) { o[8 * hf + i] = v[8 * hf + i] * rstd * g0[i] + b0[i]; o[8 * hf + 4 + i] = v[8 * hf + 4 + i] * rstd * g1[i] + b1[i]; } }
; __global__ void __launch_bounds__(NWAVES * 64, 2) mk_fwd(Args args) {
;     ...
;                 raw = load_raw(t2);
;                 __builtin_amdgcn_sched_barrier(0);
;                 float o[2][16];
; #pragma unroll
;                 for (int j = 0; j < 2; ++j) {
;                     float v[16], x1[16];
; #pragma unroll
;                     for (int hf = 0; hf < 2; ++hf) { float f[8]; unpack8(xr[j][hf], f);
; #pragma unroll
;                         for (int i = 0; i < 8; ++i) v[8 * hf + i] = f[i]; }
;                     ln_row16(v, lng1, lnb1, lane, x1);
; #pragma unroll
;                     for (int hf = 0; hf < 2; ++hf) { float f[8];
; #pragma unroll
;                         for (int i = 0; i < 8; ++i) v[8 * hf + i] = ALPHA * x1[8 * hf + i];
; #pragma unroll
;                         for (int k = 0; k < 4; ++k) { unpack8_f8(yr[j][k][hf], f);
; #pragma unroll
;                             for (int i = 0; i < 8; ++i) v[8 * hf + i] += gt[j][k] * f[i]; } }
	v_ashrrev_i32_e32 v65, 31, v64
	s_ashr_i32 s7, s6, 31
	v_lshl_add_u64 v[0:1], v[0:1], 0, s[12:13]
	v_lshlrev_b64 v[2:3], 18, v[64:65]
	s_lshl_b64 s[6:7], s[6:7], 10
	s_add_i32 s12, s11, s82
	v_lshl_add_u64 v[2:3], s[52:53], 0, v[2:3]
	s_cmpk_gt_i32 s12, 0x7fff
	v_lshl_add_u64 v[0:1], v[0:1], 0, v[94:95]
	v_lshl_add_u64 v[2:3], v[2:3], 0, s[6:7]
	s_cselect_b64 s[6:7], -1, 0
	v_mov_b64_e32 v[162:163], v[118:119]
	v_mov_b64_e32 v[154:155], v[116:117]
	v_mov_b64_e32 v[160:161], v[114:115]
	v_mov_b64_e32 v[152:153], v[112:113]
	v_lshl_add_u64 v[2:3], v[2:3], 0, v[94:95]
	global_load_dwordx2 v[118:119], v[0:1], off nt
	global_load_dwordx2 v[116:117], v[0:1], off offset:512 nt
	global_load_dwordx2 v[114:115], v[2:3], off nt
	global_load_dwordx2 v[112:113], v[2:3], off offset:512 nt
	v_mov_b32_e32 v0, s12
	v_mov_b32_e32 v1, s11
	s_or_b64 vcc, s[2:3], s[6:7]
	v_cndmask_b32_e32 v0, v0, v1, vcc
	v_ashrrev_i32_e32 v1, 31, v0
	v_lshlrev_b64 v[0:1], 6, v[0:1]
	v_lshl_add_u64 v[0:1], v[96:97], 0, v[0:1]
	global_load_dwordx4 v[0:3], v[0:1], off nt
	v_lshlrev_b32_e32 v62, 16, v37
	v_and_b32_e32 v63, 0xffff0000, v37
	v_lshlrev_b32_e32 v64, 16, v36
	v_and_b32_e32 v65, 0xffff0000, v36
	v_lshlrev_b32_e32 v36, 16, v35
	v_and_b32_e32 v37, 0xffff0000, v35
	v_lshlrev_b32_e32 v66, 16, v34
	v_and_b32_e32 v67, 0xffff0000, v34
	v_lshlrev_b32_e32 v70, 16, v28
	v_and_b32_e32 v71, 0xffff0000, v28
	s_waitcnt vmcnt(0)
	v_add_f32_e32 v3, v63, v62
	v_add_f32_e32 v28, v65, v64
	v_lshlrev_b32_e32 v34, 16, v31
	v_and_b32_e32 v35, 0xffff0000, v31
	v_lshlrev_b32_e32 v68, 16, v30
	v_and_b32_e32 v69, 0xffff0000, v30
	v_lshlrev_b32_e32 v30, 16, v29
	v_and_b32_e32 v31, 0xffff0000, v29
	v_add_f32_e32 v3, v28, v3
	v_add_f32_e32 v28, v37, v36
	v_add_f32_e32 v29, v67, v66
	v_add_f32_e32 v28, v29, v28
	v_add_f32_e32 v3, v28, v3
	v_add_f32_e32 v28, v35, v34
	v_add_f32_e32 v29, v69, v68
	v_add_f32_e32 v28, v29, v28
	v_add_f32_e32 v29, v31, v30
	v_add_f32_e32 v39, v71, v70
	v_add_f32_e32 v29, v39, v29
	v_add_f32_e32 v28, v29, v28
	v_add_f32_e32 v3, v28, v3
	s_mov_b32 s11, 0xf800000
	v_cvt_pk_f32_fp8_sdwa v[178:179], v60 src0_sel:WORD_1
	v_add_f32_dpp v3, v3, v3 quad_perm:[1,0,3,2] row_mask:0xf bank_mask:0xf bound_ctrl:1
	v_cvt_pk_f32_fp8_e32 v[180:181], v61
	v_cvt_pk_f32_fp8_e32 v[182:183], v58
	v_add_f32_dpp v3, v3, v3 quad_perm:[2,3,0,1] row_mask:0xf bank_mask:0xf bound_ctrl:1
	v_cvt_pk_f32_fp8_sdwa v[184:185], v58 src0_sel:WORD_1
	v_cvt_pk_f32_fp8_e32 v[186:187], v59
	v_add_f32_dpp v3, v3, v3 row_half_mirror row_mask:0xf bank_mask:0xf bound_ctrl:1
	v_cvt_pk_f32_fp8_sdwa v[58:59], v59 src0_sel:WORD_1
	v_cvt_pk_f32_fp8_e32 v[188:189], v56
	v_add_f32_dpp v3, v3, v3 row_mirror row_mask:0xf bank_mask:0xf bound_ctrl:1
	ds_swizzle_b32 v28, v3 offset:swizzle(SWAP,16)
	v_cvt_pk_f32_fp8_sdwa v[190:191], v56 src0_sel:WORD_1
	v_cvt_pk_f32_fp8_e32 v[192:193], v57
	v_cvt_pk_f32_fp8_sdwa v[56:57], v57 src0_sel:WORD_1
	v_cvt_pk_f32_fp8_e32 v[194:195], v54
	s_waitcnt lgkmcnt(0)
	v_add_f32_e32 v3, v3, v28
	v_mov_b32_e32 v28, v3
	s_nop 1
	v_permlane32_swap_b32_e32 v3, v28
	v_add_f32_e32 v3, v3, v28
	v_mul_f32_e32 v28, 0x3a800000, v3
	v_pk_add_f32 v[168:169], v[70:71], v[28:29] op_sel_hi:[1,0] neg_lo:[0,1] neg_hi:[0,1]
	v_pk_add_f32 v[30:31], v[30:31], v[28:29] op_sel_hi:[1,0] neg_lo:[0,1] neg_hi:[0,1]
	v_pk_add_f32 v[170:171], v[68:69], v[28:29] op_sel_hi:[1,0] neg_lo:[0,1] neg_hi:[0,1]
	v_pk_add_f32 v[34:35], v[34:35], v[28:29] op_sel_hi:[1,0] neg_lo:[0,1] neg_hi:[0,1]
	v_pk_add_f32 v[172:173], v[66:67], v[28:29] op_sel_hi:[1,0] neg_lo:[0,1] neg_hi:[0,1]
	v_pk_add_f32 v[36:37], v[36:37], v[28:29] op_sel_hi:[1,0] neg_lo:[0,1] neg_hi:[0,1]
	v_pk_add_f32 v[174:175], v[64:65], v[28:29] op_sel_hi:[1,0] neg_lo:[0,1] neg_hi:[0,1]
	v_pk_add_f32 v[28:29], v[62:63], v[28:29] op_sel_hi:[1,0] neg_lo:[0,1] neg_hi:[0,1]
	v_pk_mul_f32 v[74:75], v[174:175], v[174:175]
	v_pk_mul_f32 v[76:77], v[28:29], v[28:29]
	v_pk_mul_f32 v[70:71], v[172:173], v[172:173]
	v_pk_mul_f32 v[72:73], v[36:37], v[36:37]
	v_add_f32_e32 v3, v76, v77
	v_add_f32_e32 v39, v74, v75
	v_add_f32_e32 v3, v39, v3
	v_add_f32_e32 v39, v72, v73
	v_add_f32_e32 v41, v70, v71
	v_pk_mul_f32 v[66:67], v[170:171], v[170:171]
	v_pk_mul_f32 v[68:69], v[34:35], v[34:35]
	v_add_f32_e32 v39, v41, v39
	v_pk_mul_f32 v[62:63], v[168:169], v[168:169]
	v_pk_mul_f32 v[64:65], v[30:31], v[30:31]
	v_add_f32_e32 v3, v39, v3
	v_add_f32_e32 v39, v68, v69
	v_add_f32_e32 v41, v66, v67
	v_add_f32_e32 v39, v41, v39
	v_add_f32_e32 v41, v64, v65
	v_add_f32_e32 v43, v62, v63
	global_load_dwordx4 v[62:65], v[98:99], off offset:16
	global_load_dwordx4 v[82:85], v[98:99], off
	global_load_dwordx4 v[86:89], v[100:101], off
	global_load_dwordx4 v[90:93], v[100:101], off offset:16
	global_load_dwordx4 v[66:69], v[98:99], off offset:2048
	global_load_dwordx4 v[70:73], v[100:101], off offset:2048
	global_load_dwordx4 v[74:77], v[98:99], off offset:2064
	global_load_dwordx4 v[78:81], v[100:101], off offset:2064
	v_add_f32_e32 v41, v43, v41
	v_add_f32_e32 v39, v41, v39
	v_add_f32_e32 v3, v39, v3
	v_cvt_pk_f32_fp8_sdwa v[196:197], v54 src0_sel:WORD_1
	v_cvt_pk_f32_fp8_e32 v[198:199], v55
	v_add_f32_dpp v3, v3, v3 quad_perm:[1,0,3,2] row_mask:0xf bank_mask:0xf bound_ctrl:1
	v_cvt_pk_f32_fp8_sdwa v[54:55], v55 src0_sel:WORD_1
	v_cvt_pk_f32_fp8_e32 v[200:201], v52
	v_add_f32_dpp v3, v3, v3 quad_perm:[2,3,0,1] row_mask:0xf bank_mask:0xf bound_ctrl:1
	v_cvt_pk_f32_fp8_sdwa v[204:205], v52 src0_sel:WORD_1
	v_cvt_pk_f32_fp8_e32 v[206:207], v53
	v_add_f32_dpp v3, v3, v3 row_half_mirror row_mask:0xf bank_mask:0xf bound_ctrl:1
	v_cvt_pk_f32_fp8_sdwa v[52:53], v53 src0_sel:WORD_1
	v_cvt_pk_f32_fp8_e32 v[208:209], v50
	v_add_f32_dpp v3, v3, v3 row_mirror row_mask:0xf bank_mask:0xf bound_ctrl:1
	ds_swizzle_b32 v39, v3 offset:swizzle(SWAP,16)
	v_cvt_pk_f32_fp8_sdwa v[210:211], v50 src0_sel:WORD_1
	v_cvt_pk_f32_fp8_e32 v[212:213], v51
	v_cvt_pk_f32_fp8_sdwa v[50:51], v51 src0_sel:WORD_1
	v_cvt_pk_f32_fp8_e32 v[214:215], v48
	s_waitcnt lgkmcnt(0)
; __device__ __forceinline__ float wave_sum(float v) { v += dpp_f<0xB1>(v); v += dpp_f<0x4E>(v); v += dpp_f<0x141>(v); v += dpp_f<0x140>(v); v += xor_sw<16>(v); return sum_x32(v); }
; __device__ __forceinline__ void ln_row16(float (&v)[16], const float* lng, const float* lnb, int lane, float (&o)[16]) {
;     const float s = ((v[0] + v[1]) + (v[2] + v[3])) + ((v[4] + v[5]) + (v[6] + v[7])) + (((v[8] + v[9]) + (v[10] + v[11])) + ((v[12] + v[13]) + (v[14] + v[15])));
;     const float mean = wave_sum(s) * (1.0f / D);
; #pragma unroll
;     for (int i = 0; i < 16; ++i) v[i] -= mean;
;     const float s2 = ((v[0] * v[0] + v[1] * v[1]) + (v[2] * v[2] + v[3] * v[3])) + ((v[4] * v[4] + v[5] * v[5]) + (v[6] * v[6] + v[7] * v[7]))
;                    + (((v[8] * v[8] + v[9] * v[9]) + (v[10] * v[10] + v[11] * v[11])) + ((v[12] * v[12] + v[13] * v[13]) + (v[14] * v[14] + v[15] * v[15])));
;     const float rstd = 1.0f / sqrtf(wave_sum(s2) * (1.0f / D) + LN_EPS);
; #pragma unroll
;     for (int hf = 0; hf < 2; ++hf) { const int col = 512 * hf + 8 * lane;
;         const f32x4 g0 = *(const f32x4*)(lng + col), g1 = *(const f32x4*)(lng + col + 4), b0 = *(const f32x4*)(lnb + col), b1 = *(const f32x4*)(lnb + col + 4);
; #pragma unroll
;         for (int i = 0; i < 4; ++i) { o[8 * hf + i] = v[8 * hf + i] * rstd * g0[i] + b0[i]; o[8 * hf + 4 + i] = v[8 * hf + 4 + i] * rstd * g1[i] + b1[i]; } }
; __global__ void __launch_bounds__(NWAVES * 64, 2) mk_fwd(Args args) {
;     ...
;                     ln_row16(v, lng1, lnb1, lane, x1);
; #pragma unroll
;                     for (int hf = 0; hf < 2; ++hf) { float f[8];
; #pragma unroll
;                         for (int i = 0; i < 8; ++i) v[8 * hf + i] = ALPHA * x1[8 * hf + i];
; #pragma unroll
;                         for (int k = 0; k < 4; ++k) { unpack8_f8(yr[j][k][hf], f);
; #pragma unroll
;                             for (int i = 0; i < 8; ++i) v[8 * hf + i] += gt[j][k] * f[i]; } }
;                     ln_row16(v, lng, lnb, lane, o[j]);
	v_add_f32_e32 v3, v3, v39
	v_mov_b32_e32 v39, v3
	s_nop 1
	v_permlane32_swap_b32_e32 v3, v39
	v_add_f32_e32 v3, v3, v39
	v_fmamk_f32 v3, v3, 0x3a800000, v250
	v_mul_f32_e32 v39, 0x4f800000, v3
	v_cmp_gt_f32_e32 vcc, s11, v3
	v_cvt_pk_f32_fp8_sdwa v[216:217], v48 src0_sel:WORD_1
	v_cvt_pk_f32_fp8_e32 v[218:219], v49
	v_cndmask_b32_e32 v3, v3, v39, vcc
	v_sqrt_f32_e32 v39, v3
	v_cvt_pk_f32_fp8_sdwa v[48:49], v49 src0_sel:WORD_1
	v_cvt_pk_f32_fp8_e32 v[226:227], v46
	v_cvt_pk_f32_fp8_sdwa v[228:229], v46 src0_sel:WORD_1
	v_add_u32_e32 v41, -1, v39
	v_fma_f32 v43, -v41, v39, v3
	v_cmp_ge_f32_e64 s[6:7], 0, v43
	v_add_u32_e32 v43, 1, v39
	v_cvt_pk_f32_fp8_e32 v[230:231], v47
	v_cndmask_b32_e64 v41, v39, v41, s[6:7]
	v_fma_f32 v39, -v43, v39, v3
	v_cmp_lt_f32_e64 s[6:7], 0, v39
	v_cvt_pk_f32_fp8_sdwa v[46:47], v47 src0_sel:WORD_1
	v_cvt_pk_f32_fp8_e32 v[232:233], v156
	v_cndmask_b32_e64 v39, v41, v43, s[6:7]
	v_mul_f32_e32 v41, 0x37800000, v39
	v_cndmask_b32_e32 v39, v39, v41, vcc
	v_cmp_class_f32_e32 vcc, v3, v251
	v_cvt_pk_f32_fp8_e32 v[238:239], v154
	v_cvt_pk_f32_fp8_e32 v[244:245], v152
	v_cndmask_b32_e32 v3, v39, v3, vcc
	v_div_scale_f32 v39, s[6:7], v3, v3, 1.0
	v_rcp_f32_e32 v41, v39
	v_cvt_pk_f32_fp8_sdwa v[234:235], v156 src0_sel:WORD_1
	v_cvt_pk_f32_fp8_sdwa v[240:241], v154 src0_sel:WORD_1
	v_cvt_pk_f32_fp8_sdwa v[246:247], v152 src0_sel:WORD_1
	v_fma_f32 v43, -v39, v41, 1.0
	v_fmac_f32_e32 v41, v43, v41
	v_div_scale_f32 v43, vcc, 1.0, v3, 1.0
	v_mul_f32_e32 v45, v43, v41
	v_fma_f32 v147, -v39, v45, v43
	v_fmac_f32_e32 v45, v147, v41
	v_fma_f32 v39, -v39, v45, v43
	v_div_fmas_f32 v39, v39, v41, v45
	v_div_fixup_f32 v176, v39, v3, 1.0
	v_pk_mul_f32 v[168:169], v[168:169], v[176:177] op_sel_hi:[1,0]
	v_pk_mul_f32 v[170:171], v[170:171], v[176:177] op_sel_hi:[1,0]
	v_pk_mul_f32 v[30:31], v[30:31], v[176:177] op_sel_hi:[1,0]
	v_pk_mul_f32 v[34:35], v[34:35], v[176:177] op_sel_hi:[1,0]
	v_pk_mul_f32 v[172:173], v[172:173], v[176:177] op_sel_hi:[1,0]
	v_pk_mul_f32 v[174:175], v[174:175], v[176:177] op_sel_hi:[1,0]
	v_pk_mul_f32 v[36:37], v[36:37], v[176:177] op_sel_hi:[1,0]
	v_pk_mul_f32 v[28:29], v[28:29], v[176:177] op_sel_hi:[1,0]
	v_cvt_pk_f32_fp8_e32 v[176:177], v60
	v_cvt_pk_f32_fp8_sdwa v[60:61], v61 src0_sel:WORD_1
	s_waitcnt vmcnt(4)
	v_pk_fma_f32 v[34:35], v[64:65], v[34:35], v[92:93]
	v_pk_fma_f32 v[168:169], v[82:83], v[168:169], v[86:87]
	v_pk_mul_f32 v[176:177], v[44:45], v[176:177] op_sel_hi:[0,1]
	v_pk_mul_f32 v[60:61], v[44:45], v[60:61] op_sel_hi:[0,1]
	v_pk_fma_f32 v[34:35], v[34:35], s[60:61], v[60:61] op_sel_hi:[1,0,1]
	v_pk_fma_f32 v[168:169], v[168:169], s[60:61], v[176:177] op_sel_hi:[1,0,1]
	v_pk_fma_f32 v[34:35], v[42:43], v[58:59], v[34:35] op_sel_hi:[0,1,1]
	v_pk_fma_f32 v[34:35], v[40:41], v[56:57], v[34:35] op_sel_hi:[0,1,1]
	v_pk_fma_f32 v[34:35], v[38:39], v[54:55], v[34:35] op_sel_hi:[0,1,1]
	s_waitcnt vmcnt(2)
	v_pk_fma_f32 v[54:55], v[172:173], v[66:67], v[70:71]
	v_pk_mul_f32 v[56:57], v[44:45], v[200:201] op_sel_hi:[0,1]
	v_pk_fma_f32 v[30:31], v[84:85], v[30:31], v[88:89]
	v_pk_mul_f32 v[176:177], v[44:45], v[178:179] op_sel_hi:[0,1]
	v_pk_fma_f32 v[54:55], v[54:55], s[60:61], v[56:57] op_sel_hi:[1,0,1]
	v_pk_fma_f32 v[36:37], v[36:37], v[68:69], v[72:73]
	v_pk_mul_f32 v[56:57], v[44:45], v[204:205] op_sel_hi:[0,1]
	v_pk_fma_f32 v[30:31], v[30:31], s[60:61], v[176:177] op_sel_hi:[1,0,1]
	v_pk_mul_f32 v[176:177], v[44:45], v[180:181] op_sel_hi:[0,1]
	v_pk_fma_f32 v[36:37], v[36:37], s[60:61], v[56:57] op_sel_hi:[1,0,1]
	s_waitcnt vmcnt(0)
	v_pk_fma_f32 v[56:57], v[174:175], v[74:75], v[78:79]
	v_pk_mul_f32 v[58:59], v[44:45], v[206:207] op_sel_hi:[0,1]
	v_pk_fma_f32 v[28:29], v[28:29], v[76:77], v[80:81]
	v_pk_mul_f32 v[44:45], v[44:45], v[52:53] op_sel_hi:[0,1]
	v_pk_fma_f32 v[170:171], v[62:63], v[170:171], v[90:91]
	v_pk_fma_f32 v[56:57], v[56:57], s[60:61], v[58:59] op_sel_hi:[1,0,1]
	v_pk_fma_f32 v[28:29], v[28:29], s[60:61], v[44:45] op_sel_hi:[1,0,1]
	v_pk_fma_f32 v[170:171], v[170:171], s[60:61], v[176:177] op_sel_hi:[1,0,1]
	v_pk_fma_f32 v[56:57], v[42:43], v[212:213], v[56:57] op_sel_hi:[0,1,1]
	v_pk_fma_f32 v[28:29], v[42:43], v[50:51], v[28:29] op_sel_hi:[0,1,1]
	v_pk_fma_f32 v[168:169], v[42:43], v[182:183], v[168:169] op_sel_hi:[0,1,1]
	v_pk_fma_f32 v[30:31], v[42:43], v[184:185], v[30:31] op_sel_hi:[0,1,1]
	v_pk_fma_f32 v[170:171], v[42:43], v[186:187], v[170:171] op_sel_hi:[0,1,1]
	v_pk_fma_f32 v[54:55], v[42:43], v[208:209], v[54:55] op_sel_hi:[0,1,1]
	v_pk_fma_f32 v[36:37], v[42:43], v[210:211], v[36:37] op_sel_hi:[0,1,1]
	v_pk_fma_f32 v[56:57], v[40:41], v[218:219], v[56:57] op_sel_hi:[0,1,1]
	v_pk_fma_f32 v[28:29], v[40:41], v[48:49], v[28:29] op_sel_hi:[0,1,1]
	v_pk_fma_f32 v[168:169], v[40:41], v[188:189], v[168:169] op_sel_hi:[0,1,1]
	v_pk_fma_f32 v[30:31], v[40:41], v[190:191], v[30:31] op_sel_hi:[0,1,1]
	v_pk_fma_f32 v[170:171], v[40:41], v[192:193], v[170:171] op_sel_hi:[0,1,1]
	v_pk_fma_f32 v[54:55], v[40:41], v[214:215], v[54:55] op_sel_hi:[0,1,1]
	v_pk_fma_f32 v[36:37], v[40:41], v[216:217], v[36:37] op_sel_hi:[0,1,1]
	v_pk_fma_f32 v[56:57], v[38:39], v[230:231], v[56:57] op_sel_hi:[0,1,1]
	v_pk_fma_f32 v[28:29], v[38:39], v[46:47], v[28:29] op_sel_hi:[0,1,1]
	v_pk_fma_f32 v[168:169], v[38:39], v[194:195], v[168:169] op_sel_hi:[0,1,1]
	v_pk_fma_f32 v[30:31], v[38:39], v[196:197], v[30:31] op_sel_hi:[0,1,1]
	v_pk_fma_f32 v[170:171], v[38:39], v[198:199], v[170:171] op_sel_hi:[0,1,1]
	v_pk_fma_f32 v[54:55], v[38:39], v[226:227], v[54:55] op_sel_hi:[0,1,1]
	v_pk_fma_f32 v[36:37], v[38:39], v[228:229], v[36:37] op_sel_hi:[0,1,1]
	v_add_f32_e32 v3, v28, v29
	v_add_f32_e32 v38, v56, v57
	v_add_f32_e32 v3, v38, v3
	v_add_f32_e32 v38, v36, v37
	v_add_f32_e32 v39, v54, v55
	v_add_f32_e32 v38, v39, v38
	v_add_f32_e32 v3, v38, v3
	v_add_f32_e32 v38, v34, v35
	v_add_f32_e32 v39, v170, v171
	v_add_f32_e32 v38, v39, v38
	v_add_f32_e32 v39, v30, v31
	v_add_f32_e32 v40, v168, v169
	v_add_f32_e32 v39, v40, v39
	v_add_f32_e32 v38, v39, v38
	v_add_f32_e32 v3, v38, v3
	v_lshlrev_b32_e32 v184, 16, v27
	v_and_b32_e32 v185, 0xffff0000, v27
	v_add_f32_dpp v3, v3, v3 quad_perm:[1,0,3,2] row_mask:0xf bank_mask:0xf bound_ctrl:1
	v_lshlrev_b32_e32 v186, 16, v26
	v_and_b32_e32 v187, 0xffff0000, v26
	v_add_f32_dpp v3, v3, v3 quad_perm:[2,3,0,1] row_mask:0xf bank_mask:0xf bound_ctrl:1
	v_lshlrev_b32_e32 v26, 16, v25
	v_and_b32_e32 v27, 0xffff0000, v25
	v_add_f32_dpp v3, v3, v3 row_half_mirror row_mask:0xf bank_mask:0xf bound_ctrl:1
	v_lshlrev_b32_e32 v188, 16, v24
	v_and_b32_e32 v189, 0xffff0000, v24
	v_add_f32_dpp v3, v3, v3 row_mirror row_mask:0xf bank_mask:0xf bound_ctrl:1
	ds_swizzle_b32 v38, v3 offset:swizzle(SWAP,16)
	v_lshlrev_b32_e32 v24, 16, v23
	v_and_b32_e32 v25, 0xffff0000, v23
	v_lshlrev_b32_e32 v190, 16, v22
	v_and_b32_e32 v191, 0xffff0000, v22
	s_waitcnt lgkmcnt(0)
; __device__ __forceinline__ float wave_sum(float v) { v += dpp_f<0xB1>(v); v += dpp_f<0x4E>(v); v += dpp_f<0x141>(v); v += dpp_f<0x140>(v); v += xor_sw<16>(v); return sum_x32(v); }
; __device__ __forceinline__ void ln_row16(float (&v)[16], const float* lng, const float* lnb, int lane, float (&o)[16]) {
;     const float s = ((v[0] + v[1]) + (v[2] + v[3])) + ((v[4] + v[5]) + (v[6] + v[7])) + (((v[8] + v[9]) + (v[10] + v[11])) + ((v[12] + v[13]) + (v[14] + v[15])));
;     const float mean = wave_sum(s) * (1.0f / D);
; #pragma unroll
;     for (int i = 0; i < 16; ++i) v[i] -= mean;
;     const float s2 = ((v[0] * v[0] + v[1] * v[1]) + (v[2] * v[2] + v[3] * v[3])) + ((v[4] * v[4] + v[5] * v[5]) + (v[6] * v[6] + v[7] * v[7]))
;                    + (((v[8] * v[8] + v[9] * v[9]) + (v[10] * v[10] + v[11] * v[11])) + ((v[12] * v[12] + v[13] * v[13]) + (v[14] * v[14] + v[15] * v[15])));
;     const float rstd = 1.0f / sqrtf(wave_sum(s2) * (1.0f / D) + LN_EPS);
; #pragma unroll
;     for (int hf = 0; hf < 2; ++hf) { const int col = 512 * hf + 8 * lane;
;         const f32x4 g0 = *(const f32x4*)(lng + col), g1 = *(const f32x4*)(lng + col + 4), b0 = *(const f32x4*)(lnb + col), b1 = *(const f32x4*)(lnb + col + 4);
; #pragma unroll
;         for (int i = 0; i < 4; ++i) { o[8 * hf + i] = v[8 * hf + i] * rstd * g0[i] + b0[i]; o[8 * hf + 4 + i] = v[8 * hf + 4 + i] * rstd * g1[i] + b1[i]; } }
; __global__ void __launch_bounds__(NWAVES * 64, 2) mk_fwd(Args args) {
;     ...
;                     ln_row16(v, lng, lnb, lane, o[j]);
	v_add_f32_e32 v3, v3, v38
	v_mov_b32_e32 v38, v3
	s_nop 1
	v_permlane32_swap_b32_e32 v3, v38
	v_add_f32_e32 v3, v3, v38
	v_mul_f32_e32 v38, 0x3a800000, v3
	v_pk_add_f32 v[176:177], v[168:169], v[38:39] op_sel_hi:[1,0] neg_lo:[0,1] neg_hi:[0,1]
	v_pk_add_f32 v[178:179], v[30:31], v[38:39] op_sel_hi:[1,0] neg_lo:[0,1] neg_hi:[0,1]
	v_pk_add_f32 v[180:181], v[170:171], v[38:39] op_sel_hi:[1,0] neg_lo:[0,1] neg_hi:[0,1]
	v_pk_add_f32 v[182:183], v[34:35], v[38:39] op_sel_hi:[1,0] neg_lo:[0,1] neg_hi:[0,1]
	v_pk_add_f32 v[172:173], v[54:55], v[38:39] op_sel_hi:[1,0] neg_lo:[0,1] neg_hi:[0,1]
	v_pk_add_f32 v[168:169], v[36:37], v[38:39] op_sel_hi:[1,0] neg_lo:[0,1] neg_hi:[0,1]
	v_pk_add_f32 v[174:175], v[56:57], v[38:39] op_sel_hi:[1,0] neg_lo:[0,1] neg_hi:[0,1]
	v_pk_add_f32 v[170:171], v[28:29], v[38:39] op_sel_hi:[1,0] neg_lo:[0,1] neg_hi:[0,1]
	v_pk_mul_f32 v[28:29], v[176:177], v[176:177]
	v_pk_mul_f32 v[30:31], v[178:179], v[178:179]
	v_pk_mul_f32 v[34:35], v[180:181], v[180:181]
	v_pk_mul_f32 v[36:37], v[182:183], v[182:183]
	v_pk_mul_f32 v[38:39], v[172:173], v[172:173]
	v_pk_mul_f32 v[40:41], v[168:169], v[168:169]
	v_pk_mul_f32 v[42:43], v[174:175], v[174:175]
	v_pk_mul_f32 v[44:45], v[170:171], v[170:171]
	v_add_f32_e32 v42, v42, v43
	v_add_f32_e32 v3, v44, v45
	v_add_f32_e32 v40, v40, v41
	v_add_f32_e32 v38, v38, v39
	v_add_f32_e32 v36, v36, v37
	v_add_f32_e32 v34, v34, v35
	v_add_f32_e32 v30, v30, v31
	v_add_f32_e32 v28, v28, v29
	v_add_f32_e32 v3, v42, v3
	v_add_f32_e32 v38, v38, v40
	v_add_f32_e32 v34, v34, v36
	v_add_f32_e32 v28, v28, v30
	v_add_f32_e32 v3, v38, v3
	v_add_f32_e32 v28, v28, v34
	v_add_f32_e32 v3, v28, v3
	v_lshlrev_b32_e32 v22, 16, v21
	v_and_b32_e32 v23, 0xffff0000, v21
	v_add_f32_dpp v3, v3, v3 quad_perm:[1,0,3,2] row_mask:0xf bank_mask:0xf bound_ctrl:1
	v_lshlrev_b32_e32 v192, 16, v20
	v_and_b32_e32 v193, 0xffff0000, v20
	v_add_f32_dpp v3, v3, v3 quad_perm:[2,3,0,1] row_mask:0xf bank_mask:0xf bound_ctrl:1
	v_add_f32_e32 v20, v185, v184
	v_add_f32_e32 v21, v187, v186
	v_add_f32_dpp v3, v3, v3 row_half_mirror row_mask:0xf bank_mask:0xf bound_ctrl:1
	v_add_f32_e32 v20, v21, v20
	v_add_f32_e32 v21, v27, v26
	v_add_f32_dpp v3, v3, v3 row_mirror row_mask:0xf bank_mask:0xf bound_ctrl:1
	ds_swizzle_b32 v28, v3 offset:swizzle(SWAP,16)
	v_add_f32_e32 v194, v189, v188
	v_add_f32_e32 v21, v194, v21
	v_add_f32_e32 v20, v21, v20
	v_add_f32_e32 v21, v25, v24
	s_waitcnt lgkmcnt(0)
	v_add_f32_e32 v3, v3, v28
	v_mov_b32_e32 v28, v3
	s_nop 1
	v_permlane32_swap_b32_e32 v3, v28
	v_add_f32_e32 v3, v3, v28
	v_fmamk_f32 v3, v3, 0x3a800000, v250
	v_mul_f32_e32 v28, 0x4f800000, v3
	v_cmp_gt_f32_e32 vcc, s11, v3
	v_add_f32_e32 v194, v191, v190
	v_add_f32_e32 v21, v194, v21
	v_cndmask_b32_e32 v3, v3, v28, vcc
	global_load_dwordx4 v[28:31], v[102:103], off offset:16
	global_load_dwordx4 v[38:41], v[102:103], off
	global_load_dwordx4 v[34:37], v[104:105], off offset:16
	global_load_dwordx4 v[42:45], v[104:105], off
	v_sqrt_f32_e32 v46, v3
	v_add_f32_e32 v194, v23, v22
	v_add_f32_e32 v195, v193, v192
	v_add_f32_e32 v194, v195, v194
	v_add_u32_e32 v47, -1, v46
	v_fma_f32 v48, -v47, v46, v3
	v_cmp_ge_f32_e64 s[6:7], 0, v48
	v_add_u32_e32 v48, 1, v46
	v_add_f32_e32 v21, v194, v21
	v_cndmask_b32_e64 v47, v46, v47, s[6:7]
	v_fma_f32 v46, -v48, v46, v3
	v_add_f32_e32 v20, v21, v20
	v_cmp_lt_f32_e64 s[6:7], 0, v46
	v_cvt_pk_f32_fp8_e32 v[212:213], v163
	v_add_f32_dpp v20, v20, v20 quad_perm:[1,0,3,2] row_mask:0xf bank_mask:0xf bound_ctrl:1
	v_cndmask_b32_e64 v46, v47, v48, s[6:7]
	v_mul_f32_e32 v47, 0x37800000, v46
	v_add_f32_dpp v20, v20, v20 quad_perm:[2,3,0,1] row_mask:0xf bank_mask:0xf bound_ctrl:1
	v_cndmask_b32_e32 v46, v46, v47, vcc
	v_cmp_class_f32_e32 vcc, v3, v251
	v_add_f32_dpp v20, v20, v20 row_half_mirror row_mask:0xf bank_mask:0xf bound_ctrl:1
	v_cvt_pk_f32_fp8_e32 v[218:219], v161
	v_cndmask_b32_e32 v3, v46, v3, vcc
	v_add_f32_dpp v20, v20, v20 row_mirror row_mask:0xf bank_mask:0xf bound_ctrl:1
	ds_swizzle_b32 v21, v20 offset:swizzle(SWAP,16)
	v_div_scale_f32 v147, s[6:7], v3, v3, 1.0
	v_rcp_f32_e32 v149, v147
	global_load_dwordx4 v[46:49], v[102:103], off offset:2064
	global_load_dwordx4 v[54:57], v[102:103], off offset:2048
	global_load_dwordx4 v[50:53], v[104:105], off offset:2064
	global_load_dwordx4 v[58:61], v[104:105], off offset:2048
	s_waitcnt lgkmcnt(0)
; __device__ __forceinline__ void unpack8(const u32x4 w, float (&f)[8]) { f[0] = bf_lo(w.x); f[1] = bf_hi(w.x); f[2] = bf_lo(w.y); f[3] = bf_hi(w.y); f[4] = bf_lo(w.z); f[5] = bf_hi(w.z); f[6] = bf_lo(w.w); f[7] = bf_hi(w.w); }
; __device__ __forceinline__ void ln_row16(float (&v)[16], const float* lng, const float* lnb, int lane, float (&o)[16]) {
;     const float s = ((v[0] + v[1]) + (v[2] + v[3])) + ((v[4] + v[5]) + (v[6] + v[7])) + (((v[8] + v[9]) + (v[10] + v[11])) + ((v[12] + v[13]) + (v[14] + v[15])));
;     const float mean = wave_sum(s) * (1.0f / D);
; #pragma unroll
;     for (int i = 0; i < 16; ++i) v[i] -= mean;
;     const float s2 = ((v[0] * v[0] + v[1] * v[1]) + (v[2] * v[2] + v[3] * v[3])) + ((v[4] * v[4] + v[5] * v[5]) + (v[6] * v[6] + v[7] * v[7]))
;                    + (((v[8] * v[8] + v[9] * v[9]) + (v[10] * v[10] + v[11] * v[11])) + ((v[12] * v[12] + v[13] * v[13]) + (v[14] * v[14] + v[15] * v[15])));
;     const float rstd = 1.0f / sqrtf(wave_sum(s2) * (1.0f / D) + LN_EPS);
; #pragma unroll
;     for (int hf = 0; hf < 2; ++hf) { const int col = 512 * hf + 8 * lane;
;         const f32x4 g0 = *(const f32x4*)(lng + col), g1 = *(const f32x4*)(lng + col + 4), b0 = *(const f32x4*)(lnb + col), b1 = *(const f32x4*)(lnb + col + 4);
; #pragma unroll
;         for (int i = 0; i < 4; ++i) { o[8 * hf + i] = v[8 * hf + i] * rstd * g0[i] + b0[i]; o[8 * hf + 4 + i] = v[8 * hf + 4 + i] * rstd * g1[i] + b1[i]; } }
; __global__ void __launch_bounds__(NWAVES * 64, 2) mk_fwd(Args args) {
;     ...
;                     float v[16], x1[16];
; #pragma unroll
;                     for (int hf = 0; hf < 2; ++hf) { float f[8]; unpack8(xr[j][hf], f);
; #pragma unroll
;                         for (int i = 0; i < 8; ++i) v[8 * hf + i] = f[i]; }
;                     ln_row16(v, lng1, lnb1, lane, x1);
; #pragma unroll
;                     for (int hf = 0; hf < 2; ++hf) { float f[8];
; #pragma unroll
;                         for (int i = 0; i < 8; ++i) v[8 * hf + i] = ALPHA * x1[8 * hf + i];
; #pragma unroll
;                         for (int k = 0; k < 4; ++k) { unpack8_f8(yr[j][k][hf], f);
; #pragma unroll
;                             for (int i = 0; i < 8; ++i) v[8 * hf + i] += gt[j][k] * f[i]; } }
;                     ln_row16(v, lng, lnb, lane, o[j]);
	v_add_f32_e32 v20, v20, v21
	v_mov_b32_e32 v21, v20
	v_fma_f32 v151, -v147, v149, 1.0
	v_fmac_f32_e32 v149, v151, v149
	v_div_scale_f32 v151, vcc, 1.0, v3, 1.0
	v_permlane32_swap_b32_e32 v20, v21
	v_mul_f32_e32 v202, v151, v149
	v_add_f32_e32 v20, v20, v21
	v_fma_f32 v194, -v147, v202, v151
	v_mul_f32_e32 v20, 0x3a800000, v20
	v_fmac_f32_e32 v202, v194, v149
	v_pk_add_f32 v[192:193], v[192:193], v[20:21] op_sel_hi:[1,0] neg_lo:[0,1] neg_hi:[0,1]
	v_pk_add_f32 v[194:195], v[22:23], v[20:21] op_sel_hi:[1,0] neg_lo:[0,1] neg_hi:[0,1]
	v_pk_add_f32 v[190:191], v[190:191], v[20:21] op_sel_hi:[1,0] neg_lo:[0,1] neg_hi:[0,1]
	v_pk_add_f32 v[196:197], v[24:25], v[20:21] op_sel_hi:[1,0] neg_lo:[0,1] neg_hi:[0,1]
	v_pk_add_f32 v[188:189], v[188:189], v[20:21] op_sel_hi:[1,0] neg_lo:[0,1] neg_hi:[0,1]
	v_pk_add_f32 v[198:199], v[26:27], v[20:21] op_sel_hi:[1,0] neg_lo:[0,1] neg_hi:[0,1]
	v_pk_add_f32 v[186:187], v[186:187], v[20:21] op_sel_hi:[1,0] neg_lo:[0,1] neg_hi:[0,1]
	v_pk_add_f32 v[184:185], v[184:185], v[20:21] op_sel_hi:[1,0] neg_lo:[0,1] neg_hi:[0,1]
	v_pk_mul_f32 v[20:21], v[192:193], v[192:193]
	v_pk_mul_f32 v[22:23], v[194:195], v[194:195]
	v_pk_mul_f32 v[24:25], v[190:191], v[190:191]
	v_pk_mul_f32 v[26:27], v[196:197], v[196:197]
	v_pk_mul_f32 v[200:201], v[188:189], v[188:189]
	v_pk_mul_f32 v[204:205], v[198:199], v[198:199]
	v_pk_mul_f32 v[206:207], v[186:187], v[186:187]
	v_pk_mul_f32 v[208:209], v[184:185], v[184:185]
	v_fma_f32 v147, -v147, v202, v151
	v_add_f32_e32 v151, v208, v209
	v_add_f32_e32 v206, v206, v207
	v_add_f32_e32 v204, v204, v205
	v_add_f32_e32 v200, v200, v201
	v_add_f32_e32 v26, v26, v27
	v_add_f32_e32 v24, v24, v25
	v_add_f32_e32 v22, v22, v23
	v_add_f32_e32 v20, v20, v21
	v_add_f32_e32 v151, v206, v151
	v_add_f32_e32 v200, v200, v204
	v_add_f32_e32 v24, v24, v26
	v_add_f32_e32 v20, v20, v22
	v_add_f32_e32 v151, v200, v151
	v_add_f32_e32 v20, v20, v24
	v_add_f32_e32 v20, v20, v151
	v_cvt_pk_f32_fp8_e32 v[206:207], v165
	v_cvt_pk_f32_fp8_sdwa v[204:205], v164 src0_sel:WORD_1
	v_add_f32_dpp v20, v20, v20 quad_perm:[1,0,3,2] row_mask:0xf bank_mask:0xf bound_ctrl:1
	v_cvt_pk_f32_fp8_e32 v[208:209], v162
	v_cvt_pk_f32_fp8_sdwa v[210:211], v162 src0_sel:WORD_1
	v_add_f32_dpp v20, v20, v20 quad_perm:[2,3,0,1] row_mask:0xf bank_mask:0xf bound_ctrl:1
	v_cvt_pk_f32_fp8_sdwa v[162:163], v163 src0_sel:WORD_1
	v_cvt_pk_f32_fp8_e32 v[214:215], v160
	v_add_f32_dpp v20, v20, v20 row_half_mirror row_mask:0xf bank_mask:0xf bound_ctrl:1
	v_cvt_pk_f32_fp8_sdwa v[216:217], v160 src0_sel:WORD_1
	v_cvt_pk_f32_fp8_sdwa v[160:161], v161 src0_sel:WORD_1
	v_add_f32_dpp v24, v20, v20 row_mirror row_mask:0xf bank_mask:0xf bound_ctrl:1
	ds_swizzle_b32 v25, v24 offset:swizzle(SWAP,16)
	v_div_fmas_f32 v20, v147, v149, v202
	v_div_fixup_f32 v200, v20, v3, 1.0
	v_pk_mul_f32 v[20:21], v[176:177], v[200:201] op_sel_hi:[1,0]
	v_pk_mul_f32 v[22:23], v[180:181], v[200:201] op_sel_hi:[1,0]
	s_waitcnt lgkmcnt(0)
	v_add_f32_e32 v3, v24, v25
	v_mov_b32_e32 v24, v3
	s_nop 1
	v_permlane32_swap_b32_e32 v3, v24
	v_add_f32_e32 v3, v3, v24
	v_fmamk_f32 v3, v3, 0x3a800000, v250
	v_mul_f32_e32 v24, 0x4f800000, v3
	v_cmp_gt_f32_e32 vcc, s11, v3
	v_pk_mul_f32 v[176:177], v[182:183], v[200:201] op_sel_hi:[1,0]
	v_cvt_pk_f32_fp8_e32 v[226:227], v158
	v_cndmask_b32_e32 v3, v3, v24, vcc
	v_sqrt_f32_e32 v26, v3
	s_waitcnt vmcnt(4)
	v_pk_fma_f32 v[24:25], v[38:39], v[20:21], v[42:43]
	v_pk_fma_f32 v[20:21], v[28:29], v[22:23], v[34:35]
	v_pk_mul_f32 v[22:23], v[178:179], v[200:201] op_sel_hi:[1,0]
	v_add_u32_e32 v27, -1, v26
	v_fma_f32 v147, -v27, v26, v3
	v_cmp_ge_f32_e64 s[6:7], 0, v147
	v_add_u32_e32 v147, 1, v26
	v_cvt_pk_f32_fp8_sdwa v[228:229], v158 src0_sel:WORD_1
	v_cndmask_b32_e64 v27, v26, v27, s[6:7]
	v_fma_f32 v26, -v147, v26, v3
	v_cmp_lt_f32_e64 s[6:7], 0, v26
	v_cvt_pk_f32_fp8_e32 v[230:231], v159
	v_cvt_pk_f32_fp8_e32 v[236:237], v157
	v_cndmask_b32_e64 v26, v27, v147, s[6:7]
	v_mul_f32_e32 v27, 0x37800000, v26
	v_cndmask_b32_e32 v26, v26, v27, vcc
	v_cmp_class_f32_e32 vcc, v3, v251
	v_cvt_pk_f32_fp8_e32 v[242:243], v155
	v_cvt_pk_f32_fp8_sdwa v[158:159], v159 src0_sel:WORD_1
	v_cndmask_b32_e32 v3, v26, v3, vcc
	v_div_scale_f32 v147, s[6:7], v3, v3, 1.0
	v_rcp_f32_e32 v149, v147
	v_pk_fma_f32 v[26:27], v[40:41], v[22:23], v[44:45]
	v_pk_fma_f32 v[22:23], v[30:31], v[176:177], v[36:37]
	v_cvt_pk_f32_fp8_e32 v[248:249], v153
	v_fma_f32 v151, -v147, v149, 1.0
	v_fmac_f32_e32 v149, v151, v149
	v_div_scale_f32 v151, vcc, 1.0, v3, 1.0
	v_mul_f32_e32 v176, v151, v149
	v_fma_f32 v177, -v147, v176, v151
	v_fmac_f32_e32 v176, v177, v149
	v_fma_f32 v147, -v147, v176, v151
	v_div_fmas_f32 v147, v147, v149, v176
	v_div_fixup_f32 v176, v147, v3, 1.0
	v_pk_mul_f32 v[178:179], v[192:193], v[176:177] op_sel_hi:[1,0]
	v_pk_mul_f32 v[180:181], v[190:191], v[176:177] op_sel_hi:[1,0]
	v_pk_mul_f32 v[182:183], v[194:195], v[176:177] op_sel_hi:[1,0]
	v_pk_mul_f32 v[190:191], v[196:197], v[176:177] op_sel_hi:[1,0]
	v_pk_mul_f32 v[188:189], v[188:189], v[176:177] op_sel_hi:[1,0]
	v_pk_mul_f32 v[186:187], v[186:187], v[176:177] op_sel_hi:[1,0]
	v_pk_mul_f32 v[192:193], v[198:199], v[176:177] op_sel_hi:[1,0]
	v_pk_mul_f32 v[176:177], v[184:185], v[176:177] op_sel_hi:[1,0]
	v_cvt_pk_f32_fp8_e32 v[184:185], v166
	v_cvt_pk_f32_fp8_sdwa v[194:195], v166 src0_sel:WORD_1
	v_cvt_pk_f32_fp8_e32 v[196:197], v167
	v_pk_fma_f32 v[82:83], v[82:83], v[178:179], v[86:87]
	v_pk_mul_f32 v[86:87], v[150:151], v[184:185] op_sel_hi:[0,1]
	v_pk_fma_f32 v[82:83], v[82:83], s[60:61], v[86:87] op_sel_hi:[1,0,1]
	v_pk_fma_f32 v[84:85], v[84:85], v[182:183], v[88:89]
; __device__ __forceinline__ float wave_sum(float v) { v += dpp_f<0xB1>(v); v += dpp_f<0x4E>(v); v += dpp_f<0x141>(v); v += dpp_f<0x140>(v); v += xor_sw<16>(v); return sum_x32(v); }
; __device__ __forceinline__ void ln_row16(float (&v)[16], const float* lng, const float* lnb, int lane, float (&o)[16]) {
;     const float s = ((v[0] + v[1]) + (v[2] + v[3])) + ((v[4] + v[5]) + (v[6] + v[7])) + (((v[8] + v[9]) + (v[10] + v[11])) + ((v[12] + v[13]) + (v[14] + v[15])));
;     const float mean = wave_sum(s) * (1.0f / D);
; #pragma unroll
;     for (int i = 0; i < 16; ++i) v[i] -= mean;
;     const float s2 = ((v[0] * v[0] + v[1] * v[1]) + (v[2] * v[2] + v[3] * v[3])) + ((v[4] * v[4] + v[5] * v[5]) + (v[6] * v[6] + v[7] * v[7]))
;                    + (((v[8] * v[8] + v[9] * v[9]) + (v[10] * v[10] + v[11] * v[11])) + ((v[12] * v[12] + v[13] * v[13]) + (v[14] * v[14] + v[15] * v[15])));
;     const float rstd = 1.0f / sqrtf(wave_sum(s2) * (1.0f / D) + LN_EPS);
; #pragma unroll
;     for (int hf = 0; hf < 2; ++hf) { const int col = 512 * hf + 8 * lane;
;         const f32x4 g0 = *(const f32x4*)(lng + col), g1 = *(const f32x4*)(lng + col + 4), b0 = *(const f32x4*)(lnb + col), b1 = *(const f32x4*)(lnb + col + 4);
; #pragma unroll
;         for (int i = 0; i < 4; ++i) { o[8 * hf + i] = v[8 * hf + i] * rstd * g0[i] + b0[i]; o[8 * hf + 4 + i] = v[8 * hf + 4 + i] * rstd * g1[i] + b1[i]; } }
; __global__ void __launch_bounds__(NWAVES * 64, 2) mk_fwd(Args args) {
;     ...
;                     for (int hf = 0; hf < 2; ++hf) { float f[8];
; #pragma unroll
;                         for (int i = 0; i < 8; ++i) v[8 * hf + i] = ALPHA * x1[8 * hf + i];
; #pragma unroll
;                         for (int k = 0; k < 4; ++k) { unpack8_f8(yr[j][k][hf], f);
; #pragma unroll
;                             for (int i = 0; i < 8; ++i) v[8 * hf + i] += gt[j][k] * f[i]; } }
;                     ln_row16(v, lng, lnb, lane, o[j]);
	v_pk_mul_f32 v[86:87], v[150:151], v[194:195] op_sel_hi:[0,1]
	v_cvt_pk_f32_fp8_sdwa v[166:167], v167 src0_sel:WORD_1
	v_pk_fma_f32 v[84:85], v[84:85], s[60:61], v[86:87] op_sel_hi:[1,0,1]
	v_pk_fma_f32 v[62:63], v[62:63], v[180:181], v[90:91]
	v_pk_mul_f32 v[86:87], v[150:151], v[196:197] op_sel_hi:[0,1]
	v_pk_fma_f32 v[62:63], v[62:63], s[60:61], v[86:87] op_sel_hi:[1,0,1]
	v_cvt_pk_f32_fp8_e32 v[198:199], v164
	v_cvt_pk_f32_fp8_sdwa v[164:165], v165 src0_sel:WORD_1
	v_pk_fma_f32 v[62:63], v[148:149], v[206:207], v[62:63] op_sel_hi:[0,1,1]
	v_pk_fma_f32 v[62:63], v[146:147], v[212:213], v[62:63] op_sel_hi:[0,1,1]
	v_pk_fma_f32 v[86:87], v[32:33], v[218:219], v[62:63] op_sel_hi:[0,1,1]
	v_pk_fma_f32 v[62:63], v[64:65], v[190:191], v[92:93]
	v_pk_mul_f32 v[64:65], v[150:151], v[166:167] op_sel_hi:[0,1]
	v_pk_fma_f32 v[62:63], v[62:63], s[60:61], v[64:65] op_sel_hi:[1,0,1]
	v_cvt_pk_f32_fp8_sdwa v[156:157], v157 src0_sel:WORD_1
	v_pk_fma_f32 v[62:63], v[148:149], v[164:165], v[62:63] op_sel_hi:[0,1,1]
	v_pk_fma_f32 v[62:63], v[146:147], v[162:163], v[62:63] op_sel_hi:[0,1,1]
	v_pk_fma_f32 v[64:65], v[32:33], v[160:161], v[62:63] op_sel_hi:[0,1,1]
	v_pk_fma_f32 v[62:63], v[188:189], v[66:67], v[70:71]
	v_pk_mul_f32 v[66:67], v[150:151], v[226:227] op_sel_hi:[0,1]
	v_pk_fma_f32 v[62:63], v[62:63], s[60:61], v[66:67] op_sel_hi:[1,0,1]
	v_pk_mul_f32 v[66:67], v[150:151], v[228:229] op_sel_hi:[0,1]
	v_pk_fma_f32 v[62:63], v[148:149], v[232:233], v[62:63] op_sel_hi:[0,1,1]
	v_pk_fma_f32 v[62:63], v[146:147], v[238:239], v[62:63] op_sel_hi:[0,1,1]
	v_pk_fma_f32 v[70:71], v[32:33], v[244:245], v[62:63] op_sel_hi:[0,1,1]
	v_pk_fma_f32 v[62:63], v[192:193], v[68:69], v[72:73]
	v_cvt_pk_f32_fp8_sdwa v[154:155], v155 src0_sel:WORD_1
	v_pk_fma_f32 v[62:63], v[62:63], s[60:61], v[66:67] op_sel_hi:[1,0,1]
	v_pk_mul_f32 v[66:67], v[150:151], v[230:231] op_sel_hi:[0,1]
	v_pk_fma_f32 v[62:63], v[148:149], v[234:235], v[62:63] op_sel_hi:[0,1,1]
	v_pk_fma_f32 v[62:63], v[146:147], v[240:241], v[62:63] op_sel_hi:[0,1,1]
	v_pk_fma_f32 v[68:69], v[32:33], v[246:247], v[62:63] op_sel_hi:[0,1,1]
	v_pk_fma_f32 v[62:63], v[186:187], v[74:75], v[78:79]
	v_cvt_pk_f32_fp8_sdwa v[152:153], v153 src0_sel:WORD_1
	v_pk_fma_f32 v[62:63], v[62:63], s[60:61], v[66:67] op_sel_hi:[1,0,1]
	v_pk_mul_f32 v[66:67], v[150:151], v[158:159] op_sel_hi:[0,1]
	v_pk_fma_f32 v[62:63], v[148:149], v[236:237], v[62:63] op_sel_hi:[0,1,1]
	v_pk_fma_f32 v[62:63], v[146:147], v[242:243], v[62:63] op_sel_hi:[0,1,1]
	v_pk_fma_f32 v[72:73], v[32:33], v[248:249], v[62:63] op_sel_hi:[0,1,1]
	v_pk_fma_f32 v[62:63], v[176:177], v[76:77], v[80:81]
	v_pk_fma_f32 v[82:83], v[148:149], v[198:199], v[82:83] op_sel_hi:[0,1,1]
	v_pk_fma_f32 v[62:63], v[62:63], s[60:61], v[66:67] op_sel_hi:[1,0,1]
	v_pk_fma_f32 v[84:85], v[148:149], v[204:205], v[84:85] op_sel_hi:[0,1,1]
	v_pk_fma_f32 v[62:63], v[148:149], v[156:157], v[62:63] op_sel_hi:[0,1,1]
	v_pk_fma_f32 v[62:63], v[146:147], v[154:155], v[62:63] op_sel_hi:[0,1,1]
	v_pk_fma_f32 v[82:83], v[146:147], v[208:209], v[82:83] op_sel_hi:[0,1,1]
	v_pk_fma_f32 v[84:85], v[146:147], v[210:211], v[84:85] op_sel_hi:[0,1,1]
	v_pk_fma_f32 v[88:89], v[32:33], v[152:153], v[62:63] op_sel_hi:[0,1,1]
	v_pk_fma_f32 v[82:83], v[32:33], v[214:215], v[82:83] op_sel_hi:[0,1,1]
	v_pk_fma_f32 v[84:85], v[32:33], v[216:217], v[84:85] op_sel_hi:[0,1,1]
	v_add_f32_e32 v3, v88, v89
	v_add_f32_e32 v32, v72, v73
	v_add_f32_e32 v3, v32, v3
	v_add_f32_e32 v32, v68, v69
	v_add_f32_e32 v62, v70, v71
	v_add_f32_e32 v32, v62, v32
	v_add_f32_e32 v3, v32, v3
	v_add_f32_e32 v32, v64, v65
	v_add_f32_e32 v62, v86, v87
	v_add_f32_e32 v32, v62, v32
	v_add_f32_e32 v62, v84, v85
	v_add_f32_e32 v63, v82, v83
	v_add_f32_e32 v62, v63, v62
	v_add_f32_e32 v32, v62, v32
	v_add_f32_e32 v3, v32, v3
	v_pk_mul_f32 v[62:63], v[172:173], v[200:201] op_sel_hi:[1,0]
	v_pk_mul_f32 v[74:75], v[174:175], v[200:201] op_sel_hi:[1,0]
	v_add_f32_dpp v3, v3, v3 quad_perm:[1,0,3,2] row_mask:0xf bank_mask:0xf bound_ctrl:1
	s_waitcnt vmcnt(0)
	v_pk_fma_f32 v[66:67], v[62:63], v[54:55], v[58:59]
	v_pk_fma_f32 v[62:63], v[74:75], v[46:47], v[50:51]
	v_add_f32_dpp v3, v3, v3 quad_perm:[2,3,0,1] row_mask:0xf bank_mask:0xf bound_ctrl:1
	s_mov_b64 s[6:7], -1
	s_and_b64 vcc, exec, s[8:9]
	v_add_f32_dpp v3, v3, v3 row_half_mirror row_mask:0xf bank_mask:0xf bound_ctrl:1
	s_nop 1
	v_add_f32_dpp v3, v3, v3 row_mirror row_mask:0xf bank_mask:0xf bound_ctrl:1
	ds_swizzle_b32 v32, v3 offset:swizzle(SWAP,16)
	s_waitcnt lgkmcnt(0)
	v_add_f32_e32 v3, v3, v32
	v_mov_b32_e32 v32, v3
	s_nop 1
	v_permlane32_swap_b32_e32 v3, v32
	v_add_f32_e32 v3, v3, v32
	v_mul_f32_e32 v32, 0x3a800000, v3
	v_pk_add_f32 v[76:77], v[72:73], v[32:33] op_sel_hi:[1,0] neg_lo:[0,1] neg_hi:[0,1]
	v_pk_add_f32 v[72:73], v[88:89], v[32:33] op_sel_hi:[1,0] neg_lo:[0,1] neg_hi:[0,1]
	v_pk_add_f32 v[74:75], v[70:71], v[32:33] op_sel_hi:[1,0] neg_lo:[0,1] neg_hi:[0,1]
	v_pk_add_f32 v[70:71], v[68:69], v[32:33] op_sel_hi:[1,0] neg_lo:[0,1] neg_hi:[0,1]
	v_pk_mul_f32 v[146:147], v[76:77], v[76:77]
	v_pk_mul_f32 v[148:149], v[72:73], v[72:73]
	v_pk_add_f32 v[82:83], v[82:83], v[32:33] op_sel_hi:[1,0] neg_lo:[0,1] neg_hi:[0,1]
	v_pk_add_f32 v[78:79], v[84:85], v[32:33] op_sel_hi:[1,0] neg_lo:[0,1] neg_hi:[0,1]
	v_pk_add_f32 v[84:85], v[86:87], v[32:33] op_sel_hi:[1,0] neg_lo:[0,1] neg_hi:[0,1]
	v_pk_add_f32 v[80:81], v[64:65], v[32:33] op_sel_hi:[1,0] neg_lo:[0,1] neg_hi:[0,1]
	v_pk_mul_f32 v[90:91], v[74:75], v[74:75]
	v_pk_mul_f32 v[92:93], v[70:71], v[70:71]
	v_add_f32_e32 v3, v148, v149
	v_add_f32_e32 v32, v146, v147
	v_add_f32_e32 v3, v32, v3
	v_add_f32_e32 v32, v92, v93
	v_add_f32_e32 v90, v90, v91
	v_pk_mul_f32 v[64:65], v[82:83], v[82:83]
	v_pk_mul_f32 v[68:69], v[78:79], v[78:79]
	v_pk_mul_f32 v[86:87], v[84:85], v[84:85]
	v_pk_mul_f32 v[88:89], v[80:81], v[80:81]
	v_add_f32_e32 v32, v90, v32
	v_add_f32_e32 v3, v32, v3
	v_add_f32_e32 v32, v88, v89
	v_add_f32_e32 v86, v86, v87
	v_add_f32_e32 v68, v68, v69
	v_add_f32_e32 v64, v64, v65
	v_add_f32_e32 v32, v86, v32
	v_add_f32_e32 v64, v64, v68
	v_add_f32_e32 v32, v64, v32
	v_add_f32_e32 v3, v32, v3
	v_pk_mul_f32 v[64:65], v[168:169], v[200:201] op_sel_hi:[1,0]
	v_pk_mul_f32 v[86:87], v[170:171], v[200:201] op_sel_hi:[1,0]
	v_add_f32_dpp v3, v3, v3 quad_perm:[1,0,3,2] row_mask:0xf bank_mask:0xf bound_ctrl:1
	v_pk_fma_f32 v[68:69], v[64:65], v[56:57], v[60:61]
	v_pk_fma_f32 v[64:65], v[86:87], v[48:49], v[52:53]
	v_add_f32_dpp v3, v3, v3 quad_perm:[2,3,0,1] row_mask:0xf bank_mask:0xf bound_ctrl:1
	s_nop 1
	v_add_f32_dpp v3, v3, v3 row_half_mirror row_mask:0xf bank_mask:0xf bound_ctrl:1
	s_nop 1
	v_add_f32_dpp v3, v3, v3 row_mirror row_mask:0xf bank_mask:0xf bound_ctrl:1
	ds_swizzle_b32 v32, v3 offset:swizzle(SWAP,16)
	s_waitcnt lgkmcnt(0)
	v_add_f32_e32 v3, v3, v32
	v_mov_b32_e32 v32, v3
	s_nop 1
	v_permlane32_swap_b32_e32 v3, v32
	s_cbranch_vccz .LBB0_711
; __device__ __forceinline__ u32x4 pack8(const float (&f)[8]) { u32x4 o; o.x = cvt_pk_bf16(f[0], f[1]); o.y = cvt_pk_bf16(f[2], f[3]); o.z = cvt_pk_bf16(f[4], f[5]); o.w = cvt_pk_bf16(f[6], f[7]); return o; }
; __device__ __forceinline__ float wave_max(float v) { v = fmaxf(v, dpp_f<0xB1>(v)); v = fmaxf(v, dpp_f<0x4E>(v)); v = fmaxf(v, dpp_f<0x141>(v)); v = fmaxf(v, dpp_f<0x140>(v)); v = fmaxf(v, xor_sw<16>(v)); return max_x32(v); }
; __device__ __forceinline__ float q8_row16(const float (&o)[16], unsigned char* qrow, int lane) {
;     float am = 0.f;
; #pragma unroll
;     for (int i = 0; i < 16; ++i) am = fmaxf(am, fabsf(o[i]));
;     am = wave_max(am);
;     const float qs = am > 0.f ? am * (1.0f / 127.0f) : 1.0f, qinv = 1.0f / qs;
; #pragma unroll
;     for (int hf = 0; hf < 2; ++hf) { u32x2 q; q.x = q8x4(o[8 * hf], o[8 * hf + 1], o[8 * hf + 2], o[8 * hf + 3], qinv); q.y = q8x4(o[8 * hf + 4], o[8 * hf + 5], o[8 * hf + 6], o[8 * hf + 7], qinv);
;         *(u32x2*)(qrow + 512 * hf + 8 * lane) = q; }
;     return qs;
; }
; __device__ __forceinline__ void store_bf16_row16(const float (&o)[16], bf16_t* row, int lane) {
; #pragma unroll
;     for (int hf = 0; hf < 2; ++hf) { const float (&oh)[8] = *(const float (*)[8])(o + 8 * hf); *(u32x4*)(row + 512 * hf + 8 * lane) = pack8(oh); }
; }
; __global__ void __launch_bounds__(NWAVES * 64, 2) mk_fwd(Args args) {
;     ...
;                     } else {
;                         store_bf16_row16(o[j], XBo + (size_t)t * D, lane);
;                         const float qs = q8_row16(o[j], XQo + (size_t)t * D, lane);
;                         if (lane == 0) SXo[t] = qs;
	v_max3_f32 v89, |v24|, 0, |v25|
	v_max3_f32 v89, v89, |v26|, |v27|
	v_max3_f32 v89, v89, |v20|, |v21|
	v_max3_f32 v89, v89, |v22|, |v23|
	v_max3_f32 v89, v89, |v66|, |v67|
	v_max3_f32 v89, v89, |v68|, |v69|
	v_max3_f32 v89, v89, |v62|, |v63|
	v_max3_f32 v89, v89, |v64|, |v65|
	s_ashr_i32 s11, s10, 31
	s_lshl_b64 s[12:13], s[10:11], 11
	v_mov_b32_dpp v90, v89 quad_perm:[1,0,3,2] row_mask:0xf bank_mask:0xf bound_ctrl:1
	v_max_f32_e32 v90, v90, v90
	v_max_f32_e32 v89, v89, v90
	v_lshl_add_u64 v[92:93], v[106:107], 0, s[12:13]
	v_cvt_pk_bf16_f32 v86, v24, v25
	v_mov_b32_dpp v90, v89 quad_perm:[2,3,0,1] row_mask:0xf bank_mask:0xf bound_ctrl:1
	v_max_f32_e32 v90, v90, v90
	v_max_f32_e32 v89, v89, v90
	v_cvt_pk_bf16_f32 v87, v26, v27
	v_cvt_pk_bf16_f32 v88, v20, v21
	v_mov_b32_dpp v90, v89 row_half_mirror row_mask:0xf bank_mask:0xf bound_ctrl:1
	v_max_f32_e32 v90, v90, v90
	v_max_f32_e32 v89, v89, v90
	s_lshl_b64 s[6:7], s[10:11], 10
	s_nop 0
	v_mov_b32_dpp v90, v89 row_mirror row_mask:0xf bank_mask:0xf bound_ctrl:1
	v_max_f32_e32 v90, v90, v90
	v_max_f32_e32 v90, v89, v90
	ds_swizzle_b32 v91, v90 offset:swizzle(SWAP,16)
	v_cvt_pk_bf16_f32 v89, v22, v23
	global_store_dwordx4 v[92:93], v[86:89], off
	s_waitcnt lgkmcnt(0)
	s_nop 0
	v_max_f32_e32 v86, v91, v91
	v_max_f32_e32 v86, v90, v86
	v_mov_b32_e32 v87, v86
	s_nop 1
	v_permlane32_swap_b32_e32 v86, v87
	v_max_f32_e32 v87, v87, v87
	v_max_f32_e32 v86, v86, v86
	v_max_f32_e32 v86, v86, v87
	v_mul_f32_e32 v87, 0x3c010204, v86
	v_cmp_lt_f32_e32 vcc, 0, v86
	v_cvt_pk_bf16_f32 v88, v66, v67
	v_cvt_pk_bf16_f32 v89, v68, v69
	v_cndmask_b32_e32 v86, 1.0, v87, vcc
	v_div_scale_f32 v87, s[12:13], v86, v86, 1.0
	v_rcp_f32_e32 v146, v87
	v_cvt_pk_bf16_f32 v90, v62, v63
	v_cvt_pk_bf16_f32 v91, v64, v65
	global_store_dwordx4 v[92:93], v[88:91], off offset:1024
	s_nop 1
	v_fma_f32 v88, -v87, v146, 1.0
	v_fmac_f32_e32 v146, v88, v146
	v_div_scale_f32 v88, vcc, 1.0, v86, 1.0
	v_mul_f32_e32 v89, v88, v146
	v_fma_f32 v90, -v87, v89, v88
	v_fmac_f32_e32 v89, v90, v146
	v_fma_f32 v87, -v87, v89, v88
	v_div_fmas_f32 v87, v87, v146, v89
	v_div_fixup_f32 v87, v87, v86, 1.0
	v_fmaak_f32 v90, v24, v87, 0x4b400000
	v_fmaak_f32 v91, v25, v87, 0x4b400000
	v_fmaak_f32 v92, v26, v87, 0x4b400000
	v_fmaak_f32 v93, v27, v87, 0x4b400000
	v_perm_b32 v92, v93, v92, s61
	v_perm_b32 v90, v91, v90, s61
	v_perm_b32 v90, v92, v90, s79
	v_fmaak_f32 v91, v20, v87, 0x4b400000
	v_fmaak_f32 v92, v21, v87, 0x4b400000
	v_fmaak_f32 v93, v22, v87, 0x4b400000
	v_fmaak_f32 v146, v23, v87, 0x4b400000
	v_perm_b32 v93, v146, v93, s61
	v_perm_b32 v91, v92, v91, s61
	v_lshl_add_u64 v[88:89], v[108:109], 0, s[6:7]
	v_perm_b32 v91, v93, v91, s79
	global_store_dwordx2 v[88:89], v[90:91], off
	v_fmaak_f32 v90, v66, v87, 0x4b400000
	v_fmaak_f32 v91, v67, v87, 0x4b400000
	v_fmaak_f32 v92, v68, v87, 0x4b400000
	v_fmaak_f32 v93, v69, v87, 0x4b400000
	v_perm_b32 v92, v93, v92, s61
	v_perm_b32 v90, v91, v90, s61
	v_perm_b32 v90, v92, v90, s79
	v_fmaak_f32 v91, v62, v87, 0x4b400000
	v_fmaak_f32 v92, v63, v87, 0x4b400000
	v_fmaak_f32 v93, v64, v87, 0x4b400000
	v_fmaak_f32 v87, v65, v87, 0x4b400000
	v_perm_b32 v87, v87, v93, s61
	v_perm_b32 v91, v92, v91, s61
	v_perm_b32 v91, v87, v91, s79
	global_store_dwordx2 v[88:89], v[90:91], off offset:512
	s_and_saveexec_b64 s[6:7], s[4:5]
	s_cbranch_execz .LBB0_710
	s_lshl_b64 s[12:13], s[10:11], 2
	v_readlane_b32 s14, v254, 11
	v_readlane_b32 s15, v254, 12
	s_add_u32 s12, s14, s12
	s_addc_u32 s13, s15, s13
	global_store_dword v33, v86, s[12:13]
